# v_W minus 58 dead destination-zeroing moves before fp8 convert pairs and 66 duplicate lgkmcnt waits in the K-loops
# speedup vs baseline: 1.0050x; 1.0002x over previous
.LBB0_216:
	v_add_u32_e32 v130, s88, v196
	v_add_u32_e32 v134, s89, v196
	ds_read_b128 v[158:161], v130
	ds_read_b128 v[150:153], v130 offset:1024
	ds_read_b128 v[154:157], v130 offset:2048
	ds_read_b128 v[146:149], v130 offset:3072
	ds_read_b128 v[142:145], v134
	ds_read_b128 v[130:133], v134 offset:1024
	ds_read_b128 v[138:141], v134 offset:2048
	ds_read_b128 v[134:137], v134 offset:3072
	s_add_u32 s25, s50, 0xfff80080
	s_addc_u32 s56, s51, -1
	s_and_b64 s[18:19], s[18:19], exec
	s_cselect_b32 s59, s31, s56
	s_cselect_b32 s58, s4, s25
	s_cselect_b32 s57, s5, s64
	s_cselect_b32 s56, s29, s92
	s_add_i32 m0, s39, 0xc000
	ds_read_b128 v[186:189], v198
	ds_read_b128 v[190:193], v198 offset:1024
	ds_read_b128 v[200:203], v198 offset:2048
	ds_read_b128 v[204:207], v198 offset:3072
	ds_read_b128 v[208:211], v198 offset:4096
	ds_read_b128 v[212:215], v198 offset:5120
	ds_read_b128 v[216:219], v198 offset:6144
	ds_read_b128 v[220:223], v198 offset:7168
	global_load_lds_dwordx4 v170, s[50:51]
	s_add_i32 m0, s39, 0xe000
	s_nop 0
	global_load_lds_dwordx4 v172, s[50:51]
	s_waitcnt vmcnt(8)
	s_waitcnt lgkmcnt(0)
	s_barrier
	s_setprio 1
	v_mfma_i32_16x16x64_i8 v[126:129], v[158:161], v[186:189], v[126:129]
	v_mfma_i32_16x16x64_i8 v[122:125], v[154:157], v[186:189], v[122:125]
	v_mfma_i32_16x16x64_i8 v[106:109], v[154:157], v[200:203], v[106:109]
	v_mfma_i32_16x16x64_i8 v[110:113], v[158:161], v[200:203], v[110:113]
	v_mfma_i32_16x16x64_i8 v[94:97], v[158:161], v[208:211], v[94:97]
	v_mfma_i32_16x16x64_i8 v[90:93], v[154:157], v[208:211], v[90:93]
	v_mfma_i32_16x16x64_i8 v[74:77], v[154:157], v[216:219], v[74:77]
	v_mfma_i32_16x16x64_i8 v[78:81], v[158:161], v[216:219], v[78:81]
	s_nop 0
	v_mfma_i32_16x16x64_i8 v[126:129], v[150:153], v[190:193], v[126:129]
	v_mfma_i32_16x16x64_i8 v[122:125], v[146:149], v[190:193], v[122:125]
	v_mfma_i32_16x16x64_i8 v[106:109], v[146:149], v[204:207], v[106:109]
	v_mfma_i32_16x16x64_i8 v[110:113], v[150:153], v[204:207], v[110:113]
	v_mfma_i32_16x16x64_i8 v[94:97], v[150:153], v[212:215], v[94:97]
	v_mfma_i32_16x16x64_i8 v[90:93], v[146:149], v[212:215], v[90:93]
	v_mfma_i32_16x16x64_i8 v[74:77], v[146:149], v[220:223], v[74:77]
	v_mfma_i32_16x16x64_i8 v[78:81], v[150:153], v[220:223], v[78:81]
	v_mfma_i32_16x16x64_i8 v[118:121], v[142:145], v[186:189], v[118:121]
	v_mfma_i32_16x16x64_i8 v[114:117], v[138:141], v[186:189], v[114:117]
	v_mfma_i32_16x16x64_i8 v[98:101], v[138:141], v[200:203], v[98:101]
	v_mfma_i32_16x16x64_i8 v[102:105], v[142:145], v[200:203], v[102:105]
	v_mfma_i32_16x16x64_i8 v[86:89], v[142:145], v[208:211], v[86:89]
	v_mfma_i32_16x16x64_i8 v[82:85], v[138:141], v[208:211], v[82:85]
	v_mfma_i32_16x16x64_i8 v[66:69], v[138:141], v[216:219], v[66:69]
	v_mfma_i32_16x16x64_i8 v[70:73], v[142:145], v[216:219], v[70:73]
	s_nop 0
	v_mfma_i32_16x16x64_i8 v[118:121], v[130:133], v[190:193], v[118:121]
	v_mfma_i32_16x16x64_i8 v[114:117], v[134:137], v[190:193], v[114:117]
	v_mfma_i32_16x16x64_i8 v[98:101], v[134:137], v[204:207], v[98:101]
	v_mfma_i32_16x16x64_i8 v[102:105], v[130:133], v[204:207], v[102:105]
	v_mfma_i32_16x16x64_i8 v[86:89], v[130:133], v[212:215], v[86:89]
	v_mfma_i32_16x16x64_i8 v[82:85], v[134:137], v[212:215], v[82:85]
	v_mfma_i32_16x16x64_i8 v[66:69], v[134:137], v[220:223], v[66:69]
	v_mfma_i32_16x16x64_i8 v[70:73], v[130:133], v[220:223], v[70:73]
	s_setprio 0
	s_barrier
	s_add_i32 s18, s88, s7
	s_mov_b32 m0, s18
	ds_read_b128 v[200:203], v198 offset:16384
	ds_read_b128 v[204:207], v198 offset:17408
	ds_read_b128 v[208:211], v198 offset:18432
	ds_read_b128 v[212:215], v198 offset:19456
	ds_read_b128 v[216:219], v198 offset:20480
	ds_read_b128 v[220:223], v198 offset:21504
	ds_read_b128 v[224:227], v198 offset:22528
	ds_read_b128 v[228:231], v198 offset:23552
	global_load_lds_dwordx4 v164, s[56:57]
	s_add_i32 m0, s18, 0x2000
	s_add_u32 s18, s56, 0x80000
	s_addc_u32 s19, s57, 0
	s_add_i32 s25, s89, s7
	global_load_lds_dwordx4 v168, s[56:57]
	s_mov_b32 m0, s25
	s_nop 0
	global_load_lds_dwordx4 v164, s[18:19]
	s_add_i32 m0, s25, 0x2000
	s_nop 0
	global_load_lds_dwordx4 v168, s[18:19]
	s_mov_b32 m0, s39
	s_nop 0
	global_load_lds_dwordx4 v162, s[58:59]
	s_mov_b32 m0, s43
	s_nop 0
	global_load_lds_dwordx4 v166, s[58:59]
	s_waitcnt vmcnt(8)
	s_waitcnt lgkmcnt(0)
	s_barrier
	s_setprio 1
	v_mfma_i32_16x16x64_i8 v[62:65], v[158:161], v[200:203], v[62:65]
	v_mfma_i32_16x16x64_i8 v[58:61], v[154:157], v[200:203], v[58:61]
	v_mfma_i32_16x16x64_i8 v[42:45], v[154:157], v[208:211], v[42:45]
	v_mfma_i32_16x16x64_i8 v[46:49], v[158:161], v[208:211], v[46:49]
	v_mfma_i32_16x16x64_i8 v[30:33], v[158:161], v[216:219], v[30:33]
	v_mfma_i32_16x16x64_i8 v[26:29], v[154:157], v[216:219], v[26:29]
	v_mfma_i32_16x16x64_i8 v[10:13], v[154:157], v[224:227], v[10:13]
	v_mfma_i32_16x16x64_i8 v[14:17], v[158:161], v[224:227], v[14:17]
	s_nop 0
	v_mfma_i32_16x16x64_i8 v[62:65], v[150:153], v[204:207], v[62:65]
	v_mfma_i32_16x16x64_i8 v[58:61], v[146:149], v[204:207], v[58:61]
	v_mfma_i32_16x16x64_i8 v[42:45], v[146:149], v[212:215], v[42:45]
	v_mfma_i32_16x16x64_i8 v[46:49], v[150:153], v[212:215], v[46:49]
	v_mfma_i32_16x16x64_i8 v[30:33], v[150:153], v[220:223], v[30:33]
	v_mfma_i32_16x16x64_i8 v[26:29], v[146:149], v[220:223], v[26:29]
	v_mfma_i32_16x16x64_i8 v[10:13], v[146:149], v[228:231], v[10:13]
	v_mfma_i32_16x16x64_i8 v[14:17], v[150:153], v[228:231], v[14:17]
	v_mfma_i32_16x16x64_i8 v[54:57], v[142:145], v[200:203], v[54:57]
	v_mfma_i32_16x16x64_i8 v[50:53], v[138:141], v[200:203], v[50:53]
	v_mfma_i32_16x16x64_i8 v[34:37], v[138:141], v[208:211], v[34:37]
	v_mfma_i32_16x16x64_i8 v[38:41], v[142:145], v[208:211], v[38:41]
	v_mfma_i32_16x16x64_i8 v[22:25], v[142:145], v[216:219], v[22:25]
	v_mfma_i32_16x16x64_i8 v[18:21], v[138:141], v[216:219], v[18:21]
	v_mfma_i32_16x16x64_i8 v[2:5], v[138:141], v[224:227], v[2:5]
	v_mfma_i32_16x16x64_i8 v[6:9], v[142:145], v[224:227], v[6:9]
	s_nop 0
	v_mfma_i32_16x16x64_i8 v[54:57], v[130:133], v[204:207], v[54:57]
	v_mfma_i32_16x16x64_i8 v[50:53], v[134:137], v[204:207], v[50:53]
	v_mfma_i32_16x16x64_i8 v[34:37], v[134:137], v[212:215], v[34:37]
	v_mfma_i32_16x16x64_i8 v[38:41], v[130:133], v[212:215], v[38:41]
	v_mfma_i32_16x16x64_i8 v[22:25], v[130:133], v[220:223], v[22:25]
	v_mfma_i32_16x16x64_i8 v[18:21], v[134:137], v[220:223], v[18:21]
	v_mfma_i32_16x16x64_i8 v[2:5], v[134:137], v[228:231], v[2:5]
	v_mfma_i32_16x16x64_i8 v[6:9], v[130:133], v[228:231], v[6:9]
	s_setprio 0
	s_barrier
	s_add_i32 s25, 0, 0x18000
	s_add_i32 vcc_lo, 0, 0x1c000
	v_add_u32_e32 v142, s25, v196
	v_add_u32_e32 v158, vcc_lo, v196
	ds_read_b128 v[130:133], v142
	ds_read_b128 v[134:137], v142 offset:1024
	ds_read_b128 v[138:141], v142 offset:2048
	ds_read_b128 v[142:145], v142 offset:3072
	ds_read_b128 v[146:149], v158
	ds_read_b128 v[150:153], v158 offset:1024
	ds_read_b128 v[154:157], v158 offset:2048
	ds_read_b128 v[158:161], v158 offset:3072
	s_add_u32 s18, s58, 0x80000
	s_addc_u32 s19, s59, 0
	s_mov_b32 m0, s61
	ds_read_b128 v[200:203], v198 offset:32768
	ds_read_b128 v[204:207], v198 offset:33792
	ds_read_b128 v[208:211], v198 offset:34816
	ds_read_b128 v[212:215], v198 offset:35840
	ds_read_b128 v[216:219], v198 offset:36864
	ds_read_b128 v[220:223], v198 offset:37888
	ds_read_b128 v[224:227], v198 offset:38912
	ds_read_b128 v[228:231], v198 offset:39936
	global_load_lds_dwordx4 v162, s[18:19]
	s_mov_b32 m0, s62
	s_nop 0
	global_load_lds_dwordx4 v166, s[18:19]
	s_waitcnt vmcnt(8)
	s_waitcnt lgkmcnt(0)
	s_barrier
	s_setprio 1
	v_mfma_i32_16x16x64_i8 v[126:129], v[130:133], v[200:203], v[126:129]
	v_mfma_i32_16x16x64_i8 v[122:125], v[138:141], v[200:203], v[122:125]
	v_mfma_i32_16x16x64_i8 v[106:109], v[138:141], v[208:211], v[106:109]
	v_mfma_i32_16x16x64_i8 v[110:113], v[130:133], v[208:211], v[110:113]
	v_mfma_i32_16x16x64_i8 v[94:97], v[130:133], v[216:219], v[94:97]
	v_mfma_i32_16x16x64_i8 v[90:93], v[138:141], v[216:219], v[90:93]
	v_mfma_i32_16x16x64_i8 v[74:77], v[138:141], v[224:227], v[74:77]
	v_mfma_i32_16x16x64_i8 v[78:81], v[130:133], v[224:227], v[78:81]
	s_nop 0
	v_mfma_i32_16x16x64_i8 v[126:129], v[134:137], v[204:207], v[126:129]
	v_mfma_i32_16x16x64_i8 v[122:125], v[142:145], v[204:207], v[122:125]
	v_mfma_i32_16x16x64_i8 v[106:109], v[142:145], v[212:215], v[106:109]
	v_mfma_i32_16x16x64_i8 v[110:113], v[134:137], v[212:215], v[110:113]
	v_mfma_i32_16x16x64_i8 v[94:97], v[134:137], v[220:223], v[94:97]
	v_mfma_i32_16x16x64_i8 v[90:93], v[142:145], v[220:223], v[90:93]
	v_mfma_i32_16x16x64_i8 v[74:77], v[142:145], v[228:231], v[74:77]
	v_mfma_i32_16x16x64_i8 v[78:81], v[134:137], v[228:231], v[78:81]
	v_mfma_i32_16x16x64_i8 v[118:121], v[146:149], v[200:203], v[118:121]
	v_mfma_i32_16x16x64_i8 v[114:117], v[154:157], v[200:203], v[114:117]
	v_mfma_i32_16x16x64_i8 v[98:101], v[154:157], v[208:211], v[98:101]
	v_mfma_i32_16x16x64_i8 v[102:105], v[146:149], v[208:211], v[102:105]
	v_mfma_i32_16x16x64_i8 v[86:89], v[146:149], v[216:219], v[86:89]
	v_mfma_i32_16x16x64_i8 v[82:85], v[154:157], v[216:219], v[82:85]
	v_mfma_i32_16x16x64_i8 v[66:69], v[154:157], v[224:227], v[66:69]
	v_mfma_i32_16x16x64_i8 v[70:73], v[146:149], v[224:227], v[70:73]
	s_nop 0
	v_mfma_i32_16x16x64_i8 v[118:121], v[150:153], v[204:207], v[118:121]
	v_mfma_i32_16x16x64_i8 v[114:117], v[158:161], v[204:207], v[114:117]
	v_mfma_i32_16x16x64_i8 v[98:101], v[158:161], v[212:215], v[98:101]
	v_mfma_i32_16x16x64_i8 v[102:105], v[150:153], v[212:215], v[102:105]
	v_mfma_i32_16x16x64_i8 v[86:89], v[150:153], v[220:223], v[86:89]
	v_mfma_i32_16x16x64_i8 v[82:85], v[158:161], v[220:223], v[82:85]
	v_mfma_i32_16x16x64_i8 v[66:69], v[158:161], v[228:231], v[66:69]
	v_mfma_i32_16x16x64_i8 v[70:73], v[150:153], v[228:231], v[70:73]
	s_setprio 0
	s_barrier
	s_add_i32 s18, s25, s7
	s_mov_b32 m0, s18
	s_add_u32 s98, s56, 0x80
	s_addc_u32 s99, s57, 0
	s_add_u32 s100, s58, 0x80
	s_addc_u32 s101, s59, 0
	ds_read_b128 v[200:203], v198 offset:49152
	ds_read_b128 v[204:207], v198 offset:50176
	ds_read_b128 v[208:211], v198 offset:51200
	ds_read_b128 v[212:215], v198 offset:52224
	ds_read_b128 v[216:219], v198 offset:53248
	ds_read_b128 v[220:223], v198 offset:54272
	ds_read_b128 v[224:227], v198 offset:55296
	ds_read_b128 v[228:231], v198 offset:56320
	global_load_lds_dwordx4 v164, s[98:99]
	s_add_i32 m0, s18, 0x2000
	s_add_u32 s18, s56, 0x80080
	s_addc_u32 s19, s57, 0
	s_add_i32 s25, vcc_lo, s7
	global_load_lds_dwordx4 v168, s[98:99]
	s_mov_b32 m0, s25
	s_nop 0
	global_load_lds_dwordx4 v164, s[18:19]
	s_add_i32 m0, s25, 0x2000
	s_nop 0
	global_load_lds_dwordx4 v168, s[18:19]
	s_mov_b32 m0, s67
	s_nop 0
	global_load_lds_dwordx4 v162, s[100:101]
	s_mov_b32 m0, s68
	s_nop 0
	global_load_lds_dwordx4 v166, s[100:101]
	s_waitcnt vmcnt(8)
	s_waitcnt lgkmcnt(0)
	s_barrier
	s_setprio 1
	v_mfma_i32_16x16x64_i8 v[62:65], v[130:133], v[200:203], v[62:65]
	v_mfma_i32_16x16x64_i8 v[58:61], v[138:141], v[200:203], v[58:61]
	v_mfma_i32_16x16x64_i8 v[42:45], v[138:141], v[208:211], v[42:45]
	v_mfma_i32_16x16x64_i8 v[46:49], v[130:133], v[208:211], v[46:49]
	v_mfma_i32_16x16x64_i8 v[30:33], v[130:133], v[216:219], v[30:33]
	v_mfma_i32_16x16x64_i8 v[26:29], v[138:141], v[216:219], v[26:29]
	v_mfma_i32_16x16x64_i8 v[10:13], v[138:141], v[224:227], v[10:13]
	v_mfma_i32_16x16x64_i8 v[14:17], v[130:133], v[224:227], v[14:17]
	s_nop 0
	v_mfma_i32_16x16x64_i8 v[62:65], v[134:137], v[204:207], v[62:65]
	v_mfma_i32_16x16x64_i8 v[58:61], v[142:145], v[204:207], v[58:61]
	v_mfma_i32_16x16x64_i8 v[42:45], v[142:145], v[212:215], v[42:45]
	v_mfma_i32_16x16x64_i8 v[46:49], v[134:137], v[212:215], v[46:49]
	v_mfma_i32_16x16x64_i8 v[30:33], v[134:137], v[220:223], v[30:33]
	v_mfma_i32_16x16x64_i8 v[26:29], v[142:145], v[220:223], v[26:29]
	v_mfma_i32_16x16x64_i8 v[10:13], v[142:145], v[228:231], v[10:13]
	v_mfma_i32_16x16x64_i8 v[14:17], v[134:137], v[228:231], v[14:17]
	v_mfma_i32_16x16x64_i8 v[54:57], v[146:149], v[200:203], v[54:57]
	v_mfma_i32_16x16x64_i8 v[50:53], v[154:157], v[200:203], v[50:53]
	v_mfma_i32_16x16x64_i8 v[34:37], v[154:157], v[208:211], v[34:37]
	v_mfma_i32_16x16x64_i8 v[38:41], v[146:149], v[208:211], v[38:41]
	v_mfma_i32_16x16x64_i8 v[22:25], v[146:149], v[216:219], v[22:25]
	v_mfma_i32_16x16x64_i8 v[18:21], v[154:157], v[216:219], v[18:21]
	v_mfma_i32_16x16x64_i8 v[2:5], v[154:157], v[224:227], v[2:5]
	v_mfma_i32_16x16x64_i8 v[6:9], v[146:149], v[224:227], v[6:9]
	s_nop 0
	v_mfma_i32_16x16x64_i8 v[54:57], v[150:153], v[204:207], v[54:57]
	v_mfma_i32_16x16x64_i8 v[50:53], v[158:161], v[204:207], v[50:53]
	v_mfma_i32_16x16x64_i8 v[34:37], v[158:161], v[212:215], v[34:37]
	v_mfma_i32_16x16x64_i8 v[38:41], v[150:153], v[212:215], v[38:41]
	v_mfma_i32_16x16x64_i8 v[22:25], v[150:153], v[220:223], v[22:25]
	v_mfma_i32_16x16x64_i8 v[18:21], v[158:161], v[220:223], v[18:21]
	v_mfma_i32_16x16x64_i8 v[2:5], v[158:161], v[228:231], v[2:5]
	v_mfma_i32_16x16x64_i8 v[6:9], v[150:153], v[228:231], v[6:9]
	s_setprio 0
	s_barrier
	s_add_i32 s65, s65, 2
	s_add_u32 s50, s50, 0x100
	s_addc_u32 s51, s51, 0
	s_add_u32 s92, s92, 0x100
	s_addc_u32 s64, s64, 0
	s_cmp_gt_u32 s65, 29
	s_cbranch_scc1 .LBB0_219

.LBB0_221:
	s_lshl_b32 s4, s49, 11
	s_and_b32 s4, s4, 0x800
	s_add_i32 s4, s4, 0
	s_add_i32 s4, s4, 0x22000
	s_lshl_b32 s5, s66, 2
	s_add_i32 s5, s4, s5
	v_lshl_add_u32 v131, v195, 2, s5
	s_lshl_b32 s5, s63, 2
	s_add_i32 s4, s4, s5
	v_lshl_add_u32 v149, v1, 2, s4
	ds_read_b128 v[150:153], v131 offset:1024
	ds_read_b128 v[154:157], v131 offset:1040
	ds_read_b128 v[158:161], v131 offset:1536
	ds_read_b128 v[184:187], v131 offset:1552
	ds_read2_b32 v[146:147], v149 offset1:16
	v_cvt_f32_i32_e32 v135, v126
	v_cvt_f32_i32_e32 v134, v118
	s_waitcnt lgkmcnt(0)
	v_mul_f32_e32 v180, 0x3c010204, v158
	v_mov_b32_e32 v137, v150
	v_mov_b32_e32 v136, v146
	v_pk_mul_f32 v[188:189], v[180:181], v[136:137]
	v_mov_b32_e32 v183, v146
	v_pk_mul_f32 v[136:137], v[188:189], v[182:183]
	v_cvt_f32_i32_e32 v139, v122
	v_cvt_f32_i32_e32 v138, v114
	v_pk_mul_f32 v[190:191], v[136:137], v[134:135]
	v_mul_f32_e32 v134, 0x3c010204, v184
	v_mov_b32_e32 v136, v146
	v_mov_b32_e32 v137, v154
	v_mov_b32_e32 v135, v181
	v_pk_mul_f32 v[136:137], v[136:137], v[134:135]
	v_mul_f32_e32 v118, 0x3c010204, v159
	v_pk_mul_f32 v[140:141], v[136:137], v[182:183]
	v_mov_b32_e32 v150, v146
	v_pk_mul_f32 v[192:193], v[140:141], v[138:139]
	v_cvt_f32_i32_e32 v139, v127
	v_cvt_f32_i32_e32 v138, v119
	v_mov_b32_e32 v119, v181
	v_pk_mul_f32 v[126:127], v[118:119], v[150:151]
	v_mul_f32_e32 v122, 0x3c010204, v185
	v_pk_mul_f32 v[140:141], v[126:127], v[182:183]
	v_mov_b32_e32 v154, v146
	v_pk_mul_f32 v[150:151], v[140:141], v[138:139]
	v_cvt_f32_i32_e32 v141, v123
	v_cvt_f32_i32_e32 v140, v115
	v_mov_b32_e32 v123, v181
	v_pk_mul_f32 v[138:139], v[154:155], v[122:123]
	v_cvt_f32_i32_e32 v143, v128
	v_pk_mul_f32 v[114:115], v[138:139], v[182:183]
	v_cvt_f32_i32_e32 v142, v120
	v_pk_mul_f32 v[154:155], v[114:115], v[140:141]
	v_mul_f32_e32 v114, 0x3c010204, v160
	v_mul_f32_e32 v120, 0x3c010204, v161
	v_cvt_f32_i32_e32 v161, v129
	v_cvt_f32_i32_e32 v160, v121
	v_mov_b32_e32 v115, v181
	v_mov_b32_e32 v140, v146
	v_mov_b32_e32 v141, v152
	v_mov_b32_e32 v121, v181
	v_mov_b32_e32 v152, v146
	v_pk_mul_f32 v[140:141], v[114:115], v[140:141]
	v_pk_mul_f32 v[128:129], v[120:121], v[152:153]
	v_pk_mul_f32 v[144:145], v[140:141], v[182:183]
	v_pk_mul_f32 v[152:153], v[128:129], v[182:183]
	v_pk_mul_f32 v[158:159], v[144:145], v[142:143]
	v_cvt_f32_i32_e32 v184, v116
	v_mov_b32_e32 v145, v156
	v_pk_mul_f32 v[152:153], v[152:153], v[160:161]
	v_mul_f32_e32 v116, 0x3c010204, v187
	v_cvt_f32_i32_e32 v160, v117
	v_mov_b32_e32 v156, v146
	v_mov_b32_e32 v117, v181
	v_cvt_f32_i32_e32 v185, v124
	v_cvt_f32_i32_e32 v161, v125
	v_mul_f32_e32 v115, 0xbfb8aa3b, v191
	v_pk_mul_f32 v[124:125], v[156:157], v[116:117]
	v_mul_f32_e32 v117, 0xbfb8aa3b, v151
	v_exp_f32_e32 v115, v115
	v_exp_f32_e32 v117, v117
	v_mul_f32_e32 v119, 0xbfb8aa3b, v159
	v_mul_f32_e32 v121, 0xbfb8aa3b, v153
	v_exp_f32_e32 v119, v119
	v_exp_f32_e32 v121, v121
	v_add_f32_e32 v115, 1.0, v115
	v_add_f32_e32 v117, 1.0, v117
	v_rcp_f32_e32 v115, v115
	v_rcp_f32_e32 v117, v117
	v_add_f32_e32 v119, 1.0, v119
	v_add_f32_e32 v121, 1.0, v121
	v_rcp_f32_e32 v119, v119
	v_rcp_f32_e32 v121, v121
	v_mul_f32_e32 v123, 0xbfb8aa3b, v193
	v_exp_f32_e32 v123, v123
	v_mul_f32_e32 v115, v191, v115
	v_mul_f32_e32 v117, v151, v117
	v_mul_f32_e32 v115, v190, v115
	v_mul_f32_e32 v117, v150, v117
	v_mul_f32_e32 v119, v159, v119
	v_mul_f32_e32 v121, v153, v121
	v_mul_f32_e32 v119, v158, v119
	v_mul_f32_e32 v121, v152, v121
	v_med3_f32 v115, v115, s94, v199
	v_med3_f32 v117, v117, s94, v199
	v_cvt_pk_fp8_f32 v150, v115, v117
	v_med3_f32 v115, v119, s94, v199
	v_med3_f32 v117, v121, s94, v199
	v_add_f32_e32 v119, 1.0, v123
	v_mul_f32_e32 v121, 0xbfb8aa3b, v155
	v_mul_f32_e32 v142, 0x3c010204, v186
	v_mov_b32_e32 v144, v146
	v_mov_b32_e32 v143, v181
	v_rcp_f32_e32 v119, v119
	v_exp_f32_e32 v121, v121
	v_pk_mul_f32 v[144:145], v[144:145], v[142:143]
	v_pk_mul_f32 v[156:157], v[124:125], v[182:183]
	v_pk_mul_f32 v[200:201], v[144:145], v[182:183]
	v_pk_mul_f32 v[156:157], v[156:157], v[160:161]
	v_pk_mul_f32 v[184:185], v[200:201], v[184:185]
	v_cvt_pk_fp8_f32 v150, v115, v117 op_sel:[0,0,1]
	v_mul_f32_e32 v115, v193, v119
	v_add_f32_e32 v117, 1.0, v121
	v_mul_f32_e32 v119, 0xbfb8aa3b, v185
	v_mul_f32_e32 v121, 0xbfb8aa3b, v157
	v_exp_f32_e32 v119, v119
	v_exp_f32_e32 v121, v121
	v_rcp_f32_e32 v117, v117
	v_mul_f32_e32 v115, v192, v115
	v_add_f32_e32 v119, 1.0, v119
	v_add_f32_e32 v121, 1.0, v121
	v_mul_f32_e32 v117, v155, v117
	v_rcp_f32_e32 v119, v119
	v_rcp_f32_e32 v121, v121
	v_mul_f32_e32 v117, v154, v117
	v_med3_f32 v115, v115, s94, v199
	v_med3_f32 v117, v117, s94, v199
	v_cvt_pk_fp8_f32 v151, v115, v117
	v_mul_f32_e32 v119, v185, v119
	v_mul_f32_e32 v121, v157, v121
	v_mul_f32_e32 v119, v184, v119
	v_mul_f32_e32 v115, v156, v121
	v_med3_f32 v117, v119, s94, v199
	v_med3_f32 v115, v115, s94, v199
	v_cvt_pk_fp8_f32 v151, v117, v115 op_sel:[0,0,1]
	v_lshl_add_u32 v148, s42, 8, v194
	v_lshl_or_b32 v130, s38, 7, v197
	v_mov_b64_e32 v[132:133], s[96:97]
	v_ashrrev_i32_e32 v131, 31, v130
	v_mad_i64_i32 v[152:153], s[4:5], v148, s93, v[132:133]
	v_lshl_add_u64 v[152:153], v[152:153], 0, v[130:131]
	global_store_dwordx2 v[152:153], v[150:151], off
	v_cvt_f32_i32_e32 v151, v110
	v_cvt_f32_i32_e32 v150, v102
	v_mul_f32_e32 v146, v180, v147
	v_mov_b32_e32 v183, v189
	v_pk_mul_f32 v[152:153], v[182:183], v[146:147]
	v_mul_f32_e32 v146, v134, v147
	v_pk_mul_f32 v[150:151], v[152:153], v[150:151]
	v_cvt_f32_i32_e32 v153, v106
	v_mov_b32_e32 v136, v182
	v_cvt_f32_i32_e32 v107, v107
	v_cvt_f32_i32_e32 v106, v99
	v_pk_mul_f32 v[154:155], v[136:137], v[146:147]
	v_mul_f32_e32 v146, v118, v147
	v_mov_b32_e32 v126, v182
	v_cvt_f32_i32_e32 v111, v111
	v_cvt_f32_i32_e32 v110, v103
	v_pk_mul_f32 v[102:103], v[126:127], v[146:147]
	v_mul_f32_e32 v146, v122, v147
	v_mov_b32_e32 v138, v182
	v_cvt_f32_i32_e32 v152, v98
	v_pk_mul_f32 v[98:99], v[138:139], v[146:147]
	v_mul_f32_e32 v146, v114, v147
	v_pk_mul_f32 v[98:99], v[98:99], v[106:107]
	v_cvt_f32_i32_e32 v107, v112
	v_cvt_f32_i32_e32 v106, v104
	v_mov_b32_e32 v140, v182
	v_cvt_f32_i32_e32 v113, v113
	v_cvt_f32_i32_e32 v112, v105
	v_pk_mul_f32 v[102:103], v[102:103], v[110:111]
	v_pk_mul_f32 v[110:111], v[140:141], v[146:147]
	v_mul_f32_e32 v146, v142, v147
	v_mov_b32_e32 v144, v182
	v_pk_mul_f32 v[152:153], v[154:155], v[152:153]
	v_pk_mul_f32 v[154:155], v[144:145], v[146:147]
	v_mul_f32_e32 v146, v120, v147
	v_mov_b32_e32 v128, v182
	v_pk_mul_f32 v[106:107], v[110:111], v[106:107]
	v_cvt_f32_i32_e32 v110, v100
	v_pk_mul_f32 v[104:105], v[128:129], v[146:147]
	v_mul_f32_e32 v100, 0xbfb8aa3b, v151
	v_pk_mul_f32 v[104:105], v[104:105], v[112:113]
	v_exp_f32_e32 v112, v100
	v_mul_f32_e32 v113, 0xbfb8aa3b, v103
	v_cvt_f32_i32_e32 v111, v108
	v_cvt_f32_i32_e32 v109, v109
	v_add_f32_e32 v112, 1.0, v112
	v_cvt_f32_i32_e32 v108, v101
	v_rcp_f32_e32 v112, v112
	v_exp_f32_e32 v113, v113
	v_mul_f32_e32 v146, v116, v147
	v_mov_b32_e32 v124, v182
	v_pk_mul_f32 v[100:101], v[124:125], v[146:147]
	v_pk_mul_f32 v[110:111], v[154:155], v[110:111]
	v_pk_mul_f32 v[100:101], v[100:101], v[108:109]
	v_mul_f32_e32 v108, v151, v112
	v_add_f32_e32 v109, 1.0, v113
	v_mul_f32_e32 v112, 0xbfb8aa3b, v107
	v_rcp_f32_e32 v109, v109
	v_exp_f32_e32 v112, v112
	v_mul_f32_e32 v113, 0xbfb8aa3b, v105
	v_exp_f32_e32 v113, v113
	v_mul_f32_e32 v103, v103, v109
	v_add_f32_e32 v109, 1.0, v112
	v_rcp_f32_e32 v109, v109
	v_add_f32_e32 v112, 1.0, v113
	v_rcp_f32_e32 v112, v112
	v_mul_f32_e32 v102, v102, v103
	v_mul_f32_e32 v103, v107, v109
	v_mul_f32_e32 v107, 0xbfb8aa3b, v153
	v_exp_f32_e32 v107, v107
	v_mul_f32_e32 v108, v150, v108
	v_mul_f32_e32 v105, v105, v112
	v_mul_f32_e32 v103, v106, v103
	v_mul_f32_e32 v104, v104, v105
	v_med3_f32 v105, v108, s94, v199
	v_med3_f32 v106, v102, s94, v199
	v_cvt_pk_fp8_f32 v102, v105, v106
	v_add_f32_e32 v105, 1.0, v107
	v_mul_f32_e32 v106, 0xbfb8aa3b, v99
	v_rcp_f32_e32 v105, v105
	v_exp_f32_e32 v106, v106
	v_med3_f32 v103, v103, s94, v199
	v_med3_f32 v104, v104, s94, v199
	v_cvt_pk_fp8_f32 v102, v103, v104 op_sel:[0,0,1]
	v_mul_f32_e32 v103, v153, v105
	v_add_f32_e32 v104, 1.0, v106
	v_mul_f32_e32 v105, 0xbfb8aa3b, v111
	v_rcp_f32_e32 v104, v104
	v_exp_f32_e32 v105, v105
	v_mul_f32_e32 v106, 0xbfb8aa3b, v101
	v_exp_f32_e32 v106, v106
	v_mul_f32_e32 v99, v99, v104
	v_add_f32_e32 v104, 1.0, v105
	v_rcp_f32_e32 v104, v104
	v_add_f32_e32 v105, 1.0, v106
	v_rcp_f32_e32 v105, v105
	v_mul_f32_e32 v103, v152, v103
	v_mul_f32_e32 v98, v98, v99
	v_mul_f32_e32 v99, v111, v104
	v_med3_f32 v104, v103, s94, v199
	v_med3_f32 v98, v98, s94, v199
	v_cvt_pk_fp8_f32 v103, v104, v98
	v_mul_f32_e32 v101, v101, v105
	v_mul_f32_e32 v99, v110, v99
	v_mul_f32_e32 v98, v100, v101
	v_or_b32_e32 v115, 16, v148
	v_med3_f32 v99, v99, s94, v199
	v_med3_f32 v98, v98, s94, v199
	v_cvt_pk_fp8_f32 v103, v99, v98 op_sel:[0,0,1]
	v_mad_i64_i32 v[98:99], s[4:5], v115, s93, v[132:133]
	v_lshl_add_u64 v[100:101], v[98:99], 0, v[130:131]
	ds_read2_b32 v[98:99], v149 offset0:32 offset1:48
	global_store_dwordx2 v[100:101], v[102:103], off
	v_cvt_f32_i32_e32 v101, v94
	v_cvt_f32_i32_e32 v100, v86
	v_cvt_f32_i32_e32 v91, v91
	s_waitcnt lgkmcnt(0)
	v_mul_f32_e32 v102, v180, v98
	v_mov_b32_e32 v103, v98
	v_pk_mul_f32 v[102:103], v[182:183], v[102:103]
	v_cvt_f32_i32_e32 v95, v95
	v_pk_mul_f32 v[100:101], v[102:103], v[100:101]
	v_cvt_f32_i32_e32 v103, v90
	v_cvt_f32_i32_e32 v90, v83
	v_cvt_f32_i32_e32 v102, v82
	v_cvt_f32_i32_e32 v94, v87
	v_mul_f32_e32 v82, v122, v98
	v_mov_b32_e32 v83, v98
	v_pk_mul_f32 v[82:83], v[138:139], v[82:83]
	v_mul_f32_e32 v86, v118, v98
	v_mov_b32_e32 v87, v98
	v_pk_mul_f32 v[82:83], v[82:83], v[90:91]
	v_cvt_f32_i32_e32 v91, v96
	v_cvt_f32_i32_e32 v90, v88
	v_pk_mul_f32 v[86:87], v[126:127], v[86:87]
	v_cvt_f32_i32_e32 v97, v97
	v_cvt_f32_i32_e32 v96, v89
	v_pk_mul_f32 v[86:87], v[86:87], v[94:95]
	v_mul_f32_e32 v94, v114, v98
	v_mov_b32_e32 v95, v98
	v_pk_mul_f32 v[94:95], v[140:141], v[94:95]
	v_mul_f32_e32 v88, v120, v98
	v_mov_b32_e32 v89, v98
	v_pk_mul_f32 v[90:91], v[94:95], v[90:91]
	v_cvt_f32_i32_e32 v95, v92
	v_pk_mul_f32 v[88:89], v[128:129], v[88:89]
	v_mul_f32_e32 v92, 0xbfb8aa3b, v101
	v_pk_mul_f32 v[88:89], v[88:89], v[96:97]
	v_exp_f32_e32 v96, v92
	v_mul_f32_e32 v97, 0xbfb8aa3b, v87
	v_cvt_f32_i32_e32 v93, v93
	v_cvt_f32_i32_e32 v92, v85
	v_add_f32_e32 v96, 1.0, v96
	v_rcp_f32_e32 v96, v96
	v_exp_f32_e32 v97, v97
	v_cvt_f32_i32_e32 v94, v84
	v_mul_f32_e32 v84, v116, v98
	v_mov_b32_e32 v85, v98
	v_pk_mul_f32 v[84:85], v[124:125], v[84:85]
	v_mul_f32_e32 v104, v134, v98
	v_pk_mul_f32 v[84:85], v[84:85], v[92:93]
	v_mul_f32_e32 v92, v101, v96
	v_add_f32_e32 v93, 1.0, v97
	v_mul_f32_e32 v96, 0xbfb8aa3b, v91
	v_rcp_f32_e32 v93, v93
	v_exp_f32_e32 v96, v96
	v_mul_f32_e32 v97, 0xbfb8aa3b, v89
	v_exp_f32_e32 v97, v97
	v_mul_f32_e32 v87, v87, v93
	v_add_f32_e32 v93, 1.0, v96
	v_rcp_f32_e32 v93, v93
	v_mov_b32_e32 v105, v98
	v_pk_mul_f32 v[104:105], v[136:137], v[104:105]
	v_add_f32_e32 v96, 1.0, v97
	v_pk_mul_f32 v[102:103], v[104:105], v[102:103]
	v_rcp_f32_e32 v96, v96
	v_mul_f32_e32 v86, v86, v87
	v_mul_f32_e32 v87, v91, v93
	v_mul_f32_e32 v91, 0xbfb8aa3b, v103
	v_exp_f32_e32 v91, v91
	v_mul_f32_e32 v92, v100, v92
	v_mul_f32_e32 v89, v89, v96
	v_mul_f32_e32 v87, v90, v87
	v_mul_f32_e32 v88, v88, v89
	v_med3_f32 v89, v92, s94, v199
	v_med3_f32 v90, v86, s94, v199
	v_cvt_pk_fp8_f32 v86, v89, v90
	v_add_f32_e32 v89, 1.0, v91
	v_mul_f32_e32 v90, 0xbfb8aa3b, v83
	v_rcp_f32_e32 v89, v89
	v_exp_f32_e32 v90, v90
	v_mul_f32_e32 v104, v142, v98
	v_mov_b32_e32 v105, v98
	v_pk_mul_f32 v[104:105], v[144:145], v[104:105]
	v_med3_f32 v87, v87, s94, v199
	v_pk_mul_f32 v[94:95], v[104:105], v[94:95]
	v_med3_f32 v88, v88, s94, v199
	v_cvt_pk_fp8_f32 v86, v87, v88 op_sel:[0,0,1]
	v_mul_f32_e32 v87, v103, v89
	v_add_f32_e32 v88, 1.0, v90
	v_mul_f32_e32 v89, 0xbfb8aa3b, v95
	v_rcp_f32_e32 v88, v88
	v_exp_f32_e32 v89, v89
	v_mul_f32_e32 v90, 0xbfb8aa3b, v85
	v_exp_f32_e32 v90, v90
	v_mul_f32_e32 v83, v83, v88
	v_add_f32_e32 v88, 1.0, v89
	v_rcp_f32_e32 v88, v88
	v_add_f32_e32 v89, 1.0, v90
	v_rcp_f32_e32 v89, v89
	v_mul_f32_e32 v87, v102, v87
	v_mul_f32_e32 v82, v82, v83
	v_mul_f32_e32 v83, v95, v88
	v_med3_f32 v88, v87, s94, v199
	v_med3_f32 v82, v82, s94, v199
	v_cvt_pk_fp8_f32 v87, v88, v82
	v_mul_f32_e32 v85, v85, v89
	v_mul_f32_e32 v83, v94, v83
	v_mul_f32_e32 v82, v84, v85
	v_med3_f32 v83, v83, s94, v199
	v_med3_f32 v82, v82, s94, v199
	v_cvt_pk_fp8_f32 v87, v83, v82 op_sel:[0,0,1]
	v_or_b32_e32 v106, 32, v148
	v_mad_i64_i32 v[82:83], s[4:5], v106, s93, v[132:133]
	v_lshl_add_u64 v[82:83], v[82:83], 0, v[130:131]
	global_store_dwordx2 v[82:83], v[86:87], off
	v_cvt_f32_i32_e32 v83, v78
	v_cvt_f32_i32_e32 v82, v70
	v_mul_f32_e32 v98, v180, v99
	v_pk_mul_f32 v[84:85], v[182:183], v[98:99]
	v_cvt_f32_i32_e32 v79, v79
	v_pk_mul_f32 v[82:83], v[84:85], v[82:83]
	v_cvt_f32_i32_e32 v85, v74
	v_cvt_f32_i32_e32 v84, v66
	v_cvt_f32_i32_e32 v78, v71
	v_mul_f32_e32 v98, v134, v99
	v_pk_mul_f32 v[86:87], v[136:137], v[98:99]
	v_mul_f32_e32 v98, v118, v99
	v_pk_mul_f32 v[70:71], v[86:87], v[84:85]
	v_pk_mul_f32 v[84:85], v[126:127], v[98:99]
	v_cvt_f32_i32_e32 v75, v75
	v_cvt_f32_i32_e32 v74, v67
	v_pk_mul_f32 v[78:79], v[84:85], v[78:79]
	v_cvt_f32_i32_e32 v85, v80
	v_cvt_f32_i32_e32 v84, v72
	v_mul_f32_e32 v98, v122, v99
	v_pk_mul_f32 v[66:67], v[138:139], v[98:99]
	v_mul_f32_e32 v98, v114, v99
	v_pk_mul_f32 v[66:67], v[66:67], v[74:75]
	v_pk_mul_f32 v[74:75], v[140:141], v[98:99]
	v_cvt_f32_i32_e32 v81, v81
	v_pk_mul_f32 v[74:75], v[74:75], v[84:85]
	v_cvt_f32_i32_e32 v85, v76
	v_cvt_f32_i32_e32 v84, v68
	v_cvt_f32_i32_e32 v80, v73
	v_mul_f32_e32 v98, v142, v99
	v_pk_mul_f32 v[86:87], v[144:145], v[98:99]
	v_mul_f32_e32 v98, v120, v99
	v_pk_mul_f32 v[72:73], v[86:87], v[84:85]
	v_pk_mul_f32 v[84:85], v[128:129], v[98:99]
	v_mul_f32_e32 v68, 0xbfb8aa3b, v83
	v_pk_mul_f32 v[80:81], v[84:85], v[80:81]
	v_exp_f32_e32 v84, v68
	v_cvt_f32_i32_e32 v77, v77
	v_cvt_f32_i32_e32 v76, v69
	v_mul_f32_e32 v85, 0xbfb8aa3b, v79
	v_add_f32_e32 v84, 1.0, v84
	v_rcp_f32_e32 v84, v84
	v_exp_f32_e32 v85, v85
	v_mul_f32_e32 v98, v116, v99
	v_pk_mul_f32 v[68:69], v[124:125], v[98:99]
	v_or_b32_e32 v88, 48, v148
	v_pk_mul_f32 v[68:69], v[68:69], v[76:77]
	v_mul_f32_e32 v76, v83, v84
	v_mul_f32_e32 v76, v82, v76
	v_add_f32_e32 v77, 1.0, v85
	v_mul_f32_e32 v82, 0xbfb8aa3b, v75
	v_rcp_f32_e32 v77, v77
	v_exp_f32_e32 v82, v82
	v_mul_f32_e32 v83, 0xbfb8aa3b, v81
	v_exp_f32_e32 v83, v83
	v_mul_f32_e32 v77, v79, v77
	v_add_f32_e32 v79, 1.0, v82
	v_rcp_f32_e32 v79, v79
	v_add_f32_e32 v82, 1.0, v83
	v_rcp_f32_e32 v82, v82
	v_mul_f32_e32 v77, v78, v77
	v_mul_f32_e32 v75, v75, v79
	v_mul_f32_e32 v79, 0xbfb8aa3b, v71
	v_exp_f32_e32 v79, v79
	v_mul_f32_e32 v75, v74, v75
	v_mul_f32_e32 v74, v81, v82
	v_mul_f32_e32 v78, v80, v74
	v_med3_f32 v76, v76, s94, v199
	v_med3_f32 v77, v77, s94, v199
	v_cvt_pk_fp8_f32 v74, v76, v77
	v_add_f32_e32 v77, 1.0, v79
	v_med3_f32 v76, v78, s94, v199
	v_rcp_f32_e32 v77, v77
	v_mul_f32_e32 v78, 0xbfb8aa3b, v67
	v_exp_f32_e32 v78, v78
	v_med3_f32 v75, v75, s94, v199
	v_mul_f32_e32 v71, v71, v77
	v_cvt_pk_fp8_f32 v74, v75, v76 op_sel:[0,0,1]
	v_mul_f32_e32 v70, v70, v71
	v_add_f32_e32 v71, 1.0, v78
	v_mul_f32_e32 v75, 0xbfb8aa3b, v73
	v_mul_f32_e32 v76, 0xbfb8aa3b, v69
	v_rcp_f32_e32 v71, v71
	v_exp_f32_e32 v75, v75
	v_exp_f32_e32 v76, v76
	v_med3_f32 v70, v70, s94, v199
	v_mul_f32_e32 v67, v67, v71
	v_add_f32_e32 v71, 1.0, v75
	v_add_f32_e32 v75, 1.0, v76
	v_rcp_f32_e32 v75, v75
	v_rcp_f32_e32 v71, v71
	v_mul_f32_e32 v66, v66, v67
	v_med3_f32 v66, v66, s94, v199
	v_mul_f32_e32 v69, v69, v75
	v_cvt_pk_fp8_f32 v75, v70, v66
	v_mul_f32_e32 v67, v73, v71
	v_mul_f32_e32 v67, v72, v67
	v_mul_f32_e32 v66, v68, v69
	v_med3_f32 v67, v67, s94, v199
	v_med3_f32 v66, v66, s94, v199
	v_cvt_pk_fp8_f32 v75, v67, v66 op_sel:[0,0,1]
	v_mad_i64_i32 v[66:67], s[4:5], v88, s93, v[132:133]
	v_lshl_add_u64 v[68:69], v[66:67], 0, v[130:131]
	ds_read2_b32 v[66:67], v149 offset0:128 offset1:144
	global_store_dwordx2 v[68:69], v[74:75], off
	v_cvt_f32_i32_e32 v69, v62
	v_cvt_f32_i32_e32 v68, v54
	v_cvt_f32_i32_e32 v59, v59
	s_waitcnt lgkmcnt(0)
	v_mul_f32_e32 v70, v180, v66
	v_mov_b32_e32 v71, v66
	v_pk_mul_f32 v[70:71], v[182:183], v[70:71]
	v_cvt_f32_i32_e32 v63, v63
	v_pk_mul_f32 v[68:69], v[70:71], v[68:69]
	v_cvt_f32_i32_e32 v71, v58
	v_cvt_f32_i32_e32 v58, v51
	v_cvt_f32_i32_e32 v70, v50
	v_cvt_f32_i32_e32 v62, v55
	v_mul_f32_e32 v50, v122, v66
	v_mov_b32_e32 v51, v66
	v_pk_mul_f32 v[50:51], v[138:139], v[50:51]
	v_mul_f32_e32 v54, v118, v66
	v_mov_b32_e32 v55, v66
	v_pk_mul_f32 v[50:51], v[50:51], v[58:59]
	v_cvt_f32_i32_e32 v59, v64
	v_cvt_f32_i32_e32 v58, v56
	v_pk_mul_f32 v[54:55], v[126:127], v[54:55]
	v_cvt_f32_i32_e32 v65, v65
	v_cvt_f32_i32_e32 v64, v57
	v_pk_mul_f32 v[54:55], v[54:55], v[62:63]
	v_mul_f32_e32 v62, v114, v66
	v_mov_b32_e32 v63, v66
	v_pk_mul_f32 v[62:63], v[140:141], v[62:63]
	v_mul_f32_e32 v56, v120, v66
	v_mov_b32_e32 v57, v66
	v_pk_mul_f32 v[58:59], v[62:63], v[58:59]
	v_cvt_f32_i32_e32 v63, v60
	v_pk_mul_f32 v[56:57], v[128:129], v[56:57]
	v_mul_f32_e32 v60, 0xbfb8aa3b, v69
	v_pk_mul_f32 v[56:57], v[56:57], v[64:65]
	v_exp_f32_e32 v64, v60
	v_mul_f32_e32 v65, 0xbfb8aa3b, v55
	v_cvt_f32_i32_e32 v61, v61
	v_cvt_f32_i32_e32 v60, v53
	v_add_f32_e32 v64, 1.0, v64
	v_rcp_f32_e32 v64, v64
	v_exp_f32_e32 v65, v65
	v_cvt_f32_i32_e32 v62, v52
	v_mul_f32_e32 v52, v116, v66
	v_mov_b32_e32 v53, v66
	v_pk_mul_f32 v[52:53], v[124:125], v[52:53]
	v_mul_f32_e32 v72, v134, v66
	v_pk_mul_f32 v[52:53], v[52:53], v[60:61]
	v_mul_f32_e32 v60, v69, v64
	v_add_f32_e32 v61, 1.0, v65
	v_mul_f32_e32 v64, 0xbfb8aa3b, v59
	v_rcp_f32_e32 v61, v61
	v_exp_f32_e32 v64, v64
	v_mul_f32_e32 v65, 0xbfb8aa3b, v57
	v_exp_f32_e32 v65, v65
	v_mul_f32_e32 v55, v55, v61
	v_add_f32_e32 v61, 1.0, v64
	v_rcp_f32_e32 v61, v61
	v_mov_b32_e32 v73, v66
	v_pk_mul_f32 v[72:73], v[136:137], v[72:73]
	v_add_f32_e32 v64, 1.0, v65
	v_pk_mul_f32 v[70:71], v[72:73], v[70:71]
	v_rcp_f32_e32 v64, v64
	v_mul_f32_e32 v54, v54, v55
	v_mul_f32_e32 v55, v59, v61
	v_mul_f32_e32 v59, 0xbfb8aa3b, v71
	v_exp_f32_e32 v59, v59
	v_mul_f32_e32 v60, v68, v60
	v_mul_f32_e32 v57, v57, v64
	v_mul_f32_e32 v55, v58, v55
	v_mul_f32_e32 v56, v56, v57
	v_med3_f32 v57, v60, s94, v199
	v_med3_f32 v58, v54, s94, v199
	v_cvt_pk_fp8_f32 v54, v57, v58
	v_add_f32_e32 v57, 1.0, v59
	v_mul_f32_e32 v58, 0xbfb8aa3b, v51
	v_rcp_f32_e32 v57, v57
	v_exp_f32_e32 v58, v58
	v_mul_f32_e32 v72, v142, v66
	v_mov_b32_e32 v73, v66
	v_pk_mul_f32 v[72:73], v[144:145], v[72:73]
	v_med3_f32 v55, v55, s94, v199
	v_pk_mul_f32 v[62:63], v[72:73], v[62:63]
	v_med3_f32 v56, v56, s94, v199
	v_cvt_pk_fp8_f32 v54, v55, v56 op_sel:[0,0,1]
	v_mul_f32_e32 v55, v71, v57
	v_add_f32_e32 v56, 1.0, v58
	v_mul_f32_e32 v57, 0xbfb8aa3b, v63
	v_rcp_f32_e32 v56, v56
	v_exp_f32_e32 v57, v57
	v_mul_f32_e32 v58, 0xbfb8aa3b, v53
	v_exp_f32_e32 v58, v58
	v_mul_f32_e32 v51, v51, v56
	v_add_f32_e32 v56, 1.0, v57
	v_rcp_f32_e32 v56, v56
	v_add_f32_e32 v57, 1.0, v58
	v_rcp_f32_e32 v57, v57
	v_mul_f32_e32 v55, v70, v55
	v_mul_f32_e32 v50, v50, v51
	v_mul_f32_e32 v51, v63, v56
	v_med3_f32 v56, v55, s94, v199
	v_med3_f32 v50, v50, s94, v199
	v_cvt_pk_fp8_f32 v55, v56, v50
	v_mul_f32_e32 v53, v53, v57
	v_mul_f32_e32 v51, v62, v51
	v_mul_f32_e32 v50, v52, v53
	v_med3_f32 v51, v51, s94, v199
	v_med3_f32 v50, v50, s94, v199
	v_cvt_pk_fp8_f32 v55, v51, v50 op_sel:[0,0,1]
	v_add_u32_e32 v74, 0x80, v148
	v_mad_i64_i32 v[50:51], s[4:5], v74, s93, v[132:133]
	v_lshl_add_u64 v[50:51], v[50:51], 0, v[130:131]
	global_store_dwordx2 v[50:51], v[54:55], off
	v_cvt_f32_i32_e32 v51, v46
	v_cvt_f32_i32_e32 v50, v38
	v_mul_f32_e32 v66, v180, v67
	v_pk_mul_f32 v[52:53], v[182:183], v[66:67]
	v_cvt_f32_i32_e32 v47, v47
	v_pk_mul_f32 v[50:51], v[52:53], v[50:51]
	v_cvt_f32_i32_e32 v53, v42
	v_cvt_f32_i32_e32 v52, v34
	v_cvt_f32_i32_e32 v46, v39
	v_mul_f32_e32 v66, v134, v67
	v_pk_mul_f32 v[54:55], v[136:137], v[66:67]
	v_mul_f32_e32 v66, v118, v67
	v_pk_mul_f32 v[38:39], v[54:55], v[52:53]
	v_pk_mul_f32 v[52:53], v[126:127], v[66:67]
	v_cvt_f32_i32_e32 v43, v43
	v_cvt_f32_i32_e32 v42, v35
	v_pk_mul_f32 v[46:47], v[52:53], v[46:47]
	v_cvt_f32_i32_e32 v53, v48
	v_cvt_f32_i32_e32 v52, v40
	v_mul_f32_e32 v66, v122, v67
	v_pk_mul_f32 v[34:35], v[138:139], v[66:67]
	v_mul_f32_e32 v66, v114, v67
	v_pk_mul_f32 v[34:35], v[34:35], v[42:43]
	v_pk_mul_f32 v[42:43], v[140:141], v[66:67]
	v_cvt_f32_i32_e32 v49, v49
	v_pk_mul_f32 v[42:43], v[42:43], v[52:53]
	v_cvt_f32_i32_e32 v53, v44
	v_cvt_f32_i32_e32 v52, v36
	v_cvt_f32_i32_e32 v48, v41
	v_mul_f32_e32 v66, v142, v67
	v_pk_mul_f32 v[54:55], v[144:145], v[66:67]
	v_mul_f32_e32 v66, v120, v67
	v_pk_mul_f32 v[40:41], v[54:55], v[52:53]
	v_pk_mul_f32 v[52:53], v[128:129], v[66:67]
	v_mul_f32_e32 v36, 0xbfb8aa3b, v51
	v_pk_mul_f32 v[48:49], v[52:53], v[48:49]
	v_exp_f32_e32 v52, v36
	v_cvt_f32_i32_e32 v45, v45
	v_cvt_f32_i32_e32 v44, v37
	v_mul_f32_e32 v53, 0xbfb8aa3b, v47
	v_add_f32_e32 v52, 1.0, v52
	v_rcp_f32_e32 v52, v52
	v_exp_f32_e32 v53, v53
	v_mul_f32_e32 v66, v116, v67
	v_pk_mul_f32 v[36:37], v[124:125], v[66:67]
	v_add_u32_e32 v56, 0x90, v148
	v_pk_mul_f32 v[36:37], v[36:37], v[44:45]
	v_mul_f32_e32 v44, v51, v52
	v_mul_f32_e32 v44, v50, v44
	v_add_f32_e32 v45, 1.0, v53
	v_mul_f32_e32 v50, 0xbfb8aa3b, v43
	v_rcp_f32_e32 v45, v45
	v_exp_f32_e32 v50, v50
	v_mul_f32_e32 v51, 0xbfb8aa3b, v49
	v_exp_f32_e32 v51, v51
	v_mul_f32_e32 v45, v47, v45
	v_add_f32_e32 v47, 1.0, v50
	v_rcp_f32_e32 v47, v47
	v_add_f32_e32 v50, 1.0, v51
	v_rcp_f32_e32 v50, v50
	v_mul_f32_e32 v45, v46, v45
	v_mul_f32_e32 v43, v43, v47
	v_mul_f32_e32 v47, 0xbfb8aa3b, v39
	v_exp_f32_e32 v47, v47
	v_mul_f32_e32 v43, v42, v43
	v_mul_f32_e32 v42, v49, v50
	v_mul_f32_e32 v46, v48, v42
	v_med3_f32 v44, v44, s94, v199
	v_med3_f32 v45, v45, s94, v199
	v_cvt_pk_fp8_f32 v42, v44, v45
	v_add_f32_e32 v45, 1.0, v47
	v_med3_f32 v44, v46, s94, v199
	v_rcp_f32_e32 v45, v45
	v_mul_f32_e32 v46, 0xbfb8aa3b, v35
	v_exp_f32_e32 v46, v46
	v_med3_f32 v43, v43, s94, v199
	v_mul_f32_e32 v39, v39, v45
	v_cvt_pk_fp8_f32 v42, v43, v44 op_sel:[0,0,1]
	v_mul_f32_e32 v38, v38, v39
	v_add_f32_e32 v39, 1.0, v46
	v_mul_f32_e32 v43, 0xbfb8aa3b, v41
	v_mul_f32_e32 v44, 0xbfb8aa3b, v37
	v_rcp_f32_e32 v39, v39
	v_exp_f32_e32 v43, v43
	v_exp_f32_e32 v44, v44
	v_med3_f32 v38, v38, s94, v199
	v_mul_f32_e32 v35, v35, v39
	v_add_f32_e32 v39, 1.0, v43
	v_add_f32_e32 v43, 1.0, v44
	v_rcp_f32_e32 v43, v43
	v_rcp_f32_e32 v39, v39
	v_mul_f32_e32 v34, v34, v35
	v_med3_f32 v34, v34, s94, v199
	v_mul_f32_e32 v37, v37, v43
	v_cvt_pk_fp8_f32 v43, v38, v34
	v_mul_f32_e32 v35, v41, v39
	v_mul_f32_e32 v35, v40, v35
	v_mul_f32_e32 v34, v36, v37
	v_med3_f32 v35, v35, s94, v199
	v_med3_f32 v34, v34, s94, v199
	v_cvt_pk_fp8_f32 v43, v35, v34 op_sel:[0,0,1]
	v_mad_i64_i32 v[34:35], s[4:5], v56, s93, v[132:133]
	v_lshl_add_u64 v[36:37], v[34:35], 0, v[130:131]
	ds_read2_b32 v[34:35], v149 offset0:160 offset1:176
	global_store_dwordx2 v[36:37], v[42:43], off
	v_cvt_f32_i32_e32 v37, v30
	v_cvt_f32_i32_e32 v36, v22
	v_cvt_f32_i32_e32 v27, v27
	s_waitcnt lgkmcnt(0)
	v_mul_f32_e32 v38, v180, v34
	v_mov_b32_e32 v39, v34
	v_pk_mul_f32 v[38:39], v[182:183], v[38:39]
	v_cvt_f32_i32_e32 v31, v31
	v_pk_mul_f32 v[36:37], v[38:39], v[36:37]
	v_cvt_f32_i32_e32 v39, v26
	v_cvt_f32_i32_e32 v26, v19
	v_cvt_f32_i32_e32 v38, v18
	v_cvt_f32_i32_e32 v30, v23
	v_mul_f32_e32 v18, v122, v34
	v_mov_b32_e32 v19, v34
	v_pk_mul_f32 v[18:19], v[138:139], v[18:19]
	v_mul_f32_e32 v22, v118, v34
	v_mov_b32_e32 v23, v34
	v_pk_mul_f32 v[18:19], v[18:19], v[26:27]
	v_cvt_f32_i32_e32 v27, v32
	v_cvt_f32_i32_e32 v26, v24
	v_pk_mul_f32 v[22:23], v[126:127], v[22:23]
	v_cvt_f32_i32_e32 v33, v33
	v_cvt_f32_i32_e32 v32, v25
	v_pk_mul_f32 v[22:23], v[22:23], v[30:31]
	v_mul_f32_e32 v30, v114, v34
	v_mov_b32_e32 v31, v34
	v_pk_mul_f32 v[30:31], v[140:141], v[30:31]
	v_mul_f32_e32 v24, v120, v34
	v_mov_b32_e32 v25, v34
	v_pk_mul_f32 v[26:27], v[30:31], v[26:27]
	v_cvt_f32_i32_e32 v31, v28
	v_pk_mul_f32 v[24:25], v[128:129], v[24:25]
	v_mul_f32_e32 v28, 0xbfb8aa3b, v37
	v_pk_mul_f32 v[24:25], v[24:25], v[32:33]
	v_exp_f32_e32 v32, v28
	v_mul_f32_e32 v33, 0xbfb8aa3b, v23
	v_cvt_f32_i32_e32 v29, v29
	v_cvt_f32_i32_e32 v28, v21
	v_add_f32_e32 v32, 1.0, v32
	v_rcp_f32_e32 v32, v32
	v_exp_f32_e32 v33, v33
	v_cvt_f32_i32_e32 v30, v20
	v_mul_f32_e32 v20, v116, v34
	v_mov_b32_e32 v21, v34
	v_pk_mul_f32 v[20:21], v[124:125], v[20:21]
	v_mul_f32_e32 v40, v134, v34
	v_pk_mul_f32 v[20:21], v[20:21], v[28:29]
	v_mul_f32_e32 v28, v37, v32
	v_add_f32_e32 v29, 1.0, v33
	v_mul_f32_e32 v32, 0xbfb8aa3b, v27
	v_rcp_f32_e32 v29, v29
	v_exp_f32_e32 v32, v32
	v_mul_f32_e32 v33, 0xbfb8aa3b, v25
	v_exp_f32_e32 v33, v33
	v_mul_f32_e32 v23, v23, v29
	v_add_f32_e32 v29, 1.0, v32
	v_rcp_f32_e32 v29, v29
	v_mov_b32_e32 v41, v34
	v_pk_mul_f32 v[40:41], v[136:137], v[40:41]
	v_add_f32_e32 v32, 1.0, v33
	v_pk_mul_f32 v[38:39], v[40:41], v[38:39]
	v_rcp_f32_e32 v32, v32
	v_mul_f32_e32 v22, v22, v23
	v_mul_f32_e32 v23, v27, v29
	v_mul_f32_e32 v27, 0xbfb8aa3b, v39
	v_exp_f32_e32 v27, v27
	v_mul_f32_e32 v28, v36, v28
	v_mul_f32_e32 v25, v25, v32
	v_mul_f32_e32 v23, v26, v23
	v_mul_f32_e32 v24, v24, v25
	v_med3_f32 v25, v28, s94, v199
	v_med3_f32 v26, v22, s94, v199
	v_cvt_pk_fp8_f32 v22, v25, v26
	v_add_f32_e32 v25, 1.0, v27
	v_mul_f32_e32 v26, 0xbfb8aa3b, v19
	v_rcp_f32_e32 v25, v25
	v_exp_f32_e32 v26, v26
	v_mul_f32_e32 v40, v142, v34
	v_mov_b32_e32 v41, v34
	v_pk_mul_f32 v[40:41], v[144:145], v[40:41]
	v_med3_f32 v23, v23, s94, v199
	v_pk_mul_f32 v[30:31], v[40:41], v[30:31]
	v_med3_f32 v24, v24, s94, v199
	v_cvt_pk_fp8_f32 v22, v23, v24 op_sel:[0,0,1]
	v_mul_f32_e32 v23, v39, v25
	v_add_f32_e32 v24, 1.0, v26
	v_mul_f32_e32 v25, 0xbfb8aa3b, v31
	v_rcp_f32_e32 v24, v24
	v_exp_f32_e32 v25, v25
	v_mul_f32_e32 v26, 0xbfb8aa3b, v21
	v_exp_f32_e32 v26, v26
	v_mul_f32_e32 v19, v19, v24
	v_add_f32_e32 v24, 1.0, v25
	v_rcp_f32_e32 v24, v24
	v_add_f32_e32 v25, 1.0, v26
	v_rcp_f32_e32 v25, v25
	v_mul_f32_e32 v23, v38, v23
	v_mul_f32_e32 v18, v18, v19
	v_mul_f32_e32 v19, v31, v24
	v_med3_f32 v24, v23, s94, v199
	v_med3_f32 v18, v18, s94, v199
	v_cvt_pk_fp8_f32 v23, v24, v18
	v_mul_f32_e32 v21, v21, v25
	v_mul_f32_e32 v19, v30, v19
	v_mul_f32_e32 v18, v20, v21
	v_med3_f32 v19, v19, s94, v199
	v_med3_f32 v18, v18, s94, v199
	v_cvt_pk_fp8_f32 v23, v19, v18 op_sel:[0,0,1]
	v_add_u32_e32 v42, 0xa0, v148
	v_mad_i64_i32 v[18:19], s[4:5], v42, s93, v[132:133]
	v_lshl_add_u64 v[18:19], v[18:19], 0, v[130:131]
	global_store_dwordx2 v[18:19], v[22:23], off
	v_cvt_f32_i32_e32 v19, v14
	v_cvt_f32_i32_e32 v18, v6
	v_mul_f32_e32 v34, v180, v35
	v_pk_mul_f32 v[20:21], v[182:183], v[34:35]
	v_cvt_f32_i32_e32 v15, v15
	v_pk_mul_f32 v[18:19], v[20:21], v[18:19]
	v_cvt_f32_i32_e32 v21, v10
	v_cvt_f32_i32_e32 v20, v2
	v_cvt_f32_i32_e32 v14, v7
	v_mul_f32_e32 v34, v134, v35
	v_pk_mul_f32 v[22:23], v[136:137], v[34:35]
	v_mul_f32_e32 v34, v118, v35
	v_pk_mul_f32 v[6:7], v[22:23], v[20:21]
	v_pk_mul_f32 v[20:21], v[126:127], v[34:35]
	v_cvt_f32_i32_e32 v11, v11
	v_cvt_f32_i32_e32 v10, v3
	v_pk_mul_f32 v[14:15], v[20:21], v[14:15]
	v_cvt_f32_i32_e32 v21, v16
	v_cvt_f32_i32_e32 v20, v8
	v_mul_f32_e32 v34, v122, v35
	v_pk_mul_f32 v[2:3], v[138:139], v[34:35]
	v_mul_f32_e32 v34, v114, v35
	v_pk_mul_f32 v[2:3], v[2:3], v[10:11]
	v_pk_mul_f32 v[10:11], v[140:141], v[34:35]
	v_cvt_f32_i32_e32 v17, v17
	v_pk_mul_f32 v[10:11], v[10:11], v[20:21]
	v_cvt_f32_i32_e32 v21, v12
	v_cvt_f32_i32_e32 v20, v4
	v_cvt_f32_i32_e32 v16, v9
	v_mul_f32_e32 v34, v142, v35
	v_pk_mul_f32 v[22:23], v[144:145], v[34:35]
	v_mul_f32_e32 v34, v120, v35
	v_pk_mul_f32 v[8:9], v[22:23], v[20:21]
	v_pk_mul_f32 v[20:21], v[128:129], v[34:35]
	v_mul_f32_e32 v4, 0xbfb8aa3b, v19
	v_pk_mul_f32 v[16:17], v[20:21], v[16:17]
	v_exp_f32_e32 v20, v4
	v_cvt_f32_i32_e32 v13, v13
	v_cvt_f32_i32_e32 v12, v5
	v_mul_f32_e32 v21, 0xbfb8aa3b, v15
	v_add_f32_e32 v20, 1.0, v20
	v_rcp_f32_e32 v20, v20
	v_exp_f32_e32 v21, v21
	v_mul_f32_e32 v34, v116, v35
	v_pk_mul_f32 v[4:5], v[124:125], v[34:35]
	v_add_u32_e32 v24, 0xb0, v148
	v_pk_mul_f32 v[4:5], v[4:5], v[12:13]
	v_mul_f32_e32 v12, v19, v20
	v_mul_f32_e32 v12, v18, v12
	v_add_f32_e32 v13, 1.0, v21
	v_mul_f32_e32 v18, 0xbfb8aa3b, v11
	v_rcp_f32_e32 v13, v13
	v_exp_f32_e32 v18, v18
	v_mul_f32_e32 v19, 0xbfb8aa3b, v17
	v_exp_f32_e32 v19, v19
	v_mul_f32_e32 v13, v15, v13
	v_add_f32_e32 v15, 1.0, v18
	v_rcp_f32_e32 v15, v15
	v_add_f32_e32 v18, 1.0, v19
	v_rcp_f32_e32 v18, v18
	v_mul_f32_e32 v13, v14, v13
	v_mul_f32_e32 v11, v11, v15
	v_mul_f32_e32 v15, 0xbfb8aa3b, v7
	v_exp_f32_e32 v15, v15
	v_mul_f32_e32 v11, v10, v11
	v_mul_f32_e32 v10, v17, v18
	v_mul_f32_e32 v14, v16, v10
	v_med3_f32 v12, v12, s94, v199
	v_med3_f32 v13, v13, s94, v199
	v_cvt_pk_fp8_f32 v10, v12, v13
	v_add_f32_e32 v13, 1.0, v15
	v_med3_f32 v12, v14, s94, v199
	v_rcp_f32_e32 v13, v13
	v_mul_f32_e32 v14, 0xbfb8aa3b, v3
	v_exp_f32_e32 v14, v14
	v_med3_f32 v11, v11, s94, v199
	v_mul_f32_e32 v7, v7, v13
	v_cvt_pk_fp8_f32 v10, v11, v12 op_sel:[0,0,1]
	v_mul_f32_e32 v6, v6, v7
	v_add_f32_e32 v7, 1.0, v14
	v_mul_f32_e32 v11, 0xbfb8aa3b, v9
	v_mul_f32_e32 v12, 0xbfb8aa3b, v5
	v_rcp_f32_e32 v7, v7
	v_exp_f32_e32 v11, v11
	v_exp_f32_e32 v12, v12
	v_med3_f32 v6, v6, s94, v199
	v_mul_f32_e32 v3, v3, v7
	v_add_f32_e32 v7, 1.0, v11
	v_add_f32_e32 v11, 1.0, v12
	v_rcp_f32_e32 v11, v11
	v_rcp_f32_e32 v7, v7
	v_mul_f32_e32 v2, v2, v3
	v_med3_f32 v2, v2, s94, v199
	v_mul_f32_e32 v5, v5, v11
	v_cvt_pk_fp8_f32 v11, v6, v2
	v_mul_f32_e32 v3, v9, v7
	v_mul_f32_e32 v3, v8, v3
	v_mul_f32_e32 v2, v4, v5
	v_med3_f32 v3, v3, s94, v199
	v_med3_f32 v2, v2, s94, v199
	v_cvt_pk_fp8_f32 v11, v3, v2 op_sel:[0,0,1]
	v_mad_i64_i32 v[2:3], s[4:5], v24, s93, v[132:133]
	v_lshl_add_u64 v[2:3], v[2:3], 0, v[130:131]
	s_andn2_b64 vcc, exec, s[0:1]
	s_mov_b64 s[0:1], -1
	global_store_dwordx2 v[2:3], v[10:11], off
	s_cbranch_vccnz .LBB0_212
	s_andn2_b64 vcc, exec, s[12:13]
	s_cbranch_vccnz .LBB0_211
	s_barrier
	s_branch .LBB0_211

.LBB0_242:
	ds_read_b128 v[150:153], v146
	ds_read_b128 v[154:157], v146 offset:1024
	ds_read_b128 v[158:161], v146 offset:2048
	ds_read_b128 v[162:165], v146 offset:3072
	ds_read_b128 v[166:169], v147
	ds_read_b128 v[170:173], v147 offset:1024
	ds_read_b128 v[174:177], v147 offset:2048
	ds_read_b128 v[178:181], v147 offset:3072
	s_add_u32 s36, s34, 0xfff00080
	s_addc_u32 s37, s35, -1
	s_cmp_eq_u32 s25, 60
	s_cselect_b32 s39, s5, s37
	s_cselect_b32 s38, s18, s36
	s_cselect_b32 s37, s17, s24
	s_cselect_b32 s36, s19, s21
	v_lshl_add_u64 v[142:143], s[34:35], 0, v[138:139]
	s_add_i32 m0, s31, 0xc000
	ds_read_b128 v[182:185], v148
	ds_read_b128 v[186:189], v148 offset:1024
	ds_read_b128 v[190:193], v148 offset:2048
	ds_read_b128 v[194:197], v148 offset:3072
	ds_read_b128 v[198:201], v148 offset:4096
	ds_read_b128 v[202:205], v148 offset:5120
	ds_read_b128 v[206:209], v148 offset:6144
	ds_read_b128 v[210:213], v148 offset:7168
	global_load_lds_dwordx4 v[142:143], off
	v_lshl_add_u64 v[142:143], s[34:35], 0, v[140:141]
	s_add_i32 m0, s31, 0xe000
	s_nop 0
	global_load_lds_dwordx4 v[142:143], off
	s_waitcnt vmcnt(8)
	s_waitcnt lgkmcnt(0)
	s_barrier
	s_setprio 1
	v_mfma_f32_16x16x32_bf16 v[126:129], v[150:153], v[182:185], v[126:129]
	v_mfma_f32_16x16x32_bf16 v[122:125], v[158:161], v[182:185], v[122:125]
	v_mfma_f32_16x16x32_bf16 v[114:117], v[150:153], v[190:193], v[114:117]
	v_mfma_f32_16x16x32_bf16 v[106:109], v[158:161], v[190:193], v[106:109]
	v_mfma_f32_16x16x32_bf16 v[98:101], v[150:153], v[198:201], v[98:101]
	v_mfma_f32_16x16x32_bf16 v[90:93], v[158:161], v[198:201], v[90:93]
	v_mfma_f32_16x16x32_bf16 v[78:81], v[150:153], v[206:209], v[78:81]
	v_mfma_f32_16x16x32_bf16 v[74:77], v[158:161], v[206:209], v[74:77]
	v_mfma_f32_16x16x32_bf16 v[126:129], v[154:157], v[186:189], v[126:129]
	v_mfma_f32_16x16x32_bf16 v[122:125], v[162:165], v[186:189], v[122:125]
	v_mfma_f32_16x16x32_bf16 v[114:117], v[154:157], v[194:197], v[114:117]
	v_mfma_f32_16x16x32_bf16 v[106:109], v[162:165], v[194:197], v[106:109]
	v_mfma_f32_16x16x32_bf16 v[98:101], v[154:157], v[202:205], v[98:101]
	v_mfma_f32_16x16x32_bf16 v[90:93], v[162:165], v[202:205], v[90:93]
	v_mfma_f32_16x16x32_bf16 v[78:81], v[154:157], v[210:213], v[78:81]
	v_mfma_f32_16x16x32_bf16 v[74:77], v[162:165], v[210:213], v[74:77]
	v_mfma_f32_16x16x32_bf16 v[118:121], v[166:169], v[182:185], v[118:121]
	v_mfma_f32_16x16x32_bf16 v[110:113], v[174:177], v[182:185], v[110:113]
	v_mfma_f32_16x16x32_bf16 v[102:105], v[166:169], v[190:193], v[102:105]
	v_mfma_f32_16x16x32_bf16 v[94:97], v[174:177], v[190:193], v[94:97]
	v_mfma_f32_16x16x32_bf16 v[86:89], v[166:169], v[198:201], v[86:89]
	v_mfma_f32_16x16x32_bf16 v[82:85], v[174:177], v[198:201], v[82:85]
	v_mfma_f32_16x16x32_bf16 v[70:73], v[166:169], v[206:209], v[70:73]
	v_mfma_f32_16x16x32_bf16 v[66:69], v[174:177], v[206:209], v[66:69]
	v_mfma_f32_16x16x32_bf16 v[118:121], v[170:173], v[186:189], v[118:121]
	v_mfma_f32_16x16x32_bf16 v[110:113], v[178:181], v[186:189], v[110:113]
	v_mfma_f32_16x16x32_bf16 v[102:105], v[170:173], v[194:197], v[102:105]
	v_mfma_f32_16x16x32_bf16 v[94:97], v[178:181], v[194:197], v[94:97]
	v_mfma_f32_16x16x32_bf16 v[86:89], v[170:173], v[202:205], v[86:89]
	v_mfma_f32_16x16x32_bf16 v[82:85], v[178:181], v[202:205], v[82:85]
	v_mfma_f32_16x16x32_bf16 v[70:73], v[170:173], v[210:213], v[70:73]
	v_mfma_f32_16x16x32_bf16 v[66:69], v[178:181], v[210:213], v[66:69]
	s_setprio 0
	s_barrier
	s_add_i32 s61, s59, s42
	v_lshl_add_u64 v[142:143], s[36:37], 0, v[132:133]
	s_mov_b32 m0, s61
	ds_read_b128 v[182:185], v148 offset:16384
	ds_read_b128 v[186:189], v148 offset:17408
	ds_read_b128 v[190:193], v148 offset:18432
	ds_read_b128 v[194:197], v148 offset:19456
	ds_read_b128 v[198:201], v148 offset:20480
	ds_read_b128 v[202:205], v148 offset:21504
	ds_read_b128 v[206:209], v148 offset:22528
	ds_read_b128 v[210:213], v148 offset:23552
	global_load_lds_dwordx4 v[142:143], off
	s_add_i32 m0, s61, 0x2000
	s_add_u32 s62, s36, 0x100000
	v_lshl_add_u64 v[214:215], s[36:37], 0, v[136:137]
	s_addc_u32 s63, s37, 0
	s_add_i32 s61, s60, s42
	global_load_lds_dwordx4 v[214:215], off
	v_lshl_add_u64 v[216:217], s[62:63], 0, v[132:133]
	s_mov_b32 m0, s61
	v_lshl_add_u64 v[218:219], s[38:39], 0, v[134:135]
	global_load_lds_dwordx4 v[216:217], off
	v_lshl_add_u64 v[216:217], s[62:63], 0, v[136:137]
	s_add_i32 m0, s61, 0x2000
	s_nop 0
	global_load_lds_dwordx4 v[216:217], off
	v_lshl_add_u64 v[216:217], s[38:39], 0, v[130:131]
	s_mov_b32 m0, s31
	s_nop 0
	global_load_lds_dwordx4 v[216:217], off
	s_mov_b32 m0, s49
	s_nop 0
	global_load_lds_dwordx4 v[218:219], off
	s_waitcnt vmcnt(8)
	s_waitcnt lgkmcnt(0)
	s_barrier
	s_setprio 1
	v_mfma_f32_16x16x32_bf16 v[62:65], v[150:153], v[182:185], v[62:65]
	v_mfma_f32_16x16x32_bf16 v[58:61], v[158:161], v[182:185], v[58:61]
	v_mfma_f32_16x16x32_bf16 v[50:53], v[150:153], v[190:193], v[50:53]
	v_mfma_f32_16x16x32_bf16 v[42:45], v[158:161], v[190:193], v[42:45]
	v_mfma_f32_16x16x32_bf16 v[34:37], v[150:153], v[198:201], v[34:37]
	v_mfma_f32_16x16x32_bf16 v[26:29], v[158:161], v[198:201], v[26:29]
	v_mfma_f32_16x16x32_bf16 v[18:21], v[150:153], v[206:209], v[18:21]
	v_mfma_f32_16x16x32_bf16 v[10:13], v[158:161], v[206:209], v[10:13]
	v_mfma_f32_16x16x32_bf16 v[62:65], v[154:157], v[186:189], v[62:65]
	v_mfma_f32_16x16x32_bf16 v[58:61], v[162:165], v[186:189], v[58:61]
	v_mfma_f32_16x16x32_bf16 v[50:53], v[154:157], v[194:197], v[50:53]
	v_mfma_f32_16x16x32_bf16 v[42:45], v[162:165], v[194:197], v[42:45]
	v_mfma_f32_16x16x32_bf16 v[34:37], v[154:157], v[202:205], v[34:37]
	v_mfma_f32_16x16x32_bf16 v[26:29], v[162:165], v[202:205], v[26:29]
	v_mfma_f32_16x16x32_bf16 v[18:21], v[154:157], v[210:213], v[18:21]
	v_mfma_f32_16x16x32_bf16 v[10:13], v[162:165], v[210:213], v[10:13]
	v_mfma_f32_16x16x32_bf16 v[54:57], v[166:169], v[182:185], v[54:57]
	v_mfma_f32_16x16x32_bf16 v[46:49], v[174:177], v[182:185], v[46:49]
	v_mfma_f32_16x16x32_bf16 v[38:41], v[166:169], v[190:193], v[38:41]
	v_mfma_f32_16x16x32_bf16 v[30:33], v[174:177], v[190:193], v[30:33]
	v_mfma_f32_16x16x32_bf16 v[22:25], v[166:169], v[198:201], v[22:25]
	v_mfma_f32_16x16x32_bf16 v[14:17], v[174:177], v[198:201], v[14:17]
	v_mfma_f32_16x16x32_bf16 v[6:9], v[166:169], v[206:209], v[6:9]
	v_mfma_f32_16x16x32_bf16 v[2:5], v[174:177], v[206:209], v[2:5]
	v_mfma_f32_16x16x32_bf16 v[54:57], v[170:173], v[186:189], v[54:57]
	v_mfma_f32_16x16x32_bf16 v[46:49], v[178:181], v[186:189], v[46:49]
	v_mfma_f32_16x16x32_bf16 v[38:41], v[170:173], v[194:197], v[38:41]
	v_mfma_f32_16x16x32_bf16 v[30:33], v[178:181], v[194:197], v[30:33]
	v_mfma_f32_16x16x32_bf16 v[22:25], v[170:173], v[202:205], v[22:25]
	v_mfma_f32_16x16x32_bf16 v[14:17], v[178:181], v[202:205], v[14:17]
	v_mfma_f32_16x16x32_bf16 v[6:9], v[170:173], v[210:213], v[6:9]
	v_mfma_f32_16x16x32_bf16 v[2:5], v[178:181], v[210:213], v[2:5]
	s_setprio 0
	s_barrier
	s_add_i32 s61, 0, 0x18000
	v_add_u32_e32 v149, s61, v144
	s_add_i32 s62, 0, 0x1c000
	ds_read_b128 v[150:153], v149
	ds_read_b128 v[154:157], v149 offset:1024
	ds_read_b128 v[158:161], v149 offset:2048
	ds_read_b128 v[162:165], v149 offset:3072
	v_add_u32_e32 v149, s62, v144
	ds_read_b128 v[166:169], v149
	ds_read_b128 v[170:173], v149 offset:1024
	ds_read_b128 v[174:177], v149 offset:2048
	ds_read_b128 v[178:181], v149 offset:3072
	s_add_u32 s38, s38, 0x100000
	s_addc_u32 s39, s39, 0
	s_mov_b32 m0, s50
	v_lshl_add_u64 v[220:221], s[38:39], 0, v[130:131]
	ds_read_b128 v[182:185], v148 offset:32768
	ds_read_b128 v[186:189], v148 offset:33792
	ds_read_b128 v[190:193], v148 offset:34816
	ds_read_b128 v[194:197], v148 offset:35840
	ds_read_b128 v[198:201], v148 offset:36864
	ds_read_b128 v[202:205], v148 offset:37888
	ds_read_b128 v[206:209], v148 offset:38912
	ds_read_b128 v[210:213], v148 offset:39936
	global_load_lds_dwordx4 v[220:221], off
	v_lshl_add_u64 v[220:221], s[38:39], 0, v[134:135]
	s_mov_b32 m0, s51
	s_nop 0
	global_load_lds_dwordx4 v[220:221], off
	s_waitcnt vmcnt(8)
	s_waitcnt lgkmcnt(0)
	s_barrier
	s_setprio 1
	v_mfma_f32_16x16x32_bf16 v[126:129], v[150:153], v[182:185], v[126:129]
	v_mfma_f32_16x16x32_bf16 v[122:125], v[158:161], v[182:185], v[122:125]
	v_mfma_f32_16x16x32_bf16 v[114:117], v[150:153], v[190:193], v[114:117]
	v_mfma_f32_16x16x32_bf16 v[106:109], v[158:161], v[190:193], v[106:109]
	v_mfma_f32_16x16x32_bf16 v[98:101], v[150:153], v[198:201], v[98:101]
	v_mfma_f32_16x16x32_bf16 v[90:93], v[158:161], v[198:201], v[90:93]
	v_mfma_f32_16x16x32_bf16 v[78:81], v[150:153], v[206:209], v[78:81]
	v_mfma_f32_16x16x32_bf16 v[74:77], v[158:161], v[206:209], v[74:77]
	v_mfma_f32_16x16x32_bf16 v[126:129], v[154:157], v[186:189], v[126:129]
	v_mfma_f32_16x16x32_bf16 v[122:125], v[162:165], v[186:189], v[122:125]
	v_mfma_f32_16x16x32_bf16 v[114:117], v[154:157], v[194:197], v[114:117]
	v_mfma_f32_16x16x32_bf16 v[106:109], v[162:165], v[194:197], v[106:109]
	v_mfma_f32_16x16x32_bf16 v[98:101], v[154:157], v[202:205], v[98:101]
	v_mfma_f32_16x16x32_bf16 v[90:93], v[162:165], v[202:205], v[90:93]
	v_mfma_f32_16x16x32_bf16 v[78:81], v[154:157], v[210:213], v[78:81]
	v_mfma_f32_16x16x32_bf16 v[74:77], v[162:165], v[210:213], v[74:77]
	v_mfma_f32_16x16x32_bf16 v[118:121], v[166:169], v[182:185], v[118:121]
	v_mfma_f32_16x16x32_bf16 v[110:113], v[174:177], v[182:185], v[110:113]
	v_mfma_f32_16x16x32_bf16 v[102:105], v[166:169], v[190:193], v[102:105]
	v_mfma_f32_16x16x32_bf16 v[94:97], v[174:177], v[190:193], v[94:97]
	v_mfma_f32_16x16x32_bf16 v[86:89], v[166:169], v[198:201], v[86:89]
	v_mfma_f32_16x16x32_bf16 v[82:85], v[174:177], v[198:201], v[82:85]
	v_mfma_f32_16x16x32_bf16 v[70:73], v[166:169], v[206:209], v[70:73]
	v_mfma_f32_16x16x32_bf16 v[66:69], v[174:177], v[206:209], v[66:69]
	v_mfma_f32_16x16x32_bf16 v[118:121], v[170:173], v[186:189], v[118:121]
	v_mfma_f32_16x16x32_bf16 v[110:113], v[178:181], v[186:189], v[110:113]
	v_mfma_f32_16x16x32_bf16 v[102:105], v[170:173], v[194:197], v[102:105]
	v_mfma_f32_16x16x32_bf16 v[94:97], v[178:181], v[194:197], v[94:97]
	v_mfma_f32_16x16x32_bf16 v[86:89], v[170:173], v[202:205], v[86:89]
	v_mfma_f32_16x16x32_bf16 v[82:85], v[178:181], v[202:205], v[82:85]
	v_mfma_f32_16x16x32_bf16 v[70:73], v[170:173], v[210:213], v[70:73]
	v_mfma_f32_16x16x32_bf16 v[66:69], v[178:181], v[210:213], v[66:69]
	s_setprio 0
	s_barrier
	s_add_i32 s38, s61, s42
	v_lshl_add_u64 v[142:143], v[142:143], 0, s[10:11]
	s_mov_b32 m0, s38
	ds_read_b128 v[182:185], v148 offset:49152
	ds_read_b128 v[186:189], v148 offset:50176
	ds_read_b128 v[190:193], v148 offset:51200
	ds_read_b128 v[194:197], v148 offset:52224
	ds_read_b128 v[198:201], v148 offset:53248
	ds_read_b128 v[202:205], v148 offset:54272
	ds_read_b128 v[206:209], v148 offset:55296
	ds_read_b128 v[210:213], v148 offset:56320
	global_load_lds_dwordx4 v[142:143], off
	s_add_i32 m0, s38, 0x2000
	s_add_u32 s36, s36, 0x100080
	v_lshl_add_u64 v[142:143], v[214:215], 0, s[10:11]
	s_addc_u32 s37, s37, 0
	s_add_i32 s38, s62, s42
	global_load_lds_dwordx4 v[142:143], off
	v_lshl_add_u64 v[142:143], s[36:37], 0, v[132:133]
	s_mov_b32 m0, s38
	s_nop 0
	global_load_lds_dwordx4 v[142:143], off
	v_lshl_add_u64 v[142:143], s[36:37], 0, v[136:137]
	s_add_i32 m0, s38, 0x2000
	s_nop 0
	global_load_lds_dwordx4 v[142:143], off
	v_lshl_add_u64 v[142:143], v[216:217], 0, s[10:11]
	s_mov_b32 m0, s57
	s_nop 0
	global_load_lds_dwordx4 v[142:143], off
	v_lshl_add_u64 v[142:143], v[218:219], 0, s[10:11]
	s_mov_b32 m0, s58
	s_nop 0
	global_load_lds_dwordx4 v[142:143], off
	s_waitcnt vmcnt(8)
	s_waitcnt lgkmcnt(0)
	s_barrier
	s_setprio 1
	v_mfma_f32_16x16x32_bf16 v[62:65], v[150:153], v[182:185], v[62:65]
	v_mfma_f32_16x16x32_bf16 v[58:61], v[158:161], v[182:185], v[58:61]
	v_mfma_f32_16x16x32_bf16 v[50:53], v[150:153], v[190:193], v[50:53]
	v_mfma_f32_16x16x32_bf16 v[42:45], v[158:161], v[190:193], v[42:45]
	v_mfma_f32_16x16x32_bf16 v[34:37], v[150:153], v[198:201], v[34:37]
	v_mfma_f32_16x16x32_bf16 v[26:29], v[158:161], v[198:201], v[26:29]
	v_mfma_f32_16x16x32_bf16 v[18:21], v[150:153], v[206:209], v[18:21]
	v_mfma_f32_16x16x32_bf16 v[10:13], v[158:161], v[206:209], v[10:13]
	v_mfma_f32_16x16x32_bf16 v[62:65], v[154:157], v[186:189], v[62:65]
	v_mfma_f32_16x16x32_bf16 v[58:61], v[162:165], v[186:189], v[58:61]
	v_mfma_f32_16x16x32_bf16 v[50:53], v[154:157], v[194:197], v[50:53]
	v_mfma_f32_16x16x32_bf16 v[42:45], v[162:165], v[194:197], v[42:45]
	v_mfma_f32_16x16x32_bf16 v[34:37], v[154:157], v[202:205], v[34:37]
	v_mfma_f32_16x16x32_bf16 v[26:29], v[162:165], v[202:205], v[26:29]
	v_mfma_f32_16x16x32_bf16 v[18:21], v[154:157], v[210:213], v[18:21]
	v_mfma_f32_16x16x32_bf16 v[10:13], v[162:165], v[210:213], v[10:13]
	v_mfma_f32_16x16x32_bf16 v[54:57], v[166:169], v[182:185], v[54:57]
	v_mfma_f32_16x16x32_bf16 v[46:49], v[174:177], v[182:185], v[46:49]
	v_mfma_f32_16x16x32_bf16 v[38:41], v[166:169], v[190:193], v[38:41]
	v_mfma_f32_16x16x32_bf16 v[30:33], v[174:177], v[190:193], v[30:33]
	v_mfma_f32_16x16x32_bf16 v[22:25], v[166:169], v[198:201], v[22:25]
	v_mfma_f32_16x16x32_bf16 v[14:17], v[174:177], v[198:201], v[14:17]
	v_mfma_f32_16x16x32_bf16 v[6:9], v[166:169], v[206:209], v[6:9]
	v_mfma_f32_16x16x32_bf16 v[2:5], v[174:177], v[206:209], v[2:5]
	v_mfma_f32_16x16x32_bf16 v[54:57], v[170:173], v[186:189], v[54:57]
	v_mfma_f32_16x16x32_bf16 v[46:49], v[178:181], v[186:189], v[46:49]
	v_mfma_f32_16x16x32_bf16 v[38:41], v[170:173], v[194:197], v[38:41]
	v_mfma_f32_16x16x32_bf16 v[30:33], v[178:181], v[194:197], v[30:33]
	v_mfma_f32_16x16x32_bf16 v[22:25], v[170:173], v[202:205], v[22:25]
	v_mfma_f32_16x16x32_bf16 v[14:17], v[178:181], v[202:205], v[14:17]
	v_mfma_f32_16x16x32_bf16 v[6:9], v[170:173], v[210:213], v[6:9]
	v_mfma_f32_16x16x32_bf16 v[2:5], v[178:181], v[210:213], v[2:5]
	s_setprio 0
	s_barrier
	s_add_i32 s25, s25, 2
	s_add_u32 s34, s34, 0x100
	s_addc_u32 s35, s35, 0
	s_add_u32 s21, s21, 0x100
	s_addc_u32 s24, s24, 0
	s_cmp_gt_u32 s25, 61
	s_cbranch_scc0 .LBB0_242
	s_and_b64 vcc, exec, s[12:13]
	s_cbranch_vccz .LBB0_245
	s_barrier

.LBB0_318:
	ds_read_b128 v[26:29], v185
	ds_read_b128 v[30:33], v185 offset:1024
	ds_read_b128 v[18:21], v185 offset:2048
	ds_read_b128 v[22:25], v185 offset:3072
	ds_read_b128 v[10:13], v186
	ds_read_b128 v[14:17], v186 offset:1024
	ds_read_b128 v[2:5], v186 offset:2048
	ds_read_b128 v[6:9], v186 offset:3072
	s_add_u32 s24, s26, 0xffea8080
	s_addc_u32 s25, s27, -1
	s_cmpk_eq_i32 s58, 0x52
	s_cselect_b32 s31, s5, s25
	s_cselect_b32 s30, s4, s24
	s_cselect_b32 s29, s21, s51
	s_cselect_b32 s28, s20, s50
	v_lshl_add_u64 v[212:213], s[26:27], 0, v[166:167]
	s_add_i32 m0, s7, 0xc000
	ds_read_b128 v[174:177], v187
	ds_read_b128 v[178:181], v187 offset:1024
	ds_read_b128 v[188:191], v187 offset:2048
	ds_read_b128 v[192:195], v187 offset:3072
	ds_read_b128 v[196:199], v187 offset:4096
	ds_read_b128 v[200:203], v187 offset:5120
	ds_read_b128 v[204:207], v187 offset:6144
	ds_read_b128 v[208:211], v187 offset:7168
	global_load_lds_dwordx4 v[212:213], off
	v_lshl_add_u64 v[212:213], s[26:27], 0, v[168:169]
	s_add_i32 m0, s7, 0xe000
	s_nop 0
	global_load_lds_dwordx4 v[212:213], off
	s_waitcnt vmcnt(8)
	s_waitcnt lgkmcnt(0)
	s_barrier
	s_setprio 1
	v_mfma_f32_16x16x128_f8f6f4 v[158:161], v[26:33], v[174:181], v[158:161]
	v_mfma_f32_16x16x128_f8f6f4 v[154:157], v[18:25], v[174:181], v[154:157]
	v_mfma_f32_16x16x128_f8f6f4 v[138:141], v[18:25], v[188:195], v[138:141]
	v_mfma_f32_16x16x128_f8f6f4 v[142:145], v[26:33], v[188:195], v[142:145]
	v_mfma_f32_16x16x128_f8f6f4 v[126:129], v[26:33], v[196:203], v[126:129]
	v_mfma_f32_16x16x128_f8f6f4 v[122:125], v[18:25], v[196:203], v[122:125]
	v_mfma_f32_16x16x128_f8f6f4 v[106:109], v[18:25], v[204:211], v[106:109]
	v_mfma_f32_16x16x128_f8f6f4 v[110:113], v[26:33], v[204:211], v[110:113]
	v_mfma_f32_16x16x128_f8f6f4 v[102:105], v[10:17], v[204:211], v[102:105]
	v_mfma_f32_16x16x128_f8f6f4 v[98:101], v[2:9], v[204:211], v[98:101]
	v_mfma_f32_16x16x128_f8f6f4 v[146:149], v[2:9], v[174:181], v[146:149]
	v_mfma_f32_16x16x128_f8f6f4 v[150:153], v[10:17], v[174:181], v[150:153]
	v_mfma_f32_16x16x128_f8f6f4 v[134:137], v[10:17], v[188:195], v[134:137]
	v_mfma_f32_16x16x128_f8f6f4 v[130:133], v[2:9], v[188:195], v[130:133]
	v_mfma_f32_16x16x128_f8f6f4 v[114:117], v[2:9], v[196:203], v[114:117]
	v_mfma_f32_16x16x128_f8f6f4 v[118:121], v[10:17], v[196:203], v[118:121]
	s_setprio 0
	s_barrier
	s_add_i32 s24, s42, s3
	v_lshl_add_u64 v[174:175], s[28:29], 0, v[164:165]
	s_mov_b32 m0, s24
	ds_read_b128 v[188:191], v187 offset:16384
	ds_read_b128 v[192:195], v187 offset:17408
	ds_read_b128 v[196:199], v187 offset:18432
	ds_read_b128 v[200:203], v187 offset:19456
	ds_read_b128 v[204:207], v187 offset:20480
	ds_read_b128 v[208:211], v187 offset:21504
	ds_read_b128 v[212:215], v187 offset:22528
	ds_read_b128 v[216:219], v187 offset:23552
	global_load_lds_dwordx4 v[174:175], off
	s_add_i32 m0, s24, 0x2000
	s_add_u32 s24, s28, 0x158000
	v_lshl_add_u64 v[176:177], s[28:29], 0, v[162:163]
	s_addc_u32 s25, s29, 0
	s_add_i32 s59, s43, s3
	global_load_lds_dwordx4 v[176:177], off
	v_lshl_add_u64 v[178:179], s[24:25], 0, v[164:165]
	s_mov_b32 m0, s59
	v_lshl_add_u64 v[180:181], s[30:31], 0, v[162:163]
	global_load_lds_dwordx4 v[178:179], off
	v_lshl_add_u64 v[178:179], s[24:25], 0, v[162:163]
	s_add_i32 m0, s59, 0x2000
	s_nop 0
	global_load_lds_dwordx4 v[178:179], off
	v_lshl_add_u64 v[178:179], s[30:31], 0, v[164:165]
	s_mov_b32 m0, s7
	s_nop 0
	global_load_lds_dwordx4 v[178:179], off
	s_mov_b32 m0, s17
	s_nop 0
	global_load_lds_dwordx4 v[180:181], off
	s_waitcnt vmcnt(8)
	s_waitcnt lgkmcnt(0)
	s_barrier
	s_setprio 1
	v_mfma_f32_16x16x128_f8f6f4 v[78:81], v[26:33], v[196:203], v[78:81]
	v_mfma_f32_16x16x128_f8f6f4 v[74:77], v[18:25], v[196:203], v[74:77]
	v_mfma_f32_16x16x128_f8f6f4 v[90:93], v[18:25], v[188:195], v[90:93]
	v_mfma_f32_16x16x128_f8f6f4 v[94:97], v[26:33], v[188:195], v[94:97]
	v_mfma_f32_16x16x128_f8f6f4 v[62:65], v[26:33], v[204:211], v[62:65]
	v_mfma_f32_16x16x128_f8f6f4 v[58:61], v[18:25], v[204:211], v[58:61]
	v_mfma_f32_16x16x128_f8f6f4 v[42:45], v[18:25], v[212:219], v[42:45]
	v_mfma_f32_16x16x128_f8f6f4 v[46:49], v[26:33], v[212:219], v[46:49]
	v_mfma_f32_16x16x128_f8f6f4 v[38:41], v[10:17], v[212:219], v[38:41]
	v_mfma_f32_16x16x128_f8f6f4 v[34:37], v[2:9], v[212:219], v[34:37]
	v_mfma_f32_16x16x128_f8f6f4 v[82:85], v[2:9], v[188:195], v[82:85]
	v_mfma_f32_16x16x128_f8f6f4 v[86:89], v[10:17], v[188:195], v[86:89]
	v_mfma_f32_16x16x128_f8f6f4 v[70:73], v[10:17], v[196:203], v[70:73]
	v_mfma_f32_16x16x128_f8f6f4 v[66:69], v[2:9], v[196:203], v[66:69]
	v_mfma_f32_16x16x128_f8f6f4 v[50:53], v[2:9], v[204:211], v[50:53]
	v_mfma_f32_16x16x128_f8f6f4 v[54:57], v[10:17], v[204:211], v[54:57]
	s_setprio 0
	s_barrier
	s_add_i32 s59, 0, 0x18000
	s_add_i32 s60, 0, 0x1c000
	v_add_u32_e32 v14, s59, v183
	v_add_u32_e32 v30, s60, v183
	ds_read_b128 v[2:5], v14
	ds_read_b128 v[6:9], v14 offset:1024
	ds_read_b128 v[10:13], v14 offset:2048
	ds_read_b128 v[14:17], v14 offset:3072
	ds_read_b128 v[18:21], v30
	ds_read_b128 v[22:25], v30 offset:1024
	ds_read_b128 v[26:29], v30 offset:2048
	ds_read_b128 v[30:33], v30 offset:3072
	s_add_u32 s24, s30, 0x158000
	s_addc_u32 s25, s31, 0
	s_mov_b32 m0, s34
	v_lshl_add_u64 v[220:221], s[24:25], 0, v[164:165]
	ds_read_b128 v[188:191], v187 offset:32768
	ds_read_b128 v[192:195], v187 offset:33792
	ds_read_b128 v[196:199], v187 offset:34816
	ds_read_b128 v[200:203], v187 offset:35840
	ds_read_b128 v[204:207], v187 offset:36864
	ds_read_b128 v[208:211], v187 offset:37888
	ds_read_b128 v[212:215], v187 offset:38912
	ds_read_b128 v[216:219], v187 offset:39936
	global_load_lds_dwordx4 v[220:221], off
	v_lshl_add_u64 v[220:221], s[24:25], 0, v[162:163]
	s_mov_b32 m0, s35
	s_nop 0
	global_load_lds_dwordx4 v[220:221], off
	s_waitcnt vmcnt(8)
	s_waitcnt lgkmcnt(0)
	s_barrier
	s_setprio 1
	v_mfma_f32_16x16x128_f8f6f4 v[122:125], v[10:17], v[204:211], v[122:125]
	v_mfma_f32_16x16x128_f8f6f4 v[126:129], v[2:9], v[204:211], v[126:129]
	v_mfma_f32_16x16x128_f8f6f4 v[158:161], v[2:9], v[188:195], v[158:161]
	v_mfma_f32_16x16x128_f8f6f4 v[154:157], v[10:17], v[188:195], v[154:157]
	v_mfma_f32_16x16x128_f8f6f4 v[138:141], v[10:17], v[196:203], v[138:141]
	v_mfma_f32_16x16x128_f8f6f4 v[142:145], v[2:9], v[196:203], v[142:145]
	v_mfma_f32_16x16x128_f8f6f4 v[110:113], v[2:9], v[212:219], v[110:113]
	v_mfma_f32_16x16x128_f8f6f4 v[106:109], v[10:17], v[212:219], v[106:109]
	v_mfma_f32_16x16x128_f8f6f4 v[102:105], v[18:25], v[212:219], v[102:105]
	v_mfma_f32_16x16x128_f8f6f4 v[98:101], v[26:33], v[212:219], v[98:101]
	v_mfma_f32_16x16x128_f8f6f4 v[146:149], v[26:33], v[188:195], v[146:149]
	v_mfma_f32_16x16x128_f8f6f4 v[150:153], v[18:25], v[188:195], v[150:153]
	v_mfma_f32_16x16x128_f8f6f4 v[134:137], v[18:25], v[196:203], v[134:137]
	v_mfma_f32_16x16x128_f8f6f4 v[130:133], v[26:33], v[196:203], v[130:133]
	v_mfma_f32_16x16x128_f8f6f4 v[114:117], v[26:33], v[204:211], v[114:117]
	v_mfma_f32_16x16x128_f8f6f4 v[118:121], v[18:25], v[204:211], v[118:121]
	s_setprio 0
	s_barrier
	s_add_i32 s24, s59, s3
	v_lshl_add_u64 v[174:175], v[174:175], 0, s[12:13]
	s_mov_b32 m0, s24
	ds_read_b128 v[188:191], v187 offset:49152
	ds_read_b128 v[192:195], v187 offset:50176
	ds_read_b128 v[196:199], v187 offset:51200
	ds_read_b128 v[200:203], v187 offset:52224
	ds_read_b128 v[204:207], v187 offset:53248
	ds_read_b128 v[208:211], v187 offset:54272
	ds_read_b128 v[212:215], v187 offset:55296
	ds_read_b128 v[216:219], v187 offset:56320
	global_load_lds_dwordx4 v[174:175], off
	s_add_i32 m0, s24, 0x2000
	s_add_u32 s24, s28, 0x158080
	v_lshl_add_u64 v[174:175], v[176:177], 0, s[12:13]
	s_addc_u32 s25, s29, 0
	s_add_i32 s28, s60, s3
	global_load_lds_dwordx4 v[174:175], off
	v_lshl_add_u64 v[174:175], s[24:25], 0, v[164:165]
	s_mov_b32 m0, s28
	s_nop 0
	global_load_lds_dwordx4 v[174:175], off
	v_lshl_add_u64 v[174:175], s[24:25], 0, v[162:163]
	s_add_i32 m0, s28, 0x2000
	s_nop 0
	global_load_lds_dwordx4 v[174:175], off
	v_lshl_add_u64 v[174:175], v[178:179], 0, s[12:13]
	s_mov_b32 m0, s38
	s_nop 0
	global_load_lds_dwordx4 v[174:175], off
	v_lshl_add_u64 v[174:175], v[180:181], 0, s[12:13]
	s_mov_b32 m0, s39
	s_nop 0
	global_load_lds_dwordx4 v[174:175], off
	s_waitcnt vmcnt(8)
	s_waitcnt lgkmcnt(0)
	s_barrier
	s_setprio 1
	v_mfma_f32_16x16x128_f8f6f4 v[62:65], v[2:9], v[204:211], v[62:65]
	v_mfma_f32_16x16x128_f8f6f4 v[58:61], v[10:17], v[204:211], v[58:61]
	v_mfma_f32_16x16x128_f8f6f4 v[90:93], v[10:17], v[188:195], v[90:93]
	v_mfma_f32_16x16x128_f8f6f4 v[94:97], v[2:9], v[188:195], v[94:97]
	v_mfma_f32_16x16x128_f8f6f4 v[78:81], v[2:9], v[196:203], v[78:81]
	v_mfma_f32_16x16x128_f8f6f4 v[74:77], v[10:17], v[196:203], v[74:77]
	v_mfma_f32_16x16x128_f8f6f4 v[42:45], v[10:17], v[212:219], v[42:45]
	v_mfma_f32_16x16x128_f8f6f4 v[46:49], v[2:9], v[212:219], v[46:49]
	v_mfma_f32_16x16x128_f8f6f4 v[38:41], v[18:25], v[212:219], v[38:41]
	v_mfma_f32_16x16x128_f8f6f4 v[34:37], v[26:33], v[212:219], v[34:37]
	v_mfma_f32_16x16x128_f8f6f4 v[82:85], v[26:33], v[188:195], v[82:85]
	v_mfma_f32_16x16x128_f8f6f4 v[86:89], v[18:25], v[188:195], v[86:89]
	v_mfma_f32_16x16x128_f8f6f4 v[70:73], v[18:25], v[196:203], v[70:73]
	v_mfma_f32_16x16x128_f8f6f4 v[66:69], v[26:33], v[196:203], v[66:69]
	v_mfma_f32_16x16x128_f8f6f4 v[50:53], v[26:33], v[204:211], v[50:53]
	v_mfma_f32_16x16x128_f8f6f4 v[54:57], v[18:25], v[204:211], v[54:57]
	s_setprio 0
	s_barrier
	s_add_i32 s58, s58, 2
	s_add_u32 s26, s26, 0x100
	s_addc_u32 s27, s27, 0
	s_add_u32 s50, s50, 0x100
	s_addc_u32 s51, s51, 0
	s_cmpk_gt_u32 s58, 0x53
	s_cbranch_scc0 .LBB0_318
	s_and_b64 vcc, exec, s[14:15]
	s_cbranch_vccz .LBB0_321
	s_barrier

.LBB0_332:
	s_add_u32 s6, s61, s4
	s_addc_u32 s7, s62, s5
	s_add_u32 s6, s6, 0x32800100
	s_addc_u32 s7, s7, 0
	s_add_u32 s24, s63, s4
	s_addc_u32 s25, s68, s5
	s_add_i32 s64, 0, 0x10000
	s_cmpk_eq_i32 s4, 0x2a00
	s_cselect_b32 s13, s1, s7
	s_cselect_b32 s12, s0, s6
	s_cselect_b32 s7, s29, s25
	s_cselect_b32 s6, s28, s24
	s_add_i32 s65, 0, 0x14000
	v_add_u32_e32 v2, s64, v188
	v_add_u32_e32 v6, s65, v188
	ds_read_b128 v[26:29], v2
	ds_read_b128 v[30:33], v2 offset:1024
	ds_read_b128 v[18:21], v2 offset:2048
	ds_read_b128 v[22:25], v2 offset:3072
	ds_read_b128 v[10:13], v6
	ds_read_b128 v[14:17], v6 offset:1024
	ds_read_b128 v[2:5], v6 offset:2048
	ds_read_b128 v[6:9], v6 offset:3072
	v_lshl_add_u64 v[214:215], v[168:169], 0, s[4:5]
	s_add_i32 m0, s18, 0xc000
	ds_read_b128 v[172:175], v189
	ds_read_b128 v[176:179], v189 offset:1024
	ds_read_b128 v[190:193], v189 offset:2048
	ds_read_b128 v[194:197], v189 offset:3072
	ds_read_b128 v[198:201], v189 offset:4096
	ds_read_b128 v[202:205], v189 offset:5120
	ds_read_b128 v[206:209], v189 offset:6144
	ds_read_b128 v[210:213], v189 offset:7168
	global_load_lds_dwordx4 v[214:215], off
	v_lshl_add_u64 v[214:215], v[170:171], 0, s[4:5]
	s_add_i32 m0, s18, 0xe000
	s_nop 0
	global_load_lds_dwordx4 v[214:215], off
	s_waitcnt vmcnt(8)
	s_waitcnt lgkmcnt(0)
	s_barrier
	s_setprio 1
	v_mfma_f32_16x16x128_f8f6f4 v[70:73], v[26:33], v[172:179], v[70:73]
	v_mfma_f32_16x16x128_f8f6f4 v[66:69], v[18:25], v[172:179], v[66:69]
	v_mfma_f32_16x16x128_f8f6f4 v[74:77], v[18:25], v[190:197], v[74:77]
	v_mfma_f32_16x16x128_f8f6f4 v[78:81], v[26:33], v[190:197], v[78:81]
	v_mfma_f32_16x16x128_f8f6f4 v[86:89], v[26:33], v[198:205], v[86:89]
	v_mfma_f32_16x16x128_f8f6f4 v[82:85], v[18:25], v[198:205], v[82:85]
	v_mfma_f32_16x16x128_f8f6f4 v[90:93], v[18:25], v[206:213], v[90:93]
	v_mfma_f32_16x16x128_f8f6f4 v[94:97], v[26:33], v[206:213], v[94:97]
	v_mfma_f32_16x16x128_f8f6f4 v[134:137], v[10:17], v[206:213], v[134:137]
	v_mfma_f32_16x16x128_f8f6f4 v[130:133], v[2:9], v[206:213], v[130:133]
	v_mfma_f32_16x16x128_f8f6f4 v[154:157], v[2:9], v[172:179], v[154:157]
	v_mfma_f32_16x16x128_f8f6f4 v[158:161], v[10:17], v[172:179], v[158:161]
	v_mfma_f32_16x16x128_f8f6f4 v[150:153], v[10:17], v[190:197], v[150:153]
	v_mfma_f32_16x16x128_f8f6f4 v[146:149], v[2:9], v[190:197], v[146:149]
	v_mfma_f32_16x16x128_f8f6f4 v[138:141], v[2:9], v[198:205], v[138:141]
	v_mfma_f32_16x16x128_f8f6f4 v[142:145], v[10:17], v[198:205], v[142:145]
	s_setprio 0
	s_barrier
	s_add_i32 s24, s64, s17
	v_lshl_add_u64 v[172:173], s[6:7], 0, v[162:163]
	s_mov_b32 m0, s24
	ds_read_b128 v[190:193], v189 offset:16384
	ds_read_b128 v[194:197], v189 offset:17408
	ds_read_b128 v[198:201], v189 offset:18432
	ds_read_b128 v[202:205], v189 offset:19456
	ds_read_b128 v[206:209], v189 offset:20480
	ds_read_b128 v[210:213], v189 offset:21504
	ds_read_b128 v[214:217], v189 offset:22528
	ds_read_b128 v[218:221], v189 offset:23552
	global_load_lds_dwordx4 v[172:173], off
	s_add_i32 m0, s24, 0x2000
	s_add_u32 s24, s6, 0x158000
	v_lshl_add_u64 v[174:175], s[6:7], 0, v[166:167]
	s_addc_u32 s25, s7, 0
	s_add_i32 s64, s65, s17
	global_load_lds_dwordx4 v[174:175], off
	v_lshl_add_u64 v[176:177], s[24:25], 0, v[162:163]
	s_mov_b32 m0, s64
	v_lshl_add_u64 v[178:179], s[12:13], 0, v[166:167]
	global_load_lds_dwordx4 v[176:177], off
	v_lshl_add_u64 v[176:177], s[24:25], 0, v[166:167]
	s_add_i32 m0, s64, 0x2000
	s_nop 0
	global_load_lds_dwordx4 v[176:177], off
	v_lshl_add_u64 v[176:177], s[12:13], 0, v[162:163]
	s_mov_b32 m0, s18
	s_nop 0
	global_load_lds_dwordx4 v[176:177], off
	s_mov_b32 m0, s19
	s_nop 0
	global_load_lds_dwordx4 v[178:179], off
	s_waitcnt vmcnt(8)
	s_waitcnt lgkmcnt(0)
	s_barrier
	s_setprio 1
	v_mfma_f32_16x16x128_f8f6f4 v[110:113], v[26:33], v[198:205], v[110:113]
	v_mfma_f32_16x16x128_f8f6f4 v[106:109], v[18:25], v[198:205], v[106:109]
	v_mfma_f32_16x16x128_f8f6f4 v[98:101], v[18:25], v[190:197], v[98:101]
	v_mfma_f32_16x16x128_f8f6f4 v[102:105], v[26:33], v[190:197], v[102:105]
	v_mfma_f32_16x16x128_f8f6f4 v[118:121], v[26:33], v[206:213], v[118:121]
	v_mfma_f32_16x16x128_f8f6f4 v[114:117], v[18:25], v[206:213], v[114:117]
	v_mfma_f32_16x16x128_f8f6f4 v[122:125], v[18:25], v[214:221], v[122:125]
	v_mfma_f32_16x16x128_f8f6f4 v[126:129], v[26:33], v[214:221], v[126:129]
	v_mfma_f32_16x16x128_f8f6f4 v[62:65], v[10:17], v[214:221], v[62:65]
	v_mfma_f32_16x16x128_f8f6f4 v[58:61], v[2:9], v[214:221], v[58:61]
	v_mfma_f32_16x16x128_f8f6f4 v[34:37], v[2:9], v[190:197], v[34:37]
	v_mfma_f32_16x16x128_f8f6f4 v[38:41], v[10:17], v[190:197], v[38:41]
	v_mfma_f32_16x16x128_f8f6f4 v[46:49], v[10:17], v[198:205], v[46:49]
	v_mfma_f32_16x16x128_f8f6f4 v[42:45], v[2:9], v[198:205], v[42:45]
	v_mfma_f32_16x16x128_f8f6f4 v[50:53], v[2:9], v[206:213], v[50:53]
	v_mfma_f32_16x16x128_f8f6f4 v[54:57], v[10:17], v[206:213], v[54:57]
	s_setprio 0
	s_barrier
	s_add_i32 s24, 0, 0x18000
	s_add_i32 s25, 0, 0x1c000
	v_add_u32_e32 v14, s24, v188
	v_add_u32_e32 v30, s25, v188
	ds_read_b128 v[2:5], v14
	ds_read_b128 v[6:9], v14 offset:1024
	ds_read_b128 v[10:13], v14 offset:2048
	ds_read_b128 v[14:17], v14 offset:3072
	ds_read_b128 v[18:21], v30
	ds_read_b128 v[22:25], v30 offset:1024
	ds_read_b128 v[26:29], v30 offset:2048
	ds_read_b128 v[30:33], v30 offset:3072
	s_add_u32 s12, s12, 0x158000
	s_addc_u32 s13, s13, 0
	s_mov_b32 m0, s93
	v_lshl_add_u64 v[222:223], s[12:13], 0, v[162:163]
	ds_read_b128 v[190:193], v189 offset:32768
	ds_read_b128 v[194:197], v189 offset:33792
	ds_read_b128 v[198:201], v189 offset:34816
	ds_read_b128 v[202:205], v189 offset:35840
	ds_read_b128 v[206:209], v189 offset:36864
	ds_read_b128 v[210:213], v189 offset:37888
	ds_read_b128 v[214:217], v189 offset:38912
	ds_read_b128 v[218:221], v189 offset:39936
	global_load_lds_dwordx4 v[222:223], off
	v_lshl_add_u64 v[222:223], s[12:13], 0, v[166:167]
	s_mov_b32 m0, s94
	s_nop 0
	global_load_lds_dwordx4 v[222:223], off
	s_waitcnt vmcnt(8)
	s_waitcnt lgkmcnt(0)
	s_barrier
	s_setprio 1
	v_mfma_f32_16x16x128_f8f6f4 v[82:85], v[10:17], v[206:213], v[82:85]
	v_mfma_f32_16x16x128_f8f6f4 v[86:89], v[2:9], v[206:213], v[86:89]
	v_mfma_f32_16x16x128_f8f6f4 v[70:73], v[2:9], v[190:197], v[70:73]
	v_mfma_f32_16x16x128_f8f6f4 v[66:69], v[10:17], v[190:197], v[66:69]
	v_mfma_f32_16x16x128_f8f6f4 v[74:77], v[10:17], v[198:205], v[74:77]
	v_mfma_f32_16x16x128_f8f6f4 v[78:81], v[2:9], v[198:205], v[78:81]
	v_mfma_f32_16x16x128_f8f6f4 v[94:97], v[2:9], v[214:221], v[94:97]
	v_mfma_f32_16x16x128_f8f6f4 v[90:93], v[10:17], v[214:221], v[90:93]
	v_mfma_f32_16x16x128_f8f6f4 v[134:137], v[18:25], v[214:221], v[134:137]
	v_mfma_f32_16x16x128_f8f6f4 v[130:133], v[26:33], v[214:221], v[130:133]
	v_mfma_f32_16x16x128_f8f6f4 v[154:157], v[26:33], v[190:197], v[154:157]
	v_mfma_f32_16x16x128_f8f6f4 v[158:161], v[18:25], v[190:197], v[158:161]
	v_mfma_f32_16x16x128_f8f6f4 v[150:153], v[18:25], v[198:205], v[150:153]
	v_mfma_f32_16x16x128_f8f6f4 v[146:149], v[26:33], v[198:205], v[146:149]
	v_mfma_f32_16x16x128_f8f6f4 v[138:141], v[26:33], v[206:213], v[138:141]
	v_mfma_f32_16x16x128_f8f6f4 v[142:145], v[18:25], v[206:213], v[142:145]
	s_setprio 0
	s_barrier
	s_add_i32 s12, s24, s17
	v_lshl_add_u64 v[172:173], v[172:173], 0, s[76:77]
	s_mov_b32 m0, s12
	ds_read_b128 v[190:193], v189 offset:49152
	ds_read_b128 v[194:197], v189 offset:50176
	ds_read_b128 v[198:201], v189 offset:51200
	ds_read_b128 v[202:205], v189 offset:52224
	ds_read_b128 v[206:209], v189 offset:53248
	ds_read_b128 v[210:213], v189 offset:54272
	ds_read_b128 v[214:217], v189 offset:55296
	ds_read_b128 v[218:221], v189 offset:56320
	global_load_lds_dwordx4 v[172:173], off
	s_add_i32 m0, s12, 0x2000
	s_add_u32 s6, s6, 0x158080
	v_lshl_add_u64 v[172:173], v[174:175], 0, s[76:77]
	s_addc_u32 s7, s7, 0
	s_add_i32 s12, s25, s17
	global_load_lds_dwordx4 v[172:173], off
	v_lshl_add_u64 v[172:173], s[6:7], 0, v[162:163]
	s_mov_b32 m0, s12
	s_nop 0
	global_load_lds_dwordx4 v[172:173], off
	v_lshl_add_u64 v[172:173], s[6:7], 0, v[166:167]
	s_add_i32 m0, s12, 0x2000
	s_nop 0
	global_load_lds_dwordx4 v[172:173], off
	v_lshl_add_u64 v[172:173], v[176:177], 0, s[76:77]
	s_mov_b32 m0, s95
	s_nop 0
	global_load_lds_dwordx4 v[172:173], off
	v_lshl_add_u64 v[172:173], v[178:179], 0, s[76:77]
	s_mov_b32 m0, vcc_lo
	s_nop 0
	global_load_lds_dwordx4 v[172:173], off
	s_waitcnt vmcnt(8)
	s_waitcnt lgkmcnt(0)
	s_barrier
	s_setprio 1
	v_mfma_f32_16x16x128_f8f6f4 v[118:121], v[2:9], v[206:213], v[118:121]
	v_mfma_f32_16x16x128_f8f6f4 v[114:117], v[10:17], v[206:213], v[114:117]
	v_mfma_f32_16x16x128_f8f6f4 v[98:101], v[10:17], v[190:197], v[98:101]
	v_mfma_f32_16x16x128_f8f6f4 v[102:105], v[2:9], v[190:197], v[102:105]
	v_mfma_f32_16x16x128_f8f6f4 v[110:113], v[2:9], v[198:205], v[110:113]
	v_mfma_f32_16x16x128_f8f6f4 v[106:109], v[10:17], v[198:205], v[106:109]
	v_mfma_f32_16x16x128_f8f6f4 v[122:125], v[10:17], v[214:221], v[122:125]
	v_mfma_f32_16x16x128_f8f6f4 v[126:129], v[2:9], v[214:221], v[126:129]
	v_mfma_f32_16x16x128_f8f6f4 v[62:65], v[18:25], v[214:221], v[62:65]
	v_mfma_f32_16x16x128_f8f6f4 v[58:61], v[26:33], v[214:221], v[58:61]
	v_mfma_f32_16x16x128_f8f6f4 v[34:37], v[26:33], v[190:197], v[34:37]
	v_mfma_f32_16x16x128_f8f6f4 v[38:41], v[18:25], v[190:197], v[38:41]
	v_mfma_f32_16x16x128_f8f6f4 v[46:49], v[18:25], v[198:205], v[46:49]
	v_mfma_f32_16x16x128_f8f6f4 v[42:45], v[26:33], v[198:205], v[42:45]
	v_mfma_f32_16x16x128_f8f6f4 v[50:53], v[26:33], v[206:213], v[50:53]
	v_mfma_f32_16x16x128_f8f6f4 v[54:57], v[18:25], v[206:213], v[54:57]
	s_setprio 0
	s_barrier
	s_add_i32 vcc_hi, vcc_hi, 2
	s_add_u32 s4, s4, 0x100
	s_addc_u32 s5, s5, 0
	s_cmpk_lt_u32 vcc_hi, 0x54
	s_cbranch_scc1 .LBB0_332
	s_waitcnt vmcnt(0)
	s_mov_b64 s[12:13], s[54:55]
	s_cmpk_gt_u32 s89, 0xff
	s_cbranch_scc1 .LBB0_335
	s_barrier

.LBB0_758:
	ds_read_b128 v[148:151], v146
	ds_read_b128 v[152:155], v146 offset:1024
	ds_read_b128 v[156:159], v146 offset:2048
	ds_read_b128 v[160:163], v146 offset:3072
	ds_read_b128 v[164:167], v147
	ds_read_b128 v[168:171], v147 offset:1024
	ds_read_b128 v[172:175], v147 offset:2048
	ds_read_b128 v[176:179], v147 offset:3072
	s_add_u32 s16, s42, s14
	s_addc_u32 s17, s43, s15
	s_add_u32 s16, s16, 0x2a800100
	s_addc_u32 s17, s17, 0
	s_add_u32 s60, s48, s14
	s_addc_u32 s61, s49, s15
	s_cmpk_eq_i32 s14, 0x700
	s_cselect_b32 s21, s13, s17
	s_cselect_b32 s20, s12, s16
	s_cselect_b32 s17, s11, s61
	s_cselect_b32 s16, s10, s60
	s_mov_b32 m0, s51
	v_lshl_add_u64 v[212:213], v[138:139], 0, s[14:15]
	ds_read_b128 v[180:183], v145
	ds_read_b128 v[184:187], v145 offset:1024
	ds_read_b128 v[188:191], v145 offset:2048
	ds_read_b128 v[192:195], v145 offset:3072
	ds_read_b128 v[196:199], v145 offset:4096
	ds_read_b128 v[200:203], v145 offset:5120
	ds_read_b128 v[204:207], v145 offset:6144
	ds_read_b128 v[208:211], v145 offset:7168
	global_load_lds_dwordx4 v[212:213], off
	v_lshl_add_u64 v[212:213], v[140:141], 0, s[14:15]
	s_mov_b32 m0, s58
	s_nop 0
	global_load_lds_dwordx4 v[212:213], off
	s_waitcnt vmcnt(8)
	s_waitcnt lgkmcnt(0)
	s_barrier
	s_setprio 1
	v_mfma_f32_16x16x32_bf16 v[126:129], v[148:151], v[180:183], v[126:129]
	v_mfma_f32_16x16x32_bf16 v[122:125], v[156:159], v[180:183], v[122:125]
	v_mfma_f32_16x16x32_bf16 v[118:121], v[148:151], v[188:191], v[118:121]
	v_mfma_f32_16x16x32_bf16 v[114:117], v[156:159], v[188:191], v[114:117]
	v_mfma_f32_16x16x32_bf16 v[106:109], v[148:151], v[196:199], v[106:109]
	v_mfma_f32_16x16x32_bf16 v[98:101], v[156:159], v[196:199], v[98:101]
	v_mfma_f32_16x16x32_bf16 v[90:93], v[148:151], v[204:207], v[90:93]
	v_mfma_f32_16x16x32_bf16 v[82:85], v[156:159], v[204:207], v[82:85]
	v_mfma_f32_16x16x32_bf16 v[126:129], v[152:155], v[184:187], v[126:129]
	v_mfma_f32_16x16x32_bf16 v[122:125], v[160:163], v[184:187], v[122:125]
	v_mfma_f32_16x16x32_bf16 v[118:121], v[152:155], v[192:195], v[118:121]
	v_mfma_f32_16x16x32_bf16 v[114:117], v[160:163], v[192:195], v[114:117]
	v_mfma_f32_16x16x32_bf16 v[106:109], v[152:155], v[200:203], v[106:109]
	v_mfma_f32_16x16x32_bf16 v[98:101], v[160:163], v[200:203], v[98:101]
	v_mfma_f32_16x16x32_bf16 v[90:93], v[152:155], v[208:211], v[90:93]
	v_mfma_f32_16x16x32_bf16 v[82:85], v[160:163], v[208:211], v[82:85]
	v_mfma_f32_16x16x32_bf16 v[110:113], v[164:167], v[180:183], v[110:113]
	v_mfma_f32_16x16x32_bf16 v[102:105], v[172:175], v[180:183], v[102:105]
	v_mfma_f32_16x16x32_bf16 v[94:97], v[164:167], v[188:191], v[94:97]
	v_mfma_f32_16x16x32_bf16 v[86:89], v[172:175], v[188:191], v[86:89]
	v_mfma_f32_16x16x32_bf16 v[78:81], v[164:167], v[196:199], v[78:81]
	v_mfma_f32_16x16x32_bf16 v[74:77], v[172:175], v[196:199], v[74:77]
	v_mfma_f32_16x16x32_bf16 v[70:73], v[164:167], v[204:207], v[70:73]
	v_mfma_f32_16x16x32_bf16 v[66:69], v[172:175], v[204:207], v[66:69]
	v_mfma_f32_16x16x32_bf16 v[110:113], v[168:171], v[184:187], v[110:113]
	v_mfma_f32_16x16x32_bf16 v[102:105], v[176:179], v[184:187], v[102:105]
	v_mfma_f32_16x16x32_bf16 v[94:97], v[168:171], v[192:195], v[94:97]
	v_mfma_f32_16x16x32_bf16 v[86:89], v[176:179], v[192:195], v[86:89]
	v_mfma_f32_16x16x32_bf16 v[78:81], v[168:171], v[200:203], v[78:81]
	v_mfma_f32_16x16x32_bf16 v[74:77], v[176:179], v[200:203], v[74:77]
	v_mfma_f32_16x16x32_bf16 v[70:73], v[168:171], v[208:211], v[70:73]
	v_mfma_f32_16x16x32_bf16 v[66:69], v[176:179], v[208:211], v[66:69]
	s_setprio 0
	s_barrier
	s_mov_b32 m0, s59
	v_lshl_add_u64 v[212:213], s[16:17], 0, v[130:131]
	ds_read_b128 v[180:183], v145 offset:16384
	ds_read_b128 v[184:187], v145 offset:17408
	ds_read_b128 v[188:191], v145 offset:18432
	ds_read_b128 v[192:195], v145 offset:19456
	ds_read_b128 v[196:199], v145 offset:20480
	ds_read_b128 v[200:203], v145 offset:21504
	ds_read_b128 v[204:207], v145 offset:22528
	ds_read_b128 v[208:211], v145 offset:23552
	global_load_lds_dwordx4 v[212:213], off
	s_add_i32 m0, s59, 0x2000
	s_add_u32 s60, s16, 0x100000
	v_lshl_add_u64 v[214:215], s[16:17], 0, v[136:137]
	s_addc_u32 s61, s17, 0
	s_add_i32 s62, s26, s31
	global_load_lds_dwordx4 v[214:215], off
	v_lshl_add_u64 v[216:217], s[60:61], 0, v[130:131]
	s_mov_b32 m0, s62
	v_lshl_add_u64 v[218:219], s[20:21], 0, v[134:135]
	global_load_lds_dwordx4 v[216:217], off
	v_lshl_add_u64 v[216:217], s[60:61], 0, v[136:137]
	s_add_i32 m0, s62, 0x2000
	s_nop 0
	global_load_lds_dwordx4 v[216:217], off
	v_lshl_add_u64 v[216:217], s[20:21], 0, v[132:133]
	s_mov_b32 m0, s7
	s_nop 0
	global_load_lds_dwordx4 v[216:217], off
	s_mov_b32 m0, s34
	s_nop 0
	global_load_lds_dwordx4 v[218:219], off
	s_waitcnt vmcnt(8)
	s_waitcnt lgkmcnt(0)
	s_barrier
	s_setprio 1
	v_mfma_f32_16x16x32_bf16 v[62:65], v[148:151], v[180:183], v[62:65]
	v_mfma_f32_16x16x32_bf16 v[58:61], v[156:159], v[180:183], v[58:61]
	v_mfma_f32_16x16x32_bf16 v[54:57], v[148:151], v[188:191], v[54:57]
	v_mfma_f32_16x16x32_bf16 v[50:53], v[156:159], v[188:191], v[50:53]
	v_mfma_f32_16x16x32_bf16 v[42:45], v[148:151], v[196:199], v[42:45]
	v_mfma_f32_16x16x32_bf16 v[34:37], v[156:159], v[196:199], v[34:37]
	v_mfma_f32_16x16x32_bf16 v[26:29], v[148:151], v[204:207], v[26:29]
	v_mfma_f32_16x16x32_bf16 v[18:21], v[156:159], v[204:207], v[18:21]
	v_mfma_f32_16x16x32_bf16 v[62:65], v[152:155], v[184:187], v[62:65]
	v_mfma_f32_16x16x32_bf16 v[58:61], v[160:163], v[184:187], v[58:61]
	v_mfma_f32_16x16x32_bf16 v[54:57], v[152:155], v[192:195], v[54:57]
	v_mfma_f32_16x16x32_bf16 v[50:53], v[160:163], v[192:195], v[50:53]
	v_mfma_f32_16x16x32_bf16 v[42:45], v[152:155], v[200:203], v[42:45]
	v_mfma_f32_16x16x32_bf16 v[34:37], v[160:163], v[200:203], v[34:37]
	v_mfma_f32_16x16x32_bf16 v[26:29], v[152:155], v[208:211], v[26:29]
	v_mfma_f32_16x16x32_bf16 v[18:21], v[160:163], v[208:211], v[18:21]
	v_mfma_f32_16x16x32_bf16 v[46:49], v[164:167], v[180:183], v[46:49]
	v_mfma_f32_16x16x32_bf16 v[38:41], v[172:175], v[180:183], v[38:41]
	v_mfma_f32_16x16x32_bf16 v[30:33], v[164:167], v[188:191], v[30:33]
	v_mfma_f32_16x16x32_bf16 v[22:25], v[172:175], v[188:191], v[22:25]
	v_mfma_f32_16x16x32_bf16 v[14:17], v[164:167], v[196:199], v[14:17]
	v_mfma_f32_16x16x32_bf16 v[10:13], v[172:175], v[196:199], v[10:13]
	v_mfma_f32_16x16x32_bf16 v[6:9], v[164:167], v[204:207], v[6:9]
	v_mfma_f32_16x16x32_bf16 v[2:5], v[172:175], v[204:207], v[2:5]
	v_mfma_f32_16x16x32_bf16 v[46:49], v[168:171], v[184:187], v[46:49]
	v_mfma_f32_16x16x32_bf16 v[38:41], v[176:179], v[184:187], v[38:41]
	v_mfma_f32_16x16x32_bf16 v[30:33], v[168:171], v[192:195], v[30:33]
	v_mfma_f32_16x16x32_bf16 v[22:25], v[176:179], v[192:195], v[22:25]
	v_mfma_f32_16x16x32_bf16 v[14:17], v[168:171], v[200:203], v[14:17]
	v_mfma_f32_16x16x32_bf16 v[10:13], v[176:179], v[200:203], v[10:13]
	v_mfma_f32_16x16x32_bf16 v[6:9], v[168:171], v[208:211], v[6:9]
	v_mfma_f32_16x16x32_bf16 v[2:5], v[176:179], v[208:211], v[2:5]
	s_setprio 0
	s_barrier
	s_add_i32 s60, 0, 0x18000
	s_add_i32 s61, 0, 0x1c000
	v_add_u32_e32 v160, s60, v144
	v_add_u32_e32 v176, s61, v144
	ds_read_b128 v[148:151], v160
	ds_read_b128 v[152:155], v160 offset:1024
	ds_read_b128 v[156:159], v160 offset:2048
	ds_read_b128 v[160:163], v160 offset:3072
	ds_read_b128 v[164:167], v176
	ds_read_b128 v[168:171], v176 offset:1024
	ds_read_b128 v[172:175], v176 offset:2048
	ds_read_b128 v[176:179], v176 offset:3072
	s_add_u32 s20, s20, 0x100000
	s_addc_u32 s21, s21, 0
	s_mov_b32 m0, s35
	v_lshl_add_u64 v[220:221], s[20:21], 0, v[132:133]
	ds_read_b128 v[180:183], v145 offset:32768
	ds_read_b128 v[184:187], v145 offset:33792
	ds_read_b128 v[188:191], v145 offset:34816
	ds_read_b128 v[192:195], v145 offset:35840
	ds_read_b128 v[196:199], v145 offset:36864
	ds_read_b128 v[200:203], v145 offset:37888
	ds_read_b128 v[204:207], v145 offset:38912
	ds_read_b128 v[208:211], v145 offset:39936
	global_load_lds_dwordx4 v[220:221], off
	v_lshl_add_u64 v[220:221], s[20:21], 0, v[134:135]
	s_mov_b32 m0, s38
	s_nop 0
	global_load_lds_dwordx4 v[220:221], off
	s_waitcnt vmcnt(8)
	s_waitcnt lgkmcnt(0)
	s_barrier
	s_setprio 1
	v_mfma_f32_16x16x32_bf16 v[126:129], v[148:151], v[180:183], v[126:129]
	v_mfma_f32_16x16x32_bf16 v[122:125], v[156:159], v[180:183], v[122:125]
	v_mfma_f32_16x16x32_bf16 v[118:121], v[148:151], v[188:191], v[118:121]
	v_mfma_f32_16x16x32_bf16 v[114:117], v[156:159], v[188:191], v[114:117]
	v_mfma_f32_16x16x32_bf16 v[106:109], v[148:151], v[196:199], v[106:109]
	v_mfma_f32_16x16x32_bf16 v[98:101], v[156:159], v[196:199], v[98:101]
	v_mfma_f32_16x16x32_bf16 v[90:93], v[148:151], v[204:207], v[90:93]
	v_mfma_f32_16x16x32_bf16 v[82:85], v[156:159], v[204:207], v[82:85]
	v_mfma_f32_16x16x32_bf16 v[126:129], v[152:155], v[184:187], v[126:129]
	v_mfma_f32_16x16x32_bf16 v[122:125], v[160:163], v[184:187], v[122:125]
	v_mfma_f32_16x16x32_bf16 v[118:121], v[152:155], v[192:195], v[118:121]
	v_mfma_f32_16x16x32_bf16 v[114:117], v[160:163], v[192:195], v[114:117]
	v_mfma_f32_16x16x32_bf16 v[106:109], v[152:155], v[200:203], v[106:109]
	v_mfma_f32_16x16x32_bf16 v[98:101], v[160:163], v[200:203], v[98:101]
	v_mfma_f32_16x16x32_bf16 v[90:93], v[152:155], v[208:211], v[90:93]
	v_mfma_f32_16x16x32_bf16 v[82:85], v[160:163], v[208:211], v[82:85]
	v_mfma_f32_16x16x32_bf16 v[110:113], v[164:167], v[180:183], v[110:113]
	v_mfma_f32_16x16x32_bf16 v[102:105], v[172:175], v[180:183], v[102:105]
	v_mfma_f32_16x16x32_bf16 v[94:97], v[164:167], v[188:191], v[94:97]
	v_mfma_f32_16x16x32_bf16 v[86:89], v[172:175], v[188:191], v[86:89]
	v_mfma_f32_16x16x32_bf16 v[78:81], v[164:167], v[196:199], v[78:81]
	v_mfma_f32_16x16x32_bf16 v[74:77], v[172:175], v[196:199], v[74:77]
	v_mfma_f32_16x16x32_bf16 v[70:73], v[164:167], v[204:207], v[70:73]
	v_mfma_f32_16x16x32_bf16 v[66:69], v[172:175], v[204:207], v[66:69]
	v_mfma_f32_16x16x32_bf16 v[110:113], v[168:171], v[184:187], v[110:113]
	v_mfma_f32_16x16x32_bf16 v[102:105], v[176:179], v[184:187], v[102:105]
	v_mfma_f32_16x16x32_bf16 v[94:97], v[168:171], v[192:195], v[94:97]
	v_mfma_f32_16x16x32_bf16 v[86:89], v[176:179], v[192:195], v[86:89]
	v_mfma_f32_16x16x32_bf16 v[78:81], v[168:171], v[200:203], v[78:81]
	v_mfma_f32_16x16x32_bf16 v[74:77], v[176:179], v[200:203], v[74:77]
	v_mfma_f32_16x16x32_bf16 v[70:73], v[168:171], v[208:211], v[70:73]
	v_mfma_f32_16x16x32_bf16 v[66:69], v[176:179], v[208:211], v[66:69]
	s_setprio 0
	s_barrier
	s_add_i32 s20, s60, s31
	v_lshl_add_u64 v[212:213], v[212:213], 0, s[4:5]
	s_mov_b32 m0, s20
	ds_read_b128 v[180:183], v145 offset:49152
	ds_read_b128 v[184:187], v145 offset:50176
	ds_read_b128 v[188:191], v145 offset:51200
	ds_read_b128 v[192:195], v145 offset:52224
	ds_read_b128 v[196:199], v145 offset:53248
	ds_read_b128 v[200:203], v145 offset:54272
	ds_read_b128 v[204:207], v145 offset:55296
	ds_read_b128 v[208:211], v145 offset:56320
	global_load_lds_dwordx4 v[212:213], off
	s_add_i32 m0, s20, 0x2000
	s_add_u32 s16, s16, 0x100080
	v_lshl_add_u64 v[212:213], v[214:215], 0, s[4:5]
	s_addc_u32 s17, s17, 0
	s_add_i32 s20, s61, s31
	global_load_lds_dwordx4 v[212:213], off
	v_lshl_add_u64 v[212:213], s[16:17], 0, v[130:131]
	s_mov_b32 m0, s20
	s_nop 0
	global_load_lds_dwordx4 v[212:213], off
	v_lshl_add_u64 v[212:213], s[16:17], 0, v[136:137]
	s_add_i32 m0, s20, 0x2000
	s_nop 0
	global_load_lds_dwordx4 v[212:213], off
	v_lshl_add_u64 v[212:213], v[216:217], 0, s[4:5]
	s_mov_b32 m0, s40
	s_nop 0
	global_load_lds_dwordx4 v[212:213], off
	v_lshl_add_u64 v[212:213], v[218:219], 0, s[4:5]
	s_mov_b32 m0, s41
	s_nop 0
	global_load_lds_dwordx4 v[212:213], off
	s_waitcnt vmcnt(8)
	s_waitcnt lgkmcnt(0)
	s_barrier
	s_setprio 1
	v_mfma_f32_16x16x32_bf16 v[62:65], v[148:151], v[180:183], v[62:65]
	v_mfma_f32_16x16x32_bf16 v[58:61], v[156:159], v[180:183], v[58:61]
	v_mfma_f32_16x16x32_bf16 v[54:57], v[148:151], v[188:191], v[54:57]
	v_mfma_f32_16x16x32_bf16 v[50:53], v[156:159], v[188:191], v[50:53]
	v_mfma_f32_16x16x32_bf16 v[42:45], v[148:151], v[196:199], v[42:45]
	v_mfma_f32_16x16x32_bf16 v[34:37], v[156:159], v[196:199], v[34:37]
	v_mfma_f32_16x16x32_bf16 v[26:29], v[148:151], v[204:207], v[26:29]
	v_mfma_f32_16x16x32_bf16 v[18:21], v[156:159], v[204:207], v[18:21]
	v_mfma_f32_16x16x32_bf16 v[62:65], v[152:155], v[184:187], v[62:65]
	v_mfma_f32_16x16x32_bf16 v[58:61], v[160:163], v[184:187], v[58:61]
	v_mfma_f32_16x16x32_bf16 v[54:57], v[152:155], v[192:195], v[54:57]
	v_mfma_f32_16x16x32_bf16 v[50:53], v[160:163], v[192:195], v[50:53]
	v_mfma_f32_16x16x32_bf16 v[42:45], v[152:155], v[200:203], v[42:45]
	v_mfma_f32_16x16x32_bf16 v[34:37], v[160:163], v[200:203], v[34:37]
	v_mfma_f32_16x16x32_bf16 v[26:29], v[152:155], v[208:211], v[26:29]
	v_mfma_f32_16x16x32_bf16 v[18:21], v[160:163], v[208:211], v[18:21]
	v_mfma_f32_16x16x32_bf16 v[46:49], v[164:167], v[180:183], v[46:49]
	v_mfma_f32_16x16x32_bf16 v[38:41], v[172:175], v[180:183], v[38:41]
	v_mfma_f32_16x16x32_bf16 v[30:33], v[164:167], v[188:191], v[30:33]
	v_mfma_f32_16x16x32_bf16 v[22:25], v[172:175], v[188:191], v[22:25]
	v_mfma_f32_16x16x32_bf16 v[14:17], v[164:167], v[196:199], v[14:17]
	v_mfma_f32_16x16x32_bf16 v[10:13], v[172:175], v[196:199], v[10:13]
	v_mfma_f32_16x16x32_bf16 v[6:9], v[164:167], v[204:207], v[6:9]
	v_mfma_f32_16x16x32_bf16 v[2:5], v[172:175], v[204:207], v[2:5]
	v_mfma_f32_16x16x32_bf16 v[46:49], v[168:171], v[184:187], v[46:49]
	v_mfma_f32_16x16x32_bf16 v[38:41], v[176:179], v[184:187], v[38:41]
	v_mfma_f32_16x16x32_bf16 v[30:33], v[168:171], v[192:195], v[30:33]
	v_mfma_f32_16x16x32_bf16 v[22:25], v[176:179], v[192:195], v[22:25]
	v_mfma_f32_16x16x32_bf16 v[14:17], v[168:171], v[200:203], v[14:17]
	v_mfma_f32_16x16x32_bf16 v[10:13], v[176:179], v[200:203], v[10:13]
	v_mfma_f32_16x16x32_bf16 v[6:9], v[168:171], v[208:211], v[6:9]
	v_mfma_f32_16x16x32_bf16 v[2:5], v[176:179], v[208:211], v[2:5]
	s_setprio 0
	s_barrier
	s_add_i32 s50, s50, 2
	s_add_u32 s14, s14, 0x100
	s_addc_u32 s15, s15, 0
	s_cmp_gt_u32 s50, 13
	s_cbranch_scc0 .LBB0_758
	s_cmpk_lt_u32 s30, 0x100
	s_cbranch_scc0 .LBB0_754
	s_barrier
	s_branch .LBB0_754

.LBB0_768:
	ds_read_b128 v[130:133], v1
	ds_read_b128 v[134:137], v1 offset:1024
	ds_read_b128 v[138:141], v1 offset:2048
	ds_read_b128 v[142:145], v1 offset:3072
	ds_read_b128 v[180:183], v176
	ds_read_b128 v[184:187], v176 offset:1024
	ds_read_b128 v[188:191], v176 offset:2048
	ds_read_b128 v[192:195], v176 offset:3072
	s_add_u32 s1, s16, 0xfff00080
	s_addc_u32 s20, s17, -1
	s_add_u32 s49, s16, 0xdb300080
	s_addc_u32 s21, s17, -1
	s_cmp_eq_u32 s0, 60
	s_cselect_b32 s25, s55, s20
	s_cselect_b32 s24, s54, s1
	s_cselect_b32 s21, s9, s21
	s_cselect_b32 s20, s8, s49
	s_mov_b32 m0, s35
	v_lshl_add_u64 v[228:229], s[16:17], 0, v[172:173]
	ds_read_b128 v[196:199], v177
	ds_read_b128 v[200:203], v177 offset:1024
	ds_read_b128 v[204:207], v177 offset:2048
	ds_read_b128 v[208:211], v177 offset:3072
	ds_read_b128 v[212:215], v177 offset:4096
	ds_read_b128 v[216:219], v177 offset:5120
	ds_read_b128 v[220:223], v177 offset:6144
	ds_read_b128 v[224:227], v177 offset:7168
	global_load_lds_dwordx4 v[228:229], off
	v_lshl_add_u64 v[228:229], s[16:17], 0, v[174:175]
	s_mov_b32 m0, s36
	s_nop 0
	global_load_lds_dwordx4 v[228:229], off
	s_waitcnt vmcnt(8)
	s_waitcnt lgkmcnt(0)
	s_barrier
	s_setprio 1
	v_mfma_f32_16x16x32_bf16 v[126:129], v[130:133], v[196:199], v[126:129]
	v_mfma_f32_16x16x32_bf16 v[122:125], v[138:141], v[196:199], v[122:125]
	v_mfma_f32_16x16x32_bf16 v[114:117], v[130:133], v[204:207], v[114:117]
	v_mfma_f32_16x16x32_bf16 v[106:109], v[138:141], v[204:207], v[106:109]
	v_mfma_f32_16x16x32_bf16 v[98:101], v[130:133], v[212:215], v[98:101]
	v_mfma_f32_16x16x32_bf16 v[90:93], v[138:141], v[212:215], v[90:93]
	v_mfma_f32_16x16x32_bf16 v[82:85], v[130:133], v[220:223], v[82:85]
	v_mfma_f32_16x16x32_bf16 v[74:77], v[138:141], v[220:223], v[74:77]
	v_mfma_f32_16x16x32_bf16 v[126:129], v[134:137], v[200:203], v[126:129]
	v_mfma_f32_16x16x32_bf16 v[122:125], v[142:145], v[200:203], v[122:125]
	v_mfma_f32_16x16x32_bf16 v[114:117], v[134:137], v[208:211], v[114:117]
	v_mfma_f32_16x16x32_bf16 v[106:109], v[142:145], v[208:211], v[106:109]
	v_mfma_f32_16x16x32_bf16 v[98:101], v[134:137], v[216:219], v[98:101]
	v_mfma_f32_16x16x32_bf16 v[90:93], v[142:145], v[216:219], v[90:93]
	v_mfma_f32_16x16x32_bf16 v[82:85], v[134:137], v[224:227], v[82:85]
	v_mfma_f32_16x16x32_bf16 v[74:77], v[142:145], v[224:227], v[74:77]
	v_mfma_f32_16x16x32_bf16 v[118:121], v[180:183], v[196:199], v[118:121]
	v_mfma_f32_16x16x32_bf16 v[110:113], v[188:191], v[196:199], v[110:113]
	v_mfma_f32_16x16x32_bf16 v[102:105], v[180:183], v[204:207], v[102:105]
	v_mfma_f32_16x16x32_bf16 v[94:97], v[188:191], v[204:207], v[94:97]
	v_mfma_f32_16x16x32_bf16 v[86:89], v[180:183], v[212:215], v[86:89]
	v_mfma_f32_16x16x32_bf16 v[78:81], v[188:191], v[212:215], v[78:81]
	v_mfma_f32_16x16x32_bf16 v[70:73], v[180:183], v[220:223], v[70:73]
	v_mfma_f32_16x16x32_bf16 v[66:69], v[188:191], v[220:223], v[66:69]
	v_mfma_f32_16x16x32_bf16 v[118:121], v[184:187], v[200:203], v[118:121]
	v_mfma_f32_16x16x32_bf16 v[110:113], v[192:195], v[200:203], v[110:113]
	v_mfma_f32_16x16x32_bf16 v[102:105], v[184:187], v[208:211], v[102:105]
	v_mfma_f32_16x16x32_bf16 v[94:97], v[192:195], v[208:211], v[94:97]
	v_mfma_f32_16x16x32_bf16 v[86:89], v[184:187], v[216:219], v[86:89]
	v_mfma_f32_16x16x32_bf16 v[78:81], v[192:195], v[216:219], v[78:81]
	v_mfma_f32_16x16x32_bf16 v[70:73], v[184:187], v[224:227], v[70:73]
	v_mfma_f32_16x16x32_bf16 v[66:69], v[192:195], v[224:227], v[66:69]
	s_setprio 0
	s_barrier
	s_mov_b32 m0, s37
	v_lshl_add_u64 v[228:229], s[20:21], 0, v[150:151]
	s_add_u32 s50, s20, 0x100000
	ds_read_b128 v[196:199], v177 offset:16384
	ds_read_b128 v[200:203], v177 offset:17408
	ds_read_b128 v[204:207], v177 offset:18432
	ds_read_b128 v[208:211], v177 offset:19456
	ds_read_b128 v[212:215], v177 offset:20480
	ds_read_b128 v[216:219], v177 offset:21504
	ds_read_b128 v[220:223], v177 offset:22528
	ds_read_b128 v[224:227], v177 offset:23552
	global_load_lds_dwordx4 v[228:229], off
	v_lshl_add_u64 v[230:231], s[20:21], 0, v[146:147]
	s_mov_b32 m0, s38
	s_addc_u32 s51, s21, 0
	global_load_lds_dwordx4 v[230:231], off
	v_lshl_add_u64 v[232:233], s[50:51], 0, v[150:151]
	s_mov_b32 m0, s39
	v_lshl_add_u64 v[234:235], s[24:25], 0, v[148:149]
	global_load_lds_dwordx4 v[232:233], off
	v_lshl_add_u64 v[232:233], s[50:51], 0, v[146:147]
	s_mov_b32 m0, s40
	s_nop 0
	global_load_lds_dwordx4 v[232:233], off
	v_lshl_add_u64 v[232:233], s[24:25], 0, v[152:153]
	s_mov_b32 m0, s26
	s_nop 0
	global_load_lds_dwordx4 v[232:233], off
	s_mov_b32 m0, s27
	s_nop 0
	global_load_lds_dwordx4 v[234:235], off
	s_waitcnt vmcnt(8)
	s_waitcnt lgkmcnt(0)
	s_barrier
	s_setprio 1
	v_mfma_f32_16x16x32_bf16 v[62:65], v[130:133], v[196:199], v[62:65]
	v_mfma_f32_16x16x32_bf16 v[58:61], v[138:141], v[196:199], v[58:61]
	v_mfma_f32_16x16x32_bf16 v[50:53], v[130:133], v[204:207], v[50:53]
	v_mfma_f32_16x16x32_bf16 v[42:45], v[138:141], v[204:207], v[42:45]
	v_mfma_f32_16x16x32_bf16 v[34:37], v[130:133], v[212:215], v[34:37]
	v_mfma_f32_16x16x32_bf16 v[26:29], v[138:141], v[212:215], v[26:29]
	v_mfma_f32_16x16x32_bf16 v[18:21], v[130:133], v[220:223], v[18:21]
	v_mfma_f32_16x16x32_bf16 v[10:13], v[138:141], v[220:223], v[10:13]
	v_mfma_f32_16x16x32_bf16 v[62:65], v[134:137], v[200:203], v[62:65]
	v_mfma_f32_16x16x32_bf16 v[58:61], v[142:145], v[200:203], v[58:61]
	v_mfma_f32_16x16x32_bf16 v[50:53], v[134:137], v[208:211], v[50:53]
	v_mfma_f32_16x16x32_bf16 v[42:45], v[142:145], v[208:211], v[42:45]
	v_mfma_f32_16x16x32_bf16 v[34:37], v[134:137], v[216:219], v[34:37]
	v_mfma_f32_16x16x32_bf16 v[26:29], v[142:145], v[216:219], v[26:29]
	v_mfma_f32_16x16x32_bf16 v[18:21], v[134:137], v[224:227], v[18:21]
	v_mfma_f32_16x16x32_bf16 v[10:13], v[142:145], v[224:227], v[10:13]
	v_mfma_f32_16x16x32_bf16 v[54:57], v[180:183], v[196:199], v[54:57]
	v_mfma_f32_16x16x32_bf16 v[46:49], v[188:191], v[196:199], v[46:49]
	v_mfma_f32_16x16x32_bf16 v[38:41], v[180:183], v[204:207], v[38:41]
	v_mfma_f32_16x16x32_bf16 v[30:33], v[188:191], v[204:207], v[30:33]
	v_mfma_f32_16x16x32_bf16 v[22:25], v[180:183], v[212:215], v[22:25]
	v_mfma_f32_16x16x32_bf16 v[14:17], v[188:191], v[212:215], v[14:17]
	v_mfma_f32_16x16x32_bf16 v[6:9], v[180:183], v[220:223], v[6:9]
	v_mfma_f32_16x16x32_bf16 v[2:5], v[188:191], v[220:223], v[2:5]
	v_mfma_f32_16x16x32_bf16 v[54:57], v[184:187], v[200:203], v[54:57]
	v_mfma_f32_16x16x32_bf16 v[46:49], v[192:195], v[200:203], v[46:49]
	v_mfma_f32_16x16x32_bf16 v[38:41], v[184:187], v[208:211], v[38:41]
	v_mfma_f32_16x16x32_bf16 v[30:33], v[192:195], v[208:211], v[30:33]
	v_mfma_f32_16x16x32_bf16 v[22:25], v[184:187], v[216:219], v[22:25]
	v_mfma_f32_16x16x32_bf16 v[14:17], v[192:195], v[216:219], v[14:17]
	v_mfma_f32_16x16x32_bf16 v[6:9], v[184:187], v[224:227], v[6:9]
	v_mfma_f32_16x16x32_bf16 v[2:5], v[192:195], v[224:227], v[2:5]
	s_setprio 0
	s_barrier
	ds_read_b128 v[130:133], v178
	ds_read_b128 v[134:137], v178 offset:1024
	ds_read_b128 v[138:141], v178 offset:2048
	ds_read_b128 v[142:145], v178 offset:3072
	ds_read_b128 v[180:183], v179
	ds_read_b128 v[184:187], v179 offset:1024
	ds_read_b128 v[188:191], v179 offset:2048
	ds_read_b128 v[192:195], v179 offset:3072
	s_add_u32 s24, s24, 0x100000
	s_addc_u32 s25, s25, 0
	s_mov_b32 m0, s28
	v_lshl_add_u64 v[236:237], s[24:25], 0, v[152:153]
	ds_read_b128 v[196:199], v177 offset:32768
	ds_read_b128 v[200:203], v177 offset:33792
	ds_read_b128 v[204:207], v177 offset:34816
	ds_read_b128 v[208:211], v177 offset:35840
	ds_read_b128 v[212:215], v177 offset:36864
	ds_read_b128 v[216:219], v177 offset:37888
	ds_read_b128 v[220:223], v177 offset:38912
	ds_read_b128 v[224:227], v177 offset:39936
	global_load_lds_dwordx4 v[236:237], off
	v_lshl_add_u64 v[236:237], s[24:25], 0, v[148:149]
	s_mov_b32 m0, s29
	s_nop 0
	global_load_lds_dwordx4 v[236:237], off
	s_waitcnt vmcnt(8)
	s_waitcnt lgkmcnt(0)
	s_barrier
	s_setprio 1
	v_mfma_f32_16x16x32_bf16 v[126:129], v[130:133], v[196:199], v[126:129]
	v_mfma_f32_16x16x32_bf16 v[122:125], v[138:141], v[196:199], v[122:125]
	v_mfma_f32_16x16x32_bf16 v[114:117], v[130:133], v[204:207], v[114:117]
	v_mfma_f32_16x16x32_bf16 v[106:109], v[138:141], v[204:207], v[106:109]
	v_mfma_f32_16x16x32_bf16 v[98:101], v[130:133], v[212:215], v[98:101]
	v_mfma_f32_16x16x32_bf16 v[90:93], v[138:141], v[212:215], v[90:93]
	v_mfma_f32_16x16x32_bf16 v[82:85], v[130:133], v[220:223], v[82:85]
	v_mfma_f32_16x16x32_bf16 v[74:77], v[138:141], v[220:223], v[74:77]
	v_mfma_f32_16x16x32_bf16 v[126:129], v[134:137], v[200:203], v[126:129]
	v_mfma_f32_16x16x32_bf16 v[122:125], v[142:145], v[200:203], v[122:125]
	v_mfma_f32_16x16x32_bf16 v[114:117], v[134:137], v[208:211], v[114:117]
	v_mfma_f32_16x16x32_bf16 v[106:109], v[142:145], v[208:211], v[106:109]
	v_mfma_f32_16x16x32_bf16 v[98:101], v[134:137], v[216:219], v[98:101]
	v_mfma_f32_16x16x32_bf16 v[90:93], v[142:145], v[216:219], v[90:93]
	v_mfma_f32_16x16x32_bf16 v[82:85], v[134:137], v[224:227], v[82:85]
	v_mfma_f32_16x16x32_bf16 v[74:77], v[142:145], v[224:227], v[74:77]
	v_mfma_f32_16x16x32_bf16 v[118:121], v[180:183], v[196:199], v[118:121]
	v_mfma_f32_16x16x32_bf16 v[110:113], v[188:191], v[196:199], v[110:113]
	v_mfma_f32_16x16x32_bf16 v[102:105], v[180:183], v[204:207], v[102:105]
	v_mfma_f32_16x16x32_bf16 v[94:97], v[188:191], v[204:207], v[94:97]
	v_mfma_f32_16x16x32_bf16 v[86:89], v[180:183], v[212:215], v[86:89]
	v_mfma_f32_16x16x32_bf16 v[78:81], v[188:191], v[212:215], v[78:81]
	v_mfma_f32_16x16x32_bf16 v[70:73], v[180:183], v[220:223], v[70:73]
	v_mfma_f32_16x16x32_bf16 v[66:69], v[188:191], v[220:223], v[66:69]
	v_mfma_f32_16x16x32_bf16 v[118:121], v[184:187], v[200:203], v[118:121]
	v_mfma_f32_16x16x32_bf16 v[110:113], v[192:195], v[200:203], v[110:113]
	v_mfma_f32_16x16x32_bf16 v[102:105], v[184:187], v[208:211], v[102:105]
	v_mfma_f32_16x16x32_bf16 v[94:97], v[192:195], v[208:211], v[94:97]
	v_mfma_f32_16x16x32_bf16 v[86:89], v[184:187], v[216:219], v[86:89]
	v_mfma_f32_16x16x32_bf16 v[78:81], v[192:195], v[216:219], v[78:81]
	v_mfma_f32_16x16x32_bf16 v[70:73], v[184:187], v[224:227], v[70:73]
	v_mfma_f32_16x16x32_bf16 v[66:69], v[192:195], v[224:227], v[66:69]
	s_setprio 0
	s_barrier
	s_mov_b32 m0, s41
	v_lshl_add_u64 v[228:229], v[228:229], 0, s[14:15]
	s_add_u32 s20, s20, 0x100080
	ds_read_b128 v[196:199], v177 offset:49152
	ds_read_b128 v[200:203], v177 offset:50176
	ds_read_b128 v[204:207], v177 offset:51200
	ds_read_b128 v[208:211], v177 offset:52224
	ds_read_b128 v[212:215], v177 offset:53248
	ds_read_b128 v[216:219], v177 offset:54272
	ds_read_b128 v[220:223], v177 offset:55296
	ds_read_b128 v[224:227], v177 offset:56320
	global_load_lds_dwordx4 v[228:229], off
	v_lshl_add_u64 v[228:229], v[230:231], 0, s[14:15]
	s_mov_b32 m0, s42
	s_addc_u32 s21, s21, 0
	global_load_lds_dwordx4 v[228:229], off
	v_lshl_add_u64 v[228:229], s[20:21], 0, v[150:151]
	s_mov_b32 m0, s43
	s_nop 0
	global_load_lds_dwordx4 v[228:229], off
	v_lshl_add_u64 v[228:229], s[20:21], 0, v[146:147]
	s_mov_b32 m0, s48
	s_nop 0
	global_load_lds_dwordx4 v[228:229], off
	v_lshl_add_u64 v[228:229], v[232:233], 0, s[14:15]
	s_mov_b32 m0, s31
	s_nop 0
	global_load_lds_dwordx4 v[228:229], off
	v_lshl_add_u64 v[228:229], v[234:235], 0, s[14:15]
	s_mov_b32 m0, s34
	s_nop 0
	global_load_lds_dwordx4 v[228:229], off
	s_waitcnt vmcnt(8)
	s_waitcnt lgkmcnt(0)
	s_barrier
	s_setprio 1
	v_mfma_f32_16x16x32_bf16 v[62:65], v[130:133], v[196:199], v[62:65]
	v_mfma_f32_16x16x32_bf16 v[58:61], v[138:141], v[196:199], v[58:61]
	v_mfma_f32_16x16x32_bf16 v[50:53], v[130:133], v[204:207], v[50:53]
	v_mfma_f32_16x16x32_bf16 v[42:45], v[138:141], v[204:207], v[42:45]
	v_mfma_f32_16x16x32_bf16 v[34:37], v[130:133], v[212:215], v[34:37]
	v_mfma_f32_16x16x32_bf16 v[26:29], v[138:141], v[212:215], v[26:29]
	v_mfma_f32_16x16x32_bf16 v[18:21], v[130:133], v[220:223], v[18:21]
	v_mfma_f32_16x16x32_bf16 v[10:13], v[138:141], v[220:223], v[10:13]
	v_mfma_f32_16x16x32_bf16 v[62:65], v[134:137], v[200:203], v[62:65]
	v_mfma_f32_16x16x32_bf16 v[58:61], v[142:145], v[200:203], v[58:61]
	v_mfma_f32_16x16x32_bf16 v[50:53], v[134:137], v[208:211], v[50:53]
	v_mfma_f32_16x16x32_bf16 v[42:45], v[142:145], v[208:211], v[42:45]
	v_mfma_f32_16x16x32_bf16 v[34:37], v[134:137], v[216:219], v[34:37]
	v_mfma_f32_16x16x32_bf16 v[26:29], v[142:145], v[216:219], v[26:29]
	v_mfma_f32_16x16x32_bf16 v[18:21], v[134:137], v[224:227], v[18:21]
	v_mfma_f32_16x16x32_bf16 v[10:13], v[142:145], v[224:227], v[10:13]
	v_mfma_f32_16x16x32_bf16 v[54:57], v[180:183], v[196:199], v[54:57]
	v_mfma_f32_16x16x32_bf16 v[46:49], v[188:191], v[196:199], v[46:49]
	v_mfma_f32_16x16x32_bf16 v[38:41], v[180:183], v[204:207], v[38:41]
	v_mfma_f32_16x16x32_bf16 v[30:33], v[188:191], v[204:207], v[30:33]
	v_mfma_f32_16x16x32_bf16 v[22:25], v[180:183], v[212:215], v[22:25]
	v_mfma_f32_16x16x32_bf16 v[14:17], v[188:191], v[212:215], v[14:17]
	v_mfma_f32_16x16x32_bf16 v[6:9], v[180:183], v[220:223], v[6:9]
	v_mfma_f32_16x16x32_bf16 v[2:5], v[188:191], v[220:223], v[2:5]
	v_mfma_f32_16x16x32_bf16 v[54:57], v[184:187], v[200:203], v[54:57]
	v_mfma_f32_16x16x32_bf16 v[46:49], v[192:195], v[200:203], v[46:49]
	v_mfma_f32_16x16x32_bf16 v[38:41], v[184:187], v[208:211], v[38:41]
	v_mfma_f32_16x16x32_bf16 v[30:33], v[192:195], v[208:211], v[30:33]
	v_mfma_f32_16x16x32_bf16 v[22:25], v[184:187], v[216:219], v[22:25]
	v_mfma_f32_16x16x32_bf16 v[14:17], v[192:195], v[216:219], v[14:17]
	v_mfma_f32_16x16x32_bf16 v[6:9], v[184:187], v[224:227], v[6:9]
	v_mfma_f32_16x16x32_bf16 v[2:5], v[192:195], v[224:227], v[2:5]
	s_setprio 0
	s_barrier
	s_add_i32 s0, s0, 2
	s_add_u32 s16, s16, 0x100
	s_addc_u32 s17, s17, 0
	s_cmp_gt_u32 s0, 61
	s_cbranch_scc0 .LBB0_768
	s_and_b64 vcc, exec, s[10:11]
	s_cbranch_vccz .LBB0_771
	s_barrier

.LBB0_788:
	v_add_u32_e32 v130, s15, v190
	v_add_u32_e32 v134, s50, v190
	ds_read_b128 v[158:161], v130
	ds_read_b128 v[150:153], v130 offset:1024
	ds_read_b128 v[154:157], v130 offset:2048
	ds_read_b128 v[146:149], v130 offset:3072
	ds_read_b128 v[142:145], v134
	ds_read_b128 v[130:133], v134 offset:1024
	ds_read_b128 v[138:141], v134 offset:2048
	ds_read_b128 v[134:137], v134 offset:3072
	s_add_u32 s36, s34, 0xfff80080
	s_addc_u32 s37, s35, -1
	s_and_b64 s[0:1], s[0:1], exec
	s_cselect_b32 s39, s21, s37
	s_cselect_b32 s38, s60, s36
	s_cselect_b32 s37, s17, s63
	s_cselect_b32 s36, s61, s62
	s_add_i32 m0, s29, 0xc000
	ds_read_b128 v[182:185], v193
	ds_read_b128 v[186:189], v193 offset:1024
	ds_read_b128 v[194:197], v193 offset:2048
	ds_read_b128 v[198:201], v193 offset:3072
	ds_read_b128 v[202:205], v193 offset:4096
	ds_read_b128 v[206:209], v193 offset:5120
	ds_read_b128 v[210:213], v193 offset:6144
	ds_read_b128 v[214:217], v193 offset:7168
	global_load_lds_dwordx4 v172, s[34:35]
	s_add_i32 m0, s29, 0xe000
	s_nop 0
	global_load_lds_dwordx4 v174, s[34:35]
	s_waitcnt vmcnt(8)
	s_waitcnt lgkmcnt(0)
	s_barrier
	s_setprio 1
	v_mfma_i32_16x16x64_i8 v[126:129], v[158:161], v[182:185], v[126:129]
	v_mfma_i32_16x16x64_i8 v[122:125], v[154:157], v[182:185], v[122:125]
	v_mfma_i32_16x16x64_i8 v[106:109], v[154:157], v[194:197], v[106:109]
	v_mfma_i32_16x16x64_i8 v[114:117], v[158:161], v[194:197], v[114:117]
	v_mfma_i32_16x16x64_i8 v[98:101], v[158:161], v[202:205], v[98:101]
	v_mfma_i32_16x16x64_i8 v[90:93], v[154:157], v[202:205], v[90:93]
	v_mfma_i32_16x16x64_i8 v[74:77], v[154:157], v[210:213], v[74:77]
	v_mfma_i32_16x16x64_i8 v[82:85], v[158:161], v[210:213], v[82:85]
	s_nop 0
	v_mfma_i32_16x16x64_i8 v[126:129], v[150:153], v[186:189], v[126:129]
	v_mfma_i32_16x16x64_i8 v[122:125], v[146:149], v[186:189], v[122:125]
	v_mfma_i32_16x16x64_i8 v[106:109], v[146:149], v[198:201], v[106:109]
	v_mfma_i32_16x16x64_i8 v[114:117], v[150:153], v[198:201], v[114:117]
	v_mfma_i32_16x16x64_i8 v[98:101], v[150:153], v[206:209], v[98:101]
	v_mfma_i32_16x16x64_i8 v[90:93], v[146:149], v[206:209], v[90:93]
	v_mfma_i32_16x16x64_i8 v[74:77], v[146:149], v[214:217], v[74:77]
	v_mfma_i32_16x16x64_i8 v[82:85], v[150:153], v[214:217], v[82:85]
	v_mfma_i32_16x16x64_i8 v[118:121], v[142:145], v[182:185], v[118:121]
	v_mfma_i32_16x16x64_i8 v[110:113], v[138:141], v[182:185], v[110:113]
	v_mfma_i32_16x16x64_i8 v[94:97], v[138:141], v[194:197], v[94:97]
	v_mfma_i32_16x16x64_i8 v[102:105], v[142:145], v[194:197], v[102:105]
	v_mfma_i32_16x16x64_i8 v[86:89], v[142:145], v[202:205], v[86:89]
	v_mfma_i32_16x16x64_i8 v[78:81], v[138:141], v[202:205], v[78:81]
	v_mfma_i32_16x16x64_i8 v[66:69], v[138:141], v[210:213], v[66:69]
	v_mfma_i32_16x16x64_i8 v[70:73], v[142:145], v[210:213], v[70:73]
	s_nop 0
	v_mfma_i32_16x16x64_i8 v[118:121], v[130:133], v[186:189], v[118:121]
	v_mfma_i32_16x16x64_i8 v[110:113], v[134:137], v[186:189], v[110:113]
	v_mfma_i32_16x16x64_i8 v[94:97], v[134:137], v[198:201], v[94:97]
	v_mfma_i32_16x16x64_i8 v[102:105], v[130:133], v[198:201], v[102:105]
	v_mfma_i32_16x16x64_i8 v[86:89], v[130:133], v[206:209], v[86:89]
	v_mfma_i32_16x16x64_i8 v[78:81], v[134:137], v[206:209], v[78:81]
	v_mfma_i32_16x16x64_i8 v[66:69], v[134:137], v[214:217], v[66:69]
	v_mfma_i32_16x16x64_i8 v[70:73], v[130:133], v[214:217], v[70:73]
	s_setprio 0
	s_barrier
	s_add_i32 s0, s15, s40
	s_mov_b32 m0, s0
	ds_read_b128 v[194:197], v193 offset:16384
	ds_read_b128 v[198:201], v193 offset:17408
	ds_read_b128 v[202:205], v193 offset:18432
	ds_read_b128 v[206:209], v193 offset:19456
	ds_read_b128 v[210:213], v193 offset:20480
	ds_read_b128 v[214:217], v193 offset:21504
	ds_read_b128 v[218:221], v193 offset:22528
	ds_read_b128 v[222:225], v193 offset:23552
	global_load_lds_dwordx4 v164, s[36:37]
	s_add_i32 m0, s0, 0x2000
	s_add_u32 s0, s36, 0x80000
	s_addc_u32 s1, s37, 0
	s_add_i32 s66, s50, s40
	global_load_lds_dwordx4 v168, s[36:37]
	s_mov_b32 m0, s66
	s_nop 0
	global_load_lds_dwordx4 v164, s[0:1]
	s_add_i32 m0, s66, 0x2000
	s_nop 0
	global_load_lds_dwordx4 v168, s[0:1]
	s_mov_b32 m0, s29
	s_nop 0
	global_load_lds_dwordx4 v162, s[38:39]
	s_mov_b32 m0, s31
	s_nop 0
	global_load_lds_dwordx4 v166, s[38:39]
	s_waitcnt vmcnt(8)
	s_waitcnt lgkmcnt(0)
	s_barrier
	s_setprio 1
	v_mfma_i32_16x16x64_i8 v[62:65], v[158:161], v[194:197], v[62:65]
	v_mfma_i32_16x16x64_i8 v[58:61], v[154:157], v[194:197], v[58:61]
	v_mfma_i32_16x16x64_i8 v[42:45], v[154:157], v[202:205], v[42:45]
	v_mfma_i32_16x16x64_i8 v[50:53], v[158:161], v[202:205], v[50:53]
	v_mfma_i32_16x16x64_i8 v[34:37], v[158:161], v[210:213], v[34:37]
	v_mfma_i32_16x16x64_i8 v[26:29], v[154:157], v[210:213], v[26:29]
	v_mfma_i32_16x16x64_i8 v[10:13], v[154:157], v[218:221], v[10:13]
	v_mfma_i32_16x16x64_i8 v[18:21], v[158:161], v[218:221], v[18:21]
	s_nop 0
	v_mfma_i32_16x16x64_i8 v[62:65], v[150:153], v[198:201], v[62:65]
	v_mfma_i32_16x16x64_i8 v[58:61], v[146:149], v[198:201], v[58:61]
	v_mfma_i32_16x16x64_i8 v[42:45], v[146:149], v[206:209], v[42:45]
	v_mfma_i32_16x16x64_i8 v[50:53], v[150:153], v[206:209], v[50:53]
	v_mfma_i32_16x16x64_i8 v[34:37], v[150:153], v[214:217], v[34:37]
	v_mfma_i32_16x16x64_i8 v[26:29], v[146:149], v[214:217], v[26:29]
	v_mfma_i32_16x16x64_i8 v[10:13], v[146:149], v[222:225], v[10:13]
	v_mfma_i32_16x16x64_i8 v[18:21], v[150:153], v[222:225], v[18:21]
	v_mfma_i32_16x16x64_i8 v[54:57], v[142:145], v[194:197], v[54:57]
	v_mfma_i32_16x16x64_i8 v[46:49], v[138:141], v[194:197], v[46:49]
	v_mfma_i32_16x16x64_i8 v[30:33], v[138:141], v[202:205], v[30:33]
	v_mfma_i32_16x16x64_i8 v[38:41], v[142:145], v[202:205], v[38:41]
	v_mfma_i32_16x16x64_i8 v[22:25], v[142:145], v[210:213], v[22:25]
	v_mfma_i32_16x16x64_i8 v[14:17], v[138:141], v[210:213], v[14:17]
	v_mfma_i32_16x16x64_i8 v[2:5], v[138:141], v[218:221], v[2:5]
	v_mfma_i32_16x16x64_i8 v[6:9], v[142:145], v[218:221], v[6:9]
	s_nop 0
	v_mfma_i32_16x16x64_i8 v[54:57], v[130:133], v[198:201], v[54:57]
	v_mfma_i32_16x16x64_i8 v[46:49], v[134:137], v[198:201], v[46:49]
	v_mfma_i32_16x16x64_i8 v[30:33], v[134:137], v[206:209], v[30:33]
	v_mfma_i32_16x16x64_i8 v[38:41], v[130:133], v[206:209], v[38:41]
	v_mfma_i32_16x16x64_i8 v[22:25], v[130:133], v[214:217], v[22:25]
	v_mfma_i32_16x16x64_i8 v[14:17], v[134:137], v[214:217], v[14:17]
	v_mfma_i32_16x16x64_i8 v[2:5], v[134:137], v[222:225], v[2:5]
	v_mfma_i32_16x16x64_i8 v[6:9], v[130:133], v[222:225], v[6:9]
	s_setprio 0
	s_barrier
	s_add_i32 s66, 0, 0x18000
	s_add_i32 s67, 0, 0x1c000
	v_add_u32_e32 v142, s66, v190
	v_add_u32_e32 v158, s67, v190
	ds_read_b128 v[130:133], v142
	ds_read_b128 v[134:137], v142 offset:1024
	ds_read_b128 v[138:141], v142 offset:2048
	ds_read_b128 v[142:145], v142 offset:3072
	ds_read_b128 v[146:149], v158
	ds_read_b128 v[150:153], v158 offset:1024
	ds_read_b128 v[154:157], v158 offset:2048
	ds_read_b128 v[158:161], v158 offset:3072
	s_add_u32 s0, s38, 0x80000
	s_addc_u32 s1, s39, 0
	s_mov_b32 m0, s42
	ds_read_b128 v[194:197], v193 offset:32768
	ds_read_b128 v[198:201], v193 offset:33792
	ds_read_b128 v[202:205], v193 offset:34816
	ds_read_b128 v[206:209], v193 offset:35840
	ds_read_b128 v[210:213], v193 offset:36864
	ds_read_b128 v[214:217], v193 offset:37888
	ds_read_b128 v[218:221], v193 offset:38912
	ds_read_b128 v[222:225], v193 offset:39936
	global_load_lds_dwordx4 v162, s[0:1]
	s_mov_b32 m0, s43
	s_nop 0
	global_load_lds_dwordx4 v166, s[0:1]
	s_waitcnt vmcnt(8)
	s_waitcnt lgkmcnt(0)
	s_barrier
	s_setprio 1
	v_mfma_i32_16x16x64_i8 v[126:129], v[130:133], v[194:197], v[126:129]
	v_mfma_i32_16x16x64_i8 v[122:125], v[138:141], v[194:197], v[122:125]
	v_mfma_i32_16x16x64_i8 v[106:109], v[138:141], v[202:205], v[106:109]
	v_mfma_i32_16x16x64_i8 v[114:117], v[130:133], v[202:205], v[114:117]
	v_mfma_i32_16x16x64_i8 v[98:101], v[130:133], v[210:213], v[98:101]
	v_mfma_i32_16x16x64_i8 v[90:93], v[138:141], v[210:213], v[90:93]
	v_mfma_i32_16x16x64_i8 v[74:77], v[138:141], v[218:221], v[74:77]
	v_mfma_i32_16x16x64_i8 v[82:85], v[130:133], v[218:221], v[82:85]
	s_nop 0
	v_mfma_i32_16x16x64_i8 v[126:129], v[134:137], v[198:201], v[126:129]
	v_mfma_i32_16x16x64_i8 v[122:125], v[142:145], v[198:201], v[122:125]
	v_mfma_i32_16x16x64_i8 v[106:109], v[142:145], v[206:209], v[106:109]
	v_mfma_i32_16x16x64_i8 v[114:117], v[134:137], v[206:209], v[114:117]
	v_mfma_i32_16x16x64_i8 v[98:101], v[134:137], v[214:217], v[98:101]
	v_mfma_i32_16x16x64_i8 v[90:93], v[142:145], v[214:217], v[90:93]
	v_mfma_i32_16x16x64_i8 v[74:77], v[142:145], v[222:225], v[74:77]
	v_mfma_i32_16x16x64_i8 v[82:85], v[134:137], v[222:225], v[82:85]
	v_mfma_i32_16x16x64_i8 v[118:121], v[146:149], v[194:197], v[118:121]
	v_mfma_i32_16x16x64_i8 v[110:113], v[154:157], v[194:197], v[110:113]
	v_mfma_i32_16x16x64_i8 v[94:97], v[154:157], v[202:205], v[94:97]
	v_mfma_i32_16x16x64_i8 v[102:105], v[146:149], v[202:205], v[102:105]
	v_mfma_i32_16x16x64_i8 v[86:89], v[146:149], v[210:213], v[86:89]
	v_mfma_i32_16x16x64_i8 v[78:81], v[154:157], v[210:213], v[78:81]
	v_mfma_i32_16x16x64_i8 v[66:69], v[154:157], v[218:221], v[66:69]
	v_mfma_i32_16x16x64_i8 v[70:73], v[146:149], v[218:221], v[70:73]
	s_nop 0
	v_mfma_i32_16x16x64_i8 v[118:121], v[150:153], v[198:201], v[118:121]
	v_mfma_i32_16x16x64_i8 v[110:113], v[158:161], v[198:201], v[110:113]
	v_mfma_i32_16x16x64_i8 v[94:97], v[158:161], v[206:209], v[94:97]
	v_mfma_i32_16x16x64_i8 v[102:105], v[150:153], v[206:209], v[102:105]
	v_mfma_i32_16x16x64_i8 v[86:89], v[150:153], v[214:217], v[86:89]
	v_mfma_i32_16x16x64_i8 v[78:81], v[158:161], v[214:217], v[78:81]
	v_mfma_i32_16x16x64_i8 v[66:69], v[158:161], v[222:225], v[66:69]
	v_mfma_i32_16x16x64_i8 v[70:73], v[150:153], v[222:225], v[70:73]
	s_setprio 0
	s_barrier
	s_add_i32 s0, s66, s40
	s_mov_b32 m0, s0
	s_add_u32 s98, s36, 0x80
	s_addc_u32 s99, s37, 0
	s_add_u32 s100, s38, 0x80
	s_addc_u32 s101, s39, 0
	ds_read_b128 v[194:197], v193 offset:49152
	ds_read_b128 v[198:201], v193 offset:50176
	ds_read_b128 v[202:205], v193 offset:51200
	ds_read_b128 v[206:209], v193 offset:52224
	ds_read_b128 v[210:213], v193 offset:53248
	ds_read_b128 v[214:217], v193 offset:54272
	ds_read_b128 v[218:221], v193 offset:55296
	ds_read_b128 v[222:225], v193 offset:56320
	global_load_lds_dwordx4 v164, s[98:99]
	s_add_i32 m0, s0, 0x2000
	s_add_u32 s0, s36, 0x80080
	s_addc_u32 s1, s37, 0
	s_add_i32 s36, s67, s40
	global_load_lds_dwordx4 v168, s[98:99]
	s_mov_b32 m0, s36
	s_nop 0
	global_load_lds_dwordx4 v164, s[0:1]
	s_add_i32 m0, s36, 0x2000
	s_nop 0
	global_load_lds_dwordx4 v168, s[0:1]
	s_mov_b32 m0, s48
	s_nop 0
	global_load_lds_dwordx4 v162, s[100:101]
	s_mov_b32 m0, s49
	s_nop 0
	global_load_lds_dwordx4 v166, s[100:101]
	s_waitcnt vmcnt(8)
	s_waitcnt lgkmcnt(0)
	s_barrier
	s_setprio 1
	v_mfma_i32_16x16x64_i8 v[62:65], v[130:133], v[194:197], v[62:65]
	v_mfma_i32_16x16x64_i8 v[58:61], v[138:141], v[194:197], v[58:61]
	v_mfma_i32_16x16x64_i8 v[42:45], v[138:141], v[202:205], v[42:45]
	v_mfma_i32_16x16x64_i8 v[50:53], v[130:133], v[202:205], v[50:53]
	v_mfma_i32_16x16x64_i8 v[34:37], v[130:133], v[210:213], v[34:37]
	v_mfma_i32_16x16x64_i8 v[26:29], v[138:141], v[210:213], v[26:29]
	v_mfma_i32_16x16x64_i8 v[10:13], v[138:141], v[218:221], v[10:13]
	v_mfma_i32_16x16x64_i8 v[18:21], v[130:133], v[218:221], v[18:21]
	s_nop 0
	v_mfma_i32_16x16x64_i8 v[62:65], v[134:137], v[198:201], v[62:65]
	v_mfma_i32_16x16x64_i8 v[58:61], v[142:145], v[198:201], v[58:61]
	v_mfma_i32_16x16x64_i8 v[42:45], v[142:145], v[206:209], v[42:45]
	v_mfma_i32_16x16x64_i8 v[50:53], v[134:137], v[206:209], v[50:53]
	v_mfma_i32_16x16x64_i8 v[34:37], v[134:137], v[214:217], v[34:37]
	v_mfma_i32_16x16x64_i8 v[26:29], v[142:145], v[214:217], v[26:29]
	v_mfma_i32_16x16x64_i8 v[10:13], v[142:145], v[222:225], v[10:13]
	v_mfma_i32_16x16x64_i8 v[18:21], v[134:137], v[222:225], v[18:21]
	v_mfma_i32_16x16x64_i8 v[54:57], v[146:149], v[194:197], v[54:57]
	v_mfma_i32_16x16x64_i8 v[46:49], v[154:157], v[194:197], v[46:49]
	v_mfma_i32_16x16x64_i8 v[30:33], v[154:157], v[202:205], v[30:33]
	v_mfma_i32_16x16x64_i8 v[38:41], v[146:149], v[202:205], v[38:41]
	v_mfma_i32_16x16x64_i8 v[22:25], v[146:149], v[210:213], v[22:25]
	v_mfma_i32_16x16x64_i8 v[14:17], v[154:157], v[210:213], v[14:17]
	v_mfma_i32_16x16x64_i8 v[2:5], v[154:157], v[218:221], v[2:5]
	v_mfma_i32_16x16x64_i8 v[6:9], v[146:149], v[218:221], v[6:9]
	s_nop 0
	v_mfma_i32_16x16x64_i8 v[54:57], v[150:153], v[198:201], v[54:57]
	v_mfma_i32_16x16x64_i8 v[46:49], v[158:161], v[198:201], v[46:49]
	v_mfma_i32_16x16x64_i8 v[30:33], v[158:161], v[206:209], v[30:33]
	v_mfma_i32_16x16x64_i8 v[38:41], v[150:153], v[206:209], v[38:41]
	v_mfma_i32_16x16x64_i8 v[22:25], v[150:153], v[214:217], v[22:25]
	v_mfma_i32_16x16x64_i8 v[14:17], v[158:161], v[214:217], v[14:17]
	v_mfma_i32_16x16x64_i8 v[2:5], v[158:161], v[222:225], v[2:5]
	v_mfma_i32_16x16x64_i8 v[6:9], v[150:153], v[222:225], v[6:9]
	s_setprio 0
	s_barrier
	s_add_i32 s64, s64, 2
	s_add_u32 s34, s34, 0x100
	s_addc_u32 s35, s35, 0
	s_add_u32 s62, s62, 0x100
	s_addc_u32 s63, s63, 0
	s_cmp_gt_u32 s64, 29
	s_cbranch_scc1 .LBB0_791

.LBB0_1051:
	s_add_u32 s8, s17, s6
	s_addc_u32 s9, s48, s7
	s_add_u32 s8, s8, 0x32800100
	s_addc_u32 s9, s9, 0
	s_add_u32 s65, s49, s6
	s_addc_u32 s68, s50, s7
	s_add_i32 s69, 0, 0x10000
	s_cmpk_eq_i32 s6, 0xf00
	s_cselect_b32 s41, s5, s9
	s_cselect_b32 s40, s4, s8
	s_cselect_b32 s9, s21, s68
	s_cselect_b32 s8, s20, s65
	s_add_i32 s65, 0, 0x14000
	v_add_u32_e32 v130, s69, v187
	v_add_u32_e32 v134, s65, v187
	ds_read_b128 v[158:161], v130
	ds_read_b128 v[150:153], v130 offset:1024
	ds_read_b128 v[154:157], v130 offset:2048
	ds_read_b128 v[146:149], v130 offset:3072
	ds_read_b128 v[142:145], v134
	ds_read_b128 v[130:133], v134 offset:1024
	ds_read_b128 v[138:141], v134 offset:2048
	ds_read_b128 v[134:137], v134 offset:3072
	v_lshl_add_u64 v[214:215], v[168:169], 0, s[6:7]
	s_add_i32 m0, s43, 0xc000
	ds_read_b128 v[172:175], v188
	ds_read_b128 v[176:179], v188 offset:1024
	ds_read_b128 v[190:193], v188 offset:2048
	ds_read_b128 v[194:197], v188 offset:3072
	ds_read_b128 v[198:201], v188 offset:4096
	ds_read_b128 v[202:205], v188 offset:5120
	ds_read_b128 v[206:209], v188 offset:6144
	ds_read_b128 v[210:213], v188 offset:7168
	global_load_lds_dwordx4 v[214:215], off
	v_lshl_add_u64 v[214:215], v[170:171], 0, s[6:7]
	s_add_i32 m0, s43, 0xe000
	s_nop 0
	global_load_lds_dwordx4 v[214:215], off
	s_waitcnt vmcnt(8)
	s_waitcnt lgkmcnt(0)
	s_barrier
	s_setprio 1
	v_mfma_i32_16x16x64_i8 v[70:73], v[158:161], v[172:175], v[70:73]
	v_mfma_i32_16x16x64_i8 v[34:37], v[154:157], v[172:175], v[34:37]
	v_mfma_i32_16x16x64_i8 v[54:57], v[154:157], v[190:193], v[54:57]
	v_mfma_i32_16x16x64_i8 v[102:105], v[158:161], v[190:193], v[102:105]
	v_mfma_i32_16x16x64_i8 v[114:117], v[158:161], v[198:201], v[114:117]
	v_mfma_i32_16x16x64_i8 v[86:89], v[154:157], v[198:201], v[86:89]
	v_mfma_i32_16x16x64_i8 v[110:113], v[154:157], v[206:209], v[110:113]
	v_mfma_i32_16x16x64_i8 v[126:129], v[158:161], v[206:209], v[126:129]
	s_nop 0
	v_mfma_i32_16x16x64_i8 v[70:73], v[150:153], v[176:179], v[70:73]
	v_mfma_i32_16x16x64_i8 v[34:37], v[146:149], v[176:179], v[34:37]
	v_mfma_i32_16x16x64_i8 v[54:57], v[146:149], v[194:197], v[54:57]
	v_mfma_i32_16x16x64_i8 v[102:105], v[150:153], v[194:197], v[102:105]
	v_mfma_i32_16x16x64_i8 v[114:117], v[150:153], v[202:205], v[114:117]
	v_mfma_i32_16x16x64_i8 v[86:89], v[146:149], v[202:205], v[86:89]
	v_mfma_i32_16x16x64_i8 v[110:113], v[146:149], v[210:213], v[110:113]
	v_mfma_i32_16x16x64_i8 v[126:129], v[150:153], v[210:213], v[126:129]
	v_mfma_i32_16x16x64_i8 v[18:21], v[142:145], v[172:175], v[18:21]
	v_mfma_i32_16x16x64_i8 v[2:5], v[138:141], v[172:175], v[2:5]
	v_mfma_i32_16x16x64_i8 v[6:9], v[138:141], v[190:193], v[6:9]
	v_mfma_i32_16x16x64_i8 v[38:41], v[142:145], v[190:193], v[38:41]
	v_mfma_i32_16x16x64_i8 v[66:69], v[142:145], v[198:201], v[66:69]
	v_mfma_i32_16x16x64_i8 v[26:29], v[138:141], v[198:201], v[26:29]
	v_mfma_i32_16x16x64_i8 v[50:53], v[138:141], v[206:209], v[50:53]
	v_mfma_i32_16x16x64_i8 v[90:93], v[142:145], v[206:209], v[90:93]
	s_nop 0
	v_mfma_i32_16x16x64_i8 v[18:21], v[130:133], v[176:179], v[18:21]
	v_mfma_i32_16x16x64_i8 v[2:5], v[134:137], v[176:179], v[2:5]
	v_mfma_i32_16x16x64_i8 v[6:9], v[134:137], v[194:197], v[6:9]
	v_mfma_i32_16x16x64_i8 v[38:41], v[130:133], v[194:197], v[38:41]
	v_mfma_i32_16x16x64_i8 v[66:69], v[130:133], v[202:205], v[66:69]
	v_mfma_i32_16x16x64_i8 v[26:29], v[134:137], v[202:205], v[26:29]
	v_mfma_i32_16x16x64_i8 v[50:53], v[134:137], v[210:213], v[50:53]
	v_mfma_i32_16x16x64_i8 v[90:93], v[130:133], v[210:213], v[90:93]
	s_setprio 0
	s_barrier
	s_add_i32 s68, s69, s42
	s_mov_b32 m0, s68
	ds_read_b128 v[190:193], v188 offset:16384
	ds_read_b128 v[194:197], v188 offset:17408
	ds_read_b128 v[198:201], v188 offset:18432
	ds_read_b128 v[202:205], v188 offset:19456
	ds_read_b128 v[206:209], v188 offset:20480
	ds_read_b128 v[210:213], v188 offset:21504
	ds_read_b128 v[214:217], v188 offset:22528
	ds_read_b128 v[218:221], v188 offset:23552
	global_load_lds_dwordx4 v162, s[8:9]
	s_add_i32 m0, s68, 0x2000
	s_add_u32 s68, s8, 0x80000
	s_addc_u32 s69, s9, 0
	s_add_i32 s65, s65, s42
	global_load_lds_dwordx4 v166, s[8:9]
	s_mov_b32 m0, s65
	s_nop 0
	global_load_lds_dwordx4 v162, s[68:69]
	s_add_i32 m0, s65, 0x2000
	s_nop 0
	global_load_lds_dwordx4 v166, s[68:69]
	s_mov_b32 m0, s43
	s_nop 0
	global_load_lds_dwordx4 v162, s[40:41]
	s_mov_b32 m0, s60
	s_nop 0
	global_load_lds_dwordx4 v166, s[40:41]
	s_waitcnt vmcnt(8)
	s_waitcnt lgkmcnt(0)
	s_barrier
	s_setprio 1
	v_mfma_i32_16x16x64_i8 v[122:125], v[158:161], v[190:193], v[122:125]
	v_mfma_i32_16x16x64_i8 v[118:121], v[154:157], v[190:193], v[118:121]
	v_mfma_i32_16x16x64_i8 v[94:97], v[154:157], v[198:201], v[94:97]
	v_mfma_i32_16x16x64_i8 v[98:101], v[158:161], v[198:201], v[98:101]
	v_mfma_i32_16x16x64_i8 v[62:65], v[158:161], v[206:209], v[62:65]
	v_mfma_i32_16x16x64_i8 v[58:61], v[154:157], v[206:209], v[58:61]
	v_mfma_i32_16x16x64_i8 v[22:25], v[154:157], v[214:217], v[22:25]
	v_mfma_i32_16x16x64_i8 v[30:33], v[158:161], v[214:217], v[30:33]
	s_nop 0
	v_mfma_i32_16x16x64_i8 v[122:125], v[150:153], v[194:197], v[122:125]
	v_mfma_i32_16x16x64_i8 v[118:121], v[146:149], v[194:197], v[118:121]
	v_mfma_i32_16x16x64_i8 v[94:97], v[146:149], v[202:205], v[94:97]
	v_mfma_i32_16x16x64_i8 v[98:101], v[150:153], v[202:205], v[98:101]
	v_mfma_i32_16x16x64_i8 v[62:65], v[150:153], v[210:213], v[62:65]
	v_mfma_i32_16x16x64_i8 v[58:61], v[146:149], v[210:213], v[58:61]
	v_mfma_i32_16x16x64_i8 v[22:25], v[146:149], v[218:221], v[22:25]
	v_mfma_i32_16x16x64_i8 v[30:33], v[150:153], v[218:221], v[30:33]
	v_mfma_i32_16x16x64_i8 v[106:109], v[142:145], v[190:193], v[106:109]
	v_mfma_i32_16x16x64_i8 v[82:85], v[138:141], v[190:193], v[82:85]
	v_mfma_i32_16x16x64_i8 v[74:77], v[138:141], v[198:201], v[74:77]
	v_mfma_i32_16x16x64_i8 v[78:81], v[142:145], v[198:201], v[78:81]
	v_mfma_i32_16x16x64_i8 v[46:49], v[142:145], v[206:209], v[46:49]
	v_mfma_i32_16x16x64_i8 v[42:45], v[138:141], v[206:209], v[42:45]
	v_mfma_i32_16x16x64_i8 v[10:13], v[138:141], v[214:217], v[10:13]
	v_mfma_i32_16x16x64_i8 v[14:17], v[142:145], v[214:217], v[14:17]
	s_nop 0
	v_mfma_i32_16x16x64_i8 v[106:109], v[130:133], v[194:197], v[106:109]
	v_mfma_i32_16x16x64_i8 v[82:85], v[134:137], v[194:197], v[82:85]
	v_mfma_i32_16x16x64_i8 v[74:77], v[134:137], v[202:205], v[74:77]
	v_mfma_i32_16x16x64_i8 v[78:81], v[130:133], v[202:205], v[78:81]
	v_mfma_i32_16x16x64_i8 v[46:49], v[130:133], v[210:213], v[46:49]
	v_mfma_i32_16x16x64_i8 v[42:45], v[134:137], v[210:213], v[42:45]
	v_mfma_i32_16x16x64_i8 v[10:13], v[134:137], v[218:221], v[10:13]
	v_mfma_i32_16x16x64_i8 v[14:17], v[130:133], v[218:221], v[14:17]
	s_setprio 0
	s_barrier
	s_add_i32 s65, 0, 0x18000
	s_add_i32 s68, 0, 0x1c000
	v_add_u32_e32 v142, s65, v187
	v_add_u32_e32 v158, s68, v187
	ds_read_b128 v[130:133], v142
	ds_read_b128 v[134:137], v142 offset:1024
	ds_read_b128 v[138:141], v142 offset:2048
	ds_read_b128 v[142:145], v142 offset:3072
	ds_read_b128 v[146:149], v158
	ds_read_b128 v[150:153], v158 offset:1024
	ds_read_b128 v[154:157], v158 offset:2048
	ds_read_b128 v[158:161], v158 offset:3072
	s_add_u32 s40, s40, 0x80000
	s_addc_u32 s41, s41, 0
	s_add_u32 s100, s40, 0xfff80080
	s_addc_u32 s101, s41, -1
	s_mov_b32 m0, s61
	ds_read_b128 v[190:193], v188 offset:32768
	ds_read_b128 v[194:197], v188 offset:33792
	ds_read_b128 v[198:201], v188 offset:34816
	ds_read_b128 v[202:205], v188 offset:35840
	ds_read_b128 v[206:209], v188 offset:36864
	ds_read_b128 v[210:213], v188 offset:37888
	ds_read_b128 v[214:217], v188 offset:38912
	ds_read_b128 v[218:221], v188 offset:39936
	global_load_lds_dwordx4 v162, s[40:41]
	s_mov_b32 m0, s62
	s_nop 0
	global_load_lds_dwordx4 v166, s[40:41]
	s_waitcnt vmcnt(8)
	s_waitcnt lgkmcnt(0)
	s_barrier
	s_setprio 1
	v_mfma_i32_16x16x64_i8 v[70:73], v[130:133], v[190:193], v[70:73]
	v_mfma_i32_16x16x64_i8 v[34:37], v[138:141], v[190:193], v[34:37]
	v_mfma_i32_16x16x64_i8 v[54:57], v[138:141], v[198:201], v[54:57]
	v_mfma_i32_16x16x64_i8 v[102:105], v[130:133], v[198:201], v[102:105]
	v_mfma_i32_16x16x64_i8 v[114:117], v[130:133], v[206:209], v[114:117]
	v_mfma_i32_16x16x64_i8 v[86:89], v[138:141], v[206:209], v[86:89]
	v_mfma_i32_16x16x64_i8 v[110:113], v[138:141], v[214:217], v[110:113]
	v_mfma_i32_16x16x64_i8 v[126:129], v[130:133], v[214:217], v[126:129]
	s_nop 0
	v_mfma_i32_16x16x64_i8 v[70:73], v[134:137], v[194:197], v[70:73]
	v_mfma_i32_16x16x64_i8 v[34:37], v[142:145], v[194:197], v[34:37]
	v_mfma_i32_16x16x64_i8 v[54:57], v[142:145], v[202:205], v[54:57]
	v_mfma_i32_16x16x64_i8 v[102:105], v[134:137], v[202:205], v[102:105]
	v_mfma_i32_16x16x64_i8 v[114:117], v[134:137], v[210:213], v[114:117]
	v_mfma_i32_16x16x64_i8 v[86:89], v[142:145], v[210:213], v[86:89]
	v_mfma_i32_16x16x64_i8 v[110:113], v[142:145], v[218:221], v[110:113]
	v_mfma_i32_16x16x64_i8 v[126:129], v[134:137], v[218:221], v[126:129]
	v_mfma_i32_16x16x64_i8 v[18:21], v[146:149], v[190:193], v[18:21]
	v_mfma_i32_16x16x64_i8 v[2:5], v[154:157], v[190:193], v[2:5]
	v_mfma_i32_16x16x64_i8 v[6:9], v[154:157], v[198:201], v[6:9]
	v_mfma_i32_16x16x64_i8 v[38:41], v[146:149], v[198:201], v[38:41]
	v_mfma_i32_16x16x64_i8 v[66:69], v[146:149], v[206:209], v[66:69]
	v_mfma_i32_16x16x64_i8 v[26:29], v[154:157], v[206:209], v[26:29]
	v_mfma_i32_16x16x64_i8 v[50:53], v[154:157], v[214:217], v[50:53]
	v_mfma_i32_16x16x64_i8 v[90:93], v[146:149], v[214:217], v[90:93]
	s_nop 0
	v_mfma_i32_16x16x64_i8 v[18:21], v[150:153], v[194:197], v[18:21]
	v_mfma_i32_16x16x64_i8 v[2:5], v[158:161], v[194:197], v[2:5]
	v_mfma_i32_16x16x64_i8 v[6:9], v[158:161], v[202:205], v[6:9]
	v_mfma_i32_16x16x64_i8 v[38:41], v[150:153], v[202:205], v[38:41]
	v_mfma_i32_16x16x64_i8 v[66:69], v[150:153], v[210:213], v[66:69]
	v_mfma_i32_16x16x64_i8 v[26:29], v[158:161], v[210:213], v[26:29]
	v_mfma_i32_16x16x64_i8 v[50:53], v[158:161], v[218:221], v[50:53]
	v_mfma_i32_16x16x64_i8 v[90:93], v[150:153], v[218:221], v[90:93]
	s_setprio 0
	s_barrier
	s_add_i32 s40, s65, s42
	s_mov_b32 m0, s40
	s_add_u32 s98, s8, 0x80
	s_addc_u32 s99, s9, 0
	ds_read_b128 v[190:193], v188 offset:49152
	ds_read_b128 v[194:197], v188 offset:50176
	ds_read_b128 v[198:201], v188 offset:51200
	ds_read_b128 v[202:205], v188 offset:52224
	ds_read_b128 v[206:209], v188 offset:53248
	ds_read_b128 v[210:213], v188 offset:54272
	ds_read_b128 v[214:217], v188 offset:55296
	ds_read_b128 v[218:221], v188 offset:56320
	global_load_lds_dwordx4 v162, s[98:99]
	s_add_i32 m0, s40, 0x2000
	s_add_u32 s8, s8, 0x80080
	s_addc_u32 s9, s9, 0
	s_add_i32 s40, s68, s42
	global_load_lds_dwordx4 v166, s[98:99]
	s_mov_b32 m0, s40
	s_nop 0
	global_load_lds_dwordx4 v162, s[8:9]
	s_add_i32 m0, s40, 0x2000
	s_nop 0
	global_load_lds_dwordx4 v166, s[8:9]
	s_mov_b32 m0, s66
	s_nop 0
	global_load_lds_dwordx4 v162, s[100:101]
	s_mov_b32 m0, s67
	s_nop 0
	global_load_lds_dwordx4 v166, s[100:101]
	s_waitcnt vmcnt(8)
	s_waitcnt lgkmcnt(0)
	s_barrier
	s_setprio 1
	v_mfma_i32_16x16x64_i8 v[122:125], v[130:133], v[190:193], v[122:125]
	v_mfma_i32_16x16x64_i8 v[118:121], v[138:141], v[190:193], v[118:121]
	v_mfma_i32_16x16x64_i8 v[94:97], v[138:141], v[198:201], v[94:97]
	v_mfma_i32_16x16x64_i8 v[98:101], v[130:133], v[198:201], v[98:101]
	v_mfma_i32_16x16x64_i8 v[62:65], v[130:133], v[206:209], v[62:65]
	v_mfma_i32_16x16x64_i8 v[58:61], v[138:141], v[206:209], v[58:61]
	v_mfma_i32_16x16x64_i8 v[22:25], v[138:141], v[214:217], v[22:25]
	v_mfma_i32_16x16x64_i8 v[30:33], v[130:133], v[214:217], v[30:33]
	s_nop 0
	v_mfma_i32_16x16x64_i8 v[122:125], v[134:137], v[194:197], v[122:125]
	v_mfma_i32_16x16x64_i8 v[118:121], v[142:145], v[194:197], v[118:121]
	v_mfma_i32_16x16x64_i8 v[94:97], v[142:145], v[202:205], v[94:97]
	v_mfma_i32_16x16x64_i8 v[98:101], v[134:137], v[202:205], v[98:101]
	v_mfma_i32_16x16x64_i8 v[62:65], v[134:137], v[210:213], v[62:65]
	v_mfma_i32_16x16x64_i8 v[58:61], v[142:145], v[210:213], v[58:61]
	v_mfma_i32_16x16x64_i8 v[22:25], v[142:145], v[218:221], v[22:25]
	v_mfma_i32_16x16x64_i8 v[30:33], v[134:137], v[218:221], v[30:33]
	v_mfma_i32_16x16x64_i8 v[106:109], v[146:149], v[190:193], v[106:109]
	v_mfma_i32_16x16x64_i8 v[82:85], v[154:157], v[190:193], v[82:85]
	v_mfma_i32_16x16x64_i8 v[74:77], v[154:157], v[198:201], v[74:77]
	v_mfma_i32_16x16x64_i8 v[78:81], v[146:149], v[198:201], v[78:81]
	v_mfma_i32_16x16x64_i8 v[46:49], v[146:149], v[206:209], v[46:49]
	v_mfma_i32_16x16x64_i8 v[42:45], v[154:157], v[206:209], v[42:45]
	v_mfma_i32_16x16x64_i8 v[10:13], v[154:157], v[214:217], v[10:13]
	v_mfma_i32_16x16x64_i8 v[14:17], v[146:149], v[214:217], v[14:17]
	s_nop 0
	v_mfma_i32_16x16x64_i8 v[106:109], v[150:153], v[194:197], v[106:109]
	v_mfma_i32_16x16x64_i8 v[82:85], v[158:161], v[194:197], v[82:85]
	v_mfma_i32_16x16x64_i8 v[74:77], v[158:161], v[202:205], v[74:77]
	v_mfma_i32_16x16x64_i8 v[78:81], v[150:153], v[202:205], v[78:81]
	v_mfma_i32_16x16x64_i8 v[46:49], v[150:153], v[210:213], v[46:49]
	v_mfma_i32_16x16x64_i8 v[42:45], v[158:161], v[210:213], v[42:45]
	v_mfma_i32_16x16x64_i8 v[10:13], v[158:161], v[218:221], v[10:13]
	v_mfma_i32_16x16x64_i8 v[14:17], v[150:153], v[218:221], v[14:17]
	s_setprio 0
	s_barrier
	s_add_i32 s64, s64, 2
	s_add_u32 s6, s6, 0x100
	s_addc_u32 s7, s7, 0
	s_cmp_gt_u32 s64, 29
	s_cbranch_scc0 .LBB0_1051
	s_waitcnt vmcnt(0)
	s_cmpk_lt_u32 s59, 0x100
	s_cbranch_scc0 .LBB0_1054
	s_barrier

.LBB0_1173:
	ds_read_b128 v[158:161], v184
	ds_read_b128 v[150:153], v184 offset:1024
	ds_read_b128 v[154:157], v184 offset:2048
	ds_read_b128 v[146:149], v184 offset:3072
	ds_read_b128 v[142:145], v185
	ds_read_b128 v[130:133], v185 offset:1024
	ds_read_b128 v[138:141], v185 offset:2048
	ds_read_b128 v[134:137], v185 offset:3072
	s_add_u32 s38, s36, 0xfff80080
	s_addc_u32 s39, s37, -1
	s_cmp_eq_u32 s65, 28
	s_cselect_b32 s41, s18, s39
	s_cselect_b32 s40, s19, s38
	s_cselect_b32 s39, s25, s64
	s_cselect_b32 s38, s27, s63
	v_lshl_add_u64 v[212:213], s[36:37], 0, v[166:167]
	s_add_i32 m0, s35, 0xc000
	ds_read_b128 v[174:177], v186
	ds_read_b128 v[178:181], v186 offset:1024
	ds_read_b128 v[188:191], v186 offset:2048
	ds_read_b128 v[192:195], v186 offset:3072
	ds_read_b128 v[196:199], v186 offset:4096
	ds_read_b128 v[200:203], v186 offset:5120
	ds_read_b128 v[204:207], v186 offset:6144
	ds_read_b128 v[208:211], v186 offset:7168
	global_load_lds_dwordx4 v[212:213], off
	v_lshl_add_u64 v[212:213], s[36:37], 0, v[168:169]
	s_add_i32 m0, s35, 0xe000
	s_nop 0
	global_load_lds_dwordx4 v[212:213], off
	s_waitcnt vmcnt(8)
	s_waitcnt lgkmcnt(0)
	s_barrier
	s_setprio 1
	v_mfma_i32_16x16x64_i8 v[126:129], v[158:161], v[174:177], v[126:129]
	v_mfma_i32_16x16x64_i8 v[122:125], v[154:157], v[174:177], v[122:125]
	v_mfma_i32_16x16x64_i8 v[106:109], v[154:157], v[188:191], v[106:109]
	v_mfma_i32_16x16x64_i8 v[110:113], v[158:161], v[188:191], v[110:113]
	v_mfma_i32_16x16x64_i8 v[94:97], v[158:161], v[196:199], v[94:97]
	v_mfma_i32_16x16x64_i8 v[90:93], v[154:157], v[196:199], v[90:93]
	v_mfma_i32_16x16x64_i8 v[74:77], v[154:157], v[204:207], v[74:77]
	v_mfma_i32_16x16x64_i8 v[78:81], v[158:161], v[204:207], v[78:81]
	s_nop 0
	v_mfma_i32_16x16x64_i8 v[126:129], v[150:153], v[178:181], v[126:129]
	v_mfma_i32_16x16x64_i8 v[122:125], v[146:149], v[178:181], v[122:125]
	v_mfma_i32_16x16x64_i8 v[106:109], v[146:149], v[192:195], v[106:109]
	v_mfma_i32_16x16x64_i8 v[110:113], v[150:153], v[192:195], v[110:113]
	v_mfma_i32_16x16x64_i8 v[94:97], v[150:153], v[200:203], v[94:97]
	v_mfma_i32_16x16x64_i8 v[90:93], v[146:149], v[200:203], v[90:93]
	v_mfma_i32_16x16x64_i8 v[74:77], v[146:149], v[208:211], v[74:77]
	v_mfma_i32_16x16x64_i8 v[78:81], v[150:153], v[208:211], v[78:81]
	v_mfma_i32_16x16x64_i8 v[118:121], v[142:145], v[174:177], v[118:121]
	v_mfma_i32_16x16x64_i8 v[114:117], v[138:141], v[174:177], v[114:117]
	v_mfma_i32_16x16x64_i8 v[98:101], v[138:141], v[188:191], v[98:101]
	v_mfma_i32_16x16x64_i8 v[102:105], v[142:145], v[188:191], v[102:105]
	v_mfma_i32_16x16x64_i8 v[86:89], v[142:145], v[196:199], v[86:89]
	v_mfma_i32_16x16x64_i8 v[82:85], v[138:141], v[196:199], v[82:85]
	v_mfma_i32_16x16x64_i8 v[66:69], v[138:141], v[204:207], v[66:69]
	v_mfma_i32_16x16x64_i8 v[70:73], v[142:145], v[204:207], v[70:73]
	s_nop 0
	v_mfma_i32_16x16x64_i8 v[118:121], v[130:133], v[178:181], v[118:121]
	v_mfma_i32_16x16x64_i8 v[114:117], v[134:137], v[178:181], v[114:117]
	v_mfma_i32_16x16x64_i8 v[98:101], v[134:137], v[192:195], v[98:101]
	v_mfma_i32_16x16x64_i8 v[102:105], v[130:133], v[192:195], v[102:105]
	v_mfma_i32_16x16x64_i8 v[86:89], v[130:133], v[200:203], v[86:89]
	v_mfma_i32_16x16x64_i8 v[82:85], v[134:137], v[200:203], v[82:85]
	v_mfma_i32_16x16x64_i8 v[66:69], v[134:137], v[208:211], v[66:69]
	v_mfma_i32_16x16x64_i8 v[70:73], v[130:133], v[208:211], v[70:73]
	s_setprio 0
	s_barrier
	s_add_i32 s66, s51, s3
	v_lshl_add_u64 v[174:175], s[38:39], 0, v[164:165]
	s_mov_b32 m0, s66
	ds_read_b128 v[188:191], v186 offset:16384
	ds_read_b128 v[192:195], v186 offset:17408
	ds_read_b128 v[196:199], v186 offset:18432
	ds_read_b128 v[200:203], v186 offset:19456
	ds_read_b128 v[204:207], v186 offset:20480
	ds_read_b128 v[208:211], v186 offset:21504
	ds_read_b128 v[212:215], v186 offset:22528
	ds_read_b128 v[216:219], v186 offset:23552
	global_load_lds_dwordx4 v[174:175], off
	s_add_i32 m0, s66, 0x2000
	s_add_u32 s66, s38, 0x80000
	v_lshl_add_u64 v[176:177], s[38:39], 0, v[162:163]
	s_addc_u32 s67, s39, 0
	s_add_i32 s68, s58, s3
	global_load_lds_dwordx4 v[176:177], off
	v_lshl_add_u64 v[178:179], s[66:67], 0, v[164:165]
	s_mov_b32 m0, s68
	v_lshl_add_u64 v[180:181], s[40:41], 0, v[162:163]
	global_load_lds_dwordx4 v[178:179], off
	v_lshl_add_u64 v[178:179], s[66:67], 0, v[162:163]
	s_add_i32 m0, s68, 0x2000
	s_nop 0
	global_load_lds_dwordx4 v[178:179], off
	v_lshl_add_u64 v[178:179], s[40:41], 0, v[164:165]
	s_mov_b32 m0, s35
	s_nop 0
	global_load_lds_dwordx4 v[178:179], off
	s_mov_b32 m0, s42
	s_nop 0
	global_load_lds_dwordx4 v[180:181], off
	s_waitcnt vmcnt(8)
	s_waitcnt lgkmcnt(0)
	s_barrier
	s_setprio 1
	v_mfma_i32_16x16x64_i8 v[62:65], v[158:161], v[188:191], v[62:65]
	v_mfma_i32_16x16x64_i8 v[58:61], v[154:157], v[188:191], v[58:61]
	v_mfma_i32_16x16x64_i8 v[42:45], v[154:157], v[196:199], v[42:45]
	v_mfma_i32_16x16x64_i8 v[46:49], v[158:161], v[196:199], v[46:49]
	v_mfma_i32_16x16x64_i8 v[30:33], v[158:161], v[204:207], v[30:33]
	v_mfma_i32_16x16x64_i8 v[26:29], v[154:157], v[204:207], v[26:29]
	v_mfma_i32_16x16x64_i8 v[10:13], v[154:157], v[212:215], v[10:13]
	v_mfma_i32_16x16x64_i8 v[14:17], v[158:161], v[212:215], v[14:17]
	s_nop 0
	v_mfma_i32_16x16x64_i8 v[62:65], v[150:153], v[192:195], v[62:65]
	v_mfma_i32_16x16x64_i8 v[58:61], v[146:149], v[192:195], v[58:61]
	v_mfma_i32_16x16x64_i8 v[42:45], v[146:149], v[200:203], v[42:45]
	v_mfma_i32_16x16x64_i8 v[46:49], v[150:153], v[200:203], v[46:49]
	v_mfma_i32_16x16x64_i8 v[30:33], v[150:153], v[208:211], v[30:33]
	v_mfma_i32_16x16x64_i8 v[26:29], v[146:149], v[208:211], v[26:29]
	v_mfma_i32_16x16x64_i8 v[10:13], v[146:149], v[216:219], v[10:13]
	v_mfma_i32_16x16x64_i8 v[14:17], v[150:153], v[216:219], v[14:17]
	v_mfma_i32_16x16x64_i8 v[54:57], v[142:145], v[188:191], v[54:57]
	v_mfma_i32_16x16x64_i8 v[50:53], v[138:141], v[188:191], v[50:53]
	v_mfma_i32_16x16x64_i8 v[34:37], v[138:141], v[196:199], v[34:37]
	v_mfma_i32_16x16x64_i8 v[38:41], v[142:145], v[196:199], v[38:41]
	v_mfma_i32_16x16x64_i8 v[22:25], v[142:145], v[204:207], v[22:25]
	v_mfma_i32_16x16x64_i8 v[18:21], v[138:141], v[204:207], v[18:21]
	v_mfma_i32_16x16x64_i8 v[2:5], v[138:141], v[212:215], v[2:5]
	v_mfma_i32_16x16x64_i8 v[6:9], v[142:145], v[212:215], v[6:9]
	s_nop 0
	v_mfma_i32_16x16x64_i8 v[54:57], v[130:133], v[192:195], v[54:57]
	v_mfma_i32_16x16x64_i8 v[50:53], v[134:137], v[192:195], v[50:53]
	v_mfma_i32_16x16x64_i8 v[34:37], v[134:137], v[200:203], v[34:37]
	v_mfma_i32_16x16x64_i8 v[38:41], v[130:133], v[200:203], v[38:41]
	v_mfma_i32_16x16x64_i8 v[22:25], v[130:133], v[208:211], v[22:25]
	v_mfma_i32_16x16x64_i8 v[18:21], v[134:137], v[208:211], v[18:21]
	v_mfma_i32_16x16x64_i8 v[2:5], v[134:137], v[216:219], v[2:5]
	v_mfma_i32_16x16x64_i8 v[6:9], v[130:133], v[216:219], v[6:9]
	s_setprio 0
	s_barrier
	s_add_i32 s66, 0, 0x18000
	s_add_i32 s67, 0, 0x1c000
	v_add_u32_e32 v142, s66, v182
	v_add_u32_e32 v158, s67, v182
	ds_read_b128 v[130:133], v142
	ds_read_b128 v[134:137], v142 offset:1024
	ds_read_b128 v[138:141], v142 offset:2048
	ds_read_b128 v[142:145], v142 offset:3072
	ds_read_b128 v[146:149], v158
	ds_read_b128 v[150:153], v158 offset:1024
	ds_read_b128 v[154:157], v158 offset:2048
	ds_read_b128 v[158:161], v158 offset:3072
	s_add_u32 s40, s40, 0x80000
	s_addc_u32 s41, s41, 0
	s_mov_b32 m0, s43
	v_lshl_add_u64 v[220:221], s[40:41], 0, v[164:165]
	ds_read_b128 v[188:191], v186 offset:32768
	ds_read_b128 v[192:195], v186 offset:33792
	ds_read_b128 v[196:199], v186 offset:34816
	ds_read_b128 v[200:203], v186 offset:35840
	ds_read_b128 v[204:207], v186 offset:36864
	ds_read_b128 v[208:211], v186 offset:37888
	ds_read_b128 v[212:215], v186 offset:38912
	ds_read_b128 v[216:219], v186 offset:39936
	global_load_lds_dwordx4 v[220:221], off
	v_lshl_add_u64 v[220:221], s[40:41], 0, v[162:163]
	s_mov_b32 m0, s44
	s_nop 0
	global_load_lds_dwordx4 v[220:221], off
	s_waitcnt vmcnt(8)
	s_waitcnt lgkmcnt(0)
	s_barrier
	s_setprio 1
	v_mfma_i32_16x16x64_i8 v[126:129], v[130:133], v[188:191], v[126:129]
	v_mfma_i32_16x16x64_i8 v[122:125], v[138:141], v[188:191], v[122:125]
	v_mfma_i32_16x16x64_i8 v[106:109], v[138:141], v[196:199], v[106:109]
	v_mfma_i32_16x16x64_i8 v[110:113], v[130:133], v[196:199], v[110:113]
	v_mfma_i32_16x16x64_i8 v[94:97], v[130:133], v[204:207], v[94:97]
	v_mfma_i32_16x16x64_i8 v[90:93], v[138:141], v[204:207], v[90:93]
	v_mfma_i32_16x16x64_i8 v[74:77], v[138:141], v[212:215], v[74:77]
	v_mfma_i32_16x16x64_i8 v[78:81], v[130:133], v[212:215], v[78:81]
	s_nop 0
	v_mfma_i32_16x16x64_i8 v[126:129], v[134:137], v[192:195], v[126:129]
	v_mfma_i32_16x16x64_i8 v[122:125], v[142:145], v[192:195], v[122:125]
	v_mfma_i32_16x16x64_i8 v[106:109], v[142:145], v[200:203], v[106:109]
	v_mfma_i32_16x16x64_i8 v[110:113], v[134:137], v[200:203], v[110:113]
	v_mfma_i32_16x16x64_i8 v[94:97], v[134:137], v[208:211], v[94:97]
	v_mfma_i32_16x16x64_i8 v[90:93], v[142:145], v[208:211], v[90:93]
	v_mfma_i32_16x16x64_i8 v[74:77], v[142:145], v[216:219], v[74:77]
	v_mfma_i32_16x16x64_i8 v[78:81], v[134:137], v[216:219], v[78:81]
	v_mfma_i32_16x16x64_i8 v[118:121], v[146:149], v[188:191], v[118:121]
	v_mfma_i32_16x16x64_i8 v[114:117], v[154:157], v[188:191], v[114:117]
	v_mfma_i32_16x16x64_i8 v[98:101], v[154:157], v[196:199], v[98:101]
	v_mfma_i32_16x16x64_i8 v[102:105], v[146:149], v[196:199], v[102:105]
	v_mfma_i32_16x16x64_i8 v[86:89], v[146:149], v[204:207], v[86:89]
	v_mfma_i32_16x16x64_i8 v[82:85], v[154:157], v[204:207], v[82:85]
	v_mfma_i32_16x16x64_i8 v[66:69], v[154:157], v[212:215], v[66:69]
	v_mfma_i32_16x16x64_i8 v[70:73], v[146:149], v[212:215], v[70:73]
	s_nop 0
	v_mfma_i32_16x16x64_i8 v[118:121], v[150:153], v[192:195], v[118:121]
	v_mfma_i32_16x16x64_i8 v[114:117], v[158:161], v[192:195], v[114:117]
	v_mfma_i32_16x16x64_i8 v[98:101], v[158:161], v[200:203], v[98:101]
	v_mfma_i32_16x16x64_i8 v[102:105], v[150:153], v[200:203], v[102:105]
	v_mfma_i32_16x16x64_i8 v[86:89], v[150:153], v[208:211], v[86:89]
	v_mfma_i32_16x16x64_i8 v[82:85], v[158:161], v[208:211], v[82:85]
	v_mfma_i32_16x16x64_i8 v[66:69], v[158:161], v[216:219], v[66:69]
	v_mfma_i32_16x16x64_i8 v[70:73], v[150:153], v[216:219], v[70:73]
	s_setprio 0
	s_barrier
	s_add_i32 s40, s66, s3
	v_lshl_add_u64 v[174:175], v[174:175], 0, s[8:9]
	s_mov_b32 m0, s40
	ds_read_b128 v[188:191], v186 offset:49152
	ds_read_b128 v[192:195], v186 offset:50176
	ds_read_b128 v[196:199], v186 offset:51200
	ds_read_b128 v[200:203], v186 offset:52224
	ds_read_b128 v[204:207], v186 offset:53248
	ds_read_b128 v[208:211], v186 offset:54272
	ds_read_b128 v[212:215], v186 offset:55296
	ds_read_b128 v[216:219], v186 offset:56320
	global_load_lds_dwordx4 v[174:175], off
	s_add_i32 m0, s40, 0x2000
	s_add_u32 s38, s38, 0x80080
	v_lshl_add_u64 v[174:175], v[176:177], 0, s[8:9]
	s_addc_u32 s39, s39, 0
	s_add_i32 s40, s67, s3
	global_load_lds_dwordx4 v[174:175], off
	v_lshl_add_u64 v[174:175], s[38:39], 0, v[164:165]
	s_mov_b32 m0, s40
	s_nop 0
	global_load_lds_dwordx4 v[174:175], off
	v_lshl_add_u64 v[174:175], s[38:39], 0, v[162:163]
	s_add_i32 m0, s40, 0x2000
	s_nop 0
	global_load_lds_dwordx4 v[174:175], off
	v_lshl_add_u64 v[174:175], v[178:179], 0, s[8:9]
	s_mov_b32 m0, s49
	s_nop 0
	global_load_lds_dwordx4 v[174:175], off
	v_lshl_add_u64 v[174:175], v[180:181], 0, s[8:9]
	s_mov_b32 m0, s50
	s_nop 0
	global_load_lds_dwordx4 v[174:175], off
	s_waitcnt vmcnt(8)
	s_waitcnt lgkmcnt(0)
	s_barrier
	s_setprio 1
	v_mfma_i32_16x16x64_i8 v[62:65], v[130:133], v[188:191], v[62:65]
	v_mfma_i32_16x16x64_i8 v[58:61], v[138:141], v[188:191], v[58:61]
	v_mfma_i32_16x16x64_i8 v[42:45], v[138:141], v[196:199], v[42:45]
	v_mfma_i32_16x16x64_i8 v[46:49], v[130:133], v[196:199], v[46:49]
	v_mfma_i32_16x16x64_i8 v[30:33], v[130:133], v[204:207], v[30:33]
	v_mfma_i32_16x16x64_i8 v[26:29], v[138:141], v[204:207], v[26:29]
	v_mfma_i32_16x16x64_i8 v[10:13], v[138:141], v[212:215], v[10:13]
	v_mfma_i32_16x16x64_i8 v[14:17], v[130:133], v[212:215], v[14:17]
	s_nop 0
	v_mfma_i32_16x16x64_i8 v[62:65], v[134:137], v[192:195], v[62:65]
	v_mfma_i32_16x16x64_i8 v[58:61], v[142:145], v[192:195], v[58:61]
	v_mfma_i32_16x16x64_i8 v[42:45], v[142:145], v[200:203], v[42:45]
	v_mfma_i32_16x16x64_i8 v[46:49], v[134:137], v[200:203], v[46:49]
	v_mfma_i32_16x16x64_i8 v[30:33], v[134:137], v[208:211], v[30:33]
	v_mfma_i32_16x16x64_i8 v[26:29], v[142:145], v[208:211], v[26:29]
	v_mfma_i32_16x16x64_i8 v[10:13], v[142:145], v[216:219], v[10:13]
	v_mfma_i32_16x16x64_i8 v[14:17], v[134:137], v[216:219], v[14:17]
	v_mfma_i32_16x16x64_i8 v[54:57], v[146:149], v[188:191], v[54:57]
	v_mfma_i32_16x16x64_i8 v[50:53], v[154:157], v[188:191], v[50:53]
	v_mfma_i32_16x16x64_i8 v[34:37], v[154:157], v[196:199], v[34:37]
	v_mfma_i32_16x16x64_i8 v[38:41], v[146:149], v[196:199], v[38:41]
	v_mfma_i32_16x16x64_i8 v[22:25], v[146:149], v[204:207], v[22:25]
	v_mfma_i32_16x16x64_i8 v[18:21], v[154:157], v[204:207], v[18:21]
	v_mfma_i32_16x16x64_i8 v[2:5], v[154:157], v[212:215], v[2:5]
	v_mfma_i32_16x16x64_i8 v[6:9], v[146:149], v[212:215], v[6:9]
	s_nop 0
	v_mfma_i32_16x16x64_i8 v[54:57], v[150:153], v[192:195], v[54:57]
	v_mfma_i32_16x16x64_i8 v[50:53], v[158:161], v[192:195], v[50:53]
	v_mfma_i32_16x16x64_i8 v[34:37], v[158:161], v[200:203], v[34:37]
	v_mfma_i32_16x16x64_i8 v[38:41], v[150:153], v[200:203], v[38:41]
	v_mfma_i32_16x16x64_i8 v[22:25], v[150:153], v[208:211], v[22:25]
	v_mfma_i32_16x16x64_i8 v[18:21], v[158:161], v[208:211], v[18:21]
	v_mfma_i32_16x16x64_i8 v[2:5], v[158:161], v[216:219], v[2:5]
	v_mfma_i32_16x16x64_i8 v[6:9], v[150:153], v[216:219], v[6:9]
	s_setprio 0
	s_barrier
	s_add_i32 s65, s65, 2
	s_add_u32 s36, s36, 0x100
	s_addc_u32 s37, s37, 0
	s_add_u32 s63, s63, 0x100
	s_addc_u32 s64, s64, 0
	s_cmp_gt_u32 s65, 29
	s_cbranch_scc0 .LBB0_1173
	s_and_b64 vcc, exec, s[12:13]
	s_cbranch_vccz .LBB0_1176
	s_barrier

.LBB0_1234:
	v_add_co_u32_e64 v18, s[4:5], s12, v72
	v_add_co_u32_e32 v76, vcc, 0xffffd000, v72
	s_nop 0
	v_addc_co_u32_e64 v19, s[4:5], -1, v73, s[4:5]
	v_add_co_u32_e64 v20, s[4:5], s13, v72
	global_load_dwordx4 v[14:17], v[72:73], off offset:-3072
	global_load_dwordx4 v[10:13], v[72:73], off offset:-2048
	global_load_dwordx4 v[6:9], v[72:73], off offset:-1024
	global_load_dwordx4 v[2:5], v[72:73], off
	global_load_dwordx4 v[86:89], v[46:47], off
	v_addc_co_u32_e64 v21, s[4:5], -1, v73, s[4:5]
	v_addc_co_u32_e32 v77, vcc, -1, v73, vcc
	global_load_dwordx4 v[90:93], v[18:19], off offset:-3072
	global_load_dwordx4 v[42:45], v[18:19], off offset:-2048
	global_load_dwordx4 v[38:41], v[18:19], off offset:-1024
	global_load_dwordx4 v[34:37], v[18:19], off
	global_load_dwordx4 v[30:33], v[20:21], off offset:-3072
	global_load_dwordx4 v[26:29], v[20:21], off offset:-2048
	global_load_dwordx4 v[22:25], v[20:21], off offset:-1024
	s_nop 0
	global_load_dwordx4 v[18:21], v[72:73], off offset:-4096
	global_load_dwordx4 v[94:97], v[76:77], off offset:-3072
	global_load_dwordx4 v[98:101], v[76:77], off offset:-2048
	global_load_dwordx4 v[102:105], v[76:77], off offset:-1024
	global_load_dwordx4 v[106:109], v[76:77], off
	v_mov_b32_e32 v111, 0
	v_mov_b32_e32 v112, 0
	v_mov_b32_e32 v113, 0
	s_add_i32 s3, s3, s92
	v_lshl_add_u64 v[72:73], v[72:73], 0, s[6:7]
	s_cmpk_lt_i32 s3, 0x4000
	s_waitcnt vmcnt(0)
	v_mul_f32_e32 v76, v15, v15
	v_mul_f32_e32 v77, v17, v17
	v_mul_f32_e32 v114, v11, v11
	v_mul_f32_e32 v115, v13, v13
	v_mul_f32_e32 v118, v3, v3
	v_mul_f32_e32 v119, v5, v5
	v_mul_f32_e32 v124, v39, v39
	v_mul_f32_e32 v125, v41, v41
	v_mul_f32_e32 v136, v95, v95
	v_mul_f32_e32 v137, v97, v97
	v_mul_f32_e32 v138, v99, v99
	v_mul_f32_e32 v139, v101, v101
	v_mul_f32_e32 v126, v35, v35
	v_mul_f32_e32 v127, v37, v37
	v_fmac_f32_e32 v76, v14, v14
	v_fmac_f32_e32 v77, v16, v16
	v_fmac_f32_e32 v114, v10, v10
	v_fmac_f32_e32 v115, v12, v12
	v_fmac_f32_e32 v118, v2, v2
	v_fmac_f32_e32 v119, v4, v4
	v_mul_f32_e32 v140, v103, v103
	v_mul_f32_e32 v141, v105, v105
	v_fmac_f32_e32 v124, v38, v38
	v_fmac_f32_e32 v125, v40, v40
	v_fmac_f32_e32 v136, v94, v94
	v_fmac_f32_e32 v137, v96, v96
	v_fmac_f32_e32 v138, v98, v98
	v_fmac_f32_e32 v139, v100, v100
	v_mul_f32_e32 v142, v107, v107
	v_mul_f32_e32 v143, v109, v109
	v_fmac_f32_e32 v126, v34, v34
	v_fmac_f32_e32 v127, v36, v36
	v_add_f32_e32 v76, v76, v77
	v_add_f32_e32 v77, v114, v115
	v_add_f32_e32 v115, v118, v119
	v_fmac_f32_e32 v140, v102, v102
	v_fmac_f32_e32 v141, v104, v104
	v_add_f32_e32 v118, v124, v125
	v_add_f32_e32 v124, v136, v137
	v_add_f32_e32 v125, v138, v139
	v_mul_f32_e32 v116, v7, v7
	v_mul_f32_e32 v117, v9, v9
	v_mul_f32_e32 v120, v91, v91
	v_mul_f32_e32 v121, v93, v93
	v_fmac_f32_e32 v142, v106, v106
	v_fmac_f32_e32 v143, v108, v108
	v_add_f32_e32 v119, v126, v127
	v_add_f32_e32 v126, v140, v141
	v_add_f32_e32 v124, v124, v125
	v_mul_f32_e32 v122, v43, v43
	v_mul_f32_e32 v123, v45, v45
	v_fmac_f32_e32 v116, v6, v6
	v_fmac_f32_e32 v117, v8, v8
	v_fmac_f32_e32 v120, v90, v90
	v_fmac_f32_e32 v121, v92, v92
	v_add_f32_e32 v127, v142, v143
	v_add_f32_e32 v124, v124, v126
	v_fmac_f32_e32 v122, v42, v42
	v_fmac_f32_e32 v123, v44, v44
	v_add_f32_e32 v114, v116, v117
	v_add_f32_e32 v116, v120, v121
	v_add_f32_e32 v124, v124, v127
	v_add_f32_e32 v117, v122, v123
	v_add_f32_e32 v116, v124, v116
	v_mul_f32_e32 v128, v31, v31
	v_mul_f32_e32 v129, v33, v33
	v_add_f32_e32 v116, v116, v117
	v_mul_f32_e32 v130, v27, v27
	v_mul_f32_e32 v131, v29, v29
	v_fmac_f32_e32 v128, v30, v30
	v_fmac_f32_e32 v129, v32, v32
	v_add_f32_e32 v116, v116, v118
	v_mul_f32_e32 v132, v23, v23
	v_mul_f32_e32 v133, v25, v25
	v_fmac_f32_e32 v130, v26, v26
	v_fmac_f32_e32 v131, v28, v28
	v_add_f32_e32 v120, v128, v129
	v_add_f32_e32 v116, v116, v119
	v_mul_f32_e32 v134, v19, v19
	v_mul_f32_e32 v135, v21, v21
	v_fmac_f32_e32 v132, v22, v22
	v_fmac_f32_e32 v133, v24, v24
	v_add_f32_e32 v121, v130, v131
	v_add_f32_e32 v116, v116, v120
	v_fmac_f32_e32 v134, v18, v18
	v_fmac_f32_e32 v135, v20, v20
	v_add_f32_e32 v122, v132, v133
	v_add_f32_e32 v116, v116, v121
	v_add_f32_e32 v123, v134, v135
	v_add_f32_e32 v116, v116, v122
	v_add_f32_e32 v116, v116, v123
	v_add_f32_e32 v76, v116, v76
	v_add_f32_e32 v76, v76, v77
	v_add_f32_e32 v76, v76, v114
	v_add_f32_e32 v76, v76, v115
	ds_bpermute_b32 v77, v1, v76
	s_waitcnt lgkmcnt(0)
	v_add_f32_e32 v76, v76, v77
	ds_bpermute_b32 v77, v78, v76
	s_waitcnt lgkmcnt(0)
	v_add_f32_e32 v76, v76, v77
	ds_bpermute_b32 v77, v79, v76
	s_waitcnt lgkmcnt(0)
	v_add_f32_e32 v76, v76, v77
	ds_bpermute_b32 v77, v80, v76
	s_waitcnt lgkmcnt(0)
	v_add_f32_e32 v76, v76, v77
	ds_bpermute_b32 v77, v81, v76
	s_waitcnt lgkmcnt(0)
	v_add_f32_e32 v76, v76, v77
	ds_bpermute_b32 v77, v82, v76
	s_waitcnt lgkmcnt(0)
	v_add_f32_e32 v76, v76, v77
	v_fmamk_f32 v76, v76, 0x39800000, v83
	v_mul_f32_e32 v77, 0x4f800000, v76
	v_cmp_gt_f32_e32 vcc, s14, v76
	s_nop 1
	v_cndmask_b32_e32 v76, v76, v77, vcc
	v_sqrt_f32_e32 v77, v76
	s_nop 0
	v_add_u32_e32 v114, -1, v77
	v_add_u32_e32 v115, 1, v77
	v_fma_f32 v116, -v114, v77, v76
	v_fma_f32 v117, -v115, v77, v76
	v_cmp_ge_f32_e64 s[4:5], 0, v116
	s_nop 1
	v_cndmask_b32_e64 v77, v77, v114, s[4:5]
	v_cmp_lt_f32_e64 s[4:5], 0, v117
	s_nop 1
	v_cndmask_b32_e64 v77, v77, v115, s[4:5]
	v_mul_f32_e32 v114, 0x37800000, v77
	v_cndmask_b32_e32 v77, v77, v114, vcc
	v_cmp_class_f32_e32 vcc, v76, v84
	s_nop 1
	v_cndmask_b32_e32 v76, v77, v76, vcc
	v_div_scale_f32 v77, s[4:5], v76, v76, 1.0
	v_rcp_f32_e32 v115, v77
	v_div_scale_f32 v114, vcc, 1.0, v76, 1.0
	v_fma_f32 v116, -v77, v115, 1.0
	v_fmac_f32_e32 v115, v116, v115
	v_mul_f32_e32 v116, v114, v115
	v_fma_f32 v117, -v77, v116, v114
	v_fmac_f32_e32 v116, v117, v115
	v_fma_f32 v77, -v77, v116, v114
	v_div_fmas_f32 v77, v77, v115, v116
	v_div_fixup_f32 v76, v77, v76, 1.0
	v_mul_f32_e32 v77, v94, v76
	v_mul_f32_e32 v94, v95, v76
	v_mul_f32_e32 v77, v86, v77
	v_mul_f32_e32 v86, v87, v94
	v_med3_f32 v77, v77, s15, v85
	v_med3_f32 v86, v86, s15, v85
	v_cvt_pk_fp8_f32 v110, v77, v86
	v_mul_f32_e32 v95, v96, v76
	v_mul_f32_e32 v96, v97, v76
	v_mul_f32_e32 v87, v88, v95
	v_mul_f32_e32 v88, v89, v96
	v_med3_f32 v87, v87, s15, v85
	v_med3_f32 v88, v88, s15, v85
	v_cvt_pk_fp8_f32 v110, v87, v88 op_sel:[0,0,1]
	v_mul_f32_e32 v97, v98, v76
	v_mul_f32_e32 v98, v99, v76
	v_mul_f32_e32 v99, v100, v76
	global_store_dword v[74:75], v110, off offset:-2048
	global_load_dwordx4 v[86:89], v[46:47], off offset:1024
	v_mul_f32_e32 v100, v101, v76
	v_mul_f32_e32 v101, v102, v76
	v_mul_f32_e32 v102, v103, v76
	v_mul_f32_e32 v103, v104, v76
	v_mul_f32_e32 v104, v105, v76
	v_mul_f32_e32 v105, v106, v76
	v_mul_f32_e32 v106, v107, v76
	v_mul_f32_e32 v94, v109, v76
	v_mul_f32_e32 v90, v90, v76
	v_mul_f32_e32 v91, v91, v76
	v_mul_f32_e32 v92, v92, v76
	v_mul_f32_e32 v93, v93, v76
	v_mul_f32_e32 v42, v42, v76
	v_mul_f32_e32 v43, v43, v76
	v_mul_f32_e32 v44, v44, v76
	v_mul_f32_e32 v45, v45, v76
	v_mul_f32_e32 v38, v38, v76
	v_mul_f32_e32 v39, v39, v76
	v_mul_f32_e32 v40, v40, v76
	v_mul_f32_e32 v41, v41, v76
	v_mul_f32_e32 v34, v34, v76
	v_mul_f32_e32 v35, v35, v76
	v_mul_f32_e32 v36, v36, v76
	v_mul_f32_e32 v37, v37, v76
	v_mul_f32_e32 v30, v30, v76
	v_mul_f32_e32 v31, v31, v76
	v_mul_f32_e32 v32, v32, v76
	v_mul_f32_e32 v33, v33, v76
	v_mul_f32_e32 v26, v26, v76
	v_mul_f32_e32 v27, v27, v76
	v_mul_f32_e32 v28, v28, v76
	v_mul_f32_e32 v29, v29, v76
	v_mul_f32_e32 v22, v22, v76
	v_mul_f32_e32 v23, v23, v76
	v_mul_f32_e32 v24, v24, v76
	v_mul_f32_e32 v25, v25, v76
	v_mul_f32_e32 v18, v18, v76
	v_mul_f32_e32 v19, v19, v76
	v_mul_f32_e32 v20, v20, v76
	v_mul_f32_e32 v21, v21, v76
	v_mul_f32_e32 v14, v14, v76
	v_mul_f32_e32 v15, v15, v76
	v_mul_f32_e32 v16, v16, v76
	v_mul_f32_e32 v17, v17, v76
	v_mul_f32_e32 v10, v10, v76
	v_mul_f32_e32 v11, v11, v76
	v_mul_f32_e32 v12, v12, v76
	v_mul_f32_e32 v13, v13, v76
	v_mul_f32_e32 v6, v6, v76
	v_mul_f32_e32 v7, v7, v76
	v_mul_f32_e32 v8, v8, v76
	v_mul_f32_e32 v9, v9, v76
	v_mul_f32_e32 v2, v2, v76
	v_mul_f32_e32 v3, v3, v76
	v_mul_f32_e32 v4, v4, v76
	v_mul_f32_e32 v5, v5, v76
	s_waitcnt vmcnt(0)
	v_mul_f32_e32 v77, v86, v97
	v_mul_f32_e32 v86, v87, v98
	v_med3_f32 v77, v77, s15, v85
	v_med3_f32 v86, v86, s15, v85
	v_cvt_pk_fp8_f32 v111, v77, v86
	v_mul_f32_e32 v87, v88, v99
	v_mul_f32_e32 v88, v89, v100
	v_med3_f32 v87, v87, s15, v85
	v_med3_f32 v88, v88, s15, v85
	v_cvt_pk_fp8_f32 v111, v87, v88 op_sel:[0,0,1]
	global_store_dword v[74:75], v111, off offset:-1792
	global_load_dwordx4 v[86:89], v[46:47], off offset:2048
	s_waitcnt vmcnt(0)
	v_mul_f32_e32 v77, v101, v86
	v_mul_f32_e32 v86, v102, v87
	v_med3_f32 v77, v77, s15, v85
	v_med3_f32 v86, v86, s15, v85
	v_cvt_pk_fp8_f32 v112, v77, v86
	v_mul_f32_e32 v87, v103, v88
	v_mul_f32_e32 v88, v104, v89
	v_med3_f32 v87, v87, s15, v85
	v_med3_f32 v88, v88, s15, v85
	v_cvt_pk_fp8_f32 v112, v87, v88 op_sel:[0,0,1]
	v_mul_f32_e32 v77, v108, v76
	global_store_dword v[74:75], v112, off offset:-1536
	global_load_dwordx4 v[86:89], v[46:47], off offset:3072
	s_waitcnt vmcnt(0)
	v_mul_f32_e32 v86, v105, v86
	v_mul_f32_e32 v87, v106, v87
	v_med3_f32 v86, v86, s15, v85
	v_med3_f32 v87, v87, s15, v85
	v_cvt_pk_fp8_f32 v113, v86, v87
	v_mul_f32_e32 v77, v77, v88
	v_mul_f32_e32 v88, v94, v89
	v_med3_f32 v77, v77, s15, v85
	v_med3_f32 v88, v88, s15, v85
	v_cvt_pk_fp8_f32 v113, v77, v88 op_sel:[0,0,1]
	global_store_dword v[74:75], v113, off offset:-1280
	global_load_dwordx4 v[86:89], v[48:49], off
	s_waitcnt vmcnt(0)
	v_mul_f32_e32 v86, v90, v86
	v_mul_f32_e32 v87, v91, v87
	v_med3_f32 v86, v86, s15, v85
	v_med3_f32 v87, v87, s15, v85
	v_cvt_pk_fp8_f32 v77, v86, v87
	v_mul_f32_e32 v88, v92, v88
	v_mul_f32_e32 v89, v93, v89
	v_med3_f32 v88, v88, s15, v85
	v_med3_f32 v89, v89, s15, v85
	v_cvt_pk_fp8_f32 v77, v88, v89 op_sel:[0,0,1]
	global_store_dword v[74:75], v77, off offset:-1024
	global_load_dwordx4 v[86:89], v[50:51], off
	s_waitcnt vmcnt(0)
	v_mul_f32_e32 v42, v42, v86
	v_mul_f32_e32 v43, v43, v87
	v_med3_f32 v42, v42, s15, v85
	v_med3_f32 v43, v43, s15, v85
	v_cvt_pk_fp8_f32 v77, v42, v43
	v_mul_f32_e32 v44, v44, v88
	v_mul_f32_e32 v45, v45, v89
	v_med3_f32 v44, v44, s15, v85
	v_med3_f32 v45, v45, s15, v85
	v_cvt_pk_fp8_f32 v77, v44, v45 op_sel:[0,0,1]
	global_store_dword v[74:75], v77, off offset:-768
	global_load_dwordx4 v[42:45], v[52:53], off
	s_waitcnt vmcnt(0)
	v_mul_f32_e32 v38, v38, v42
	v_mul_f32_e32 v39, v39, v43
	v_med3_f32 v38, v38, s15, v85
	v_med3_f32 v39, v39, s15, v85
	v_cvt_pk_fp8_f32 v77, v38, v39
	v_mul_f32_e32 v40, v40, v44
	v_mul_f32_e32 v41, v41, v45
	v_med3_f32 v40, v40, s15, v85
	v_med3_f32 v41, v41, s15, v85
	v_cvt_pk_fp8_f32 v77, v40, v41 op_sel:[0,0,1]
	global_store_dword v[74:75], v77, off offset:-512
	global_load_dwordx4 v[38:41], v[54:55], off
	s_waitcnt vmcnt(0)
	v_mul_f32_e32 v34, v34, v38
	v_mul_f32_e32 v35, v35, v39
	v_med3_f32 v34, v34, s15, v85
	v_med3_f32 v35, v35, s15, v85
	v_cvt_pk_fp8_f32 v42, v34, v35
	v_mul_f32_e32 v36, v36, v40
	v_mul_f32_e32 v37, v37, v41
	v_med3_f32 v36, v36, s15, v85
	v_med3_f32 v37, v37, s15, v85
	v_cvt_pk_fp8_f32 v42, v36, v37 op_sel:[0,0,1]
	global_store_dword v[74:75], v42, off offset:-256
	global_load_dwordx4 v[34:37], v[56:57], off
	s_waitcnt vmcnt(0)
	v_mul_f32_e32 v30, v30, v34
	v_mul_f32_e32 v31, v31, v35
	v_med3_f32 v30, v30, s15, v85
	v_med3_f32 v31, v31, s15, v85
	v_cvt_pk_fp8_f32 v38, v30, v31
	v_mul_f32_e32 v32, v32, v36
	v_mul_f32_e32 v33, v33, v37
	v_med3_f32 v32, v32, s15, v85
	v_med3_f32 v33, v33, s15, v85
	v_cvt_pk_fp8_f32 v38, v32, v33 op_sel:[0,0,1]
	global_store_dword v[74:75], v38, off
	global_load_dwordx4 v[30:33], v[58:59], off
	s_waitcnt vmcnt(0)
	v_mul_f32_e32 v26, v26, v30
	v_mul_f32_e32 v27, v27, v31
	v_med3_f32 v26, v26, s15, v85
	v_med3_f32 v27, v27, s15, v85
	v_cvt_pk_fp8_f32 v34, v26, v27
	v_mul_f32_e32 v28, v28, v32
	v_mul_f32_e32 v29, v29, v33
	v_med3_f32 v28, v28, s15, v85
	v_med3_f32 v29, v29, s15, v85
	v_cvt_pk_fp8_f32 v34, v28, v29 op_sel:[0,0,1]
	global_store_dword v[74:75], v34, off offset:256
	global_load_dwordx4 v[26:29], v[60:61], off
	s_waitcnt vmcnt(0)
	v_mul_f32_e32 v22, v22, v26
	v_mul_f32_e32 v23, v23, v27
	v_med3_f32 v22, v22, s15, v85
	v_med3_f32 v23, v23, s15, v85
	v_cvt_pk_fp8_f32 v30, v22, v23
	v_mul_f32_e32 v24, v24, v28
	v_mul_f32_e32 v25, v25, v29
	v_med3_f32 v24, v24, s15, v85
	v_med3_f32 v25, v25, s15, v85
	v_cvt_pk_fp8_f32 v30, v24, v25 op_sel:[0,0,1]
	global_store_dword v[74:75], v30, off offset:512
	global_load_dwordx4 v[22:25], v[62:63], off
	s_waitcnt vmcnt(0)
	v_mul_f32_e32 v18, v18, v22
	v_mul_f32_e32 v19, v19, v23
	v_med3_f32 v18, v18, s15, v85
	v_med3_f32 v19, v19, s15, v85
	v_cvt_pk_fp8_f32 v26, v18, v19
	v_mul_f32_e32 v20, v20, v24
	v_mul_f32_e32 v21, v21, v25
	v_med3_f32 v20, v20, s15, v85
	v_med3_f32 v21, v21, s15, v85
	v_cvt_pk_fp8_f32 v26, v20, v21 op_sel:[0,0,1]
	global_store_dword v[74:75], v26, off offset:768
	global_load_dwordx4 v[18:21], v[64:65], off
	s_waitcnt vmcnt(0)
	v_mul_f32_e32 v14, v14, v18
	v_mul_f32_e32 v15, v15, v19
	v_med3_f32 v14, v14, s15, v85
	v_med3_f32 v15, v15, s15, v85
	v_cvt_pk_fp8_f32 v22, v14, v15
	v_mul_f32_e32 v16, v16, v20
	v_mul_f32_e32 v17, v17, v21
	v_med3_f32 v16, v16, s15, v85
	v_med3_f32 v17, v17, s15, v85
	v_cvt_pk_fp8_f32 v22, v16, v17 op_sel:[0,0,1]
	global_store_dword v[74:75], v22, off offset:1024
	global_load_dwordx4 v[14:17], v[66:67], off
	s_waitcnt vmcnt(0)
	v_mul_f32_e32 v10, v10, v14
	v_mul_f32_e32 v11, v11, v15
	v_med3_f32 v10, v10, s15, v85
	v_med3_f32 v11, v11, s15, v85
	v_cvt_pk_fp8_f32 v18, v10, v11
	v_mul_f32_e32 v12, v12, v16
	v_mul_f32_e32 v13, v13, v17
	v_med3_f32 v12, v12, s15, v85
	v_med3_f32 v13, v13, s15, v85
	v_cvt_pk_fp8_f32 v18, v12, v13 op_sel:[0,0,1]
	global_store_dword v[74:75], v18, off offset:1280
	global_load_dwordx4 v[10:13], v[68:69], off
	s_waitcnt vmcnt(0)
	v_mul_f32_e32 v6, v6, v10
	v_mul_f32_e32 v7, v7, v11
	v_med3_f32 v6, v6, s15, v85
	v_med3_f32 v7, v7, s15, v85
	v_cvt_pk_fp8_f32 v14, v6, v7
	v_mul_f32_e32 v8, v8, v12
	v_mul_f32_e32 v9, v9, v13
	v_med3_f32 v8, v8, s15, v85
	v_med3_f32 v9, v9, s15, v85
	v_cvt_pk_fp8_f32 v14, v8, v9 op_sel:[0,0,1]
	global_store_dword v[74:75], v14, off offset:1536
	global_load_dwordx4 v[6:9], v[70:71], off
	s_waitcnt vmcnt(0)
	v_mul_f32_e32 v2, v2, v6
	v_mul_f32_e32 v3, v3, v7
	v_med3_f32 v2, v2, s15, v85
	v_med3_f32 v3, v3, s15, v85
	v_cvt_pk_fp8_f32 v10, v2, v3
	v_mul_f32_e32 v4, v4, v8
	v_mul_f32_e32 v5, v5, v9
	v_med3_f32 v2, v4, s15, v85
	v_med3_f32 v3, v5, s15, v85
	v_cvt_pk_fp8_f32 v10, v2, v3 op_sel:[0,0,1]
	global_store_dword v[74:75], v10, off offset:1792
	v_lshl_add_u64 v[74:75], v[74:75], 0, s[8:9]
	s_cbranch_scc1 .LBB0_1234
	v_readlane_b32 s93, v246, 7

.LBB0_1291:
	ds_read_b128 v[26:29], v184
	ds_read_b128 v[30:33], v184 offset:1024
	ds_read_b128 v[18:21], v184 offset:2048
	ds_read_b128 v[22:25], v184 offset:3072
	ds_read_b128 v[10:13], v185
	ds_read_b128 v[14:17], v185 offset:1024
	ds_read_b128 v[2:5], v185 offset:2048
	ds_read_b128 v[6:9], v185 offset:3072
	s_add_u32 s20, s14, s16
	s_addc_u32 s21, s15, s17
	s_add_u32 s20, s20, 0x2a800100
	s_addc_u32 s21, s21, 0
	s_add_u32 s48, s31, s16
	s_addc_u32 s49, s34, s17
	s_cmpk_eq_i32 s16, 0x700
	s_cselect_b32 s23, s9, s21
	s_cselect_b32 s22, s8, s20
	s_cselect_b32 s21, s5, s49
	s_cselect_b32 s20, s4, s48
	s_mov_b32 m0, s36
	v_lshl_add_u64 v[214:215], v[170:171], 0, s[16:17]
	ds_read_b128 v[174:177], v186
	ds_read_b128 v[178:181], v186 offset:1024
	ds_read_b128 v[190:193], v186 offset:2048
	ds_read_b128 v[194:197], v186 offset:3072
	ds_read_b128 v[198:201], v186 offset:4096
	ds_read_b128 v[202:205], v186 offset:5120
	ds_read_b128 v[206:209], v186 offset:6144
	ds_read_b128 v[210:213], v186 offset:7168
	global_load_lds_dwordx4 v[214:215], off
	v_lshl_add_u64 v[214:215], v[172:173], 0, s[16:17]
	s_mov_b32 m0, s37
	s_nop 0
	global_load_lds_dwordx4 v[214:215], off
	s_waitcnt vmcnt(8)
	s_waitcnt lgkmcnt(0)
	s_barrier
	s_setprio 1
	v_mfma_f32_16x16x128_f8f6f4 v[158:161], v[26:33], v[174:181], v[158:161]
	v_mfma_f32_16x16x128_f8f6f4 v[154:157], v[18:25], v[174:181], v[154:157]
	v_mfma_f32_16x16x128_f8f6f4 v[138:141], v[18:25], v[190:197], v[138:141]
	v_mfma_f32_16x16x128_f8f6f4 v[146:149], v[26:33], v[190:197], v[146:149]
	v_mfma_f32_16x16x128_f8f6f4 v[130:133], v[26:33], v[198:205], v[130:133]
	v_mfma_f32_16x16x128_f8f6f4 v[122:125], v[18:25], v[198:205], v[122:125]
	v_mfma_f32_16x16x128_f8f6f4 v[106:109], v[18:25], v[206:213], v[106:109]
	v_mfma_f32_16x16x128_f8f6f4 v[114:117], v[26:33], v[206:213], v[114:117]
	v_mfma_f32_16x16x128_f8f6f4 v[102:105], v[10:17], v[206:213], v[102:105]
	v_mfma_f32_16x16x128_f8f6f4 v[98:101], v[2:9], v[206:213], v[98:101]
	v_mfma_f32_16x16x128_f8f6f4 v[142:145], v[2:9], v[174:181], v[142:145]
	v_mfma_f32_16x16x128_f8f6f4 v[150:153], v[10:17], v[174:181], v[150:153]
	v_mfma_f32_16x16x128_f8f6f4 v[134:137], v[10:17], v[190:197], v[134:137]
	v_mfma_f32_16x16x128_f8f6f4 v[126:129], v[2:9], v[190:197], v[126:129]
	v_mfma_f32_16x16x128_f8f6f4 v[110:113], v[2:9], v[198:205], v[110:113]
	v_mfma_f32_16x16x128_f8f6f4 v[118:121], v[10:17], v[198:205], v[118:121]
	s_setprio 0
	s_barrier
	s_mov_b32 m0, s38
	v_lshl_add_u64 v[174:175], s[20:21], 0, v[164:165]
	s_add_u32 s48, s20, 0x80000
	ds_read_b128 v[190:193], v186 offset:16384
	ds_read_b128 v[194:197], v186 offset:17408
	ds_read_b128 v[198:201], v186 offset:18432
	ds_read_b128 v[202:205], v186 offset:19456
	ds_read_b128 v[206:209], v186 offset:20480
	ds_read_b128 v[210:213], v186 offset:21504
	ds_read_b128 v[214:217], v186 offset:22528
	ds_read_b128 v[218:221], v186 offset:23552
	global_load_lds_dwordx4 v[174:175], off
	v_lshl_add_u64 v[176:177], s[20:21], 0, v[168:169]
	s_mov_b32 m0, s39
	s_addc_u32 s49, s21, 0
	global_load_lds_dwordx4 v[176:177], off
	v_lshl_add_u64 v[178:179], s[48:49], 0, v[164:165]
	s_mov_b32 m0, s40
	v_lshl_add_u64 v[180:181], s[22:23], 0, v[166:167]
	global_load_lds_dwordx4 v[178:179], off
	v_lshl_add_u64 v[178:179], s[48:49], 0, v[168:169]
	s_mov_b32 m0, s41
	s_nop 0
	global_load_lds_dwordx4 v[178:179], off
	v_lshl_add_u64 v[178:179], s[22:23], 0, v[162:163]
	s_mov_b32 m0, s24
	s_nop 0
	global_load_lds_dwordx4 v[178:179], off
	s_mov_b32 m0, s25
	s_nop 0
	global_load_lds_dwordx4 v[180:181], off
	s_waitcnt vmcnt(8)
	s_waitcnt lgkmcnt(0)
	s_barrier
	s_setprio 1
	v_mfma_f32_16x16x128_f8f6f4 v[82:85], v[26:33], v[198:205], v[82:85]
	v_mfma_f32_16x16x128_f8f6f4 v[74:77], v[18:25], v[198:205], v[74:77]
	v_mfma_f32_16x16x128_f8f6f4 v[90:93], v[18:25], v[190:197], v[90:93]
	v_mfma_f32_16x16x128_f8f6f4 v[94:97], v[26:33], v[190:197], v[94:97]
	v_mfma_f32_16x16x128_f8f6f4 v[66:69], v[26:33], v[206:213], v[66:69]
	v_mfma_f32_16x16x128_f8f6f4 v[58:61], v[18:25], v[206:213], v[58:61]
	v_mfma_f32_16x16x128_f8f6f4 v[42:45], v[18:25], v[214:221], v[42:45]
	v_mfma_f32_16x16x128_f8f6f4 v[50:53], v[26:33], v[214:221], v[50:53]
	v_mfma_f32_16x16x128_f8f6f4 v[38:41], v[10:17], v[214:221], v[38:41]
	v_mfma_f32_16x16x128_f8f6f4 v[34:37], v[2:9], v[214:221], v[34:37]
	v_mfma_f32_16x16x128_f8f6f4 v[78:81], v[2:9], v[190:197], v[78:81]
	v_mfma_f32_16x16x128_f8f6f4 v[86:89], v[10:17], v[190:197], v[86:89]
	v_mfma_f32_16x16x128_f8f6f4 v[70:73], v[10:17], v[198:205], v[70:73]
	v_mfma_f32_16x16x128_f8f6f4 v[62:65], v[2:9], v[198:205], v[62:65]
	v_mfma_f32_16x16x128_f8f6f4 v[46:49], v[2:9], v[206:213], v[46:49]
	v_mfma_f32_16x16x128_f8f6f4 v[54:57], v[10:17], v[206:213], v[54:57]
	s_setprio 0
	s_barrier
	ds_read_b128 v[2:5], v187
	ds_read_b128 v[6:9], v187 offset:1024
	ds_read_b128 v[10:13], v187 offset:2048
	ds_read_b128 v[14:17], v187 offset:3072
	ds_read_b128 v[18:21], v188
	ds_read_b128 v[22:25], v188 offset:1024
	ds_read_b128 v[26:29], v188 offset:2048
	ds_read_b128 v[30:33], v188 offset:3072
	s_add_u32 s22, s22, 0x80000
	s_addc_u32 s23, s23, 0
	s_mov_b32 m0, s26
	v_lshl_add_u64 v[222:223], s[22:23], 0, v[162:163]
	ds_read_b128 v[190:193], v186 offset:32768
	ds_read_b128 v[194:197], v186 offset:33792
	ds_read_b128 v[198:201], v186 offset:34816
	ds_read_b128 v[202:205], v186 offset:35840
	ds_read_b128 v[206:209], v186 offset:36864
	ds_read_b128 v[210:213], v186 offset:37888
	ds_read_b128 v[214:217], v186 offset:38912
	ds_read_b128 v[218:221], v186 offset:39936
	global_load_lds_dwordx4 v[222:223], off
	v_lshl_add_u64 v[222:223], s[22:23], 0, v[166:167]
	s_mov_b32 m0, s27
	s_nop 0
	global_load_lds_dwordx4 v[222:223], off
	s_waitcnt vmcnt(8)
	s_waitcnt lgkmcnt(0)
	s_barrier
	s_setprio 1
	v_mfma_f32_16x16x128_f8f6f4 v[122:125], v[10:17], v[206:213], v[122:125]
	v_mfma_f32_16x16x128_f8f6f4 v[130:133], v[2:9], v[206:213], v[130:133]
	v_mfma_f32_16x16x128_f8f6f4 v[158:161], v[2:9], v[190:197], v[158:161]
	v_mfma_f32_16x16x128_f8f6f4 v[154:157], v[10:17], v[190:197], v[154:157]
	v_mfma_f32_16x16x128_f8f6f4 v[138:141], v[10:17], v[198:205], v[138:141]
	v_mfma_f32_16x16x128_f8f6f4 v[146:149], v[2:9], v[198:205], v[146:149]
	v_mfma_f32_16x16x128_f8f6f4 v[114:117], v[2:9], v[214:221], v[114:117]
	v_mfma_f32_16x16x128_f8f6f4 v[106:109], v[10:17], v[214:221], v[106:109]
	v_mfma_f32_16x16x128_f8f6f4 v[102:105], v[18:25], v[214:221], v[102:105]
	v_mfma_f32_16x16x128_f8f6f4 v[98:101], v[26:33], v[214:221], v[98:101]
	v_mfma_f32_16x16x128_f8f6f4 v[142:145], v[26:33], v[190:197], v[142:145]
	v_mfma_f32_16x16x128_f8f6f4 v[150:153], v[18:25], v[190:197], v[150:153]
	v_mfma_f32_16x16x128_f8f6f4 v[134:137], v[18:25], v[198:205], v[134:137]
	v_mfma_f32_16x16x128_f8f6f4 v[126:129], v[26:33], v[198:205], v[126:129]
	v_mfma_f32_16x16x128_f8f6f4 v[110:113], v[26:33], v[206:213], v[110:113]
	v_mfma_f32_16x16x128_f8f6f4 v[118:121], v[18:25], v[206:213], v[118:121]
	s_setprio 0
	s_barrier
	s_mov_b32 m0, s42
	v_lshl_add_u64 v[174:175], v[174:175], 0, s[12:13]
	s_add_u32 s20, s20, 0x80080
	ds_read_b128 v[190:193], v186 offset:49152
	ds_read_b128 v[194:197], v186 offset:50176
	ds_read_b128 v[198:201], v186 offset:51200
	ds_read_b128 v[202:205], v186 offset:52224
	ds_read_b128 v[206:209], v186 offset:53248
	ds_read_b128 v[210:213], v186 offset:54272
	ds_read_b128 v[214:217], v186 offset:55296
	ds_read_b128 v[218:221], v186 offset:56320
	global_load_lds_dwordx4 v[174:175], off
	v_lshl_add_u64 v[174:175], v[176:177], 0, s[12:13]
	s_mov_b32 m0, s43
	s_addc_u32 s21, s21, 0
	global_load_lds_dwordx4 v[174:175], off
	v_lshl_add_u64 v[174:175], s[20:21], 0, v[164:165]
	s_mov_b32 m0, s44
	s_nop 0
	global_load_lds_dwordx4 v[174:175], off
	v_lshl_add_u64 v[174:175], s[20:21], 0, v[168:169]
	s_mov_b32 m0, s45
	s_nop 0
	global_load_lds_dwordx4 v[174:175], off
	v_lshl_add_u64 v[174:175], v[178:179], 0, s[12:13]
	s_mov_b32 m0, s29
	s_nop 0
	global_load_lds_dwordx4 v[174:175], off
	v_lshl_add_u64 v[174:175], v[180:181], 0, s[12:13]
	s_mov_b32 m0, s30
	s_nop 0
	global_load_lds_dwordx4 v[174:175], off
	s_waitcnt vmcnt(8)
	s_waitcnt lgkmcnt(0)
	s_barrier
	s_setprio 1
	v_mfma_f32_16x16x128_f8f6f4 v[66:69], v[2:9], v[206:213], v[66:69]
	v_mfma_f32_16x16x128_f8f6f4 v[58:61], v[10:17], v[206:213], v[58:61]
	v_mfma_f32_16x16x128_f8f6f4 v[90:93], v[10:17], v[190:197], v[90:93]
	v_mfma_f32_16x16x128_f8f6f4 v[94:97], v[2:9], v[190:197], v[94:97]
	v_mfma_f32_16x16x128_f8f6f4 v[82:85], v[2:9], v[198:205], v[82:85]
	v_mfma_f32_16x16x128_f8f6f4 v[74:77], v[10:17], v[198:205], v[74:77]
	v_mfma_f32_16x16x128_f8f6f4 v[42:45], v[10:17], v[214:221], v[42:45]
	v_mfma_f32_16x16x128_f8f6f4 v[50:53], v[2:9], v[214:221], v[50:53]
	v_mfma_f32_16x16x128_f8f6f4 v[38:41], v[18:25], v[214:221], v[38:41]
	v_mfma_f32_16x16x128_f8f6f4 v[34:37], v[26:33], v[214:221], v[34:37]
	v_mfma_f32_16x16x128_f8f6f4 v[78:81], v[26:33], v[190:197], v[78:81]
	v_mfma_f32_16x16x128_f8f6f4 v[86:89], v[18:25], v[190:197], v[86:89]
	v_mfma_f32_16x16x128_f8f6f4 v[70:73], v[18:25], v[198:205], v[70:73]
	v_mfma_f32_16x16x128_f8f6f4 v[62:65], v[26:33], v[198:205], v[62:65]
	v_mfma_f32_16x16x128_f8f6f4 v[46:49], v[26:33], v[206:213], v[46:49]
	v_mfma_f32_16x16x128_f8f6f4 v[54:57], v[18:25], v[206:213], v[54:57]
	s_setprio 0
	s_barrier
	s_add_i32 s35, s35, 2
	s_add_u32 s16, s16, 0x100
	s_addc_u32 s17, s17, 0
	s_cmp_gt_u32 s35, 13
	s_cbranch_scc0 .LBB0_1291
	s_cmpk_lt_u32 s19, 0x100
	s_cbranch_scc0 .LBB0_1294
	s_barrier

.LBB0_1309:
	ds_read_b128 v[26:29], v189
	ds_read_b128 v[30:33], v189 offset:1024
	ds_read_b128 v[18:21], v189 offset:2048
	ds_read_b128 v[22:25], v189 offset:3072
	ds_read_b128 v[10:13], v190
	ds_read_b128 v[14:17], v190 offset:1024
	ds_read_b128 v[2:5], v190 offset:2048
	ds_read_b128 v[6:9], v190 offset:3072
	s_add_u32 s40, s38, 0xfff80080
	s_addc_u32 s41, s39, -1
	s_cmp_eq_u32 s72, 28
	s_cselect_b32 s43, s18, s41
	s_cselect_b32 s42, s19, s40
	s_cselect_b32 s41, s27, s71
	s_cselect_b32 s40, s29, s70
	v_lshl_add_u64 v[216:217], s[38:39], 0, v[170:171]
	s_add_i32 m0, s37, 0xc000
	ds_read_b128 v[178:181], v191
	ds_read_b128 v[182:185], v191 offset:1024
	ds_read_b128 v[192:195], v191 offset:2048
	ds_read_b128 v[196:199], v191 offset:3072
	ds_read_b128 v[200:203], v191 offset:4096
	ds_read_b128 v[204:207], v191 offset:5120
	ds_read_b128 v[208:211], v191 offset:6144
	ds_read_b128 v[212:215], v191 offset:7168
	global_load_lds_dwordx4 v[216:217], off
	v_lshl_add_u64 v[216:217], s[38:39], 0, v[172:173]
	s_add_i32 m0, s37, 0xe000
	s_nop 0
	global_load_lds_dwordx4 v[216:217], off
	s_waitcnt vmcnt(8)
	s_waitcnt lgkmcnt(0)
	s_barrier
	s_setprio 1
	v_mfma_f32_16x16x128_f8f6f4 v[158:161], v[26:33], v[178:185], v[158:161]
	v_mfma_f32_16x16x128_f8f6f4 v[154:157], v[18:25], v[178:185], v[154:157]
	v_mfma_f32_16x16x128_f8f6f4 v[138:141], v[18:25], v[192:199], v[138:141]
	v_mfma_f32_16x16x128_f8f6f4 v[146:149], v[26:33], v[192:199], v[146:149]
	v_mfma_f32_16x16x128_f8f6f4 v[130:133], v[26:33], v[200:207], v[130:133]
	v_mfma_f32_16x16x128_f8f6f4 v[122:125], v[18:25], v[200:207], v[122:125]
	v_mfma_f32_16x16x128_f8f6f4 v[106:109], v[18:25], v[208:215], v[106:109]
	v_mfma_f32_16x16x128_f8f6f4 v[114:117], v[26:33], v[208:215], v[114:117]
	v_mfma_f32_16x16x128_f8f6f4 v[102:105], v[10:17], v[208:215], v[102:105]
	v_mfma_f32_16x16x128_f8f6f4 v[98:101], v[2:9], v[208:215], v[98:101]
	v_mfma_f32_16x16x128_f8f6f4 v[142:145], v[2:9], v[178:185], v[142:145]
	v_mfma_f32_16x16x128_f8f6f4 v[150:153], v[10:17], v[178:185], v[150:153]
	v_mfma_f32_16x16x128_f8f6f4 v[134:137], v[10:17], v[192:199], v[134:137]
	v_mfma_f32_16x16x128_f8f6f4 v[126:129], v[2:9], v[192:199], v[126:129]
	v_mfma_f32_16x16x128_f8f6f4 v[110:113], v[2:9], v[200:207], v[110:113]
	v_mfma_f32_16x16x128_f8f6f4 v[118:121], v[10:17], v[200:207], v[118:121]
	s_setprio 0
	s_barrier
	s_add_i32 s64, s59, s3
	v_lshl_add_u64 v[178:179], s[40:41], 0, v[166:167]
	s_mov_b32 m0, s64
	ds_read_b128 v[192:195], v191 offset:16384
	ds_read_b128 v[196:199], v191 offset:17408
	ds_read_b128 v[200:203], v191 offset:18432
	ds_read_b128 v[204:207], v191 offset:19456
	ds_read_b128 v[208:211], v191 offset:20480
	ds_read_b128 v[212:215], v191 offset:21504
	ds_read_b128 v[216:219], v191 offset:22528
	ds_read_b128 v[220:223], v191 offset:23552
	global_load_lds_dwordx4 v[178:179], off
	s_add_i32 m0, s64, 0x2000
	s_add_u32 s64, s40, 0x80000
	v_lshl_add_u64 v[180:181], s[40:41], 0, v[162:163]
	s_addc_u32 s65, s41, 0
	s_add_i32 s73, s62, s3
	global_load_lds_dwordx4 v[180:181], off
	v_lshl_add_u64 v[182:183], s[64:65], 0, v[166:167]
	s_mov_b32 m0, s73
	v_lshl_add_u64 v[184:185], s[42:43], 0, v[164:165]
	global_load_lds_dwordx4 v[182:183], off
	v_lshl_add_u64 v[182:183], s[64:65], 0, v[162:163]
	s_add_i32 m0, s73, 0x2000
	s_nop 0
	global_load_lds_dwordx4 v[182:183], off
	v_lshl_add_u64 v[182:183], s[42:43], 0, v[168:169]
	s_mov_b32 m0, s37
	s_nop 0
	global_load_lds_dwordx4 v[182:183], off
	s_mov_b32 m0, s44
	s_nop 0
	global_load_lds_dwordx4 v[184:185], off
	s_waitcnt vmcnt(8)
	s_waitcnt lgkmcnt(0)
	s_barrier
	s_setprio 1
	v_mfma_f32_16x16x128_f8f6f4 v[82:85], v[26:33], v[200:207], v[82:85]
	v_mfma_f32_16x16x128_f8f6f4 v[74:77], v[18:25], v[200:207], v[74:77]
	v_mfma_f32_16x16x128_f8f6f4 v[90:93], v[18:25], v[192:199], v[90:93]
	v_mfma_f32_16x16x128_f8f6f4 v[94:97], v[26:33], v[192:199], v[94:97]
	v_mfma_f32_16x16x128_f8f6f4 v[66:69], v[26:33], v[208:215], v[66:69]
	v_mfma_f32_16x16x128_f8f6f4 v[58:61], v[18:25], v[208:215], v[58:61]
	v_mfma_f32_16x16x128_f8f6f4 v[42:45], v[18:25], v[216:223], v[42:45]
	v_mfma_f32_16x16x128_f8f6f4 v[50:53], v[26:33], v[216:223], v[50:53]
	v_mfma_f32_16x16x128_f8f6f4 v[38:41], v[10:17], v[216:223], v[38:41]
	v_mfma_f32_16x16x128_f8f6f4 v[34:37], v[2:9], v[216:223], v[34:37]
	v_mfma_f32_16x16x128_f8f6f4 v[78:81], v[2:9], v[192:199], v[78:81]
	v_mfma_f32_16x16x128_f8f6f4 v[86:89], v[10:17], v[192:199], v[86:89]
	v_mfma_f32_16x16x128_f8f6f4 v[70:73], v[10:17], v[200:207], v[70:73]
	v_mfma_f32_16x16x128_f8f6f4 v[62:65], v[2:9], v[200:207], v[62:65]
	v_mfma_f32_16x16x128_f8f6f4 v[46:49], v[2:9], v[208:215], v[46:49]
	v_mfma_f32_16x16x128_f8f6f4 v[54:57], v[10:17], v[208:215], v[54:57]
	s_setprio 0
	s_barrier
	s_add_i32 s64, 0, 0x18000
	s_add_i32 s65, 0, 0x1c000
	v_add_u32_e32 v14, s64, v187
	v_add_u32_e32 v30, s65, v187
	ds_read_b128 v[2:5], v14
	ds_read_b128 v[6:9], v14 offset:1024
	ds_read_b128 v[10:13], v14 offset:2048
	ds_read_b128 v[14:17], v14 offset:3072
	ds_read_b128 v[18:21], v30
	ds_read_b128 v[22:25], v30 offset:1024
	ds_read_b128 v[26:29], v30 offset:2048
	ds_read_b128 v[30:33], v30 offset:3072
	s_add_u32 s42, s42, 0x80000
	s_addc_u32 s43, s43, 0
	s_mov_b32 m0, s45
	v_lshl_add_u64 v[224:225], s[42:43], 0, v[168:169]
	ds_read_b128 v[192:195], v191 offset:32768
	ds_read_b128 v[196:199], v191 offset:33792
	ds_read_b128 v[200:203], v191 offset:34816
	ds_read_b128 v[204:207], v191 offset:35840
	ds_read_b128 v[208:211], v191 offset:36864
	ds_read_b128 v[212:215], v191 offset:37888
	ds_read_b128 v[216:219], v191 offset:38912
	ds_read_b128 v[220:223], v191 offset:39936
	global_load_lds_dwordx4 v[224:225], off
	v_lshl_add_u64 v[224:225], s[42:43], 0, v[164:165]
	s_mov_b32 m0, s48
	s_nop 0
	global_load_lds_dwordx4 v[224:225], off
	s_waitcnt vmcnt(8)
	s_waitcnt lgkmcnt(0)
	s_barrier
	s_setprio 1
	v_mfma_f32_16x16x128_f8f6f4 v[122:125], v[10:17], v[208:215], v[122:125]
	v_mfma_f32_16x16x128_f8f6f4 v[130:133], v[2:9], v[208:215], v[130:133]
	v_mfma_f32_16x16x128_f8f6f4 v[158:161], v[2:9], v[192:199], v[158:161]
	v_mfma_f32_16x16x128_f8f6f4 v[154:157], v[10:17], v[192:199], v[154:157]
	v_mfma_f32_16x16x128_f8f6f4 v[138:141], v[10:17], v[200:207], v[138:141]
	v_mfma_f32_16x16x128_f8f6f4 v[146:149], v[2:9], v[200:207], v[146:149]
	v_mfma_f32_16x16x128_f8f6f4 v[114:117], v[2:9], v[216:223], v[114:117]
	v_mfma_f32_16x16x128_f8f6f4 v[106:109], v[10:17], v[216:223], v[106:109]
	v_mfma_f32_16x16x128_f8f6f4 v[102:105], v[18:25], v[216:223], v[102:105]
	v_mfma_f32_16x16x128_f8f6f4 v[98:101], v[26:33], v[216:223], v[98:101]
	v_mfma_f32_16x16x128_f8f6f4 v[142:145], v[26:33], v[192:199], v[142:145]
	v_mfma_f32_16x16x128_f8f6f4 v[150:153], v[18:25], v[192:199], v[150:153]
	v_mfma_f32_16x16x128_f8f6f4 v[134:137], v[18:25], v[200:207], v[134:137]
	v_mfma_f32_16x16x128_f8f6f4 v[126:129], v[26:33], v[200:207], v[126:129]
	v_mfma_f32_16x16x128_f8f6f4 v[110:113], v[26:33], v[208:215], v[110:113]
	v_mfma_f32_16x16x128_f8f6f4 v[118:121], v[18:25], v[208:215], v[118:121]
	s_setprio 0
	s_barrier
	s_add_i32 s42, s64, s3
	v_lshl_add_u64 v[178:179], v[178:179], 0, s[12:13]
	s_mov_b32 m0, s42
	ds_read_b128 v[192:195], v191 offset:49152
	ds_read_b128 v[196:199], v191 offset:50176
	ds_read_b128 v[200:203], v191 offset:51200
	ds_read_b128 v[204:207], v191 offset:52224
	ds_read_b128 v[208:211], v191 offset:53248
	ds_read_b128 v[212:215], v191 offset:54272
	ds_read_b128 v[216:219], v191 offset:55296
	ds_read_b128 v[220:223], v191 offset:56320
	global_load_lds_dwordx4 v[178:179], off
	s_add_i32 m0, s42, 0x2000
	s_add_u32 s40, s40, 0x80080
	v_lshl_add_u64 v[178:179], v[180:181], 0, s[12:13]
	s_addc_u32 s41, s41, 0
	s_add_i32 s42, s65, s3
	global_load_lds_dwordx4 v[178:179], off
	v_lshl_add_u64 v[178:179], s[40:41], 0, v[166:167]
	s_mov_b32 m0, s42
	s_nop 0
	global_load_lds_dwordx4 v[178:179], off
	v_lshl_add_u64 v[178:179], s[40:41], 0, v[162:163]
	s_add_i32 m0, s42, 0x2000
	s_nop 0
	global_load_lds_dwordx4 v[178:179], off
	v_lshl_add_u64 v[178:179], v[182:183], 0, s[12:13]
	s_mov_b32 m0, s51
	s_nop 0
	global_load_lds_dwordx4 v[178:179], off
	v_lshl_add_u64 v[178:179], v[184:185], 0, s[12:13]
	s_mov_b32 m0, s58
	s_nop 0
	global_load_lds_dwordx4 v[178:179], off
	s_waitcnt vmcnt(8)
	s_waitcnt lgkmcnt(0)
	s_barrier
	s_setprio 1
	v_mfma_f32_16x16x128_f8f6f4 v[66:69], v[2:9], v[208:215], v[66:69]
	v_mfma_f32_16x16x128_f8f6f4 v[58:61], v[10:17], v[208:215], v[58:61]
	v_mfma_f32_16x16x128_f8f6f4 v[90:93], v[10:17], v[192:199], v[90:93]
	v_mfma_f32_16x16x128_f8f6f4 v[94:97], v[2:9], v[192:199], v[94:97]
	v_mfma_f32_16x16x128_f8f6f4 v[82:85], v[2:9], v[200:207], v[82:85]
	v_mfma_f32_16x16x128_f8f6f4 v[74:77], v[10:17], v[200:207], v[74:77]
	v_mfma_f32_16x16x128_f8f6f4 v[42:45], v[10:17], v[216:223], v[42:45]
	v_mfma_f32_16x16x128_f8f6f4 v[50:53], v[2:9], v[216:223], v[50:53]
	v_mfma_f32_16x16x128_f8f6f4 v[38:41], v[18:25], v[216:223], v[38:41]
	v_mfma_f32_16x16x128_f8f6f4 v[34:37], v[26:33], v[216:223], v[34:37]
	v_mfma_f32_16x16x128_f8f6f4 v[78:81], v[26:33], v[192:199], v[78:81]
	v_mfma_f32_16x16x128_f8f6f4 v[86:89], v[18:25], v[192:199], v[86:89]
	v_mfma_f32_16x16x128_f8f6f4 v[70:73], v[18:25], v[200:207], v[70:73]
	v_mfma_f32_16x16x128_f8f6f4 v[62:65], v[26:33], v[200:207], v[62:65]
	v_mfma_f32_16x16x128_f8f6f4 v[46:49], v[26:33], v[208:215], v[46:49]
	v_mfma_f32_16x16x128_f8f6f4 v[54:57], v[18:25], v[208:215], v[54:57]
	s_setprio 0
	s_barrier
	s_add_i32 s72, s72, 2
	s_add_u32 s38, s38, 0x100
	s_addc_u32 s39, s39, 0
	s_add_u32 s70, s70, 0x100
	s_addc_u32 s71, s71, 0
	s_cmp_gt_u32 s72, 29
	s_cbranch_scc0 .LBB0_1309
	s_and_b64 vcc, exec, s[14:15]
	s_cbranch_vccz .LBB0_1312
	s_barrier

.LBB0_1437:
	v_and_b32_e32 v188, 15, v189
	v_and_b32_e32 v2, 48, v189
	v_lshlrev_b32_e32 v3, 2, v189
	s_and_b32 s8, s6, 3
	s_lshl_b32 s9, s7, 13
	v_lshl_or_b32 v2, v188, 6, v2
	v_and_b32_e32 v3, 32, v3
	v_bitop3_b32 v4, v2, s9, v3 bitop3:0xde
	s_lshl_b32 s9, s8, 12
	v_lshl_add_u64 v[180:181], s[20:21], 0, v[154:155]
	v_bitop3_b32 v2, v2, s9, v3 bitop3:0xde
	s_add_i32 s9, s60, s72
	v_lshl_add_u64 v[178:179], s[20:21], 0, v[182:183]
	v_lshl_add_u64 v[72:73], v[180:181], 0, s[36:37]
	s_mov_b32 m0, s9
	s_add_i32 s19, s9, 0x2000
	s_waitcnt vmcnt(2)
	s_barrier
	global_load_lds_dwordx4 v[72:73], off
	v_lshl_add_u64 v[158:159], v[178:179], 0, s[36:37]
	s_mov_b32 m0, s19
	s_add_i32 s18, s67, 0x8000
	global_load_lds_dwordx4 v[158:159], off
	v_lshl_add_u64 v[70:71], v[172:173], 0, s[36:37]
	s_mov_b32 m0, s18
	s_add_i32 s43, s67, 0xa000
	global_load_lds_dwordx4 v[70:71], off
	v_lshl_add_u64 v[160:161], v[170:171], 0, s[36:37]
	s_mov_b32 m0, s43
	s_add_i32 s44, s61, s72
	global_load_lds_dwordx4 v[160:161], off
	v_lshl_add_u64 v[162:163], s[24:25], 0, v[154:155]
	s_mov_b32 m0, s44
	s_add_i32 s45, s44, 0x2000
	global_load_lds_dwordx4 v[162:163], off
	v_lshl_add_u64 v[164:165], s[24:25], 0, v[182:183]
	s_mov_b32 m0, s45
	s_add_i32 s73, 0, 0x10000
	global_load_lds_dwordx4 v[164:165], off
	v_add_u32_e32 v195, s73, v2
	s_add_i32 s75, 0, 0x14000
	s_waitcnt vmcnt(6)
	s_barrier
	v_add_u32_e32 v194, s75, v2
	v_add_u32_e32 v191, 0, v4
	v_add_u32_e32 v193, s60, v2
	v_add_u32_e32 v192, s61, v2
	ds_read_b128 v[54:57], v195
	ds_read_b128 v[58:61], v195 offset:1024
	ds_read_b128 v[196:199], v195 offset:2048
	ds_read_b128 v[200:203], v195 offset:3072
	ds_read_b128 v[10:13], v194
	ds_read_b128 v[14:17], v194 offset:1024
	ds_read_b128 v[2:5], v194 offset:2048
	ds_read_b128 v[6:9], v194 offset:3072
	s_lshl_b32 s66, s7, 6
	v_lshl_add_u64 v[176:177], s[22:23], 0, v[154:155]
	v_lshl_add_u64 v[174:175], s[22:23], 0, v[182:183]
	s_add_u32 s70, s4, 0x10080
	s_addc_u32 s71, s5, 0
	s_add_i32 s74, s67, 0xc000
	v_lshl_add_u64 v[30:31], s[70:71], 0, v[154:155]
	s_mov_b32 m0, s74
	s_add_i32 s69, s67, 0xe000
	ds_read_b128 v[22:25], v191
	ds_read_b128 v[26:29], v191 offset:1024
	ds_read_b128 v[34:37], v191 offset:2048
	ds_read_b128 v[38:41], v191 offset:3072
	ds_read_b128 v[82:85], v191 offset:4096
	ds_read_b128 v[86:89], v191 offset:5120
	ds_read_b128 v[94:97], v191 offset:6144
	ds_read_b128 v[98:101], v191 offset:7168
	global_load_lds_dwordx4 v[30:31], off
	v_lshl_add_u64 v[30:31], s[70:71], 0, v[182:183]
	s_mov_b32 m0, s69
	s_nop 0
	global_load_lds_dwordx4 v[30:31], off
	s_waitcnt vmcnt(8)
	s_waitcnt lgkmcnt(0)
	s_barrier
	s_setprio 1
	v_mov_b64_e32 v[32:33], v[20:21]
	v_mov_b64_e32 v[152:153], v[20:21]
	v_mov_b64_e32 v[92:93], v[20:21]
	v_mov_b64_e32 v[44:45], v[20:21]
	v_mov_b64_e32 v[116:117], v[20:21]
	v_mov_b64_e32 v[64:65], v[20:21]
	v_mov_b64_e32 v[80:81], v[20:21]
	v_mov_b64_e32 v[52:53], v[20:21]
	v_mov_b64_e32 v[30:31], v[18:19]
	v_mov_b64_e32 v[150:151], v[18:19]
	v_mov_b64_e32 v[90:91], v[18:19]
	v_mov_b64_e32 v[42:43], v[18:19]
	v_mov_b64_e32 v[114:115], v[18:19]
	v_mov_b64_e32 v[62:63], v[18:19]
	v_mov_b64_e32 v[78:79], v[18:19]
	v_mov_b64_e32 v[50:51], v[18:19]
	s_waitcnt lgkmcnt(0)
	v_mfma_f32_16x16x128_f8f6f4 v[30:33], v[54:61], v[22:29], v[30:33]
	v_mfma_f32_16x16x128_f8f6f4 v[150:153], v[196:203], v[22:29], v[150:153]
	v_mfma_f32_16x16x128_f8f6f4 v[42:45], v[196:203], v[34:41], v[42:45]
	v_mfma_f32_16x16x128_f8f6f4 v[90:93], v[54:61], v[34:41], v[90:93]
	v_mfma_f32_16x16x128_f8f6f4 v[114:117], v[54:61], v[82:89], v[114:117]
	v_mfma_f32_16x16x128_f8f6f4 v[62:65], v[196:203], v[82:89], v[62:65]
	v_mfma_f32_16x16x128_f8f6f4 v[50:53], v[196:203], v[94:101], v[50:53]
	v_mfma_f32_16x16x128_f8f6f4 v[78:81], v[54:61], v[94:101], v[78:81]
	v_mov_b64_e32 v[144:145], v[20:21]
	v_mov_b64_e32 v[148:149], v[20:21]
	v_mov_b64_e32 v[142:143], v[18:19]
	v_mov_b64_e32 v[146:147], v[18:19]
	v_mfma_f32_16x16x128_f8f6f4 v[142:145], v[10:17], v[22:29], v[142:145]
	v_mfma_f32_16x16x128_f8f6f4 v[146:149], v[2:9], v[22:29], v[146:149]
	v_mov_b64_e32 v[28:29], v[20:21]
	v_mov_b64_e32 v[140:141], v[20:21]
	v_mov_b64_e32 v[26:27], v[18:19]
	v_mov_b64_e32 v[138:139], v[18:19]
	v_mfma_f32_16x16x128_f8f6f4 v[26:29], v[10:17], v[34:41], v[26:29]
	v_mfma_f32_16x16x128_f8f6f4 v[138:141], v[2:9], v[34:41], v[138:141]
	v_mov_b64_e32 v[40:41], v[20:21]
	v_mov_b64_e32 v[128:129], v[20:21]
	v_mov_b64_e32 v[24:25], v[20:21]
	v_mov_b64_e32 v[76:77], v[20:21]
	v_mov_b64_e32 v[38:39], v[18:19]
	v_mov_b64_e32 v[126:127], v[18:19]
	v_mov_b64_e32 v[22:23], v[18:19]
	v_mov_b64_e32 v[74:75], v[18:19]
	v_mfma_f32_16x16x128_f8f6f4 v[38:41], v[10:17], v[82:89], v[38:41]
	v_mfma_f32_16x16x128_f8f6f4 v[126:129], v[2:9], v[82:89], v[126:129]
	v_mfma_f32_16x16x128_f8f6f4 v[22:25], v[10:17], v[94:101], v[22:25]
	v_mfma_f32_16x16x128_f8f6f4 v[74:77], v[2:9], v[94:101], v[74:77]
	s_setprio 0
	s_barrier
	s_add_i32 s70, s73, s72
	v_lshl_add_u64 v[34:35], v[180:181], 0, s[14:15]
	s_mov_b32 m0, s70
	s_add_i32 s71, s70, 0x2000
	ds_read_b128 v[204:207], v191 offset:16384
	ds_read_b128 v[208:211], v191 offset:17408
	ds_read_b128 v[212:215], v191 offset:18432
	ds_read_b128 v[216:219], v191 offset:19456
	ds_read_b128 v[220:223], v191 offset:20480
	ds_read_b128 v[224:227], v191 offset:21504
	ds_read_b128 v[228:231], v191 offset:22528
	ds_read_b128 v[232:235], v191 offset:23552
	global_load_lds_dwordx4 v[34:35], off
	v_lshl_add_u64 v[34:35], v[178:179], 0, s[14:15]
	s_mov_b32 m0, s71
	s_add_i32 s72, s75, s72
	global_load_lds_dwordx4 v[34:35], off
	v_lshl_add_u64 v[34:35], s[26:27], 0, v[154:155]
	s_mov_b32 m0, s72
	s_add_i32 s73, s72, 0x2000
	global_load_lds_dwordx4 v[34:35], off
	v_lshl_add_u64 v[34:35], s[26:27], 0, v[182:183]
	s_mov_b32 m0, s73
	s_nop 0
	global_load_lds_dwordx4 v[34:35], off
	v_lshl_add_u64 v[34:35], v[172:173], 0, s[14:15]
	s_mov_b32 m0, s67
	s_nop 0
	global_load_lds_dwordx4 v[34:35], off
	v_lshl_add_u64 v[34:35], v[170:171], 0, s[14:15]
	s_mov_b32 m0, s68
	s_nop 0
	global_load_lds_dwordx4 v[34:35], off
	s_waitcnt vmcnt(8)
	s_waitcnt lgkmcnt(0)
	s_barrier
	s_setprio 1
	v_mov_b64_e32 v[136:137], v[20:21]
	v_mov_b64_e32 v[104:105], v[20:21]
	v_mov_b64_e32 v[124:125], v[20:21]
	v_mov_b64_e32 v[100:101], v[20:21]
	v_mov_b64_e32 v[112:113], v[20:21]
	v_mov_b64_e32 v[108:109], v[20:21]
	v_mov_b64_e32 v[88:89], v[20:21]
	v_mov_b64_e32 v[84:85], v[20:21]
	v_mov_b64_e32 v[134:135], v[18:19]
	v_mov_b64_e32 v[102:103], v[18:19]
	v_mov_b64_e32 v[122:123], v[18:19]
	v_mov_b64_e32 v[98:99], v[18:19]
	v_mov_b64_e32 v[110:111], v[18:19]
	v_mov_b64_e32 v[106:107], v[18:19]
	v_mov_b64_e32 v[86:87], v[18:19]
	v_mov_b64_e32 v[82:83], v[18:19]
	s_waitcnt lgkmcnt(0)
	v_mfma_f32_16x16x128_f8f6f4 v[134:137], v[54:61], v[204:211], v[134:137]
	v_mfma_f32_16x16x128_f8f6f4 v[102:105], v[196:203], v[204:211], v[102:105]
	v_mfma_f32_16x16x128_f8f6f4 v[98:101], v[196:203], v[212:219], v[98:101]
	v_mfma_f32_16x16x128_f8f6f4 v[122:125], v[54:61], v[212:219], v[122:125]
	v_mfma_f32_16x16x128_f8f6f4 v[110:113], v[54:61], v[220:227], v[110:113]
	v_mfma_f32_16x16x128_f8f6f4 v[106:109], v[196:203], v[220:227], v[106:109]
	v_mfma_f32_16x16x128_f8f6f4 v[82:85], v[196:203], v[228:235], v[82:85]
	v_mfma_f32_16x16x128_f8f6f4 v[86:89], v[54:61], v[228:235], v[86:89]
	v_mov_b64_e32 v[36:37], v[20:21]
	v_mov_b64_e32 v[132:133], v[20:21]
	v_mov_b64_e32 v[48:49], v[20:21]
	v_mov_b64_e32 v[120:121], v[20:21]
	v_mov_b64_e32 v[68:69], v[20:21]
	v_mov_b64_e32 v[96:97], v[20:21]
	v_mov_b64_e32 v[56:57], v[20:21]
	v_mov_b64_e32 v[60:61], v[20:21]
	v_mov_b64_e32 v[34:35], v[18:19]
	v_mov_b64_e32 v[130:131], v[18:19]
	v_mov_b64_e32 v[46:47], v[18:19]
	v_mov_b64_e32 v[118:119], v[18:19]
	v_mov_b64_e32 v[66:67], v[18:19]
	v_mov_b64_e32 v[94:95], v[18:19]
	v_mov_b64_e32 v[54:55], v[18:19]
	v_mov_b64_e32 v[58:59], v[18:19]
	v_mfma_f32_16x16x128_f8f6f4 v[54:57], v[10:17], v[228:235], v[54:57]
	v_mfma_f32_16x16x128_f8f6f4 v[58:61], v[2:9], v[228:235], v[58:61]
	v_mfma_f32_16x16x128_f8f6f4 v[130:133], v[2:9], v[204:211], v[130:133]
	v_mfma_f32_16x16x128_f8f6f4 v[34:37], v[10:17], v[204:211], v[34:37]
	v_mfma_f32_16x16x128_f8f6f4 v[46:49], v[10:17], v[212:219], v[46:49]
	v_mfma_f32_16x16x128_f8f6f4 v[118:121], v[2:9], v[212:219], v[118:121]
	v_mfma_f32_16x16x128_f8f6f4 v[94:97], v[2:9], v[220:227], v[94:97]
	v_mfma_f32_16x16x128_f8f6f4 v[66:69], v[10:17], v[220:227], v[66:69]
	s_setprio 0
	s_barrier
	ds_read_b128 v[2:5], v193
	ds_read_b128 v[6:9], v193 offset:1024
	ds_read_b128 v[10:13], v193 offset:2048
	ds_read_b128 v[14:17], v193 offset:3072
	ds_read_b128 v[196:199], v192
	ds_read_b128 v[200:203], v192 offset:1024
	ds_read_b128 v[204:207], v192 offset:2048
	ds_read_b128 v[208:211], v192 offset:3072
	s_add_u32 s76, s4, 0x10100
	s_addc_u32 s77, s5, 0
	s_mov_b32 m0, s48
	v_lshl_add_u64 v[244:245], s[76:77], 0, v[154:155]
	ds_read_b128 v[212:215], v191 offset:32768
	ds_read_b128 v[216:219], v191 offset:33792
	ds_read_b128 v[220:223], v191 offset:34816
	ds_read_b128 v[224:227], v191 offset:35840
	ds_read_b128 v[228:231], v191 offset:36864
	ds_read_b128 v[232:235], v191 offset:37888
	ds_read_b128 v[236:239], v191 offset:38912
	ds_read_b128 v[240:243], v191 offset:39936
	global_load_lds_dwordx4 v[244:245], off
	v_lshl_add_u64 v[244:245], s[76:77], 0, v[182:183]
	s_mov_b32 m0, s49
	s_nop 0
	global_load_lds_dwordx4 v[244:245], off
	s_waitcnt vmcnt(8)
	s_waitcnt lgkmcnt(0)
	s_barrier
	s_setprio 1
	v_mfma_f32_16x16x128_f8f6f4 v[42:45], v[10:17], v[220:227], v[42:45]
	v_mfma_f32_16x16x128_f8f6f4 v[90:93], v[2:9], v[220:227], v[90:93]
	v_mfma_f32_16x16x128_f8f6f4 v[30:33], v[2:9], v[212:219], v[30:33]
	v_mfma_f32_16x16x128_f8f6f4 v[150:153], v[10:17], v[212:219], v[150:153]
	v_mfma_f32_16x16x128_f8f6f4 v[62:65], v[10:17], v[228:235], v[62:65]
	v_mfma_f32_16x16x128_f8f6f4 v[114:117], v[2:9], v[228:235], v[114:117]
	v_mfma_f32_16x16x128_f8f6f4 v[78:81], v[2:9], v[236:243], v[78:81]
	v_mfma_f32_16x16x128_f8f6f4 v[50:53], v[10:17], v[236:243], v[50:53]
	v_mfma_f32_16x16x128_f8f6f4 v[22:25], v[196:203], v[236:243], v[22:25]
	v_mfma_f32_16x16x128_f8f6f4 v[74:77], v[204:211], v[236:243], v[74:77]
	v_mfma_f32_16x16x128_f8f6f4 v[146:149], v[204:211], v[212:219], v[146:149]
	v_mfma_f32_16x16x128_f8f6f4 v[142:145], v[196:203], v[212:219], v[142:145]
	v_mfma_f32_16x16x128_f8f6f4 v[26:29], v[196:203], v[220:227], v[26:29]
	v_mfma_f32_16x16x128_f8f6f4 v[138:141], v[204:211], v[220:227], v[138:141]
	v_mfma_f32_16x16x128_f8f6f4 v[126:129], v[204:211], v[228:235], v[126:129]
	v_mfma_f32_16x16x128_f8f6f4 v[38:41], v[196:203], v[228:235], v[38:41]
	s_setprio 0
	s_barrier
	s_mov_b32 m0, s9
	v_lshl_add_u64 v[244:245], v[180:181], 0, s[38:39]
	ds_read_b128 v[212:215], v191 offset:49152
	ds_read_b128 v[216:219], v191 offset:50176
	ds_read_b128 v[220:223], v191 offset:51200
	ds_read_b128 v[224:227], v191 offset:52224
	ds_read_b128 v[228:231], v191 offset:53248
	ds_read_b128 v[232:235], v191 offset:54272
	ds_read_b128 v[236:239], v191 offset:55296
	ds_read_b128 v[240:243], v191 offset:56320
	global_load_lds_dwordx4 v[244:245], off
	v_lshl_add_u64 v[244:245], v[178:179], 0, s[38:39]
	s_mov_b32 m0, s19
	s_nop 0
	global_load_lds_dwordx4 v[244:245], off
	v_lshl_add_u64 v[244:245], s[28:29], 0, v[154:155]
	s_mov_b32 m0, s44
	s_nop 0
	global_load_lds_dwordx4 v[244:245], off
	v_lshl_add_u64 v[244:245], s[28:29], 0, v[182:183]
	s_mov_b32 m0, s45
	s_nop 0
	global_load_lds_dwordx4 v[244:245], off
	v_lshl_add_u64 v[244:245], v[172:173], 0, s[38:39]
	s_mov_b32 m0, s18
	s_nop 0
	global_load_lds_dwordx4 v[244:245], off
	v_lshl_add_u64 v[244:245], v[170:171], 0, s[38:39]
	s_mov_b32 m0, s43
	s_nop 0
	global_load_lds_dwordx4 v[244:245], off
	s_waitcnt vmcnt(8)
	s_waitcnt lgkmcnt(0)
	s_barrier
	s_setprio 1
	v_mfma_f32_16x16x128_f8f6f4 v[110:113], v[2:9], v[228:235], v[110:113]
	v_mfma_f32_16x16x128_f8f6f4 v[106:109], v[10:17], v[228:235], v[106:109]
	v_mfma_f32_16x16x128_f8f6f4 v[102:105], v[10:17], v[212:219], v[102:105]
	v_mfma_f32_16x16x128_f8f6f4 v[134:137], v[2:9], v[212:219], v[134:137]
	v_mfma_f32_16x16x128_f8f6f4 v[122:125], v[2:9], v[220:227], v[122:125]
	v_mfma_f32_16x16x128_f8f6f4 v[98:101], v[10:17], v[220:227], v[98:101]
	v_mfma_f32_16x16x128_f8f6f4 v[82:85], v[10:17], v[236:243], v[82:85]
	v_mfma_f32_16x16x128_f8f6f4 v[86:89], v[2:9], v[236:243], v[86:89]
	v_mfma_f32_16x16x128_f8f6f4 v[54:57], v[196:203], v[236:243], v[54:57]
	v_mfma_f32_16x16x128_f8f6f4 v[58:61], v[204:211], v[236:243], v[58:61]
	v_mfma_f32_16x16x128_f8f6f4 v[130:133], v[204:211], v[212:219], v[130:133]
	v_mfma_f32_16x16x128_f8f6f4 v[34:37], v[196:203], v[212:219], v[34:37]
	v_mfma_f32_16x16x128_f8f6f4 v[46:49], v[196:203], v[220:227], v[46:49]
	v_mfma_f32_16x16x128_f8f6f4 v[118:121], v[204:211], v[220:227], v[118:121]
	v_mfma_f32_16x16x128_f8f6f4 v[94:97], v[204:211], v[228:235], v[94:97]
	v_mfma_f32_16x16x128_f8f6f4 v[66:69], v[196:203], v[228:235], v[66:69]
	s_setprio 0
	s_barrier
	ds_read_b128 v[2:5], v195
	ds_read_b128 v[6:9], v195 offset:1024
	ds_read_b128 v[10:13], v195 offset:2048
	ds_read_b128 v[14:17], v195 offset:3072
	ds_read_b128 v[196:199], v194
	ds_read_b128 v[200:203], v194 offset:1024
	ds_read_b128 v[204:207], v194 offset:2048
	ds_read_b128 v[208:211], v194 offset:3072
	s_add_u32 s4, s4, 0x10180
	s_addc_u32 s5, s5, 0
	s_mov_b32 m0, s74
	v_lshl_add_u64 v[194:195], s[4:5], 0, v[154:155]
	ds_read_b128 v[212:215], v191
	ds_read_b128 v[216:219], v191 offset:1024
	ds_read_b128 v[220:223], v191 offset:2048
	ds_read_b128 v[224:227], v191 offset:3072
	ds_read_b128 v[228:231], v191 offset:4096
	ds_read_b128 v[232:235], v191 offset:5120
	ds_read_b128 v[236:239], v191 offset:6144
	ds_read_b128 v[240:243], v191 offset:7168
	global_load_lds_dwordx4 v[194:195], off
	v_lshl_add_u64 v[182:183], s[4:5], 0, v[182:183]
	s_mov_b32 m0, s69
	s_nop 0
	global_load_lds_dwordx4 v[182:183], off
	s_waitcnt vmcnt(8)
	s_waitcnt lgkmcnt(0)
	s_barrier
	s_setprio 1
	v_mfma_f32_16x16x128_f8f6f4 v[114:117], v[2:9], v[228:235], v[114:117]
	v_mfma_f32_16x16x128_f8f6f4 v[62:65], v[10:17], v[228:235], v[62:65]
	v_mfma_f32_16x16x128_f8f6f4 v[150:153], v[10:17], v[212:219], v[150:153]
	v_mfma_f32_16x16x128_f8f6f4 v[30:33], v[2:9], v[212:219], v[30:33]
	v_mfma_f32_16x16x128_f8f6f4 v[90:93], v[2:9], v[220:227], v[90:93]
	v_mfma_f32_16x16x128_f8f6f4 v[42:45], v[10:17], v[220:227], v[42:45]
	v_mfma_f32_16x16x128_f8f6f4 v[50:53], v[10:17], v[236:243], v[50:53]
	v_mfma_f32_16x16x128_f8f6f4 v[78:81], v[2:9], v[236:243], v[78:81]
	v_mfma_f32_16x16x128_f8f6f4 v[22:25], v[196:203], v[236:243], v[22:25]
	v_mfma_f32_16x16x128_f8f6f4 v[74:77], v[204:211], v[236:243], v[74:77]
	v_mfma_f32_16x16x128_f8f6f4 v[146:149], v[204:211], v[212:219], v[146:149]
	v_mfma_f32_16x16x128_f8f6f4 v[142:145], v[196:203], v[212:219], v[142:145]
	v_mfma_f32_16x16x128_f8f6f4 v[26:29], v[196:203], v[220:227], v[26:29]
	v_mfma_f32_16x16x128_f8f6f4 v[138:141], v[204:211], v[220:227], v[138:141]
	v_mfma_f32_16x16x128_f8f6f4 v[126:129], v[204:211], v[228:235], v[126:129]
	v_mfma_f32_16x16x128_f8f6f4 v[38:41], v[196:203], v[228:235], v[38:41]
	s_setprio 0
	s_barrier
	s_mov_b32 m0, s70
	ds_read_b128 v[212:215], v191 offset:16384
	ds_read_b128 v[216:219], v191 offset:17408
	ds_read_b128 v[220:223], v191 offset:18432
	ds_read_b128 v[224:227], v191 offset:19456
	ds_read_b128 v[228:231], v191 offset:20480
	ds_read_b128 v[232:235], v191 offset:21504
	ds_read_b128 v[236:239], v191 offset:22528
	ds_read_b128 v[240:243], v191 offset:23552
	global_load_lds_dwordx4 v[180:181], off
	s_mov_b32 m0, s71
	s_nop 0
	global_load_lds_dwordx4 v[178:179], off
	s_mov_b32 m0, s72
	s_nop 0
	global_load_lds_dwordx4 v[176:177], off
	s_mov_b32 m0, s73
	s_nop 0
	global_load_lds_dwordx4 v[174:175], off
	s_mov_b32 m0, s67
	s_nop 0
	global_load_lds_dwordx4 v[172:173], off
	s_mov_b32 m0, s68
	s_nop 0
	global_load_lds_dwordx4 v[170:171], off
	s_waitcnt vmcnt(8)
	s_waitcnt lgkmcnt(0)
	s_barrier
	s_setprio 1
	v_mfma_f32_16x16x128_f8f6f4 v[110:113], v[2:9], v[228:235], v[110:113]
	v_mfma_f32_16x16x128_f8f6f4 v[106:109], v[10:17], v[228:235], v[106:109]
	v_mfma_f32_16x16x128_f8f6f4 v[102:105], v[10:17], v[212:219], v[102:105]
	v_mfma_f32_16x16x128_f8f6f4 v[134:137], v[2:9], v[212:219], v[134:137]
	v_mfma_f32_16x16x128_f8f6f4 v[122:125], v[2:9], v[220:227], v[122:125]
	v_mfma_f32_16x16x128_f8f6f4 v[98:101], v[10:17], v[220:227], v[98:101]
	v_mfma_f32_16x16x128_f8f6f4 v[82:85], v[10:17], v[236:243], v[82:85]
	v_mfma_f32_16x16x128_f8f6f4 v[86:89], v[2:9], v[236:243], v[86:89]
	v_mfma_f32_16x16x128_f8f6f4 v[54:57], v[196:203], v[236:243], v[54:57]
	v_mfma_f32_16x16x128_f8f6f4 v[58:61], v[204:211], v[236:243], v[58:61]
	v_mfma_f32_16x16x128_f8f6f4 v[130:133], v[204:211], v[212:219], v[130:133]
	v_mfma_f32_16x16x128_f8f6f4 v[34:37], v[196:203], v[212:219], v[34:37]
	v_mfma_f32_16x16x128_f8f6f4 v[46:49], v[196:203], v[220:227], v[46:49]
	v_mfma_f32_16x16x128_f8f6f4 v[118:121], v[204:211], v[220:227], v[118:121]
	v_mfma_f32_16x16x128_f8f6f4 v[94:97], v[204:211], v[228:235], v[94:97]
	v_mfma_f32_16x16x128_f8f6f4 v[66:69], v[196:203], v[228:235], v[66:69]
	s_setprio 0
	s_barrier
	ds_read_b128 v[2:5], v193
	ds_read_b128 v[6:9], v193 offset:1024
	ds_read_b128 v[10:13], v193 offset:2048
	ds_read_b128 v[14:17], v193 offset:3072
	ds_read_b128 v[170:173], v192
	ds_read_b128 v[174:177], v192 offset:1024
	ds_read_b128 v[194:197], v192 offset:2048
	ds_read_b128 v[198:201], v192 offset:3072
	s_mov_b32 m0, s48
	ds_read_b128 v[202:205], v191 offset:32768
	ds_read_b128 v[206:209], v191 offset:33792
	ds_read_b128 v[210:213], v191 offset:34816
	ds_read_b128 v[214:217], v191 offset:35840
	ds_read_b128 v[218:221], v191 offset:36864
	ds_read_b128 v[222:225], v191 offset:37888
	ds_read_b128 v[226:229], v191 offset:38912
	ds_read_b128 v[230:233], v191 offset:39936
	global_load_lds_dwordx4 v[166:167], off
	s_mov_b32 m0, s49
	s_nop 0
	global_load_lds_dwordx4 v[168:169], off
	s_waitcnt vmcnt(8)
	s_waitcnt lgkmcnt(0)
	s_barrier
	s_setprio 1
	v_mfma_f32_16x16x128_f8f6f4 v[30:33], v[2:9], v[202:209], v[30:33]
	v_mfma_f32_16x16x128_f8f6f4 v[150:153], v[10:17], v[202:209], v[150:153]
	v_mfma_f32_16x16x128_f8f6f4 v[42:45], v[10:17], v[210:217], v[42:45]
	v_mfma_f32_16x16x128_f8f6f4 v[90:93], v[2:9], v[210:217], v[90:93]
	v_mfma_f32_16x16x128_f8f6f4 v[114:117], v[2:9], v[218:225], v[114:117]
	v_mfma_f32_16x16x128_f8f6f4 v[62:65], v[10:17], v[218:225], v[62:65]
	v_mfma_f32_16x16x128_f8f6f4 v[50:53], v[10:17], v[226:233], v[50:53]
	v_mfma_f32_16x16x128_f8f6f4 v[78:81], v[2:9], v[226:233], v[78:81]
	v_mfma_f32_16x16x128_f8f6f4 v[22:25], v[170:177], v[226:233], v[22:25]
	v_mfma_f32_16x16x128_f8f6f4 v[74:77], v[194:201], v[226:233], v[74:77]
	v_mfma_f32_16x16x128_f8f6f4 v[146:149], v[194:201], v[202:209], v[146:149]
	v_mfma_f32_16x16x128_f8f6f4 v[142:145], v[170:177], v[202:209], v[142:145]
	v_mfma_f32_16x16x128_f8f6f4 v[26:29], v[170:177], v[210:217], v[26:29]
	v_mfma_f32_16x16x128_f8f6f4 v[138:141], v[194:201], v[210:217], v[138:141]
	v_mfma_f32_16x16x128_f8f6f4 v[126:129], v[194:201], v[218:225], v[126:129]
	v_mfma_f32_16x16x128_f8f6f4 v[38:41], v[170:177], v[218:225], v[38:41]
	s_setprio 0
	s_barrier
	s_mov_b32 m0, s9
	ds_read_b128 v[202:205], v191 offset:49152
	ds_read_b128 v[206:209], v191 offset:50176
	ds_read_b128 v[210:213], v191 offset:51200
	ds_read_b128 v[214:217], v191 offset:52224
	ds_read_b128 v[218:221], v191 offset:53248
	ds_read_b128 v[222:225], v191 offset:54272
	ds_read_b128 v[226:229], v191 offset:55296
	ds_read_b128 v[230:233], v191 offset:56320
	global_load_lds_dwordx4 v[72:73], off
	s_mov_b32 m0, s19
	s_nop 0
	global_load_lds_dwordx4 v[158:159], off
	s_mov_b32 m0, s44
	s_nop 0
	global_load_lds_dwordx4 v[162:163], off
	s_mov_b32 m0, s45
	s_nop 0
	global_load_lds_dwordx4 v[164:165], off
	s_mov_b32 m0, s18
	s_nop 0
	global_load_lds_dwordx4 v[70:71], off
	s_mov_b32 m0, s43
	s_nop 0
	global_load_lds_dwordx4 v[160:161], off
	s_waitcnt vmcnt(8)
	s_waitcnt lgkmcnt(0)
	s_barrier
	s_setprio 1
	v_mfma_f32_16x16x128_f8f6f4 v[110:113], v[2:9], v[218:225], v[110:113]
	v_mfma_f32_16x16x128_f8f6f4 v[106:109], v[10:17], v[218:225], v[106:109]
	v_mfma_f32_16x16x128_f8f6f4 v[102:105], v[10:17], v[202:209], v[102:105]
	v_mfma_f32_16x16x128_f8f6f4 v[134:137], v[2:9], v[202:209], v[134:137]
	v_mfma_f32_16x16x128_f8f6f4 v[122:125], v[2:9], v[210:217], v[122:125]
	v_mfma_f32_16x16x128_f8f6f4 v[98:101], v[10:17], v[210:217], v[98:101]
	v_mfma_f32_16x16x128_f8f6f4 v[82:85], v[10:17], v[226:233], v[82:85]
	v_mfma_f32_16x16x128_f8f6f4 v[86:89], v[2:9], v[226:233], v[86:89]
	v_mfma_f32_16x16x128_f8f6f4 v[54:57], v[170:177], v[226:233], v[54:57]
	v_mfma_f32_16x16x128_f8f6f4 v[58:61], v[194:201], v[226:233], v[58:61]
	v_mfma_f32_16x16x128_f8f6f4 v[130:133], v[194:201], v[202:209], v[130:133]
	v_mfma_f32_16x16x128_f8f6f4 v[34:37], v[170:177], v[202:209], v[34:37]
	v_mfma_f32_16x16x128_f8f6f4 v[46:49], v[170:177], v[210:217], v[46:49]
	v_mfma_f32_16x16x128_f8f6f4 v[118:121], v[194:201], v[210:217], v[118:121]
	v_mfma_f32_16x16x128_f8f6f4 v[94:97], v[194:201], v[218:225], v[94:97]
	v_mfma_f32_16x16x128_f8f6f4 v[66:69], v[170:177], v[218:225], v[66:69]
	s_setprio 0
	s_barrier
	s_waitcnt vmcnt(0)
	s_cmpk_gt_u32 s65, 0xff
	s_cbranch_scc1 .LBB0_1439
	s_barrier

.LBB0_1558:
	s_add_u32 s39, s30, s38
	s_addc_u32 s44, s31, 0
	s_add_u32 s42, s39, 0x100
	s_addc_u32 s43, s44, 0
	s_and_b64 s[40:41], s[36:37], exec
	s_cselect_b32 s41, s18, s43
	s_cselect_b32 s40, s19, s42
	s_add_u32 s38, s28, s38
	s_addc_u32 s42, s29, 0
	s_add_u32 s38, s38, 0x100
	s_addc_u32 s42, s42, 0
	s_and_b64 s[36:37], s[36:37], exec
	s_cselect_b32 s43, s17, s42
	s_cselect_b32 s42, s21, s38
	s_add_u32 s76, s39, 0x10080
	ds_read_b128 v[26:29], v181
	ds_read_b128 v[30:33], v181 offset:1024
	ds_read_b128 v[18:21], v181 offset:2048
	ds_read_b128 v[22:25], v181 offset:3072
	ds_read_b128 v[10:13], v182
	ds_read_b128 v[14:17], v182 offset:1024
	ds_read_b128 v[2:5], v182 offset:2048
	ds_read_b128 v[6:9], v182 offset:3072
	s_addc_u32 s77, s44, 0
	s_add_i32 s75, s63, s15
	s_add_i32 m0, s27, 0xc000
	s_add_i32 s78, s27, 0xe000
	s_add_i32 s72, s75, 0x2000
	s_add_u32 s44, s42, 0x10000
	s_addc_u32 s45, s43, 0
	s_add_i32 s74, s64, s15
	s_add_i32 s73, s74, 0x2000
	s_add_i32 s71, 0, 0x18000
	s_add_i32 s70, 0, 0x1c000
	s_add_u32 s38, s40, 0x10000
	s_addc_u32 s39, s41, 0
	s_add_i32 s69, s71, s15
	s_add_i32 s67, s69, 0x2000
	s_add_u32 s36, s42, 0x10080
	s_addc_u32 s37, s43, 0
	s_add_i32 s68, s70, s15
	s_add_i32 s66, s68, 0x2000
	v_lshl_add_u64 v[208:209], s[76:77], 0, v[164:165]
	ds_read_b128 v[170:173], v183
	ds_read_b128 v[174:177], v183 offset:1024
	ds_read_b128 v[184:187], v183 offset:2048
	ds_read_b128 v[188:191], v183 offset:3072
	ds_read_b128 v[192:195], v183 offset:4096
	ds_read_b128 v[196:199], v183 offset:5120
	ds_read_b128 v[200:203], v183 offset:6144
	ds_read_b128 v[204:207], v183 offset:7168
	global_load_lds_dwordx4 v[208:209], off
	v_lshl_add_u64 v[208:209], s[76:77], 0, v[162:163]
	s_mov_b32 m0, s78
	s_nop 0
	global_load_lds_dwordx4 v[208:209], off
	s_waitcnt vmcnt(8)
	s_waitcnt lgkmcnt(0)
	s_barrier
	s_setprio 1
	v_mfma_f32_16x16x128_f8f6f4 v[158:161], v[26:33], v[170:177], v[158:161]
	v_mfma_f32_16x16x128_f8f6f4 v[154:157], v[18:25], v[170:177], v[154:157]
	v_mfma_f32_16x16x128_f8f6f4 v[138:141], v[18:25], v[184:191], v[138:141]
	v_mfma_f32_16x16x128_f8f6f4 v[142:145], v[26:33], v[184:191], v[142:145]
	v_mfma_f32_16x16x128_f8f6f4 v[126:129], v[26:33], v[192:199], v[126:129]
	v_mfma_f32_16x16x128_f8f6f4 v[122:125], v[18:25], v[192:199], v[122:125]
	v_mfma_f32_16x16x128_f8f6f4 v[106:109], v[18:25], v[200:207], v[106:109]
	v_mfma_f32_16x16x128_f8f6f4 v[110:113], v[26:33], v[200:207], v[110:113]
	v_mfma_f32_16x16x128_f8f6f4 v[102:105], v[10:17], v[200:207], v[102:105]
	v_mfma_f32_16x16x128_f8f6f4 v[98:101], v[2:9], v[200:207], v[98:101]
	v_mfma_f32_16x16x128_f8f6f4 v[146:149], v[2:9], v[170:177], v[146:149]
	v_mfma_f32_16x16x128_f8f6f4 v[150:153], v[10:17], v[170:177], v[150:153]
	v_mfma_f32_16x16x128_f8f6f4 v[134:137], v[10:17], v[184:191], v[134:137]
	v_mfma_f32_16x16x128_f8f6f4 v[130:133], v[2:9], v[184:191], v[130:133]
	v_mfma_f32_16x16x128_f8f6f4 v[114:117], v[2:9], v[192:199], v[114:117]
	v_mfma_f32_16x16x128_f8f6f4 v[118:121], v[10:17], v[192:199], v[118:121]
	s_setprio 0
	s_barrier
	s_mov_b32 m0, s75
	v_lshl_add_u64 v[170:171], s[42:43], 0, v[164:165]
	ds_read_b128 v[184:187], v183 offset:16384
	ds_read_b128 v[188:191], v183 offset:17408
	ds_read_b128 v[192:195], v183 offset:18432
	ds_read_b128 v[196:199], v183 offset:19456
	ds_read_b128 v[200:203], v183 offset:20480
	ds_read_b128 v[204:207], v183 offset:21504
	ds_read_b128 v[208:211], v183 offset:22528
	ds_read_b128 v[212:215], v183 offset:23552
	global_load_lds_dwordx4 v[170:171], off
	v_lshl_add_u64 v[172:173], s[42:43], 0, v[162:163]
	s_mov_b32 m0, s72
	v_lshl_add_u64 v[174:175], s[44:45], 0, v[164:165]
	global_load_lds_dwordx4 v[172:173], off
	s_mov_b32 m0, s74
	v_lshl_add_u64 v[176:177], s[40:41], 0, v[162:163]
	global_load_lds_dwordx4 v[174:175], off
	v_lshl_add_u64 v[174:175], s[44:45], 0, v[162:163]
	s_mov_b32 m0, s73
	s_nop 0
	global_load_lds_dwordx4 v[174:175], off
	v_lshl_add_u64 v[174:175], s[40:41], 0, v[164:165]
	s_mov_b32 m0, s27
	s_nop 0
	global_load_lds_dwordx4 v[174:175], off
	s_mov_b32 m0, s49
	s_nop 0
	global_load_lds_dwordx4 v[176:177], off
	s_waitcnt vmcnt(8)
	s_waitcnt lgkmcnt(0)
	s_barrier
	s_setprio 1
	v_mfma_f32_16x16x128_f8f6f4 v[78:81], v[26:33], v[192:199], v[78:81]
	v_mfma_f32_16x16x128_f8f6f4 v[74:77], v[18:25], v[192:199], v[74:77]
	v_mfma_f32_16x16x128_f8f6f4 v[90:93], v[18:25], v[184:191], v[90:93]
	v_mfma_f32_16x16x128_f8f6f4 v[94:97], v[26:33], v[184:191], v[94:97]
	v_mfma_f32_16x16x128_f8f6f4 v[62:65], v[26:33], v[200:207], v[62:65]
	v_mfma_f32_16x16x128_f8f6f4 v[58:61], v[18:25], v[200:207], v[58:61]
	v_mfma_f32_16x16x128_f8f6f4 v[42:45], v[18:25], v[208:215], v[42:45]
	v_mfma_f32_16x16x128_f8f6f4 v[54:57], v[26:33], v[208:215], v[54:57]
	v_mfma_f32_16x16x128_f8f6f4 v[38:41], v[10:17], v[208:215], v[38:41]
	v_mfma_f32_16x16x128_f8f6f4 v[34:37], v[2:9], v[208:215], v[34:37]
	v_mfma_f32_16x16x128_f8f6f4 v[82:85], v[2:9], v[184:191], v[82:85]
	v_mfma_f32_16x16x128_f8f6f4 v[86:89], v[10:17], v[184:191], v[86:89]
	v_mfma_f32_16x16x128_f8f6f4 v[70:73], v[10:17], v[192:199], v[70:73]
	v_mfma_f32_16x16x128_f8f6f4 v[66:69], v[2:9], v[192:199], v[66:69]
	v_mfma_f32_16x16x128_f8f6f4 v[46:49], v[2:9], v[200:207], v[46:49]
	v_mfma_f32_16x16x128_f8f6f4 v[50:53], v[10:17], v[200:207], v[50:53]
	s_setprio 0
	s_barrier
	v_add_u32_e32 v14, s71, v179
	v_add_u32_e32 v30, s70, v179
	ds_read_b128 v[2:5], v14
	ds_read_b128 v[6:9], v14 offset:1024
	ds_read_b128 v[10:13], v14 offset:2048
	ds_read_b128 v[14:17], v14 offset:3072
	ds_read_b128 v[18:21], v30
	ds_read_b128 v[22:25], v30 offset:1024
	ds_read_b128 v[26:29], v30 offset:2048
	ds_read_b128 v[30:33], v30 offset:3072
	s_mov_b32 m0, s50
	v_lshl_add_u64 v[216:217], s[38:39], 0, v[164:165]
	ds_read_b128 v[184:187], v183 offset:32768
	ds_read_b128 v[188:191], v183 offset:33792
	ds_read_b128 v[192:195], v183 offset:34816
	ds_read_b128 v[196:199], v183 offset:35840
	ds_read_b128 v[200:203], v183 offset:36864
	ds_read_b128 v[204:207], v183 offset:37888
	ds_read_b128 v[208:211], v183 offset:38912
	ds_read_b128 v[212:215], v183 offset:39936
	global_load_lds_dwordx4 v[216:217], off
	v_lshl_add_u64 v[216:217], s[38:39], 0, v[162:163]
	s_mov_b32 m0, s51
	s_nop 0
	global_load_lds_dwordx4 v[216:217], off
	s_waitcnt vmcnt(8)
	s_waitcnt lgkmcnt(0)
	s_barrier
	s_setprio 1
	v_mfma_f32_16x16x128_f8f6f4 v[122:125], v[10:17], v[200:207], v[122:125]
	v_mfma_f32_16x16x128_f8f6f4 v[126:129], v[2:9], v[200:207], v[126:129]
	v_mfma_f32_16x16x128_f8f6f4 v[158:161], v[2:9], v[184:191], v[158:161]
	v_mfma_f32_16x16x128_f8f6f4 v[154:157], v[10:17], v[184:191], v[154:157]
	v_mfma_f32_16x16x128_f8f6f4 v[138:141], v[10:17], v[192:199], v[138:141]
	v_mfma_f32_16x16x128_f8f6f4 v[142:145], v[2:9], v[192:199], v[142:145]
	v_mfma_f32_16x16x128_f8f6f4 v[110:113], v[2:9], v[208:215], v[110:113]
	v_mfma_f32_16x16x128_f8f6f4 v[106:109], v[10:17], v[208:215], v[106:109]
	v_mfma_f32_16x16x128_f8f6f4 v[102:105], v[18:25], v[208:215], v[102:105]
	v_mfma_f32_16x16x128_f8f6f4 v[98:101], v[26:33], v[208:215], v[98:101]
	v_mfma_f32_16x16x128_f8f6f4 v[146:149], v[26:33], v[184:191], v[146:149]
	v_mfma_f32_16x16x128_f8f6f4 v[150:153], v[18:25], v[184:191], v[150:153]
	v_mfma_f32_16x16x128_f8f6f4 v[134:137], v[18:25], v[192:199], v[134:137]
	v_mfma_f32_16x16x128_f8f6f4 v[130:133], v[26:33], v[192:199], v[130:133]
	v_mfma_f32_16x16x128_f8f6f4 v[114:117], v[26:33], v[200:207], v[114:117]
	v_mfma_f32_16x16x128_f8f6f4 v[118:121], v[18:25], v[200:207], v[118:121]
	s_setprio 0
	s_barrier
	s_mov_b32 m0, s69
	v_lshl_add_u64 v[170:171], v[170:171], 0, s[8:9]
	ds_read_b128 v[184:187], v183 offset:49152
	ds_read_b128 v[188:191], v183 offset:50176
	ds_read_b128 v[192:195], v183 offset:51200
	ds_read_b128 v[196:199], v183 offset:52224
	ds_read_b128 v[200:203], v183 offset:53248
	ds_read_b128 v[204:207], v183 offset:54272
	ds_read_b128 v[208:211], v183 offset:55296
	ds_read_b128 v[212:215], v183 offset:56320
	global_load_lds_dwordx4 v[170:171], off
	v_lshl_add_u64 v[170:171], v[172:173], 0, s[8:9]
	s_mov_b32 m0, s67
	s_nop 0
	global_load_lds_dwordx4 v[170:171], off
	v_lshl_add_u64 v[170:171], s[36:37], 0, v[164:165]
	s_mov_b32 m0, s68
	s_nop 0
	global_load_lds_dwordx4 v[170:171], off
	v_lshl_add_u64 v[170:171], s[36:37], 0, v[162:163]
	s_mov_b32 m0, s66
	s_nop 0
	global_load_lds_dwordx4 v[170:171], off
	v_lshl_add_u64 v[170:171], v[174:175], 0, s[8:9]
	s_mov_b32 m0, s61
	s_nop 0
	global_load_lds_dwordx4 v[170:171], off
	v_lshl_add_u64 v[170:171], v[176:177], 0, s[8:9]
	s_mov_b32 m0, s62
	s_nop 0
	global_load_lds_dwordx4 v[170:171], off
	s_waitcnt vmcnt(8)
	s_waitcnt lgkmcnt(0)
	s_barrier
	s_setprio 1
	v_mfma_f32_16x16x128_f8f6f4 v[62:65], v[2:9], v[200:207], v[62:65]
	v_mfma_f32_16x16x128_f8f6f4 v[58:61], v[10:17], v[200:207], v[58:61]
	v_mfma_f32_16x16x128_f8f6f4 v[90:93], v[10:17], v[184:191], v[90:93]
	v_mfma_f32_16x16x128_f8f6f4 v[94:97], v[2:9], v[184:191], v[94:97]
	v_mfma_f32_16x16x128_f8f6f4 v[78:81], v[2:9], v[192:199], v[78:81]
	v_mfma_f32_16x16x128_f8f6f4 v[74:77], v[10:17], v[192:199], v[74:77]
	v_mfma_f32_16x16x128_f8f6f4 v[42:45], v[10:17], v[208:215], v[42:45]
	v_mfma_f32_16x16x128_f8f6f4 v[54:57], v[2:9], v[208:215], v[54:57]
	v_mfma_f32_16x16x128_f8f6f4 v[38:41], v[18:25], v[208:215], v[38:41]
	v_mfma_f32_16x16x128_f8f6f4 v[34:37], v[26:33], v[208:215], v[34:37]
	v_mfma_f32_16x16x128_f8f6f4 v[82:85], v[26:33], v[184:191], v[82:85]
	v_mfma_f32_16x16x128_f8f6f4 v[86:89], v[18:25], v[184:191], v[86:89]
	v_mfma_f32_16x16x128_f8f6f4 v[70:73], v[18:25], v[192:199], v[70:73]
	v_mfma_f32_16x16x128_f8f6f4 v[66:69], v[26:33], v[192:199], v[66:69]
	v_mfma_f32_16x16x128_f8f6f4 v[46:49], v[26:33], v[200:207], v[46:49]
	v_mfma_f32_16x16x128_f8f6f4 v[50:53], v[18:25], v[200:207], v[50:53]
	s_setprio 0
	s_barrier
	s_movk_i32 s38, 0x100
	s_andn2_b64 vcc, exec, s[34:35]
	s_mov_b64 s[36:37], -1
	s_mov_b64 s[34:35], 0
	s_cbranch_vccz .LBB0_1558
	s_and_b64 vcc, exec, s[12:13]
	s_cbranch_vccz .LBB0_1561
	s_barrier

.LBB0_1619:
	v_add_co_u32_e64 v94, s[4:5], s12, v72
	v_add_co_u32_e32 v76, vcc, 0xffffd000, v72
	s_nop 0
	v_addc_co_u32_e64 v95, s[4:5], -1, v73, s[4:5]
	v_add_co_u32_e64 v96, s[4:5], s13, v72
	global_load_dwordx4 v[14:17], v[72:73], off offset:-3072
	global_load_dwordx4 v[10:13], v[72:73], off offset:-2048
	global_load_dwordx4 v[6:9], v[72:73], off offset:-1024
	global_load_dwordx4 v[2:5], v[72:73], off
	global_load_dwordx4 v[86:89], v[46:47], off
	v_addc_co_u32_e64 v97, s[4:5], -1, v73, s[4:5]
	v_addc_co_u32_e32 v77, vcc, -1, v73, vcc
	global_load_dwordx4 v[90:93], v[94:95], off offset:-3072
	global_load_dwordx4 v[42:45], v[94:95], off offset:-2048
	global_load_dwordx4 v[38:41], v[94:95], off offset:-1024
	global_load_dwordx4 v[34:37], v[94:95], off
	global_load_dwordx4 v[30:33], v[96:97], off offset:-3072
	global_load_dwordx4 v[26:29], v[96:97], off offset:-2048
	global_load_dwordx4 v[22:25], v[96:97], off offset:-1024
	global_load_dwordx4 v[18:21], v[72:73], off offset:-4096
	s_nop 0
	global_load_dwordx4 v[94:97], v[76:77], off offset:-3072
	global_load_dwordx4 v[98:101], v[76:77], off offset:-2048
	global_load_dwordx4 v[102:105], v[76:77], off offset:-1024
	global_load_dwordx4 v[106:109], v[76:77], off
	v_mov_b32_e32 v111, 0
	v_mov_b32_e32 v112, 0
	v_mov_b32_e32 v113, 0
	s_add_i32 s3, s3, s92
	v_lshl_add_u64 v[72:73], v[72:73], 0, s[6:7]
	s_cmpk_lt_i32 s3, 0x4000
	s_waitcnt vmcnt(0)
	v_mul_f32_e32 v76, v15, v15
	v_mul_f32_e32 v77, v17, v17
	v_mul_f32_e32 v114, v11, v11
	v_mul_f32_e32 v115, v13, v13
	v_mul_f32_e32 v118, v3, v3
	v_mul_f32_e32 v119, v5, v5
	v_mul_f32_e32 v124, v39, v39
	v_mul_f32_e32 v125, v41, v41
	v_mul_f32_e32 v136, v95, v95
	v_mul_f32_e32 v137, v97, v97
	v_mul_f32_e32 v138, v99, v99
	v_mul_f32_e32 v139, v101, v101
	v_mul_f32_e32 v126, v35, v35
	v_mul_f32_e32 v127, v37, v37
	v_fmac_f32_e32 v76, v14, v14
	v_fmac_f32_e32 v77, v16, v16
	v_fmac_f32_e32 v114, v10, v10
	v_fmac_f32_e32 v115, v12, v12
	v_fmac_f32_e32 v118, v2, v2
	v_fmac_f32_e32 v119, v4, v4
	v_mul_f32_e32 v140, v103, v103
	v_mul_f32_e32 v141, v105, v105
	v_fmac_f32_e32 v124, v38, v38
	v_fmac_f32_e32 v125, v40, v40
	v_fmac_f32_e32 v136, v94, v94
	v_fmac_f32_e32 v137, v96, v96
	v_fmac_f32_e32 v138, v98, v98
	v_fmac_f32_e32 v139, v100, v100
	v_mul_f32_e32 v142, v107, v107
	v_mul_f32_e32 v143, v109, v109
	v_fmac_f32_e32 v126, v34, v34
	v_fmac_f32_e32 v127, v36, v36
	v_add_f32_e32 v76, v76, v77
	v_add_f32_e32 v77, v114, v115
	v_add_f32_e32 v115, v118, v119
	v_fmac_f32_e32 v140, v102, v102
	v_fmac_f32_e32 v141, v104, v104
	v_add_f32_e32 v118, v124, v125
	v_add_f32_e32 v124, v136, v137
	v_add_f32_e32 v125, v138, v139
	v_mul_f32_e32 v116, v7, v7
	v_mul_f32_e32 v117, v9, v9
	v_mul_f32_e32 v120, v91, v91
	v_mul_f32_e32 v121, v93, v93
	v_fmac_f32_e32 v142, v106, v106
	v_fmac_f32_e32 v143, v108, v108
	v_add_f32_e32 v119, v126, v127
	v_add_f32_e32 v126, v140, v141
	v_add_f32_e32 v124, v124, v125
	v_mul_f32_e32 v122, v43, v43
	v_mul_f32_e32 v123, v45, v45
	v_fmac_f32_e32 v116, v6, v6
	v_fmac_f32_e32 v117, v8, v8
	v_fmac_f32_e32 v120, v90, v90
	v_fmac_f32_e32 v121, v92, v92
	v_add_f32_e32 v127, v142, v143
	v_add_f32_e32 v124, v124, v126
	v_fmac_f32_e32 v122, v42, v42
	v_fmac_f32_e32 v123, v44, v44
	v_add_f32_e32 v114, v116, v117
	v_add_f32_e32 v116, v120, v121
	v_add_f32_e32 v124, v124, v127
	v_add_f32_e32 v117, v122, v123
	v_add_f32_e32 v116, v124, v116
	v_mul_f32_e32 v128, v31, v31
	v_mul_f32_e32 v129, v33, v33
	v_add_f32_e32 v116, v116, v117
	v_mul_f32_e32 v130, v27, v27
	v_mul_f32_e32 v131, v29, v29
	v_fmac_f32_e32 v128, v30, v30
	v_fmac_f32_e32 v129, v32, v32
	v_add_f32_e32 v116, v116, v118
	v_mul_f32_e32 v132, v23, v23
	v_mul_f32_e32 v133, v25, v25
	v_fmac_f32_e32 v130, v26, v26
	v_fmac_f32_e32 v131, v28, v28
	v_add_f32_e32 v120, v128, v129
	v_add_f32_e32 v116, v116, v119
	v_mul_f32_e32 v134, v19, v19
	v_mul_f32_e32 v135, v21, v21
	v_fmac_f32_e32 v132, v22, v22
	v_fmac_f32_e32 v133, v24, v24
	v_add_f32_e32 v121, v130, v131
	v_add_f32_e32 v116, v116, v120
	v_fmac_f32_e32 v134, v18, v18
	v_fmac_f32_e32 v135, v20, v20
	v_add_f32_e32 v122, v132, v133
	v_add_f32_e32 v116, v116, v121
	v_add_f32_e32 v123, v134, v135
	v_add_f32_e32 v116, v116, v122
	v_add_f32_e32 v116, v116, v123
	v_add_f32_e32 v76, v116, v76
	v_add_f32_e32 v76, v76, v77
	v_add_f32_e32 v76, v76, v114
	v_add_f32_e32 v76, v76, v115
	ds_bpermute_b32 v77, v1, v76
	s_waitcnt lgkmcnt(0)
	v_add_f32_e32 v76, v76, v77
	ds_bpermute_b32 v77, v78, v76
	s_waitcnt lgkmcnt(0)
	v_add_f32_e32 v76, v76, v77
	ds_bpermute_b32 v77, v79, v76
	s_waitcnt lgkmcnt(0)
	v_add_f32_e32 v76, v76, v77
	ds_bpermute_b32 v77, v80, v76
	s_waitcnt lgkmcnt(0)
	v_add_f32_e32 v76, v76, v77
	ds_bpermute_b32 v77, v81, v76
	s_waitcnt lgkmcnt(0)
	v_add_f32_e32 v76, v76, v77
	ds_bpermute_b32 v77, v82, v76
	s_waitcnt lgkmcnt(0)
	v_add_f32_e32 v76, v76, v77
	v_fmamk_f32 v76, v76, 0x39800000, v83
	v_mul_f32_e32 v77, 0x4f800000, v76
	v_cmp_gt_f32_e32 vcc, s14, v76
	s_nop 1
	v_cndmask_b32_e32 v76, v76, v77, vcc
	v_sqrt_f32_e32 v77, v76
	s_nop 0
	v_add_u32_e32 v114, -1, v77
	v_add_u32_e32 v115, 1, v77
	v_fma_f32 v116, -v114, v77, v76
	v_fma_f32 v117, -v115, v77, v76
	v_cmp_ge_f32_e64 s[4:5], 0, v116
	s_nop 1
	v_cndmask_b32_e64 v77, v77, v114, s[4:5]
	v_cmp_lt_f32_e64 s[4:5], 0, v117
	s_nop 1
	v_cndmask_b32_e64 v77, v77, v115, s[4:5]
	v_mul_f32_e32 v114, 0x37800000, v77
	v_cndmask_b32_e32 v77, v77, v114, vcc
	v_cmp_class_f32_e32 vcc, v76, v84
	s_nop 1
	v_cndmask_b32_e32 v76, v77, v76, vcc
	v_div_scale_f32 v77, s[4:5], v76, v76, 1.0
	v_rcp_f32_e32 v115, v77
	v_div_scale_f32 v114, vcc, 1.0, v76, 1.0
	v_fma_f32 v116, -v77, v115, 1.0
	v_fmac_f32_e32 v115, v116, v115
	v_mul_f32_e32 v116, v114, v115
	v_fma_f32 v117, -v77, v116, v114
	v_fmac_f32_e32 v116, v117, v115
	v_fma_f32 v77, -v77, v116, v114
	v_div_fmas_f32 v77, v77, v115, v116
	v_div_fixup_f32 v76, v77, v76, 1.0
	v_mul_f32_e32 v77, v94, v76
	v_mul_f32_e32 v94, v95, v76
	v_mul_f32_e32 v77, v86, v77
	v_mul_f32_e32 v86, v87, v94
	v_med3_f32 v77, v77, s15, v85
	v_med3_f32 v86, v86, s15, v85
	v_cvt_pk_fp8_f32 v110, v77, v86
	v_mul_f32_e32 v95, v96, v76
	v_mul_f32_e32 v96, v97, v76
	v_mul_f32_e32 v87, v88, v95
	v_mul_f32_e32 v88, v89, v96
	v_med3_f32 v87, v87, s15, v85
	v_med3_f32 v88, v88, s15, v85
	v_cvt_pk_fp8_f32 v110, v87, v88 op_sel:[0,0,1]
	v_mul_f32_e32 v97, v98, v76
	v_mul_f32_e32 v98, v99, v76
	v_mul_f32_e32 v99, v100, v76
	global_store_dword v[74:75], v110, off offset:-2048
	global_load_dwordx4 v[86:89], v[46:47], off offset:1024
	v_mul_f32_e32 v100, v101, v76
	v_mul_f32_e32 v101, v102, v76
	v_mul_f32_e32 v102, v103, v76
	v_mul_f32_e32 v103, v104, v76
	v_mul_f32_e32 v104, v105, v76
	v_mul_f32_e32 v105, v106, v76
	v_mul_f32_e32 v106, v107, v76
	v_mul_f32_e32 v94, v109, v76
	v_mul_f32_e32 v90, v90, v76
	v_mul_f32_e32 v91, v91, v76
	v_mul_f32_e32 v92, v92, v76
	v_mul_f32_e32 v93, v93, v76
	v_mul_f32_e32 v42, v42, v76
	v_mul_f32_e32 v43, v43, v76
	v_mul_f32_e32 v44, v44, v76
	v_mul_f32_e32 v45, v45, v76
	v_mul_f32_e32 v38, v38, v76
	v_mul_f32_e32 v39, v39, v76
	v_mul_f32_e32 v40, v40, v76
	v_mul_f32_e32 v41, v41, v76
	v_mul_f32_e32 v34, v34, v76
	v_mul_f32_e32 v35, v35, v76
	v_mul_f32_e32 v36, v36, v76
	v_mul_f32_e32 v37, v37, v76
	v_mul_f32_e32 v30, v30, v76
	v_mul_f32_e32 v31, v31, v76
	v_mul_f32_e32 v32, v32, v76
	v_mul_f32_e32 v33, v33, v76
	v_mul_f32_e32 v26, v26, v76
	v_mul_f32_e32 v27, v27, v76
	v_mul_f32_e32 v28, v28, v76
	v_mul_f32_e32 v29, v29, v76
	v_mul_f32_e32 v22, v22, v76
	v_mul_f32_e32 v23, v23, v76
	v_mul_f32_e32 v24, v24, v76
	v_mul_f32_e32 v25, v25, v76
	v_mul_f32_e32 v18, v18, v76
	v_mul_f32_e32 v19, v19, v76
	v_mul_f32_e32 v20, v20, v76
	v_mul_f32_e32 v21, v21, v76
	v_mul_f32_e32 v14, v14, v76
	v_mul_f32_e32 v15, v15, v76
	v_mul_f32_e32 v16, v16, v76
	v_mul_f32_e32 v17, v17, v76
	v_mul_f32_e32 v10, v10, v76
	v_mul_f32_e32 v11, v11, v76
	v_mul_f32_e32 v12, v12, v76
	v_mul_f32_e32 v13, v13, v76
	v_mul_f32_e32 v6, v6, v76
	v_mul_f32_e32 v7, v7, v76
	v_mul_f32_e32 v8, v8, v76
	v_mul_f32_e32 v9, v9, v76
	v_mul_f32_e32 v2, v2, v76
	v_mul_f32_e32 v3, v3, v76
	v_mul_f32_e32 v4, v4, v76
	v_mul_f32_e32 v5, v5, v76
	s_waitcnt vmcnt(0)
	v_mul_f32_e32 v77, v86, v97
	v_mul_f32_e32 v86, v87, v98
	v_med3_f32 v77, v77, s15, v85
	v_med3_f32 v86, v86, s15, v85
	v_cvt_pk_fp8_f32 v111, v77, v86
	v_mul_f32_e32 v87, v88, v99
	v_mul_f32_e32 v88, v89, v100
	v_med3_f32 v87, v87, s15, v85
	v_med3_f32 v88, v88, s15, v85
	v_cvt_pk_fp8_f32 v111, v87, v88 op_sel:[0,0,1]
	global_store_dword v[74:75], v111, off offset:-1792
	global_load_dwordx4 v[86:89], v[46:47], off offset:2048
	s_waitcnt vmcnt(0)
	v_mul_f32_e32 v77, v101, v86
	v_mul_f32_e32 v86, v102, v87
	v_med3_f32 v77, v77, s15, v85
	v_med3_f32 v86, v86, s15, v85
	v_cvt_pk_fp8_f32 v112, v77, v86
	v_mul_f32_e32 v87, v103, v88
	v_mul_f32_e32 v88, v104, v89
	v_med3_f32 v87, v87, s15, v85
	v_med3_f32 v88, v88, s15, v85
	v_cvt_pk_fp8_f32 v112, v87, v88 op_sel:[0,0,1]
	v_mul_f32_e32 v77, v108, v76
	global_store_dword v[74:75], v112, off offset:-1536
	global_load_dwordx4 v[86:89], v[46:47], off offset:3072
	s_waitcnt vmcnt(0)
	v_mul_f32_e32 v86, v105, v86
	v_mul_f32_e32 v87, v106, v87
	v_med3_f32 v86, v86, s15, v85
	v_med3_f32 v87, v87, s15, v85
	v_cvt_pk_fp8_f32 v113, v86, v87
	v_mul_f32_e32 v77, v77, v88
	v_mul_f32_e32 v88, v94, v89
	v_med3_f32 v77, v77, s15, v85
	v_med3_f32 v88, v88, s15, v85
	v_cvt_pk_fp8_f32 v113, v77, v88 op_sel:[0,0,1]
	global_store_dword v[74:75], v113, off offset:-1280
	global_load_dwordx4 v[86:89], v[48:49], off
	s_waitcnt vmcnt(0)
	v_mul_f32_e32 v86, v90, v86
	v_mul_f32_e32 v87, v91, v87
	v_med3_f32 v86, v86, s15, v85
	v_med3_f32 v87, v87, s15, v85
	v_cvt_pk_fp8_f32 v77, v86, v87
	v_mul_f32_e32 v88, v92, v88
	v_mul_f32_e32 v89, v93, v89
	v_med3_f32 v88, v88, s15, v85
	v_med3_f32 v89, v89, s15, v85
	v_cvt_pk_fp8_f32 v77, v88, v89 op_sel:[0,0,1]
	global_store_dword v[74:75], v77, off offset:-1024
	global_load_dwordx4 v[86:89], v[50:51], off
	s_waitcnt vmcnt(0)
	v_mul_f32_e32 v42, v42, v86
	v_mul_f32_e32 v43, v43, v87
	v_med3_f32 v42, v42, s15, v85
	v_med3_f32 v43, v43, s15, v85
	v_cvt_pk_fp8_f32 v77, v42, v43
	v_mul_f32_e32 v44, v44, v88
	v_mul_f32_e32 v45, v45, v89
	v_med3_f32 v44, v44, s15, v85
	v_med3_f32 v45, v45, s15, v85
	v_cvt_pk_fp8_f32 v77, v44, v45 op_sel:[0,0,1]
	global_store_dword v[74:75], v77, off offset:-768
	global_load_dwordx4 v[42:45], v[52:53], off
	s_waitcnt vmcnt(0)
	v_mul_f32_e32 v38, v38, v42
	v_mul_f32_e32 v39, v39, v43
	v_med3_f32 v38, v38, s15, v85
	v_med3_f32 v39, v39, s15, v85
	v_cvt_pk_fp8_f32 v77, v38, v39
	v_mul_f32_e32 v40, v40, v44
	v_mul_f32_e32 v41, v41, v45
	v_med3_f32 v40, v40, s15, v85
	v_med3_f32 v41, v41, s15, v85
	v_cvt_pk_fp8_f32 v77, v40, v41 op_sel:[0,0,1]
	global_store_dword v[74:75], v77, off offset:-512
	global_load_dwordx4 v[38:41], v[54:55], off
	s_waitcnt vmcnt(0)
	v_mul_f32_e32 v34, v34, v38
	v_mul_f32_e32 v35, v35, v39
	v_med3_f32 v34, v34, s15, v85
	v_med3_f32 v35, v35, s15, v85
	v_cvt_pk_fp8_f32 v42, v34, v35
	v_mul_f32_e32 v36, v36, v40
	v_mul_f32_e32 v37, v37, v41
	v_med3_f32 v36, v36, s15, v85
	v_med3_f32 v37, v37, s15, v85
	v_cvt_pk_fp8_f32 v42, v36, v37 op_sel:[0,0,1]
	global_store_dword v[74:75], v42, off offset:-256
	global_load_dwordx4 v[34:37], v[56:57], off
	s_waitcnt vmcnt(0)
	v_mul_f32_e32 v30, v30, v34
	v_mul_f32_e32 v31, v31, v35
	v_med3_f32 v30, v30, s15, v85
	v_med3_f32 v31, v31, s15, v85
	v_cvt_pk_fp8_f32 v38, v30, v31
	v_mul_f32_e32 v32, v32, v36
	v_mul_f32_e32 v33, v33, v37
	v_med3_f32 v32, v32, s15, v85
	v_med3_f32 v33, v33, s15, v85
	v_cvt_pk_fp8_f32 v38, v32, v33 op_sel:[0,0,1]
	global_store_dword v[74:75], v38, off
	global_load_dwordx4 v[30:33], v[58:59], off
	s_waitcnt vmcnt(0)
	v_mul_f32_e32 v26, v26, v30
	v_mul_f32_e32 v27, v27, v31
	v_med3_f32 v26, v26, s15, v85
	v_med3_f32 v27, v27, s15, v85
	v_cvt_pk_fp8_f32 v34, v26, v27
	v_mul_f32_e32 v28, v28, v32
	v_mul_f32_e32 v29, v29, v33
	v_med3_f32 v28, v28, s15, v85
	v_med3_f32 v29, v29, s15, v85
	v_cvt_pk_fp8_f32 v34, v28, v29 op_sel:[0,0,1]
	global_store_dword v[74:75], v34, off offset:256
	global_load_dwordx4 v[26:29], v[60:61], off
	s_waitcnt vmcnt(0)
	v_mul_f32_e32 v22, v22, v26
	v_mul_f32_e32 v23, v23, v27
	v_med3_f32 v22, v22, s15, v85
	v_med3_f32 v23, v23, s15, v85
	v_cvt_pk_fp8_f32 v30, v22, v23
	v_mul_f32_e32 v24, v24, v28
	v_mul_f32_e32 v25, v25, v29
	v_med3_f32 v24, v24, s15, v85
	v_med3_f32 v25, v25, s15, v85
	v_cvt_pk_fp8_f32 v30, v24, v25 op_sel:[0,0,1]
	global_store_dword v[74:75], v30, off offset:512
	global_load_dwordx4 v[22:25], v[62:63], off
	s_waitcnt vmcnt(0)
	v_mul_f32_e32 v18, v18, v22
	v_mul_f32_e32 v19, v19, v23
	v_med3_f32 v18, v18, s15, v85
	v_med3_f32 v19, v19, s15, v85
	v_cvt_pk_fp8_f32 v26, v18, v19
	v_mul_f32_e32 v20, v20, v24
	v_mul_f32_e32 v21, v21, v25
	v_med3_f32 v20, v20, s15, v85
	v_med3_f32 v21, v21, s15, v85
	v_cvt_pk_fp8_f32 v26, v20, v21 op_sel:[0,0,1]
	global_store_dword v[74:75], v26, off offset:768
	global_load_dwordx4 v[18:21], v[64:65], off
	s_waitcnt vmcnt(0)
	v_mul_f32_e32 v14, v14, v18
	v_mul_f32_e32 v15, v15, v19
	v_med3_f32 v14, v14, s15, v85
	v_med3_f32 v15, v15, s15, v85
	v_cvt_pk_fp8_f32 v22, v14, v15
	v_mul_f32_e32 v16, v16, v20
	v_mul_f32_e32 v17, v17, v21
	v_med3_f32 v16, v16, s15, v85
	v_med3_f32 v17, v17, s15, v85
	v_cvt_pk_fp8_f32 v22, v16, v17 op_sel:[0,0,1]
	global_store_dword v[74:75], v22, off offset:1024
	global_load_dwordx4 v[14:17], v[66:67], off
	s_waitcnt vmcnt(0)
	v_mul_f32_e32 v10, v10, v14
	v_mul_f32_e32 v11, v11, v15
	v_med3_f32 v10, v10, s15, v85
	v_med3_f32 v11, v11, s15, v85
	v_cvt_pk_fp8_f32 v18, v10, v11
	v_mul_f32_e32 v12, v12, v16
	v_mul_f32_e32 v13, v13, v17
	v_med3_f32 v12, v12, s15, v85
	v_med3_f32 v13, v13, s15, v85
	v_cvt_pk_fp8_f32 v18, v12, v13 op_sel:[0,0,1]
	global_store_dword v[74:75], v18, off offset:1280
	global_load_dwordx4 v[10:13], v[68:69], off
	s_waitcnt vmcnt(0)
	v_mul_f32_e32 v6, v6, v10
	v_mul_f32_e32 v7, v7, v11
	v_med3_f32 v6, v6, s15, v85
	v_med3_f32 v7, v7, s15, v85
	v_cvt_pk_fp8_f32 v14, v6, v7
	v_mul_f32_e32 v8, v8, v12
	v_mul_f32_e32 v9, v9, v13
	v_med3_f32 v8, v8, s15, v85
	v_med3_f32 v9, v9, s15, v85
	v_cvt_pk_fp8_f32 v14, v8, v9 op_sel:[0,0,1]
	global_store_dword v[74:75], v14, off offset:1536
	global_load_dwordx4 v[6:9], v[70:71], off
	s_waitcnt vmcnt(0)
	v_mul_f32_e32 v2, v2, v6
	v_mul_f32_e32 v3, v3, v7
	v_med3_f32 v2, v2, s15, v85
	v_med3_f32 v3, v3, s15, v85
	v_cvt_pk_fp8_f32 v10, v2, v3
	v_mul_f32_e32 v4, v4, v8
	v_mul_f32_e32 v5, v5, v9
	v_med3_f32 v2, v4, s15, v85
	v_med3_f32 v3, v5, s15, v85
	v_cvt_pk_fp8_f32 v10, v2, v3 op_sel:[0,0,1]
	global_store_dword v[74:75], v10, off offset:1792
	v_lshl_add_u64 v[74:75], v[74:75], 0, s[8:9]
	s_cbranch_scc1 .LBB0_1619
	v_readlane_b32 s93, v246, 7

.LBB0_1681:
	ds_read_b128 v[26:29], v189
	ds_read_b128 v[30:33], v189 offset:1024
	ds_read_b128 v[18:21], v189 offset:2048
	ds_read_b128 v[22:25], v189 offset:3072
	ds_read_b128 v[10:13], v190
	ds_read_b128 v[14:17], v190 offset:1024
	ds_read_b128 v[2:5], v190 offset:2048
	ds_read_b128 v[6:9], v190 offset:3072
	s_add_u32 s34, s30, 0xfff80080
	s_addc_u32 s35, s31, -1
	s_cmp_eq_u32 s60, 28
	s_cselect_b32 s37, s18, s35
	s_cselect_b32 s36, s19, s34
	s_cselect_b32 s35, s21, s59
	s_cselect_b32 s34, s23, s58
	s_mov_b32 m0, s43
	s_nop 0
	global_load_lds_dwordx4 v168, s[100:101]
	s_mov_b32 m0, s44
	s_nop 0
	global_load_lds_dwordx4 v164, s[100:101]
	s_add_i32 m0, s29, 0xc000
	ds_read_b128 v[178:181], v191
	ds_read_b128 v[182:185], v191 offset:1024
	ds_read_b128 v[194:197], v191 offset:2048
	ds_read_b128 v[198:201], v191 offset:3072
	ds_read_b128 v[202:205], v191 offset:4096
	ds_read_b128 v[206:209], v191 offset:5120
	ds_read_b128 v[210:213], v191 offset:6144
	ds_read_b128 v[214:217], v191 offset:7168
	global_load_lds_dwordx4 v170, s[30:31]
	s_add_i32 m0, s29, 0xe000
	s_nop 0
	global_load_lds_dwordx4 v172, s[30:31]
	s_waitcnt vmcnt(8)
	s_waitcnt lgkmcnt(0)
	s_barrier
	s_setprio 1
	v_mfma_f32_16x16x128_f8f6f4 v[158:161], v[26:33], v[178:185], v[158:161]
	v_mfma_f32_16x16x128_f8f6f4 v[154:157], v[18:25], v[178:185], v[154:157]
	v_mfma_f32_16x16x128_f8f6f4 v[138:141], v[18:25], v[194:201], v[138:141]
	v_mfma_f32_16x16x128_f8f6f4 v[142:145], v[26:33], v[194:201], v[142:145]
	v_mfma_f32_16x16x128_f8f6f4 v[126:129], v[26:33], v[202:209], v[126:129]
	v_mfma_f32_16x16x128_f8f6f4 v[122:125], v[18:25], v[202:209], v[122:125]
	v_mfma_f32_16x16x128_f8f6f4 v[106:109], v[18:25], v[210:217], v[106:109]
	v_mfma_f32_16x16x128_f8f6f4 v[110:113], v[26:33], v[210:217], v[110:113]
	v_mfma_f32_16x16x128_f8f6f4 v[102:105], v[10:17], v[210:217], v[102:105]
	v_mfma_f32_16x16x128_f8f6f4 v[98:101], v[2:9], v[210:217], v[98:101]
	v_mfma_f32_16x16x128_f8f6f4 v[146:149], v[2:9], v[178:185], v[146:149]
	v_mfma_f32_16x16x128_f8f6f4 v[150:153], v[10:17], v[178:185], v[150:153]
	v_mfma_f32_16x16x128_f8f6f4 v[134:137], v[10:17], v[194:201], v[134:137]
	v_mfma_f32_16x16x128_f8f6f4 v[130:133], v[2:9], v[194:201], v[130:133]
	v_mfma_f32_16x16x128_f8f6f4 v[114:117], v[2:9], v[202:209], v[114:117]
	v_mfma_f32_16x16x128_f8f6f4 v[118:121], v[10:17], v[202:209], v[118:121]
	s_setprio 0
	s_barrier
	s_add_i32 s61, s45, s3
	s_mov_b32 m0, s61
	ds_read_b128 v[194:197], v191 offset:16384
	ds_read_b128 v[198:201], v191 offset:17408
	ds_read_b128 v[202:205], v191 offset:18432
	ds_read_b128 v[206:209], v191 offset:19456
	ds_read_b128 v[210:213], v191 offset:20480
	ds_read_b128 v[214:217], v191 offset:21504
	ds_read_b128 v[218:221], v191 offset:22528
	ds_read_b128 v[222:225], v191 offset:23552
	global_load_lds_dwordx4 v166, s[34:35]
	s_add_i32 m0, s61, 0x2000
	s_add_u32 s62, s34, 0x80000
	s_addc_u32 s63, s35, 0
	s_add_i32 s61, s48, s3
	global_load_lds_dwordx4 v162, s[34:35]
	s_mov_b32 m0, s61
	s_nop 0
	global_load_lds_dwordx4 v166, s[62:63]
	s_add_i32 m0, s61, 0x2000
	s_nop 0
	global_load_lds_dwordx4 v162, s[62:63]
	s_waitcnt vmcnt(6)
	s_waitcnt lgkmcnt(0)
	s_barrier
	s_setprio 1
	v_mfma_f32_16x16x128_f8f6f4 v[78:81], v[26:33], v[202:209], v[78:81]
	v_mfma_f32_16x16x128_f8f6f4 v[74:77], v[18:25], v[202:209], v[74:77]
	v_mfma_f32_16x16x128_f8f6f4 v[90:93], v[18:25], v[194:201], v[90:93]
	v_mfma_f32_16x16x128_f8f6f4 v[94:97], v[26:33], v[194:201], v[94:97]
	v_mfma_f32_16x16x128_f8f6f4 v[62:65], v[26:33], v[210:217], v[62:65]
	v_mfma_f32_16x16x128_f8f6f4 v[58:61], v[18:25], v[210:217], v[58:61]
	v_mfma_f32_16x16x128_f8f6f4 v[42:45], v[18:25], v[218:225], v[42:45]
	v_mfma_f32_16x16x128_f8f6f4 v[46:49], v[26:33], v[218:225], v[46:49]
	v_mfma_f32_16x16x128_f8f6f4 v[38:41], v[10:17], v[218:225], v[38:41]
	v_mfma_f32_16x16x128_f8f6f4 v[34:37], v[2:9], v[218:225], v[34:37]
	v_mfma_f32_16x16x128_f8f6f4 v[82:85], v[2:9], v[194:201], v[82:85]
	v_mfma_f32_16x16x128_f8f6f4 v[86:89], v[10:17], v[194:201], v[86:89]
	v_mfma_f32_16x16x128_f8f6f4 v[70:73], v[10:17], v[202:209], v[70:73]
	v_mfma_f32_16x16x128_f8f6f4 v[66:69], v[2:9], v[202:209], v[66:69]
	v_mfma_f32_16x16x128_f8f6f4 v[50:53], v[2:9], v[210:217], v[50:53]
	v_mfma_f32_16x16x128_f8f6f4 v[54:57], v[10:17], v[210:217], v[54:57]
	s_setprio 0
	s_barrier
	s_add_i32 s61, 0, 0x18000
	s_add_i32 s62, 0, 0x1c000
	v_add_u32_e32 v14, s61, v187
	v_add_u32_e32 v30, s62, v187
	ds_read_b128 v[2:5], v14
	ds_read_b128 v[6:9], v14 offset:1024
	ds_read_b128 v[10:13], v14 offset:2048
	ds_read_b128 v[14:17], v14 offset:3072
	ds_read_b128 v[18:21], v30
	ds_read_b128 v[22:25], v30 offset:1024
	ds_read_b128 v[26:29], v30 offset:2048
	ds_read_b128 v[30:33], v30 offset:3072
	s_mov_b32 m0, s29
	s_nop 0
	global_load_lds_dwordx4 v168, s[36:37]
	s_mov_b32 m0, s38
	s_nop 0
	global_load_lds_dwordx4 v164, s[36:37]
	s_add_u32 s36, s36, 0x80000
	s_addc_u32 s37, s37, 0
	s_add_u32 s100, s36, 0xfff80080
	s_addc_u32 s101, s37, -1
	s_mov_b32 m0, s39
	ds_read_b128 v[194:197], v191 offset:32768
	ds_read_b128 v[198:201], v191 offset:33792
	ds_read_b128 v[202:205], v191 offset:34816
	ds_read_b128 v[206:209], v191 offset:35840
	ds_read_b128 v[210:213], v191 offset:36864
	ds_read_b128 v[214:217], v191 offset:37888
	ds_read_b128 v[218:221], v191 offset:38912
	ds_read_b128 v[222:225], v191 offset:39936
	global_load_lds_dwordx4 v168, s[36:37]
	s_mov_b32 m0, s40
	s_nop 0
	global_load_lds_dwordx4 v164, s[36:37]
	s_waitcnt vmcnt(8)
	s_waitcnt lgkmcnt(0)
	s_barrier
	s_setprio 1
	v_mfma_f32_16x16x128_f8f6f4 v[122:125], v[10:17], v[210:217], v[122:125]
	v_mfma_f32_16x16x128_f8f6f4 v[126:129], v[2:9], v[210:217], v[126:129]
	v_mfma_f32_16x16x128_f8f6f4 v[158:161], v[2:9], v[194:201], v[158:161]
	v_mfma_f32_16x16x128_f8f6f4 v[154:157], v[10:17], v[194:201], v[154:157]
	v_mfma_f32_16x16x128_f8f6f4 v[138:141], v[10:17], v[202:209], v[138:141]
	v_mfma_f32_16x16x128_f8f6f4 v[142:145], v[2:9], v[202:209], v[142:145]
	v_mfma_f32_16x16x128_f8f6f4 v[110:113], v[2:9], v[218:225], v[110:113]
	v_mfma_f32_16x16x128_f8f6f4 v[106:109], v[10:17], v[218:225], v[106:109]
	v_mfma_f32_16x16x128_f8f6f4 v[102:105], v[18:25], v[218:225], v[102:105]
	v_mfma_f32_16x16x128_f8f6f4 v[98:101], v[26:33], v[218:225], v[98:101]
	v_mfma_f32_16x16x128_f8f6f4 v[146:149], v[26:33], v[194:201], v[146:149]
	v_mfma_f32_16x16x128_f8f6f4 v[150:153], v[18:25], v[194:201], v[150:153]
	v_mfma_f32_16x16x128_f8f6f4 v[134:137], v[18:25], v[202:209], v[134:137]
	v_mfma_f32_16x16x128_f8f6f4 v[130:133], v[26:33], v[202:209], v[130:133]
	v_mfma_f32_16x16x128_f8f6f4 v[114:117], v[26:33], v[210:217], v[114:117]
	v_mfma_f32_16x16x128_f8f6f4 v[118:121], v[18:25], v[210:217], v[118:121]
	s_setprio 0
	s_barrier
	s_add_i32 s36, s61, s3
	s_mov_b32 m0, s36
	s_add_u32 s98, s34, 0x80
	s_addc_u32 s99, s35, 0
	ds_read_b128 v[194:197], v191 offset:49152
	ds_read_b128 v[198:201], v191 offset:50176
	ds_read_b128 v[202:205], v191 offset:51200
	ds_read_b128 v[206:209], v191 offset:52224
	ds_read_b128 v[210:213], v191 offset:53248
	ds_read_b128 v[214:217], v191 offset:54272
	ds_read_b128 v[218:221], v191 offset:55296
	ds_read_b128 v[222:225], v191 offset:56320
	global_load_lds_dwordx4 v166, s[98:99]
	s_add_i32 m0, s36, 0x2000
	s_add_u32 s34, s34, 0x80080
	s_addc_u32 s35, s35, 0
	s_add_i32 s36, s62, s3
	global_load_lds_dwordx4 v162, s[98:99]
	s_mov_b32 m0, s36
	s_nop 0
	global_load_lds_dwordx4 v166, s[34:35]
	s_add_i32 m0, s36, 0x2000
	s_nop 0
	global_load_lds_dwordx4 v162, s[34:35]
	s_waitcnt vmcnt(6)
	s_waitcnt lgkmcnt(0)
	s_barrier
	s_setprio 1
	v_mfma_f32_16x16x128_f8f6f4 v[62:65], v[2:9], v[210:217], v[62:65]
	v_mfma_f32_16x16x128_f8f6f4 v[58:61], v[10:17], v[210:217], v[58:61]
	v_mfma_f32_16x16x128_f8f6f4 v[90:93], v[10:17], v[194:201], v[90:93]
	v_mfma_f32_16x16x128_f8f6f4 v[94:97], v[2:9], v[194:201], v[94:97]
	v_mfma_f32_16x16x128_f8f6f4 v[78:81], v[2:9], v[202:209], v[78:81]
	v_mfma_f32_16x16x128_f8f6f4 v[74:77], v[10:17], v[202:209], v[74:77]
	v_mfma_f32_16x16x128_f8f6f4 v[42:45], v[10:17], v[218:225], v[42:45]
	v_mfma_f32_16x16x128_f8f6f4 v[46:49], v[2:9], v[218:225], v[46:49]
	v_mfma_f32_16x16x128_f8f6f4 v[38:41], v[18:25], v[218:225], v[38:41]
	v_mfma_f32_16x16x128_f8f6f4 v[34:37], v[26:33], v[218:225], v[34:37]
	v_mfma_f32_16x16x128_f8f6f4 v[82:85], v[26:33], v[194:201], v[82:85]
	v_mfma_f32_16x16x128_f8f6f4 v[86:89], v[18:25], v[194:201], v[86:89]
	v_mfma_f32_16x16x128_f8f6f4 v[70:73], v[18:25], v[202:209], v[70:73]
	v_mfma_f32_16x16x128_f8f6f4 v[66:69], v[26:33], v[202:209], v[66:69]
	v_mfma_f32_16x16x128_f8f6f4 v[50:53], v[26:33], v[210:217], v[50:53]
	v_mfma_f32_16x16x128_f8f6f4 v[54:57], v[18:25], v[210:217], v[54:57]
	s_setprio 0
	s_barrier
	s_add_i32 s60, s60, 2
	s_add_u32 s30, s30, 0x100
	s_addc_u32 s31, s31, 0
	s_add_u32 s58, s58, 0x100
	s_addc_u32 s59, s59, 0
	s_cmp_gt_u32 s60, 29
	s_cbranch_scc0 .LBB0_1681
	s_and_b64 vcc, exec, s[12:13]
	s_cbranch_vccz .LBB0_1684
	s_barrier
.LBB0_1684:
	v_pk_mul_f32 v[10:11], v[158:159], s[14:15] op_sel_hi:[1,0]
	v_pk_mul_f32 v[8:9], v[160:161], s[14:15] op_sel_hi:[1,0]
	v_mul_f32_e32 v7, 0xbfb8aa3b, v10
	v_exp_f32_e32 v7, v7
	v_mul_f32_e32 v22, 0xbfb8aa3b, v11
	v_exp_f32_e32 v24, v22
	v_pk_mul_f32 v[18:19], v[150:151], s[16:17] op_sel_hi:[1,0]
	v_add_f32_e32 v7, 1.0, v7
	v_rcp_f32_e32 v7, v7
	v_pk_mul_f32 v[14:15], v[154:155], s[14:15] op_sel_hi:[1,0]
	v_pk_mul_f32 v[16:17], v[152:153], s[16:17] op_sel_hi:[1,0]
	v_pk_mul_f32 v[12:13], v[156:157], s[14:15] op_sel_hi:[1,0]
	v_mul_f32_e32 v7, v10, v7
	v_mul_f32_e32 v7, v7, v18
	v_add_f32_e32 v10, 1.0, v24
	v_mul_f32_e32 v18, 0xbfb8aa3b, v8
	v_rcp_f32_e32 v10, v10
	v_exp_f32_e32 v18, v18
	v_mul_f32_e32 v24, 0xbfb8aa3b, v9
	v_exp_f32_e32 v24, v24
	v_mul_f32_e32 v10, v11, v10
	v_add_f32_e32 v11, 1.0, v18
	v_rcp_f32_e32 v11, v11
	v_add_f32_e32 v18, 1.0, v24
	v_rcp_f32_e32 v18, v18
	v_mul_f32_e32 v10, v10, v19
	v_mul_f32_e32 v8, v8, v11
	v_mul_f32_e32 v11, v8, v16
	v_mul_f32_e32 v16, 0xbfb8aa3b, v14
	v_exp_f32_e32 v16, v16
	v_mul_f32_e32 v8, v9, v18
	v_mul_f32_e32 v9, v8, v17
	v_med3_f32 v7, v7, s50, v192
	v_med3_f32 v10, v10, s50, v192
	v_cvt_pk_fp8_f32 v8, v7, v10
	v_add_f32_e32 v10, 1.0, v16
	v_rcp_f32_e32 v10, v10
	v_med3_f32 v7, v11, s50, v192
	v_mul_f32_e32 v11, 0xbfb8aa3b, v15
	v_exp_f32_e32 v11, v11
	v_med3_f32 v9, v9, s50, v192
	v_cvt_pk_fp8_f32 v8, v7, v9 op_sel:[0,0,1]
	v_mul_f32_e32 v7, v14, v10
	v_mul_f32_e32 v10, 0xbfb8aa3b, v12
	v_exp_f32_e32 v10, v10
	v_add_f32_e32 v9, 1.0, v11
	v_mul_f32_e32 v11, 0xbfb8aa3b, v13
	v_exp_f32_e32 v11, v11
	v_rcp_f32_e32 v9, v9
	v_add_f32_e32 v10, 1.0, v10
	v_rcp_f32_e32 v10, v10
	v_add_f32_e32 v11, 1.0, v11
	v_pk_mul_f32 v[22:23], v[146:147], s[16:17] op_sel_hi:[1,0]
	v_mul_f32_e32 v9, v15, v9
	v_rcp_f32_e32 v11, v11
	v_mul_f32_e32 v7, v7, v22
	v_mul_f32_e32 v9, v9, v23
	v_mul_f32_e32 v10, v12, v10
	v_med3_f32 v7, v7, s50, v192
	v_med3_f32 v12, v9, s50, v192
	v_cvt_pk_fp8_f32 v9, v7, v12
	v_pk_mul_f32 v[20:21], v[148:149], s[16:17] op_sel_hi:[1,0]
	v_mul_f32_e32 v11, v13, v11
	v_mul_f32_e32 v10, v10, v20
	v_mul_f32_e32 v7, v11, v21
	v_med3_f32 v10, v10, s50, v192
	v_med3_f32 v7, v7, s50, v192
	v_cvt_pk_fp8_f32 v9, v10, v7 op_sel:[0,0,1]
	v_lshl_add_u32 v6, s28, 8, v186
	v_lshl_or_b32 v2, s51, 7, v188
	v_mov_b64_e32 v[4:5], s[96:97]
	v_ashrrev_i32_e32 v3, 31, v2
	v_mad_i64_i32 v[10:11], s[18:19], v6, s49, v[4:5]
	v_lshl_add_u64 v[10:11], v[10:11], 0, v[2:3]
	global_store_dwordx2 v[10:11], v[8:9], off
	v_pk_mul_f32 v[10:11], v[142:143], s[14:15] op_sel_hi:[1,0]
	v_pk_mul_f32 v[8:9], v[144:145], s[14:15] op_sel_hi:[1,0]
	v_mul_f32_e32 v16, 0xbfb8aa3b, v10
	v_exp_f32_e32 v22, v16
	v_pk_mul_f32 v[18:19], v[134:135], s[16:17] op_sel_hi:[1,0]
	v_pk_mul_f32 v[16:17], v[136:137], s[16:17] op_sel_hi:[1,0]
	v_pk_mul_f32 v[14:15], v[138:139], s[14:15] op_sel_hi:[1,0]
	v_add_f32_e32 v22, 1.0, v22
	v_rcp_f32_e32 v24, v22
	v_mul_f32_e32 v22, 0xbfb8aa3b, v11
	v_exp_f32_e32 v25, v22
	v_pk_mul_f32 v[12:13], v[140:141], s[14:15] op_sel_hi:[1,0]
	v_mul_f32_e32 v10, v10, v24
	v_mul_f32_e32 v10, v10, v18
	v_add_f32_e32 v18, 1.0, v25
	v_mul_f32_e32 v24, 0xbfb8aa3b, v8
	v_rcp_f32_e32 v18, v18
	v_exp_f32_e32 v24, v24
	v_mul_f32_e32 v25, 0xbfb8aa3b, v9
	v_exp_f32_e32 v25, v25
	v_mul_f32_e32 v11, v11, v18
	v_add_f32_e32 v18, 1.0, v24
	v_rcp_f32_e32 v18, v18
	v_add_f32_e32 v24, 1.0, v25
	v_rcp_f32_e32 v24, v24
	v_mul_f32_e32 v11, v11, v19
	v_mul_f32_e32 v8, v8, v18
	v_mul_f32_e32 v16, v8, v16
	v_mul_f32_e32 v8, v9, v24
	v_mul_f32_e32 v9, v8, v17
	v_mul_f32_e32 v17, 0xbfb8aa3b, v14
	v_exp_f32_e32 v17, v17
	v_med3_f32 v10, v10, s50, v192
	v_med3_f32 v11, v11, s50, v192
	v_cvt_pk_fp8_f32 v8, v10, v11
	v_add_f32_e32 v11, 1.0, v17
	v_rcp_f32_e32 v11, v11
	v_med3_f32 v10, v16, s50, v192
	v_mul_f32_e32 v16, 0xbfb8aa3b, v15
	v_med3_f32 v9, v9, s50, v192
	v_exp_f32_e32 v16, v16
	v_cvt_pk_fp8_f32 v8, v10, v9 op_sel:[0,0,1]
	v_mul_f32_e32 v9, v14, v11
	v_mul_f32_e32 v11, 0xbfb8aa3b, v12
	v_mul_f32_e32 v14, 0xbfb8aa3b, v13
	v_exp_f32_e32 v11, v11
	v_exp_f32_e32 v14, v14
	v_add_f32_e32 v10, 1.0, v16
	v_rcp_f32_e32 v10, v10
	v_add_f32_e32 v11, 1.0, v11
	v_add_f32_e32 v14, 1.0, v14
	v_rcp_f32_e32 v11, v11
	v_rcp_f32_e32 v14, v14
	v_pk_mul_f32 v[22:23], v[130:131], s[16:17] op_sel_hi:[1,0]
	v_mul_f32_e32 v10, v15, v10
	v_mul_f32_e32 v9, v9, v22
	v_mul_f32_e32 v10, v10, v23
	v_mul_f32_e32 v11, v12, v11
	v_mul_f32_e32 v12, v13, v14
	v_med3_f32 v13, v9, s50, v192
	v_med3_f32 v10, v10, s50, v192
	v_cvt_pk_fp8_f32 v9, v13, v10
	v_pk_mul_f32 v[20:21], v[132:133], s[16:17] op_sel_hi:[1,0]
	v_or_b32_e32 v7, 16, v6
	v_mul_f32_e32 v11, v11, v20
	v_mul_f32_e32 v10, v12, v21
	v_med3_f32 v11, v11, s50, v192
	v_med3_f32 v10, v10, s50, v192
	v_cvt_pk_fp8_f32 v9, v11, v10 op_sel:[0,0,1]
	v_mad_i64_i32 v[10:11], s[18:19], v7, s49, v[4:5]
	v_lshl_add_u64 v[10:11], v[10:11], 0, v[2:3]
	global_store_dwordx2 v[10:11], v[8:9], off
	v_pk_mul_f32 v[10:11], v[126:127], s[14:15] op_sel_hi:[1,0]
	v_pk_mul_f32 v[8:9], v[128:129], s[14:15] op_sel_hi:[1,0]
	v_mul_f32_e32 v16, 0xbfb8aa3b, v10
	v_exp_f32_e32 v22, v16
	v_pk_mul_f32 v[18:19], v[118:119], s[16:17] op_sel_hi:[1,0]
	v_pk_mul_f32 v[16:17], v[120:121], s[16:17] op_sel_hi:[1,0]
	v_pk_mul_f32 v[14:15], v[122:123], s[14:15] op_sel_hi:[1,0]
	v_add_f32_e32 v22, 1.0, v22
	v_rcp_f32_e32 v24, v22
	v_mul_f32_e32 v22, 0xbfb8aa3b, v11
	v_exp_f32_e32 v25, v22
	v_pk_mul_f32 v[12:13], v[124:125], s[14:15] op_sel_hi:[1,0]
	v_mul_f32_e32 v10, v10, v24
	v_mul_f32_e32 v10, v10, v18
	v_add_f32_e32 v18, 1.0, v25
	v_mul_f32_e32 v24, 0xbfb8aa3b, v8
	v_rcp_f32_e32 v18, v18
	v_exp_f32_e32 v24, v24
	v_mul_f32_e32 v25, 0xbfb8aa3b, v9
	v_exp_f32_e32 v25, v25
	v_mul_f32_e32 v11, v11, v18
	v_add_f32_e32 v18, 1.0, v24
	v_rcp_f32_e32 v18, v18
	v_add_f32_e32 v24, 1.0, v25
	v_rcp_f32_e32 v24, v24
	v_mul_f32_e32 v11, v11, v19
	v_mul_f32_e32 v8, v8, v18
	v_mul_f32_e32 v16, v8, v16
	v_mul_f32_e32 v8, v9, v24
	v_mul_f32_e32 v9, v8, v17
	v_mul_f32_e32 v17, 0xbfb8aa3b, v14
	v_exp_f32_e32 v17, v17
	v_med3_f32 v10, v10, s50, v192
	v_med3_f32 v11, v11, s50, v192
	v_cvt_pk_fp8_f32 v8, v10, v11
	v_add_f32_e32 v11, 1.0, v17
	v_rcp_f32_e32 v11, v11
	v_med3_f32 v10, v16, s50, v192
	v_mul_f32_e32 v16, 0xbfb8aa3b, v15
	v_med3_f32 v9, v9, s50, v192
	v_exp_f32_e32 v16, v16
	v_cvt_pk_fp8_f32 v8, v10, v9 op_sel:[0,0,1]
	v_mul_f32_e32 v9, v14, v11
	v_mul_f32_e32 v11, 0xbfb8aa3b, v12
	v_mul_f32_e32 v14, 0xbfb8aa3b, v13
	v_exp_f32_e32 v11, v11
	v_exp_f32_e32 v14, v14
	v_add_f32_e32 v10, 1.0, v16
	v_rcp_f32_e32 v10, v10
	v_add_f32_e32 v11, 1.0, v11
	v_add_f32_e32 v14, 1.0, v14
	v_rcp_f32_e32 v11, v11
	v_rcp_f32_e32 v14, v14
	v_pk_mul_f32 v[22:23], v[114:115], s[16:17] op_sel_hi:[1,0]
	v_mul_f32_e32 v10, v15, v10
	v_mul_f32_e32 v9, v9, v22
	v_mul_f32_e32 v10, v10, v23
	v_mul_f32_e32 v11, v12, v11
	v_mul_f32_e32 v12, v13, v14
	v_med3_f32 v13, v9, s50, v192
	v_med3_f32 v10, v10, s50, v192
	v_cvt_pk_fp8_f32 v9, v13, v10
	v_pk_mul_f32 v[20:21], v[116:117], s[16:17] op_sel_hi:[1,0]
	v_or_b32_e32 v7, 32, v6
	v_mul_f32_e32 v11, v11, v20
	v_mul_f32_e32 v10, v12, v21
	v_med3_f32 v11, v11, s50, v192
	v_med3_f32 v10, v10, s50, v192
	v_cvt_pk_fp8_f32 v9, v11, v10 op_sel:[0,0,1]
	v_mad_i64_i32 v[10:11], s[18:19], v7, s49, v[4:5]
	v_lshl_add_u64 v[10:11], v[10:11], 0, v[2:3]
	global_store_dwordx2 v[10:11], v[8:9], off
	v_pk_mul_f32 v[10:11], v[110:111], s[14:15] op_sel_hi:[1,0]
	v_pk_mul_f32 v[8:9], v[112:113], s[14:15] op_sel_hi:[1,0]
	v_mul_f32_e32 v16, 0xbfb8aa3b, v10
	v_exp_f32_e32 v22, v16
	v_pk_mul_f32 v[18:19], v[102:103], s[16:17] op_sel_hi:[1,0]
	v_pk_mul_f32 v[16:17], v[104:105], s[16:17] op_sel_hi:[1,0]
	v_pk_mul_f32 v[14:15], v[106:107], s[14:15] op_sel_hi:[1,0]
	v_add_f32_e32 v22, 1.0, v22
	v_rcp_f32_e32 v24, v22
	v_mul_f32_e32 v22, 0xbfb8aa3b, v11
	v_exp_f32_e32 v25, v22
	v_pk_mul_f32 v[12:13], v[108:109], s[14:15] op_sel_hi:[1,0]
	v_mul_f32_e32 v10, v10, v24
	v_mul_f32_e32 v10, v10, v18
	v_add_f32_e32 v18, 1.0, v25
	v_mul_f32_e32 v24, 0xbfb8aa3b, v8
	v_rcp_f32_e32 v18, v18
	v_exp_f32_e32 v24, v24
	v_mul_f32_e32 v25, 0xbfb8aa3b, v9
	v_exp_f32_e32 v25, v25
	v_mul_f32_e32 v11, v11, v18
	v_add_f32_e32 v18, 1.0, v24
	v_rcp_f32_e32 v18, v18
	v_add_f32_e32 v24, 1.0, v25
	v_rcp_f32_e32 v24, v24
	v_mul_f32_e32 v11, v11, v19
	v_mul_f32_e32 v8, v8, v18
	v_mul_f32_e32 v16, v8, v16
	v_mul_f32_e32 v8, v9, v24
	v_mul_f32_e32 v9, v8, v17
	v_mul_f32_e32 v17, 0xbfb8aa3b, v14
	v_exp_f32_e32 v17, v17
	v_med3_f32 v10, v10, s50, v192
	v_med3_f32 v11, v11, s50, v192
	v_cvt_pk_fp8_f32 v8, v10, v11
	v_add_f32_e32 v11, 1.0, v17
	v_rcp_f32_e32 v11, v11
	v_med3_f32 v10, v16, s50, v192
	v_mul_f32_e32 v16, 0xbfb8aa3b, v15
	v_med3_f32 v9, v9, s50, v192
	v_exp_f32_e32 v16, v16
	v_cvt_pk_fp8_f32 v8, v10, v9 op_sel:[0,0,1]
	v_mul_f32_e32 v9, v14, v11
	v_mul_f32_e32 v11, 0xbfb8aa3b, v12
	v_mul_f32_e32 v14, 0xbfb8aa3b, v13
	v_exp_f32_e32 v11, v11
	v_exp_f32_e32 v14, v14
	v_add_f32_e32 v10, 1.0, v16
	v_rcp_f32_e32 v10, v10
	v_add_f32_e32 v11, 1.0, v11
	v_add_f32_e32 v14, 1.0, v14
	v_rcp_f32_e32 v11, v11
	v_rcp_f32_e32 v14, v14
	v_pk_mul_f32 v[22:23], v[98:99], s[16:17] op_sel_hi:[1,0]
	v_mul_f32_e32 v10, v15, v10
	v_mul_f32_e32 v9, v9, v22
	v_mul_f32_e32 v10, v10, v23
	v_mul_f32_e32 v11, v12, v11
	v_mul_f32_e32 v12, v13, v14
	v_med3_f32 v13, v9, s50, v192
	v_med3_f32 v10, v10, s50, v192
	v_cvt_pk_fp8_f32 v9, v13, v10
	v_pk_mul_f32 v[20:21], v[100:101], s[16:17] op_sel_hi:[1,0]
	v_or_b32_e32 v7, 48, v6
	v_mul_f32_e32 v11, v11, v20
	v_mul_f32_e32 v10, v12, v21
	v_med3_f32 v11, v11, s50, v192
	v_med3_f32 v10, v10, s50, v192
	v_cvt_pk_fp8_f32 v9, v11, v10 op_sel:[0,0,1]
	v_mad_i64_i32 v[10:11], s[18:19], v7, s49, v[4:5]
	v_lshl_add_u64 v[10:11], v[10:11], 0, v[2:3]
	global_store_dwordx2 v[10:11], v[8:9], off
	v_pk_mul_f32 v[10:11], v[94:95], s[14:15] op_sel_hi:[1,0]
	v_pk_mul_f32 v[8:9], v[96:97], s[14:15] op_sel_hi:[1,0]
	v_mul_f32_e32 v16, 0xbfb8aa3b, v10
	v_exp_f32_e32 v22, v16
	v_pk_mul_f32 v[18:19], v[86:87], s[16:17] op_sel_hi:[1,0]
	v_pk_mul_f32 v[16:17], v[88:89], s[16:17] op_sel_hi:[1,0]
	v_pk_mul_f32 v[14:15], v[90:91], s[14:15] op_sel_hi:[1,0]
	v_add_f32_e32 v22, 1.0, v22
	v_rcp_f32_e32 v24, v22
	v_mul_f32_e32 v22, 0xbfb8aa3b, v11
	v_exp_f32_e32 v25, v22
	v_pk_mul_f32 v[12:13], v[92:93], s[14:15] op_sel_hi:[1,0]
	v_mul_f32_e32 v10, v10, v24
	v_mul_f32_e32 v10, v10, v18
	v_add_f32_e32 v18, 1.0, v25
	v_mul_f32_e32 v24, 0xbfb8aa3b, v8
	v_rcp_f32_e32 v18, v18
	v_exp_f32_e32 v24, v24
	v_mul_f32_e32 v25, 0xbfb8aa3b, v9
	v_exp_f32_e32 v25, v25
	v_mul_f32_e32 v11, v11, v18
	v_add_f32_e32 v18, 1.0, v24
	v_rcp_f32_e32 v18, v18
	v_add_f32_e32 v24, 1.0, v25
	v_rcp_f32_e32 v24, v24
	v_mul_f32_e32 v11, v11, v19
	v_mul_f32_e32 v8, v8, v18
	v_mul_f32_e32 v16, v8, v16
	v_mul_f32_e32 v8, v9, v24
	v_mul_f32_e32 v9, v8, v17
	v_mul_f32_e32 v17, 0xbfb8aa3b, v14
	v_exp_f32_e32 v17, v17
	v_med3_f32 v10, v10, s50, v192
	v_med3_f32 v11, v11, s50, v192
	v_cvt_pk_fp8_f32 v8, v10, v11
	v_add_f32_e32 v11, 1.0, v17
	v_rcp_f32_e32 v11, v11
	v_med3_f32 v10, v16, s50, v192
	v_mul_f32_e32 v16, 0xbfb8aa3b, v15
	v_med3_f32 v9, v9, s50, v192
	v_exp_f32_e32 v16, v16
	v_cvt_pk_fp8_f32 v8, v10, v9 op_sel:[0,0,1]
	v_mul_f32_e32 v9, v14, v11
	v_mul_f32_e32 v11, 0xbfb8aa3b, v12
	v_mul_f32_e32 v14, 0xbfb8aa3b, v13
	v_exp_f32_e32 v11, v11
	v_exp_f32_e32 v14, v14
	v_add_f32_e32 v10, 1.0, v16
	v_rcp_f32_e32 v10, v10
	v_add_f32_e32 v11, 1.0, v11
	v_add_f32_e32 v14, 1.0, v14
	v_rcp_f32_e32 v11, v11
	v_rcp_f32_e32 v14, v14
	v_pk_mul_f32 v[22:23], v[82:83], s[16:17] op_sel_hi:[1,0]
	v_mul_f32_e32 v10, v15, v10
	v_mul_f32_e32 v9, v9, v22
	v_mul_f32_e32 v10, v10, v23
	v_mul_f32_e32 v11, v12, v11
	v_mul_f32_e32 v12, v13, v14
	v_med3_f32 v13, v9, s50, v192
	v_med3_f32 v10, v10, s50, v192
	v_cvt_pk_fp8_f32 v9, v13, v10
	v_pk_mul_f32 v[20:21], v[84:85], s[16:17] op_sel_hi:[1,0]
	v_add_u32_e32 v7, 0x80, v6
	v_mul_f32_e32 v11, v11, v20
	v_mul_f32_e32 v10, v12, v21
	v_med3_f32 v11, v11, s50, v192
	v_med3_f32 v10, v10, s50, v192
	v_cvt_pk_fp8_f32 v9, v11, v10 op_sel:[0,0,1]
	v_mad_i64_i32 v[10:11], s[18:19], v7, s49, v[4:5]
	v_lshl_add_u64 v[10:11], v[10:11], 0, v[2:3]
	global_store_dwordx2 v[10:11], v[8:9], off
	v_pk_mul_f32 v[10:11], v[78:79], s[14:15] op_sel_hi:[1,0]
	v_pk_mul_f32 v[8:9], v[80:81], s[14:15] op_sel_hi:[1,0]
	v_mul_f32_e32 v16, 0xbfb8aa3b, v10
	v_exp_f32_e32 v22, v16
	v_pk_mul_f32 v[18:19], v[70:71], s[16:17] op_sel_hi:[1,0]
	v_pk_mul_f32 v[16:17], v[72:73], s[16:17] op_sel_hi:[1,0]
	v_pk_mul_f32 v[14:15], v[74:75], s[14:15] op_sel_hi:[1,0]
	v_add_f32_e32 v22, 1.0, v22
	v_rcp_f32_e32 v24, v22
	v_mul_f32_e32 v22, 0xbfb8aa3b, v11
	v_exp_f32_e32 v25, v22
	v_pk_mul_f32 v[12:13], v[76:77], s[14:15] op_sel_hi:[1,0]
	v_mul_f32_e32 v10, v10, v24
	v_mul_f32_e32 v10, v10, v18
	v_add_f32_e32 v18, 1.0, v25
	v_mul_f32_e32 v24, 0xbfb8aa3b, v8
	v_rcp_f32_e32 v18, v18
	v_exp_f32_e32 v24, v24
	v_mul_f32_e32 v25, 0xbfb8aa3b, v9
	v_exp_f32_e32 v25, v25
	v_mul_f32_e32 v11, v11, v18
	v_add_f32_e32 v18, 1.0, v24
	v_rcp_f32_e32 v18, v18
	v_add_f32_e32 v24, 1.0, v25
	v_rcp_f32_e32 v24, v24
	v_mul_f32_e32 v11, v11, v19
	v_mul_f32_e32 v8, v8, v18
	v_mul_f32_e32 v16, v8, v16
	v_mul_f32_e32 v8, v9, v24
	v_mul_f32_e32 v9, v8, v17
	v_mul_f32_e32 v17, 0xbfb8aa3b, v14
	v_exp_f32_e32 v17, v17
	v_med3_f32 v10, v10, s50, v192
	v_med3_f32 v11, v11, s50, v192
	v_cvt_pk_fp8_f32 v8, v10, v11
	v_add_f32_e32 v11, 1.0, v17
	v_rcp_f32_e32 v11, v11
	v_med3_f32 v10, v16, s50, v192
	v_mul_f32_e32 v16, 0xbfb8aa3b, v15
	v_med3_f32 v9, v9, s50, v192
	v_exp_f32_e32 v16, v16
	v_cvt_pk_fp8_f32 v8, v10, v9 op_sel:[0,0,1]
	v_mul_f32_e32 v9, v14, v11
	v_mul_f32_e32 v11, 0xbfb8aa3b, v12
	v_mul_f32_e32 v14, 0xbfb8aa3b, v13
	v_exp_f32_e32 v11, v11
	v_exp_f32_e32 v14, v14
	v_add_f32_e32 v10, 1.0, v16
	v_rcp_f32_e32 v10, v10
	v_add_f32_e32 v11, 1.0, v11
	v_add_f32_e32 v14, 1.0, v14
	v_rcp_f32_e32 v11, v11
	v_rcp_f32_e32 v14, v14
	v_pk_mul_f32 v[22:23], v[66:67], s[16:17] op_sel_hi:[1,0]
	v_mul_f32_e32 v10, v15, v10
	v_mul_f32_e32 v9, v9, v22
	v_mul_f32_e32 v10, v10, v23
	v_mul_f32_e32 v11, v12, v11
	v_mul_f32_e32 v12, v13, v14
	v_med3_f32 v13, v9, s50, v192
	v_med3_f32 v10, v10, s50, v192
	v_cvt_pk_fp8_f32 v9, v13, v10
	v_pk_mul_f32 v[20:21], v[68:69], s[16:17] op_sel_hi:[1,0]
	v_add_u32_e32 v7, 0x90, v6
	v_mul_f32_e32 v11, v11, v20
	v_mul_f32_e32 v10, v12, v21
	v_med3_f32 v11, v11, s50, v192
	v_med3_f32 v10, v10, s50, v192
	v_cvt_pk_fp8_f32 v9, v11, v10 op_sel:[0,0,1]
	v_mad_i64_i32 v[10:11], s[18:19], v7, s49, v[4:5]
	v_lshl_add_u64 v[10:11], v[10:11], 0, v[2:3]
	global_store_dwordx2 v[10:11], v[8:9], off
	v_pk_mul_f32 v[10:11], v[62:63], s[14:15] op_sel_hi:[1,0]
	v_pk_mul_f32 v[8:9], v[64:65], s[14:15] op_sel_hi:[1,0]
	v_mul_f32_e32 v16, 0xbfb8aa3b, v10
	v_exp_f32_e32 v22, v16
	v_pk_mul_f32 v[18:19], v[54:55], s[16:17] op_sel_hi:[1,0]
	v_pk_mul_f32 v[16:17], v[56:57], s[16:17] op_sel_hi:[1,0]
	v_pk_mul_f32 v[14:15], v[58:59], s[14:15] op_sel_hi:[1,0]
	v_add_f32_e32 v22, 1.0, v22
	v_rcp_f32_e32 v24, v22
	v_mul_f32_e32 v22, 0xbfb8aa3b, v11
	v_exp_f32_e32 v25, v22
	v_pk_mul_f32 v[12:13], v[60:61], s[14:15] op_sel_hi:[1,0]
	v_mul_f32_e32 v10, v10, v24
	v_mul_f32_e32 v10, v10, v18
	v_add_f32_e32 v18, 1.0, v25
	v_mul_f32_e32 v24, 0xbfb8aa3b, v8
	v_rcp_f32_e32 v18, v18
	v_exp_f32_e32 v24, v24
	v_mul_f32_e32 v25, 0xbfb8aa3b, v9
	v_exp_f32_e32 v25, v25
	v_mul_f32_e32 v11, v11, v18
	v_add_f32_e32 v18, 1.0, v24
	v_rcp_f32_e32 v18, v18
	v_add_f32_e32 v24, 1.0, v25
	v_rcp_f32_e32 v24, v24
	v_mul_f32_e32 v11, v11, v19
	v_mul_f32_e32 v8, v8, v18
	v_mul_f32_e32 v16, v8, v16
	v_mul_f32_e32 v8, v9, v24
	v_mul_f32_e32 v9, v8, v17
	v_mul_f32_e32 v17, 0xbfb8aa3b, v14
	v_exp_f32_e32 v17, v17
	v_med3_f32 v10, v10, s50, v192
	v_med3_f32 v11, v11, s50, v192
	v_cvt_pk_fp8_f32 v8, v10, v11
	v_add_f32_e32 v11, 1.0, v17
	v_rcp_f32_e32 v11, v11
	v_med3_f32 v10, v16, s50, v192
	v_mul_f32_e32 v16, 0xbfb8aa3b, v15
	v_med3_f32 v9, v9, s50, v192
	v_exp_f32_e32 v16, v16
	v_cvt_pk_fp8_f32 v8, v10, v9 op_sel:[0,0,1]
	v_mul_f32_e32 v9, v14, v11
	v_mul_f32_e32 v11, 0xbfb8aa3b, v12
	v_mul_f32_e32 v14, 0xbfb8aa3b, v13
	v_exp_f32_e32 v11, v11
	v_exp_f32_e32 v14, v14
	v_add_f32_e32 v10, 1.0, v16
	v_rcp_f32_e32 v10, v10
	v_add_f32_e32 v11, 1.0, v11
	v_add_f32_e32 v14, 1.0, v14
	v_rcp_f32_e32 v11, v11
	v_rcp_f32_e32 v14, v14
	v_pk_mul_f32 v[22:23], v[50:51], s[16:17] op_sel_hi:[1,0]
	v_mul_f32_e32 v10, v15, v10
	v_mul_f32_e32 v9, v9, v22
	v_mul_f32_e32 v10, v10, v23
	v_mul_f32_e32 v11, v12, v11
	v_mul_f32_e32 v12, v13, v14
	v_med3_f32 v13, v9, s50, v192
	v_med3_f32 v10, v10, s50, v192
	v_cvt_pk_fp8_f32 v9, v13, v10
	v_pk_mul_f32 v[20:21], v[52:53], s[16:17] op_sel_hi:[1,0]
	v_add_u32_e32 v7, 0xa0, v6
	v_mul_f32_e32 v11, v11, v20
	v_mul_f32_e32 v10, v12, v21
	v_med3_f32 v11, v11, s50, v192
	v_med3_f32 v10, v10, s50, v192
	v_cvt_pk_fp8_f32 v9, v11, v10 op_sel:[0,0,1]
	v_mad_i64_i32 v[10:11], s[18:19], v7, s49, v[4:5]
	v_lshl_add_u64 v[10:11], v[10:11], 0, v[2:3]
	global_store_dwordx2 v[10:11], v[8:9], off
	v_pk_mul_f32 v[8:9], v[46:47], s[14:15] op_sel_hi:[1,0]
	v_add_u32_e32 v22, 0xb0, v6
	v_mul_f32_e32 v14, 0xbfb8aa3b, v8
	v_exp_f32_e32 v20, v14
	v_pk_mul_f32 v[6:7], v[48:49], s[14:15] op_sel_hi:[1,0]
	v_pk_mul_f32 v[16:17], v[38:39], s[16:17] op_sel_hi:[1,0]
	v_pk_mul_f32 v[14:15], v[40:41], s[16:17] op_sel_hi:[1,0]
	v_add_f32_e32 v20, 1.0, v20
	v_rcp_f32_e32 v23, v20
	v_mul_f32_e32 v20, 0xbfb8aa3b, v9
	v_exp_f32_e32 v24, v20
	v_pk_mul_f32 v[12:13], v[42:43], s[14:15] op_sel_hi:[1,0]
	v_mul_f32_e32 v8, v8, v23
	v_mul_f32_e32 v8, v8, v16
	v_add_f32_e32 v16, 1.0, v24
	v_mul_f32_e32 v23, 0xbfb8aa3b, v6
	v_rcp_f32_e32 v16, v16
	v_exp_f32_e32 v23, v23
	v_mul_f32_e32 v24, 0xbfb8aa3b, v7
	v_exp_f32_e32 v24, v24
	v_mul_f32_e32 v9, v9, v16
	v_add_f32_e32 v16, 1.0, v23
	v_rcp_f32_e32 v16, v16
	v_add_f32_e32 v23, 1.0, v24
	v_rcp_f32_e32 v23, v23
	v_mul_f32_e32 v9, v9, v17
	v_mul_f32_e32 v6, v6, v16
	v_mul_f32_e32 v14, v6, v14
	v_mul_f32_e32 v6, v7, v23
	v_mul_f32_e32 v7, v6, v15
	v_mul_f32_e32 v15, 0xbfb8aa3b, v12
	v_exp_f32_e32 v15, v15
	v_med3_f32 v8, v8, s50, v192
	v_med3_f32 v9, v9, s50, v192
	v_cvt_pk_fp8_f32 v6, v8, v9
	v_add_f32_e32 v9, 1.0, v15
	v_rcp_f32_e32 v9, v9
	v_med3_f32 v8, v14, s50, v192
	v_mul_f32_e32 v14, 0xbfb8aa3b, v13
	v_pk_mul_f32 v[10:11], v[44:45], s[14:15] op_sel_hi:[1,0]
	v_med3_f32 v7, v7, s50, v192
	v_exp_f32_e32 v14, v14
	v_cvt_pk_fp8_f32 v6, v8, v7 op_sel:[0,0,1]
	v_mul_f32_e32 v7, v12, v9
	v_mul_f32_e32 v9, 0xbfb8aa3b, v10
	v_mul_f32_e32 v12, 0xbfb8aa3b, v11
	v_exp_f32_e32 v9, v9
	v_exp_f32_e32 v12, v12
	v_add_f32_e32 v8, 1.0, v14
	v_rcp_f32_e32 v8, v8
	v_add_f32_e32 v9, 1.0, v9
	v_add_f32_e32 v12, 1.0, v12
	v_rcp_f32_e32 v9, v9
	v_rcp_f32_e32 v12, v12
	v_pk_mul_f32 v[20:21], v[34:35], s[16:17] op_sel_hi:[1,0]
	v_mul_f32_e32 v8, v13, v8
	v_mul_f32_e32 v7, v7, v20
	v_mul_f32_e32 v8, v8, v21
	v_mul_f32_e32 v9, v10, v9
	v_mul_f32_e32 v10, v11, v12
	v_med3_f32 v11, v7, s50, v192
	v_med3_f32 v8, v8, s50, v192
	v_cvt_pk_fp8_f32 v7, v11, v8
	v_pk_mul_f32 v[18:19], v[36:37], s[16:17] op_sel_hi:[1,0]
	v_mad_i64_i32 v[4:5], s[18:19], v22, s49, v[4:5]
	v_mul_f32_e32 v9, v9, v18
	v_mul_f32_e32 v8, v10, v19
	v_med3_f32 v9, v9, s50, v192
	v_med3_f32 v8, v8, s50, v192
	v_cvt_pk_fp8_f32 v7, v9, v8 op_sel:[0,0,1]
	v_lshl_add_u64 v[2:3], v[4:5], 0, v[2:3]
	s_andn2_b64 vcc, exec, s[4:5]
	s_mov_b64 s[4:5], -1
	global_store_dwordx2 v[2:3], v[6:7], off
	s_cbranch_vccnz .LBB0_1677
	s_andn2_b64 vcc, exec, s[6:7]
	s_cbranch_vccnz .LBB0_1676
	s_barrier
	s_branch .LBB0_1676

.LBB0_1745:
	s_add_u32 s8, s49, s6
	s_addc_u32 s9, s50, s7
	s_add_u32 s8, s8, 0x32800100
	s_addc_u32 s9, s9, 0
	s_add_u32 s73, s51, s6
	s_addc_u32 s74, s54, s7
	s_add_i32 s72, 0, 0x10000
	s_cmpk_eq_i32 s6, 0x2a00
	s_cselect_b32 s37, s5, s9
	s_cselect_b32 s36, s4, s8
	s_cselect_b32 s9, s13, s74
	s_cselect_b32 s8, s12, s73
	s_add_i32 s73, 0, 0x14000
	v_add_u32_e32 v2, s72, v188
	v_add_u32_e32 v6, s73, v188
	ds_read_b128 v[26:29], v2
	ds_read_b128 v[30:33], v2 offset:1024
	ds_read_b128 v[18:21], v2 offset:2048
	ds_read_b128 v[22:25], v2 offset:3072
	ds_read_b128 v[10:13], v6
	ds_read_b128 v[14:17], v6 offset:1024
	ds_read_b128 v[2:5], v6 offset:2048
	ds_read_b128 v[6:9], v6 offset:3072
	v_lshl_add_u64 v[214:215], v[168:169], 0, s[6:7]
	s_add_i32 m0, s64, 0xc000
	ds_read_b128 v[172:175], v189
	ds_read_b128 v[176:179], v189 offset:1024
	ds_read_b128 v[190:193], v189 offset:2048
	ds_read_b128 v[194:197], v189 offset:3072
	ds_read_b128 v[198:201], v189 offset:4096
	ds_read_b128 v[202:205], v189 offset:5120
	ds_read_b128 v[206:209], v189 offset:6144
	ds_read_b128 v[210:213], v189 offset:7168
	global_load_lds_dwordx4 v[214:215], off
	v_lshl_add_u64 v[214:215], v[170:171], 0, s[6:7]
	s_add_i32 m0, s64, 0xe000
	s_nop 0
	global_load_lds_dwordx4 v[214:215], off
	s_waitcnt vmcnt(8)
	s_waitcnt lgkmcnt(0)
	s_barrier
	s_setprio 1
	v_mfma_f32_16x16x128_f8f6f4 v[158:161], v[26:33], v[172:179], v[158:161]
	v_mfma_f32_16x16x128_f8f6f4 v[154:157], v[18:25], v[172:179], v[154:157]
	v_mfma_f32_16x16x128_f8f6f4 v[118:121], v[18:25], v[190:197], v[118:121]
	v_mfma_f32_16x16x128_f8f6f4 v[122:125], v[26:33], v[190:197], v[122:125]
	v_mfma_f32_16x16x128_f8f6f4 v[126:129], v[26:33], v[198:205], v[126:129]
	v_mfma_f32_16x16x128_f8f6f4 v[114:117], v[18:25], v[198:205], v[114:117]
	v_mfma_f32_16x16x128_f8f6f4 v[106:109], v[18:25], v[206:213], v[106:109]
	v_mfma_f32_16x16x128_f8f6f4 v[110:113], v[26:33], v[206:213], v[110:113]
	v_mfma_f32_16x16x128_f8f6f4 v[102:105], v[10:17], v[206:213], v[102:105]
	v_mfma_f32_16x16x128_f8f6f4 v[98:101], v[2:9], v[206:213], v[98:101]
	v_mfma_f32_16x16x128_f8f6f4 v[146:149], v[2:9], v[172:179], v[146:149]
	v_mfma_f32_16x16x128_f8f6f4 v[150:153], v[10:17], v[172:179], v[150:153]
	v_mfma_f32_16x16x128_f8f6f4 v[142:145], v[10:17], v[190:197], v[142:145]
	v_mfma_f32_16x16x128_f8f6f4 v[138:141], v[2:9], v[190:197], v[138:141]
	v_mfma_f32_16x16x128_f8f6f4 v[130:133], v[2:9], v[198:205], v[130:133]
	v_mfma_f32_16x16x128_f8f6f4 v[134:137], v[10:17], v[198:205], v[134:137]
	s_setprio 0
	s_barrier
	s_add_i32 s72, s72, s43
	v_lshl_add_u64 v[172:173], s[8:9], 0, v[162:163]
	s_mov_b32 m0, s72
	ds_read_b128 v[190:193], v189 offset:16384
	ds_read_b128 v[194:197], v189 offset:17408
	ds_read_b128 v[198:201], v189 offset:18432
	ds_read_b128 v[202:205], v189 offset:19456
	ds_read_b128 v[206:209], v189 offset:20480
	ds_read_b128 v[210:213], v189 offset:21504
	ds_read_b128 v[214:217], v189 offset:22528
	ds_read_b128 v[218:221], v189 offset:23552
	global_load_lds_dwordx4 v[172:173], off
	s_add_i32 m0, s72, 0x2000
	s_add_u32 s74, s8, 0x158000
	v_lshl_add_u64 v[174:175], s[8:9], 0, v[166:167]
	s_addc_u32 s75, s9, 0
	s_add_i32 s72, s73, s43
	global_load_lds_dwordx4 v[174:175], off
	v_lshl_add_u64 v[176:177], s[74:75], 0, v[162:163]
	s_mov_b32 m0, s72
	v_lshl_add_u64 v[178:179], s[36:37], 0, v[166:167]
	global_load_lds_dwordx4 v[176:177], off
	v_lshl_add_u64 v[176:177], s[74:75], 0, v[166:167]
	s_add_i32 m0, s72, 0x2000
	s_nop 0
	global_load_lds_dwordx4 v[176:177], off
	v_lshl_add_u64 v[176:177], s[36:37], 0, v[162:163]
	s_mov_b32 m0, s64
	s_nop 0
	global_load_lds_dwordx4 v[176:177], off
	s_mov_b32 m0, s65
	s_nop 0
	global_load_lds_dwordx4 v[178:179], off
	s_waitcnt vmcnt(8)
	s_waitcnt lgkmcnt(0)
	s_barrier
	s_setprio 1
	v_mfma_f32_16x16x128_f8f6f4 v[78:81], v[26:33], v[198:205], v[78:81]
	v_mfma_f32_16x16x128_f8f6f4 v[74:77], v[18:25], v[198:205], v[74:77]
	v_mfma_f32_16x16x128_f8f6f4 v[90:93], v[18:25], v[190:197], v[90:93]
	v_mfma_f32_16x16x128_f8f6f4 v[94:97], v[26:33], v[190:197], v[94:97]
	v_mfma_f32_16x16x128_f8f6f4 v[62:65], v[26:33], v[206:213], v[62:65]
	v_mfma_f32_16x16x128_f8f6f4 v[58:61], v[18:25], v[206:213], v[58:61]
	v_mfma_f32_16x16x128_f8f6f4 v[42:45], v[18:25], v[214:221], v[42:45]
	v_mfma_f32_16x16x128_f8f6f4 v[46:49], v[26:33], v[214:221], v[46:49]
	v_mfma_f32_16x16x128_f8f6f4 v[38:41], v[10:17], v[214:221], v[38:41]
	v_mfma_f32_16x16x128_f8f6f4 v[34:37], v[2:9], v[214:221], v[34:37]
	v_mfma_f32_16x16x128_f8f6f4 v[82:85], v[2:9], v[190:197], v[82:85]
	v_mfma_f32_16x16x128_f8f6f4 v[86:89], v[10:17], v[190:197], v[86:89]
	v_mfma_f32_16x16x128_f8f6f4 v[70:73], v[10:17], v[198:205], v[70:73]
	v_mfma_f32_16x16x128_f8f6f4 v[66:69], v[2:9], v[198:205], v[66:69]
	v_mfma_f32_16x16x128_f8f6f4 v[50:53], v[2:9], v[206:213], v[50:53]
	v_mfma_f32_16x16x128_f8f6f4 v[54:57], v[10:17], v[206:213], v[54:57]
	s_setprio 0
	s_barrier
	s_add_i32 s72, 0, 0x18000
	s_add_i32 s73, 0, 0x1c000
	v_add_u32_e32 v14, s72, v188
	v_add_u32_e32 v30, s73, v188
	ds_read_b128 v[2:5], v14
	ds_read_b128 v[6:9], v14 offset:1024
	ds_read_b128 v[10:13], v14 offset:2048
	ds_read_b128 v[14:17], v14 offset:3072
	ds_read_b128 v[18:21], v30
	ds_read_b128 v[22:25], v30 offset:1024
	ds_read_b128 v[26:29], v30 offset:2048
	ds_read_b128 v[30:33], v30 offset:3072
	s_add_u32 s36, s36, 0x158000
	s_addc_u32 s37, s37, 0
	s_mov_b32 m0, s66
	v_lshl_add_u64 v[222:223], s[36:37], 0, v[162:163]
	ds_read_b128 v[190:193], v189 offset:32768
	ds_read_b128 v[194:197], v189 offset:33792
	ds_read_b128 v[198:201], v189 offset:34816
	ds_read_b128 v[202:205], v189 offset:35840
	ds_read_b128 v[206:209], v189 offset:36864
	ds_read_b128 v[210:213], v189 offset:37888
	ds_read_b128 v[214:217], v189 offset:38912
	ds_read_b128 v[218:221], v189 offset:39936
	global_load_lds_dwordx4 v[222:223], off
	v_lshl_add_u64 v[222:223], s[36:37], 0, v[166:167]
	s_mov_b32 m0, s67
	s_nop 0
	global_load_lds_dwordx4 v[222:223], off
	s_waitcnt vmcnt(8)
	s_waitcnt lgkmcnt(0)
	s_barrier
	s_setprio 1
	v_mfma_f32_16x16x128_f8f6f4 v[114:117], v[10:17], v[206:213], v[114:117]
	v_mfma_f32_16x16x128_f8f6f4 v[126:129], v[2:9], v[206:213], v[126:129]
	v_mfma_f32_16x16x128_f8f6f4 v[158:161], v[2:9], v[190:197], v[158:161]
	v_mfma_f32_16x16x128_f8f6f4 v[154:157], v[10:17], v[190:197], v[154:157]
	v_mfma_f32_16x16x128_f8f6f4 v[118:121], v[10:17], v[198:205], v[118:121]
	v_mfma_f32_16x16x128_f8f6f4 v[122:125], v[2:9], v[198:205], v[122:125]
	v_mfma_f32_16x16x128_f8f6f4 v[110:113], v[2:9], v[214:221], v[110:113]
	v_mfma_f32_16x16x128_f8f6f4 v[106:109], v[10:17], v[214:221], v[106:109]
	v_mfma_f32_16x16x128_f8f6f4 v[102:105], v[18:25], v[214:221], v[102:105]
	v_mfma_f32_16x16x128_f8f6f4 v[98:101], v[26:33], v[214:221], v[98:101]
	v_mfma_f32_16x16x128_f8f6f4 v[146:149], v[26:33], v[190:197], v[146:149]
	v_mfma_f32_16x16x128_f8f6f4 v[150:153], v[18:25], v[190:197], v[150:153]
	v_mfma_f32_16x16x128_f8f6f4 v[142:145], v[18:25], v[198:205], v[142:145]
	v_mfma_f32_16x16x128_f8f6f4 v[138:141], v[26:33], v[198:205], v[138:141]
	v_mfma_f32_16x16x128_f8f6f4 v[130:133], v[26:33], v[206:213], v[130:133]
	v_mfma_f32_16x16x128_f8f6f4 v[134:137], v[18:25], v[206:213], v[134:137]
	s_setprio 0
	s_barrier
	s_add_i32 s36, s72, s43
	v_lshl_add_u64 v[172:173], v[172:173], 0, s[22:23]
	s_mov_b32 m0, s36
	ds_read_b128 v[190:193], v189 offset:49152
	ds_read_b128 v[194:197], v189 offset:50176
	ds_read_b128 v[198:201], v189 offset:51200
	ds_read_b128 v[202:205], v189 offset:52224
	ds_read_b128 v[206:209], v189 offset:53248
	ds_read_b128 v[210:213], v189 offset:54272
	ds_read_b128 v[214:217], v189 offset:55296
	ds_read_b128 v[218:221], v189 offset:56320
	global_load_lds_dwordx4 v[172:173], off
	s_add_i32 m0, s36, 0x2000
	s_add_u32 s8, s8, 0x158080
	v_lshl_add_u64 v[172:173], v[174:175], 0, s[22:23]
	s_addc_u32 s9, s9, 0
	s_add_i32 s36, s73, s43
	global_load_lds_dwordx4 v[172:173], off
	v_lshl_add_u64 v[172:173], s[8:9], 0, v[162:163]
	s_mov_b32 m0, s36
	s_nop 0
	global_load_lds_dwordx4 v[172:173], off
	v_lshl_add_u64 v[172:173], s[8:9], 0, v[166:167]
	s_add_i32 m0, s36, 0x2000
	s_nop 0
	global_load_lds_dwordx4 v[172:173], off
	v_lshl_add_u64 v[172:173], v[176:177], 0, s[22:23]
	s_mov_b32 m0, s69
	s_nop 0
	global_load_lds_dwordx4 v[172:173], off
	v_lshl_add_u64 v[172:173], v[178:179], 0, s[22:23]
	s_mov_b32 m0, s70
	s_nop 0
	global_load_lds_dwordx4 v[172:173], off
	s_waitcnt vmcnt(8)
	s_waitcnt lgkmcnt(0)
	s_barrier
	s_setprio 1
	v_mfma_f32_16x16x128_f8f6f4 v[62:65], v[2:9], v[206:213], v[62:65]
	v_mfma_f32_16x16x128_f8f6f4 v[58:61], v[10:17], v[206:213], v[58:61]
	v_mfma_f32_16x16x128_f8f6f4 v[90:93], v[10:17], v[190:197], v[90:93]
	v_mfma_f32_16x16x128_f8f6f4 v[94:97], v[2:9], v[190:197], v[94:97]
	v_mfma_f32_16x16x128_f8f6f4 v[78:81], v[2:9], v[198:205], v[78:81]
	v_mfma_f32_16x16x128_f8f6f4 v[74:77], v[10:17], v[198:205], v[74:77]
	v_mfma_f32_16x16x128_f8f6f4 v[42:45], v[10:17], v[214:221], v[42:45]
	v_mfma_f32_16x16x128_f8f6f4 v[46:49], v[2:9], v[214:221], v[46:49]
	v_mfma_f32_16x16x128_f8f6f4 v[38:41], v[18:25], v[214:221], v[38:41]
	v_mfma_f32_16x16x128_f8f6f4 v[34:37], v[26:33], v[214:221], v[34:37]
	v_mfma_f32_16x16x128_f8f6f4 v[82:85], v[26:33], v[190:197], v[82:85]
	v_mfma_f32_16x16x128_f8f6f4 v[86:89], v[18:25], v[190:197], v[86:89]
	v_mfma_f32_16x16x128_f8f6f4 v[70:73], v[18:25], v[198:205], v[70:73]
	v_mfma_f32_16x16x128_f8f6f4 v[66:69], v[26:33], v[198:205], v[66:69]
	v_mfma_f32_16x16x128_f8f6f4 v[50:53], v[26:33], v[206:213], v[50:53]
	v_mfma_f32_16x16x128_f8f6f4 v[54:57], v[18:25], v[206:213], v[54:57]
	s_setprio 0
	s_barrier
	s_add_i32 s71, s71, 2
	s_add_u32 s6, s6, 0x100
	s_addc_u32 s7, s7, 0
	s_cmpk_lt_u32 s71, 0x54
	s_cbranch_scc1 .LBB0_1745
	s_waitcnt vmcnt(0)
	s_cmpk_gt_u32 s40, 0xff
	s_cbranch_scc1 .LBB0_1748
	s_barrier

.LBB0_1807:
	ds_read_b128 v[26:29], v185
	ds_read_b128 v[30:33], v185 offset:1024
	ds_read_b128 v[18:21], v185 offset:2048
	ds_read_b128 v[22:25], v185 offset:3072
	ds_read_b128 v[10:13], v186
	ds_read_b128 v[14:17], v186 offset:1024
	ds_read_b128 v[2:5], v186 offset:2048
	ds_read_b128 v[6:9], v186 offset:3072
	s_add_u32 s28, s26, 0xffea8080
	s_addc_u32 s29, s27, -1
	s_cmpk_eq_i32 s58, 0x52
	s_cselect_b32 s31, s5, s29
	s_cselect_b32 s30, s4, s28
	s_cselect_b32 s29, s25, s57
	s_cselect_b32 s28, s24, s56
	v_lshl_add_u64 v[212:213], s[26:27], 0, v[166:167]
	s_add_i32 m0, s34, 0xc000
	ds_read_b128 v[174:177], v187
	ds_read_b128 v[178:181], v187 offset:1024
	ds_read_b128 v[188:191], v187 offset:2048
	ds_read_b128 v[192:195], v187 offset:3072
	ds_read_b128 v[196:199], v187 offset:4096
	ds_read_b128 v[200:203], v187 offset:5120
	ds_read_b128 v[204:207], v187 offset:6144
	ds_read_b128 v[208:211], v187 offset:7168
	global_load_lds_dwordx4 v[212:213], off
	v_lshl_add_u64 v[212:213], s[26:27], 0, v[168:169]
	s_add_i32 m0, s34, 0xe000
	s_nop 0
	global_load_lds_dwordx4 v[212:213], off
	s_waitcnt vmcnt(8)
	s_waitcnt lgkmcnt(0)
	s_barrier
	s_setprio 1
	v_mfma_f32_16x16x128_f8f6f4 v[158:161], v[26:33], v[174:181], v[158:161]
	v_mfma_f32_16x16x128_f8f6f4 v[154:157], v[18:25], v[174:181], v[154:157]
	v_mfma_f32_16x16x128_f8f6f4 v[138:141], v[18:25], v[188:195], v[138:141]
	v_mfma_f32_16x16x128_f8f6f4 v[142:145], v[26:33], v[188:195], v[142:145]
	v_mfma_f32_16x16x128_f8f6f4 v[126:129], v[26:33], v[196:203], v[126:129]
	v_mfma_f32_16x16x128_f8f6f4 v[122:125], v[18:25], v[196:203], v[122:125]
	v_mfma_f32_16x16x128_f8f6f4 v[106:109], v[18:25], v[204:211], v[106:109]
	v_mfma_f32_16x16x128_f8f6f4 v[110:113], v[26:33], v[204:211], v[110:113]
	v_mfma_f32_16x16x128_f8f6f4 v[102:105], v[10:17], v[204:211], v[102:105]
	v_mfma_f32_16x16x128_f8f6f4 v[98:101], v[2:9], v[204:211], v[98:101]
	v_mfma_f32_16x16x128_f8f6f4 v[146:149], v[2:9], v[174:181], v[146:149]
	v_mfma_f32_16x16x128_f8f6f4 v[150:153], v[10:17], v[174:181], v[150:153]
	v_mfma_f32_16x16x128_f8f6f4 v[134:137], v[10:17], v[188:195], v[134:137]
	v_mfma_f32_16x16x128_f8f6f4 v[130:133], v[2:9], v[188:195], v[130:133]
	v_mfma_f32_16x16x128_f8f6f4 v[114:117], v[2:9], v[196:203], v[114:117]
	v_mfma_f32_16x16x128_f8f6f4 v[118:121], v[10:17], v[196:203], v[118:121]
	s_setprio 0
	s_barrier
	s_add_i32 s59, s42, s3
	v_lshl_add_u64 v[174:175], s[28:29], 0, v[164:165]
	s_mov_b32 m0, s59
	ds_read_b128 v[188:191], v187 offset:16384
	ds_read_b128 v[192:195], v187 offset:17408
	ds_read_b128 v[196:199], v187 offset:18432
	ds_read_b128 v[200:203], v187 offset:19456
	ds_read_b128 v[204:207], v187 offset:20480
	ds_read_b128 v[208:211], v187 offset:21504
	ds_read_b128 v[212:215], v187 offset:22528
	ds_read_b128 v[216:219], v187 offset:23552
	global_load_lds_dwordx4 v[174:175], off
	s_add_i32 m0, s59, 0x2000
	s_add_u32 s60, s28, 0x158000
	v_lshl_add_u64 v[176:177], s[28:29], 0, v[162:163]
	s_addc_u32 s61, s29, 0
	s_add_i32 s59, s43, s3
	global_load_lds_dwordx4 v[176:177], off
	v_lshl_add_u64 v[178:179], s[60:61], 0, v[164:165]
	s_mov_b32 m0, s59
	v_lshl_add_u64 v[180:181], s[30:31], 0, v[162:163]
	global_load_lds_dwordx4 v[178:179], off
	v_lshl_add_u64 v[178:179], s[60:61], 0, v[162:163]
	s_add_i32 m0, s59, 0x2000
	s_nop 0
	global_load_lds_dwordx4 v[178:179], off
	v_lshl_add_u64 v[178:179], s[30:31], 0, v[164:165]
	s_mov_b32 m0, s34
	s_nop 0
	global_load_lds_dwordx4 v[178:179], off
	s_mov_b32 m0, s35
	s_nop 0
	global_load_lds_dwordx4 v[180:181], off
	s_waitcnt vmcnt(8)
	s_waitcnt lgkmcnt(0)
	s_barrier
	s_setprio 1
	v_mfma_f32_16x16x128_f8f6f4 v[78:81], v[26:33], v[196:203], v[78:81]
	v_mfma_f32_16x16x128_f8f6f4 v[74:77], v[18:25], v[196:203], v[74:77]
	v_mfma_f32_16x16x128_f8f6f4 v[90:93], v[18:25], v[188:195], v[90:93]
	v_mfma_f32_16x16x128_f8f6f4 v[94:97], v[26:33], v[188:195], v[94:97]
	v_mfma_f32_16x16x128_f8f6f4 v[62:65], v[26:33], v[204:211], v[62:65]
	v_mfma_f32_16x16x128_f8f6f4 v[58:61], v[18:25], v[204:211], v[58:61]
	v_mfma_f32_16x16x128_f8f6f4 v[42:45], v[18:25], v[212:219], v[42:45]
	v_mfma_f32_16x16x128_f8f6f4 v[54:57], v[26:33], v[212:219], v[54:57]
	v_mfma_f32_16x16x128_f8f6f4 v[38:41], v[10:17], v[212:219], v[38:41]
	v_mfma_f32_16x16x128_f8f6f4 v[34:37], v[2:9], v[212:219], v[34:37]
	v_mfma_f32_16x16x128_f8f6f4 v[82:85], v[2:9], v[188:195], v[82:85]
	v_mfma_f32_16x16x128_f8f6f4 v[86:89], v[10:17], v[188:195], v[86:89]
	v_mfma_f32_16x16x128_f8f6f4 v[70:73], v[10:17], v[196:203], v[70:73]
	v_mfma_f32_16x16x128_f8f6f4 v[66:69], v[2:9], v[196:203], v[66:69]
	v_mfma_f32_16x16x128_f8f6f4 v[46:49], v[2:9], v[204:211], v[46:49]
	v_mfma_f32_16x16x128_f8f6f4 v[50:53], v[10:17], v[204:211], v[50:53]
	s_setprio 0
	s_barrier
	s_add_i32 s59, 0, 0x18000
	s_add_i32 s60, 0, 0x1c000
	v_add_u32_e32 v14, s59, v183
	v_add_u32_e32 v30, s60, v183
	ds_read_b128 v[2:5], v14
	ds_read_b128 v[6:9], v14 offset:1024
	ds_read_b128 v[10:13], v14 offset:2048
	ds_read_b128 v[14:17], v14 offset:3072
	ds_read_b128 v[18:21], v30
	ds_read_b128 v[22:25], v30 offset:1024
	ds_read_b128 v[26:29], v30 offset:2048
	ds_read_b128 v[30:33], v30 offset:3072
	s_add_u32 s30, s30, 0x158000
	s_addc_u32 s31, s31, 0
	s_mov_b32 m0, s36
	v_lshl_add_u64 v[220:221], s[30:31], 0, v[164:165]
	ds_read_b128 v[188:191], v187 offset:32768
	ds_read_b128 v[192:195], v187 offset:33792
	ds_read_b128 v[196:199], v187 offset:34816
	ds_read_b128 v[200:203], v187 offset:35840
	ds_read_b128 v[204:207], v187 offset:36864
	ds_read_b128 v[208:211], v187 offset:37888
	ds_read_b128 v[212:215], v187 offset:38912
	ds_read_b128 v[216:219], v187 offset:39936
	global_load_lds_dwordx4 v[220:221], off
	v_lshl_add_u64 v[220:221], s[30:31], 0, v[162:163]
	s_mov_b32 m0, s37
	s_nop 0
	global_load_lds_dwordx4 v[220:221], off
	s_waitcnt vmcnt(8)
	s_waitcnt lgkmcnt(0)
	s_barrier
	s_setprio 1
	v_mfma_f32_16x16x128_f8f6f4 v[122:125], v[10:17], v[204:211], v[122:125]
	v_mfma_f32_16x16x128_f8f6f4 v[126:129], v[2:9], v[204:211], v[126:129]
	v_mfma_f32_16x16x128_f8f6f4 v[158:161], v[2:9], v[188:195], v[158:161]
	v_mfma_f32_16x16x128_f8f6f4 v[154:157], v[10:17], v[188:195], v[154:157]
	v_mfma_f32_16x16x128_f8f6f4 v[138:141], v[10:17], v[196:203], v[138:141]
	v_mfma_f32_16x16x128_f8f6f4 v[142:145], v[2:9], v[196:203], v[142:145]
	v_mfma_f32_16x16x128_f8f6f4 v[110:113], v[2:9], v[212:219], v[110:113]
	v_mfma_f32_16x16x128_f8f6f4 v[106:109], v[10:17], v[212:219], v[106:109]
	v_mfma_f32_16x16x128_f8f6f4 v[102:105], v[18:25], v[212:219], v[102:105]
	v_mfma_f32_16x16x128_f8f6f4 v[98:101], v[26:33], v[212:219], v[98:101]
	v_mfma_f32_16x16x128_f8f6f4 v[146:149], v[26:33], v[188:195], v[146:149]
	v_mfma_f32_16x16x128_f8f6f4 v[150:153], v[18:25], v[188:195], v[150:153]
	v_mfma_f32_16x16x128_f8f6f4 v[134:137], v[18:25], v[196:203], v[134:137]
	v_mfma_f32_16x16x128_f8f6f4 v[130:133], v[26:33], v[196:203], v[130:133]
	v_mfma_f32_16x16x128_f8f6f4 v[114:117], v[26:33], v[204:211], v[114:117]
	v_mfma_f32_16x16x128_f8f6f4 v[118:121], v[18:25], v[204:211], v[118:121]
	s_setprio 0
	s_barrier
	s_add_i32 s30, s59, s3
	v_lshl_add_u64 v[174:175], v[174:175], 0, s[10:11]
	s_mov_b32 m0, s30
	ds_read_b128 v[188:191], v187 offset:49152
	ds_read_b128 v[192:195], v187 offset:50176
	ds_read_b128 v[196:199], v187 offset:51200
	ds_read_b128 v[200:203], v187 offset:52224
	ds_read_b128 v[204:207], v187 offset:53248
	ds_read_b128 v[208:211], v187 offset:54272
	ds_read_b128 v[212:215], v187 offset:55296
	ds_read_b128 v[216:219], v187 offset:56320
	global_load_lds_dwordx4 v[174:175], off
	s_add_i32 m0, s30, 0x2000
	s_add_u32 s28, s28, 0x158080
	v_lshl_add_u64 v[174:175], v[176:177], 0, s[10:11]
	s_addc_u32 s29, s29, 0
	s_add_i32 s30, s60, s3
	global_load_lds_dwordx4 v[174:175], off
	v_lshl_add_u64 v[174:175], s[28:29], 0, v[164:165]
	s_mov_b32 m0, s30
	s_nop 0
	global_load_lds_dwordx4 v[174:175], off
	v_lshl_add_u64 v[174:175], s[28:29], 0, v[162:163]
	s_add_i32 m0, s30, 0x2000
	s_nop 0
	global_load_lds_dwordx4 v[174:175], off
	v_lshl_add_u64 v[174:175], v[178:179], 0, s[10:11]
	s_mov_b32 m0, s40
	s_nop 0
	global_load_lds_dwordx4 v[174:175], off
	v_lshl_add_u64 v[174:175], v[180:181], 0, s[10:11]
	s_mov_b32 m0, s41
	s_nop 0
	global_load_lds_dwordx4 v[174:175], off
	s_waitcnt vmcnt(8)
	s_waitcnt lgkmcnt(0)
	s_barrier
	s_setprio 1
	v_mfma_f32_16x16x128_f8f6f4 v[62:65], v[2:9], v[204:211], v[62:65]
	v_mfma_f32_16x16x128_f8f6f4 v[58:61], v[10:17], v[204:211], v[58:61]
	v_mfma_f32_16x16x128_f8f6f4 v[90:93], v[10:17], v[188:195], v[90:93]
	v_mfma_f32_16x16x128_f8f6f4 v[94:97], v[2:9], v[188:195], v[94:97]
	v_mfma_f32_16x16x128_f8f6f4 v[78:81], v[2:9], v[196:203], v[78:81]
	v_mfma_f32_16x16x128_f8f6f4 v[74:77], v[10:17], v[196:203], v[74:77]
	v_mfma_f32_16x16x128_f8f6f4 v[42:45], v[10:17], v[212:219], v[42:45]
	v_mfma_f32_16x16x128_f8f6f4 v[54:57], v[2:9], v[212:219], v[54:57]
	v_mfma_f32_16x16x128_f8f6f4 v[38:41], v[18:25], v[212:219], v[38:41]
	v_mfma_f32_16x16x128_f8f6f4 v[34:37], v[26:33], v[212:219], v[34:37]
	v_mfma_f32_16x16x128_f8f6f4 v[82:85], v[26:33], v[188:195], v[82:85]
	v_mfma_f32_16x16x128_f8f6f4 v[86:89], v[18:25], v[188:195], v[86:89]
	v_mfma_f32_16x16x128_f8f6f4 v[70:73], v[18:25], v[196:203], v[70:73]
	v_mfma_f32_16x16x128_f8f6f4 v[66:69], v[26:33], v[196:203], v[66:69]
	v_mfma_f32_16x16x128_f8f6f4 v[46:49], v[26:33], v[204:211], v[46:49]
	v_mfma_f32_16x16x128_f8f6f4 v[50:53], v[18:25], v[204:211], v[50:53]
	s_setprio 0
	s_barrier
	s_add_i32 s58, s58, 2
	s_add_u32 s26, s26, 0x100
	s_addc_u32 s27, s27, 0
	s_add_u32 s56, s56, 0x100
	s_addc_u32 s57, s57, 0
	s_cmpk_gt_u32 s58, 0x53
	s_cbranch_scc0 .LBB0_1807
	s_and_b64 vcc, exec, s[12:13]
	s_cbranch_vccz .LBB0_1810
	s_barrier
